# v6 + peeled first K-loop iteration after every epilogue (14 GEMM loops): first two counted waits no longer drain the epilogue stores; MoE-up loop de-waterfalled
# speedup vs baseline: 1.0022x; 1.0022x over previous
;     __device__ __forceinline__ unsigned a_off(const Unit& u, const Gemm& g) const { return (unsigned)u.pm * (unsigned)(BM * 2) * (unsigned)g.K; }
;     __device__ __forceinline__ unsigned b_off(const Unit& u, const Gemm& g) const { return (unsigned)u.pn * (unsigned)(BM * 2) * (unsigned)g.K; }
;     __device__ __forceinline__ bool next(int i, Unit& u) const { return so.next(i, u); }
; template <class Epi, class Sched, bool ALIGN_EPI = false, bool SP2 = false, bool FP8 = false>
; __device__ __forceinline__ void gemm_phase(LAS unsigned char* lds, const Gemm g, const Sched& S, const Epi& E, int wbase) {
;     ...
;     for (int i = 0; i < 2; ++i) { int R, C; stage_rc(tid * 16 + i * 8192, R, C); const int Rb = Epi::PERM ? ((R & ~31) + perm32(R & 31)) : R;
;         voffA[i] = (unsigned)(R * K + C) * 2u; voffB[i] = (unsigned)(Rb * K + C) * 2u; }
;     const unsigned kstep = (unsigned)(BK * 2);
;     const unsigned hstep = (unsigned)HALF * (unsigned)K * 2u;
;     typedef __amdgpu_buffer_rsrc_t rsrc_t;
;     const rsrc_t rA0 = __builtin_amdgcn_make_buffer_rsrc((void*)g.A, 0, 0xffffffff, 0x00020000), rB0 = __builtin_amdgcn_make_buffer_rsrc((void*)g.Bt, 0, 0xffffffff, 0x00020000);
;     rsrc_t rA1 = rA0, rB1 = rB0;
;     if constexpr (Sched::TWO) { rA1 = __builtin_amdgcn_make_buffer_rsrc((void*)S.A1, 0, 0xffffffff, 0x00020000); rB1 = __builtin_amdgcn_make_buffer_rsrc((void*)S.Bt1, 0, 0xffffffff, 0x00020000); }
;     const unsigned ldsw = (unsigned)wid * 1024u;
;     const int aoff = lds_byte(wr * 64 + fr, fq * 8), boff = lds_byte(wc * 32 + fr, fq * 8);
;     ...
;     Unit cur, nxt; int ui = 0;
;     if (!S.next(0, cur)) return;
;     f32x4 acc[2][2][4][2];
;     ...
;     PG8_ZERO_ACC();
;     v8i_t At[4], B0[2], B1[2];
;     unsigned cA = S.a_off(cur, g), cB = S.b_off(cur, g); rsrc_t rAc = (Sched::TWO && cur.part) ? rA1 : rA0, rBc = (Sched::TWO && cur.part) ? rB1 : rB0;
;     S.a_ready(cur);
;     if constexpr (SP2) {
;         PG8_STAGE(PG8_SB(0, 0), rBc, cB, voffB); PG8_STAGE(PG8_SB(0, 1), rBc, cB + hstep, voffB); PG8_STAGE(PG8_SA(0, 0), rAc, cA, voffA); PG8_STAGE(PG8_SA(0, 1), rAc, cA + hstep, voffA);
;         if (wr == 1) PG8_BAR;
;         PG8_WAIT_V(2); PG8_BAR;
;         PG8_STAGE(PG8_SB(1, 0), rBc, cB + kstep, voffB); PG8_STAGE(PG8_SA(1, 0), rAc, cA + kstep, voffA); PG8_STAGE(PG8_SB(1, 1), rBc, cB + hstep + kstep, voffB);
;         PG8_WAIT_V(6); PG8_BAR;
.LBB0_251:
	v_readlane_b32 s6, v255, 11
	s_cmp_eq_u32 s6, 0
	s_cselect_b32 s6, 0, 0x200000
	s_lshl_b32 s22, s95, 6
	s_add_u32 s14, s2, 0x1f800000
	s_addc_u32 s15, s3, 0
	s_add_u32 s2, s2, s6
	s_addc_u32 s3, s3, 0
	s_add_u32 s62, s2, 0x17200000
	s_addc_u32 s63, s3, 0
	s_add_i32 s58, s42, 0x18000
	s_or_b32 s2, s28, 0x80
	s_mov_b32 s6, s38
	s_mov_b32 s7, s39
	s_mov_b32 m0, s58
	s_add_i32 s59, s42, 0x1a000
	s_waitcnt vmcnt(2)
	s_barrier
	buffer_load_dwordx4 v222, s[4:7], s2 offen lds
	s_mov_b32 m0, s59
	s_add_i32 s12, s42, 0x8000
	buffer_load_dwordx4 v193, s[4:7], s2 offen lds
	s_or_b32 s2, s29, 0x80
	s_mov_b32 m0, s12
	s_add_i32 s13, s42, 0xa000
	buffer_load_dwordx4 v192, s[36:39], s2 offen lds
	s_mov_b32 m0, s13
	s_add_i32 s65, s42, 0x1c000
	buffer_load_dwordx4 v223, s[36:39], s2 offen lds
	s_bitset1_b32 s20, 7
	s_mov_b32 m0, s65
	s_add_i32 s33, s42, 0x1e000
	buffer_load_dwordx4 v222, s[4:7], s20 offen lds
	s_mov_b32 m0, s33
	s_ashr_i32 s3, s16, 31
	buffer_load_dwordx4 v193, s[4:7], s20 offen lds
	v_bfe_u32 v253, v4, 4, 2
	s_lshr_b32 s3, s3, 26
	v_and_b32_e32 v164, 15, v4
	s_add_i32 s3, s16, s3
	v_lshlrev_b32_e32 v5, 4, v253
	v_lshlrev_b32_e32 v4, 2, v4
	s_and_b32 s2, s18, 3
	s_ashr_i32 s77, s3, 6
	v_lshl_or_b32 v5, v164, 6, v5
	s_lshl_b32 s3, s19, 13
	v_and_b32_e32 v4, 32, v4
	s_lshl_b32 s48, s19, 6
	v_bitop3_b32 v6, v5, s3, v4 bitop3:0xde
	s_lshl_b32 s3, s2, 12
	s_cmp_gt_i32 s16, 63
	s_cselect_b64 s[66:67], -1, 0
	s_add_i32 s18, s77, -2
	s_add_i32 s19, s42, 0xc000
	v_bitop3_b32 v4, v5, s3, v4 bitop3:0xde
	s_waitcnt vmcnt(6)
	s_cmpk_lt_u32 s1, 0x100
	s_mov_b32 s23, s40
	s_cselect_b64 s[78:79], -1, 0
	s_lshl_b32 s1, s2, 6
	v_add_u32_e32 v4, 0, v4
	v_mov_b32_e32 v1, v0
	v_mov_b32_e32 v2, v0
	v_mov_b32_e32 v3, v0
	s_mov_b32 s76, 0
	s_add_i32 s20, s42, 0xe000
	v_add_u32_e32 v252, 0x10000, v4
	v_add_u32_e32 v225, 0x14000, v4
	v_add_u32_e32 v172, 0, v6
	v_add_u32_e32 v173, 0x18000, v4
	v_add_u32_e32 v174, 0x1c000, v4
	s_lshl_b64 s[22:23], s[22:23], 2
	s_lshl_b32 s24, s1, 1
	s_barrier
	s_mov_b32 s100, 0
	s_branch .LBB0_254

;     __device__ __forceinline__ unsigned a_off(const Unit& u, const Gemm& g) const { return (unsigned)u.pm * (unsigned)(BM * 2) * (unsigned)g.K; }
;     __device__ __forceinline__ unsigned b_off(const Unit& u, const Gemm& g) const { return (unsigned)u.pn * (unsigned)(BM * 2) * (unsigned)g.K; }
;     __device__ __forceinline__ bool next(int i, Unit& u) const { return so.next(i, u); }
;     __device__ __forceinline__ unsigned a_off(const Unit& u, const Gemm& g) const { return (unsigned)u.pm * (unsigned)(BM * 2) * (unsigned)g.K; }
;     __device__ __forceinline__ bool next(int i, Unit& u) const { const bool ok = so.next(i >> 1, u); u.part = i & 1; return ok; }
;     __device__ __forceinline__ unsigned a_off(const Unit& u, const Gemm& g) const { return (unsigned)u.pm * (unsigned)(BM * 2) * (unsigned)g.K; }
; #define PG8_WAIT_V(n) asm volatile("s_waitcnt vmcnt(" #n ")" ::: "memory")
; #define PG8_BAR __builtin_amdgcn_s_barrier()
; template <class Epi, class Sched, bool ALIGN_EPI = false, bool SP2 = false, bool FP8 = false>
; __device__ __forceinline__ void gemm_phase(LAS unsigned char* lds, const Gemm g, const Sched& S, const Epi& E, int wbase) {
;     ...
;     PG8_ZERO_ACC();
;     ...
;         const bool has_next = S.next(ui + 1, nxt);
;         const unsigned nA = has_next ? S.a_off(nxt, g) : cA, nB = has_next ? S.b_off(nxt, g) : cB;
;         const rsrc_t rAn = (Sched::TWO && has_next) ? (nxt.part ? rA1 : rA0) : rAc, rBn = (Sched::TWO && has_next) ? (nxt.part ? rB1 : rB0) : rBc;
;         float pre_[8] = {0.f, 0.f, 0.f, 0.f, 0.f, 0.f, 0.f, 0.f};
;         if constexpr (Epi::HAS_PRE) E.pre_load(pre_, cur, wr);
;         for (int t = 0; t < nt; t += 2) {
;             const bool last = (t == nt - 2);
;             const unsigned a1 = cA + (unsigned)(t + 1) * kstep;
;             const unsigned a2 = last ? nA : cA + (unsigned)(t + 2) * kstep, b2 = last ? nB : cB + (unsigned)(t + 2) * kstep; const rsrc_t rA2 = (Sched::TWO && last) ? rAn : rAc, rB2 = (Sched::TWO && last) ? rBn : rBc;
;             const unsigned a3 = a2 + kstep, b3 = b2 + kstep;
;             if (last && has_next) S.a_ready(nxt);
;             if constexpr (SP2) {
;             PG8_LDB(B0, 0, 0); PG8_LDB(B1, 0, 1); PG8_SCHED; PG8_LDA(At, 0, 0); PG8_STAGE(PG8_SA(1, 1), rAc, a1 + hstep, voffA);
;             PG8_WAIT_V(8); PG8_WAIT_L(0); PG8_BAR; PG8_MMA(0, 0, At, B0); PG8_MMA(0, 1, At, B1); PG8_BAR; PG8_SCHED;
.LBB0_256:
	s_lshl_b32 s82, s1, 18
	s_andn2_b64 vcc, exec, s[66:67]
	s_lshl_b32 s83, s21, 18
	s_cbranch_vccnz .LBB0_260
	s_and_b64 s[2:3], s[26:27], exec
	v_mov_b64_e32 v[6:7], v[2:3]
	v_mov_b64_e32 v[18:19], v[2:3]
	v_mov_b64_e32 v[22:23], v[2:3]
	v_mov_b64_e32 v[34:35], v[2:3]
	v_mov_b64_e32 v[38:39], v[2:3]
	v_mov_b64_e32 v[50:51], v[2:3]
	v_mov_b64_e32 v[54:55], v[2:3]
	v_mov_b64_e32 v[10:11], v[2:3]
	v_mov_b64_e32 v[14:15], v[2:3]
	v_mov_b64_e32 v[26:27], v[2:3]
	v_mov_b64_e32 v[30:31], v[2:3]
	v_mov_b64_e32 v[42:43], v[2:3]
	v_mov_b64_e32 v[46:47], v[2:3]
	v_mov_b64_e32 v[58:59], v[2:3]
	s_waitcnt vmcnt(37)
	v_mov_b64_e32 v[62:63], v[2:3]
	s_waitcnt vmcnt(36)
	v_mov_b64_e32 v[66:67], v[2:3]
	s_waitcnt vmcnt(35)
	v_mov_b64_e32 v[70:71], v[2:3]
	s_waitcnt vmcnt(32)
	v_mov_b64_e32 v[82:83], v[2:3]
	s_waitcnt vmcnt(31)
	v_mov_b64_e32 v[86:87], v[2:3]
	s_waitcnt vmcnt(28)
	v_mov_b64_e32 v[98:99], v[2:3]
	s_waitcnt vmcnt(27)
	v_mov_b64_e32 v[102:103], v[2:3]
	s_waitcnt vmcnt(24)
	v_mov_b64_e32 v[114:115], v[2:3]
	s_waitcnt vmcnt(23)
	v_mov_b64_e32 v[118:119], v[2:3]
	v_mov_b64_e32 v[74:75], v[2:3]
	v_mov_b64_e32 v[78:79], v[2:3]
	v_mov_b64_e32 v[90:91], v[2:3]
	v_mov_b64_e32 v[94:95], v[2:3]
	v_mov_b64_e32 v[106:107], v[2:3]
	v_mov_b64_e32 v[110:111], v[2:3]
	s_waitcnt vmcnt(22)
	v_mov_b64_e32 v[122:123], v[2:3]
	v_mov_b64_e32 v[126:127], v[2:3]
	v_mov_b32_e32 v231, v164
	v_mov_b32_e32 v230, 0xff61b1e6
	v_mov_b32_e32 v175, v233
	s_cselect_b32 s2, s82, s29
	s_cselect_b32 s3, s83, s28
	s_add_i32 s16, s29, 0x80
	s_addk_i32 s28, 0x100
	s_mov_b32 s29, 0
	v_mov_b64_e32 v[4:5], v[0:1]
	v_mov_b64_e32 v[16:17], v[0:1]
	v_mov_b64_e32 v[20:21], v[0:1]
	v_mov_b64_e32 v[32:33], v[0:1]
	v_mov_b64_e32 v[36:37], v[0:1]
	v_mov_b64_e32 v[48:49], v[0:1]
	v_mov_b64_e32 v[52:53], v[0:1]
	v_mov_b64_e32 v[8:9], v[0:1]
	v_mov_b64_e32 v[12:13], v[0:1]
	v_mov_b64_e32 v[24:25], v[0:1]
	v_mov_b64_e32 v[28:29], v[0:1]
	v_mov_b64_e32 v[40:41], v[0:1]
	v_mov_b64_e32 v[44:45], v[0:1]
	v_mov_b64_e32 v[56:57], v[0:1]
	v_mov_b64_e32 v[60:61], v[0:1]
	v_mov_b64_e32 v[64:65], v[0:1]
	v_mov_b64_e32 v[68:69], v[0:1]
	v_mov_b64_e32 v[80:81], v[0:1]
	v_mov_b64_e32 v[84:85], v[0:1]
	v_mov_b64_e32 v[96:97], v[0:1]
	v_mov_b64_e32 v[100:101], v[0:1]
	v_mov_b64_e32 v[112:113], v[0:1]
	v_mov_b64_e32 v[116:117], v[0:1]
	v_mov_b64_e32 v[72:73], v[0:1]
	v_mov_b64_e32 v[76:77], v[0:1]
	v_mov_b64_e32 v[88:89], v[0:1]
	v_mov_b64_e32 v[92:93], v[0:1]
	v_mov_b64_e32 v[104:105], v[0:1]
	v_mov_b64_e32 v[108:109], v[0:1]
	v_mov_b64_e32 v[120:121], v[0:1]
	v_mov_b64_e32 v[124:125], v[0:1]
	s_cmp_eq_u32 s100, 1
	s_cbranch_scc0 .LBB0_258
	ds_read_b128 v[128:131], v252
	ds_read_b128 v[132:135], v252 offset:1024
	ds_read_b128 v[136:139], v252 offset:2048
	ds_read_b128 v[140:143], v252 offset:3072
	ds_read_b128 v[144:147], v225
	ds_read_b128 v[148:151], v225 offset:1024
	ds_read_b128 v[152:155], v225 offset:2048
	ds_read_b128 v[156:159], v225 offset:3072
	s_add_i32 s6, s16, 0x80
	s_cmp_eq_u32 s18, s29
	s_cselect_b32 s46, s2, s6
	s_cselect_b32 s31, s3, s28
	s_or_b32 s30, s46, 0x80
	s_add_i32 s6, s41, s16
	s_mov_b32 m0, s19
	ds_read_b128 v[176:179], v172
	ds_read_b128 v[180:183], v172 offset:1024
	ds_read_b128 v[184:187], v172 offset:2048
	ds_read_b128 v[188:191], v172 offset:3072
	ds_read_b128 v[194:197], v172 offset:4096
	ds_read_b128 v[198:201], v172 offset:5120
	ds_read_b128 v[202:205], v172 offset:6144
	ds_read_b128 v[206:209], v172 offset:7168
	buffer_load_dwordx4 v192, s[36:39], s6 offen lds
	s_mov_b32 m0, s20
	s_nop 0
	buffer_load_dwordx4 v223, s[36:39], s6 offen lds
	s_waitcnt vmcnt(32)
	s_waitcnt lgkmcnt(0)
	s_barrier
	s_setprio 1
	s_waitcnt lgkmcnt(6)
	v_mfma_scale_f32_16x16x128_f8f6f4 v[124:127], v[128:135], v[176:183], v[124:127], v224, v224 op_sel_hi:[0,0,0]
	v_mfma_scale_f32_16x16x128_f8f6f4 v[120:123], v[136:143], v[176:183], v[120:123], v224, v224 op_sel_hi:[0,0,0]
	s_waitcnt lgkmcnt(4)
	v_mfma_scale_f32_16x16x128_f8f6f4 v[108:111], v[128:135], v[184:191], v[108:111], v224, v224 op_sel_hi:[0,0,0]
	v_mfma_scale_f32_16x16x128_f8f6f4 v[104:107], v[136:143], v[184:191], v[104:107], v224, v224 op_sel_hi:[0,0,0]
	s_waitcnt lgkmcnt(2)
	v_mfma_scale_f32_16x16x128_f8f6f4 v[160:163], v[128:135], v[194:201], v[92:95], v224, v224 op_sel_hi:[0,0,0]
	v_mfma_scale_f32_16x16x128_f8f6f4 v[210:213], v[136:143], v[194:201], v[88:91], v224, v224 op_sel_hi:[0,0,0]
	s_waitcnt lgkmcnt(0)
	v_mfma_scale_f32_16x16x128_f8f6f4 v[214:217], v[128:135], v[202:209], v[76:79], v224, v224 op_sel_hi:[0,0,0]
	v_mfma_scale_f32_16x16x128_f8f6f4 v[218:221], v[136:143], v[202:209], v[72:75], v224, v224 op_sel_hi:[0,0,0]
	s_setprio 0
	s_setprio 1
	v_mfma_scale_f32_16x16x128_f8f6f4 v[116:119], v[144:151], v[176:183], v[116:119], v224, v224 op_sel_hi:[0,0,0]
	v_mfma_scale_f32_16x16x128_f8f6f4 v[112:115], v[152:159], v[176:183], v[112:115], v224, v224 op_sel_hi:[0,0,0]
	v_mfma_scale_f32_16x16x128_f8f6f4 v[100:103], v[144:151], v[184:191], v[100:103], v224, v224 op_sel_hi:[0,0,0]
	v_mfma_scale_f32_16x16x128_f8f6f4 v[96:99], v[152:159], v[184:191], v[96:99], v224, v224 op_sel_hi:[0,0,0]
	v_mfma_scale_f32_16x16x128_f8f6f4 v[176:179], v[144:151], v[194:201], v[84:87], v224, v224 op_sel_hi:[0,0,0]
	v_mfma_scale_f32_16x16x128_f8f6f4 v[180:183], v[152:159], v[194:201], v[80:83], v224, v224 op_sel_hi:[0,0,0]
	v_mfma_scale_f32_16x16x128_f8f6f4 v[184:187], v[144:151], v[202:209], v[68:71], v224, v224 op_sel_hi:[0,0,0]
	v_mfma_scale_f32_16x16x128_f8f6f4 v[188:191], v[152:159], v[202:209], v[64:67], v224, v224 op_sel_hi:[0,0,0]
	s_setprio 0
	s_barrier
; #define PG8_STAGE(bufoff, rs_, soff_, voff) do { _Pragma("unroll") for (int _i = 0; _i < 2; ++_i) \
;         __builtin_amdgcn_raw_ptr_buffer_load_lds(rs_, (LAS void*)(lds + (bufoff) + ldsw + _i * 8192), 16, (int)(voff)[_i], (int)(soff_), 0, 0); } while (0)
; #define PG8_LDA(dst, b, h) do { _Pragma("unroll") for (int m = 0; m < 4; ++m) dst[m] = PG8_LD2(lds + PG8_SA(b, h) + aoff + m * 2048); } while (0)
; #define PG8_LDB(dst, b, h) do { _Pragma("unroll") for (int n = 0; n < 2; ++n) dst[n] = PG8_LD2(lds + PG8_SB(b, h) + boff + n * 2048); } while (0)
; #define PG8_WAIT_V(n) asm volatile("s_waitcnt vmcnt(" #n ")" ::: "memory")
; #define PG8_WAIT_L(n) asm volatile("s_waitcnt lgkmcnt(" #n ")" ::: "memory")
; #define PG8_BAR __builtin_amdgcn_s_barrier()
; #define PG8_SCHED __builtin_amdgcn_sched_barrier(0)
; template <class Epi, class Sched, bool ALIGN_EPI = false, bool SP2 = false, bool FP8 = false>
; __device__ __forceinline__ void gemm_phase(LAS unsigned char* lds, const Gemm g, const Sched& S, const Epi& E, int wbase) {
;     ...
;             PG8_LDA(At, 0, 1); PG8_STAGE(PG8_SB(0, 0), rB2, b2, voffB); PG8_STAGE(PG8_SB(0, 1), rB2, b2 + hstep, voffB); PG8_STAGE(PG8_SA(0, 0), rA2, a2, voffA);
;             PG8_WAIT_V(8); PG8_WAIT_L(0); PG8_BAR; PG8_MMA(1, 0, At, B0); PG8_MMA(1, 1, At, B1); PG8_BAR; PG8_SCHED;
;             PG8_LDB(B0, 1, 0); PG8_LDB(B1, 1, 1); PG8_SCHED; PG8_LDA(At, 1, 0); PG8_STAGE(PG8_SA(0, 1), rA2, a2 + hstep, voffA);
;             PG8_WAIT_V(8); PG8_WAIT_L(0); PG8_BAR; PG8_MMA(0, 0, At, B0); PG8_MMA(0, 1, At, B1); PG8_BAR; PG8_SCHED;
	s_mov_b32 m0, s43
	s_mov_b32 s6, s38
	s_mov_b32 s7, s39
	s_nop 1
	ds_read_b128 v[64:67], v172 offset:16384
	ds_read_b128 v[68:71], v172 offset:17408
	ds_read_b128 v[72:75], v172 offset:18432
	ds_read_b128 v[76:79], v172 offset:19456
	ds_read_b128 v[80:83], v172 offset:20480
	ds_read_b128 v[84:87], v172 offset:21504
	ds_read_b128 v[88:91], v172 offset:22528
	ds_read_b128 v[92:95], v172 offset:23552
	buffer_load_dwordx4 v222, s[4:7], s31 offen lds
	s_mov_b32 m0, s44
	s_add_i32 s47, s31, s41
	buffer_load_dwordx4 v193, s[4:7], s31 offen lds
	s_mov_b32 m0, s45
	s_nop 0
	buffer_load_dwordx4 v222, s[4:7], s47 offen lds
	s_mov_b32 m0, s52
	s_nop 0
	buffer_load_dwordx4 v193, s[4:7], s47 offen lds
	s_mov_b32 m0, s42
	s_nop 0
	buffer_load_dwordx4 v192, s[36:39], s46 offen lds
	s_mov_b32 m0, s53
	s_nop 0
	buffer_load_dwordx4 v223, s[36:39], s46 offen lds
	s_waitcnt vmcnt(32)
	s_waitcnt lgkmcnt(0)
	s_barrier
	s_setprio 1
	s_waitcnt lgkmcnt(6)
	v_mfma_scale_f32_16x16x128_f8f6f4 v[60:63], v[128:135], v[64:71], v[60:63], v224, v224 op_sel_hi:[0,0,0]
	v_mfma_scale_f32_16x16x128_f8f6f4 v[56:59], v[136:143], v[64:71], v[56:59], v224, v224 op_sel_hi:[0,0,0]
	s_waitcnt lgkmcnt(4)
	v_mfma_scale_f32_16x16x128_f8f6f4 v[194:197], v[128:135], v[72:79], v[44:47], v224, v224 op_sel_hi:[0,0,0]
	v_mfma_scale_f32_16x16x128_f8f6f4 v[198:201], v[136:143], v[72:79], v[40:43], v224, v224 op_sel_hi:[0,0,0]
	s_waitcnt lgkmcnt(2)
	v_mfma_scale_f32_16x16x128_f8f6f4 v[202:205], v[128:135], v[80:87], v[28:31], v224, v224 op_sel_hi:[0,0,0]
	v_mfma_scale_f32_16x16x128_f8f6f4 v[206:209], v[136:143], v[80:87], v[24:27], v224, v224 op_sel_hi:[0,0,0]
	s_waitcnt lgkmcnt(0)
	v_mfma_scale_f32_16x16x128_f8f6f4 v[236:239], v[128:135], v[88:95], v[12:15], v224, v224 op_sel_hi:[0,0,0]
	v_mfma_scale_f32_16x16x128_f8f6f4 v[240:243], v[136:143], v[88:95], v[8:11], v224, v224 op_sel_hi:[0,0,0]
	s_setprio 0
	s_setprio 1
	v_mfma_scale_f32_16x16x128_f8f6f4 v[52:55], v[144:151], v[64:71], v[52:55], v224, v224 op_sel_hi:[0,0,0]
	v_mfma_scale_f32_16x16x128_f8f6f4 v[48:51], v[152:159], v[64:71], v[48:51], v224, v224 op_sel_hi:[0,0,0]
	v_mfma_scale_f32_16x16x128_f8f6f4 v[244:247], v[144:151], v[72:79], v[36:39], v224, v224 op_sel_hi:[0,0,0]
	v_mfma_scale_f32_16x16x128_f8f6f4 v[248:251], v[152:159], v[72:79], v[32:35], v224, v224 op_sel_hi:[0,0,0]
	v_mfma_scale_f32_16x16x128_f8f6f4 v[226:229], v[144:151], v[80:87], v[20:23], v224, v224 op_sel_hi:[0,0,0]
	v_mfma_scale_f32_16x16x128_f8f6f4 v[232:235], v[152:159], v[80:87], v[16:19], v224, v224 op_sel_hi:[0,0,0]
	v_mfma_scale_f32_16x16x128_f8f6f4 v[164:167], v[144:151], v[88:95], v[4:7], v224, v224 op_sel_hi:[0,0,0]
	v_mfma_scale_f32_16x16x128_f8f6f4 v[168:171], v[152:159], v[88:95], v[0:3], v224, v224 op_sel_hi:[0,0,0]
	s_setprio 0
	s_barrier
	s_nop 4
	ds_read_b128 v[0:3], v173
	ds_read_b128 v[4:7], v173 offset:1024
	ds_read_b128 v[16:19], v173 offset:2048
	ds_read_b128 v[20:23], v173 offset:3072
	ds_read_b128 v[128:131], v174
	ds_read_b128 v[132:135], v174 offset:1024
	ds_read_b128 v[136:139], v174 offset:2048
	ds_read_b128 v[140:143], v174 offset:3072
	s_add_i32 s46, s46, s41
	s_mov_b32 m0, s56
	ds_read_b128 v[8:11], v172 offset:32768
	ds_read_b128 v[12:15], v172 offset:33792
	ds_read_b128 v[24:27], v172 offset:34816
	ds_read_b128 v[28:31], v172 offset:35840
	ds_read_b128 v[32:35], v172 offset:36864
	ds_read_b128 v[36:39], v172 offset:37888
	ds_read_b128 v[40:43], v172 offset:38912
	ds_read_b128 v[44:47], v172 offset:39936
	buffer_load_dwordx4 v192, s[36:39], s46 offen lds
	s_mov_b32 m0, s57
	s_nop 0
	buffer_load_dwordx4 v223, s[36:39], s46 offen lds
	s_waitcnt vmcnt(8)
	s_waitcnt lgkmcnt(0)
	s_barrier
; #define PG8_STAGE(bufoff, rs_, soff_, voff) do { _Pragma("unroll") for (int _i = 0; _i < 2; ++_i) \
;         __builtin_amdgcn_raw_ptr_buffer_load_lds(rs_, (LAS void*)(lds + (bufoff) + ldsw + _i * 8192), 16, (int)(voff)[_i], (int)(soff_), 0, 0); } while (0)
; #define PG8_LDA(dst, b, h) do { _Pragma("unroll") for (int m = 0; m < 4; ++m) dst[m] = PG8_LD2(lds + PG8_SA(b, h) + aoff + m * 2048); } while (0)
; #define PG8_WAIT_V(n) asm volatile("s_waitcnt vmcnt(" #n ")" ::: "memory")
; #define PG8_WAIT_L(n) asm volatile("s_waitcnt lgkmcnt(" #n ")" ::: "memory")
; #define PG8_BAR __builtin_amdgcn_s_barrier()
; #define PG8_SCHED __builtin_amdgcn_sched_barrier(0)
; template <class Epi, class Sched, bool ALIGN_EPI = false, bool SP2 = false, bool FP8 = false>
; __device__ __forceinline__ void gemm_phase(LAS unsigned char* lds, const Gemm g, const Sched& S, const Epi& E, int wbase) {
;     ...
;             PG8_WAIT_V(8); PG8_WAIT_L(0); PG8_BAR; PG8_MMA(0, 0, At, B0); PG8_MMA(0, 1, At, B1); PG8_BAR; PG8_SCHED;
;             PG8_LDA(At, 1, 1); PG8_STAGE(PG8_SB(1, 0), rB2, b3, voffB); PG8_STAGE(PG8_SB(1, 1), rB2, b3 + hstep, voffB); PG8_STAGE(PG8_SA(1, 0), rA2, a3, voffA);
;             PG8_WAIT_V(8); PG8_WAIT_L(0); PG8_BAR; PG8_MMA(1, 0, At, B0); PG8_MMA(1, 1, At, B1); PG8_BAR; PG8_SCHED;
	s_setprio 1
	s_waitcnt lgkmcnt(6)
	v_mfma_scale_f32_16x16x128_f8f6f4 v[124:127], v[0:7], v[8:15], v[124:127], v224, v224 op_sel_hi:[0,0,0]
	v_mfma_scale_f32_16x16x128_f8f6f4 v[120:123], v[16:23], v[8:15], v[120:123], v224, v224 op_sel_hi:[0,0,0]
	s_waitcnt lgkmcnt(4)
	v_mfma_scale_f32_16x16x128_f8f6f4 v[108:111], v[0:7], v[24:31], v[108:111], v224, v224 op_sel_hi:[0,0,0]
	v_mfma_scale_f32_16x16x128_f8f6f4 v[104:107], v[16:23], v[24:31], v[104:107], v224, v224 op_sel_hi:[0,0,0]
	s_waitcnt lgkmcnt(2)
	v_mfma_scale_f32_16x16x128_f8f6f4 v[92:95], v[0:7], v[32:39], v[160:163], v224, v224 op_sel_hi:[0,0,0]
	v_mfma_scale_f32_16x16x128_f8f6f4 v[88:91], v[16:23], v[32:39], v[210:213], v224, v224 op_sel_hi:[0,0,0]
	s_waitcnt lgkmcnt(0)
	v_mfma_scale_f32_16x16x128_f8f6f4 v[76:79], v[0:7], v[40:47], v[214:217], v224, v224 op_sel_hi:[0,0,0]
	v_mfma_scale_f32_16x16x128_f8f6f4 v[72:75], v[16:23], v[40:47], v[218:221], v224, v224 op_sel_hi:[0,0,0]
	s_setprio 0
	s_setprio 1
	v_mfma_scale_f32_16x16x128_f8f6f4 v[116:119], v[128:135], v[8:15], v[116:119], v224, v224 op_sel_hi:[0,0,0]
	v_mfma_scale_f32_16x16x128_f8f6f4 v[112:115], v[136:143], v[8:15], v[112:115], v224, v224 op_sel_hi:[0,0,0]
	v_mfma_scale_f32_16x16x128_f8f6f4 v[100:103], v[128:135], v[24:31], v[100:103], v224, v224 op_sel_hi:[0,0,0]
	v_mfma_scale_f32_16x16x128_f8f6f4 v[96:99], v[136:143], v[24:31], v[96:99], v224, v224 op_sel_hi:[0,0,0]
	v_mfma_scale_f32_16x16x128_f8f6f4 v[84:87], v[128:135], v[32:39], v[176:179], v224, v224 op_sel_hi:[0,0,0]
	v_mfma_scale_f32_16x16x128_f8f6f4 v[80:83], v[136:143], v[32:39], v[180:183], v224, v224 op_sel_hi:[0,0,0]
	v_mfma_scale_f32_16x16x128_f8f6f4 v[68:71], v[128:135], v[40:47], v[184:187], v224, v224 op_sel_hi:[0,0,0]
	v_mfma_scale_f32_16x16x128_f8f6f4 v[64:67], v[136:143], v[40:47], v[188:191], v224, v224 op_sel_hi:[0,0,0]
	s_setprio 0
	s_barrier
	s_mov_b32 m0, s58
	s_bitset1_b32 s31, 7
	ds_read_b128 v[32:35], v172 offset:49152
	ds_read_b128 v[36:39], v172 offset:50176
	ds_read_b128 v[144:147], v172 offset:51200
	ds_read_b128 v[148:151], v172 offset:52224
	ds_read_b128 v[152:155], v172 offset:53248
	ds_read_b128 v[156:159], v172 offset:54272
	ds_read_b128 v[176:179], v172 offset:55296
	ds_read_b128 v[180:183], v172 offset:56320
	buffer_load_dwordx4 v222, s[4:7], s31 offen lds
	s_mov_b32 m0, s59
	s_nop 0
	buffer_load_dwordx4 v193, s[4:7], s31 offen lds
	s_add_i32 s31, s31, s41
	s_mov_b32 m0, s65
	s_nop 0
	buffer_load_dwordx4 v222, s[4:7], s31 offen lds
	s_mov_b32 m0, s33
	s_nop 0
	buffer_load_dwordx4 v193, s[4:7], s31 offen lds
	s_mov_b32 m0, s12
	s_nop 0
	buffer_load_dwordx4 v192, s[36:39], s30 offen lds
	s_mov_b32 m0, s13
	s_nop 0
	buffer_load_dwordx4 v223, s[36:39], s30 offen lds
	s_waitcnt vmcnt(8)
	s_waitcnt lgkmcnt(0)
	s_barrier
	s_setprio 1
	s_waitcnt lgkmcnt(6)
	v_mfma_scale_f32_16x16x128_f8f6f4 v[60:63], v[0:7], v[32:39], v[60:63], v224, v224 op_sel_hi:[0,0,0]
	v_mfma_scale_f32_16x16x128_f8f6f4 v[56:59], v[16:23], v[32:39], v[56:59], v224, v224 op_sel_hi:[0,0,0]
	s_waitcnt lgkmcnt(4)
	v_mfma_scale_f32_16x16x128_f8f6f4 v[44:47], v[0:7], v[144:151], v[194:197], v224, v224 op_sel_hi:[0,0,0]
	v_mfma_scale_f32_16x16x128_f8f6f4 v[40:43], v[16:23], v[144:151], v[198:201], v224, v224 op_sel_hi:[0,0,0]
	s_waitcnt lgkmcnt(2)
	v_mfma_scale_f32_16x16x128_f8f6f4 v[28:31], v[0:7], v[152:159], v[202:205], v224, v224 op_sel_hi:[0,0,0]
	v_mfma_scale_f32_16x16x128_f8f6f4 v[24:27], v[16:23], v[152:159], v[206:209], v224, v224 op_sel_hi:[0,0,0]
	s_waitcnt lgkmcnt(0)
	v_mfma_scale_f32_16x16x128_f8f6f4 v[12:15], v[0:7], v[176:183], v[236:239], v224, v224 op_sel_hi:[0,0,0]
	v_mfma_scale_f32_16x16x128_f8f6f4 v[8:11], v[16:23], v[176:183], v[240:243], v224, v224 op_sel_hi:[0,0,0]
	s_setprio 0
	s_setprio 1
	v_mfma_scale_f32_16x16x128_f8f6f4 v[52:55], v[128:135], v[32:39], v[52:55], v224, v224 op_sel_hi:[0,0,0]
	v_mfma_scale_f32_16x16x128_f8f6f4 v[48:51], v[136:143], v[32:39], v[48:51], v224, v224 op_sel_hi:[0,0,0]
	v_mfma_scale_f32_16x16x128_f8f6f4 v[36:39], v[128:135], v[144:151], v[244:247], v224, v224 op_sel_hi:[0,0,0]
	v_mfma_scale_f32_16x16x128_f8f6f4 v[32:35], v[136:143], v[144:151], v[248:251], v224, v224 op_sel_hi:[0,0,0]
	v_mfma_scale_f32_16x16x128_f8f6f4 v[20:23], v[128:135], v[152:159], v[226:229], v224, v224 op_sel_hi:[0,0,0]
	v_mfma_scale_f32_16x16x128_f8f6f4 v[16:19], v[136:143], v[152:159], v[232:235], v224, v224 op_sel_hi:[0,0,0]
	v_mfma_scale_f32_16x16x128_f8f6f4 v[4:7], v[128:135], v[176:183], v[164:167], v224, v224 op_sel_hi:[0,0,0]
	v_mfma_scale_f32_16x16x128_f8f6f4 v[0:3], v[136:143], v[176:183], v[168:171], v224, v224 op_sel_hi:[0,0,0]
	s_setprio 0
	s_barrier
	s_add_i32 s29, s29, 2
	s_addk_i32 s16, 0x100
	s_addk_i32 s28, 0x100
	s_cmp_ge_i32 s29, s77
	s_cbranch_scc0 .LBB0_258
	s_branch .Lpeel_after_258

; #define PG8_BAR __builtin_amdgcn_s_barrier()
; template <class Epi, class Sched, bool ALIGN_EPI = false, bool SP2 = false, bool FP8 = false>
; __device__ __forceinline__ void gemm_phase(LAS unsigned char* lds, const Gemm g, const Sched& S, const Epi& E, int wbase) {
;     ...
;         }
;         if constexpr (ALIGN_EPI) { if (wr == 0) PG8_BAR; }
;         { int fr_ = fr, fq_ = fq; asm volatile("" : "+v"(fr_), "+v"(fq_));
;           if constexpr (Epi::HAS_PRE) E(acc, cur, wr, wc, fr_, fq_, pre_); else E(acc, cur, wr, wc, fr_, fq_); } S.done(cur);
.Lpeel_after_258:
	s_mov_b32 s100, 1
	v_mov_b32_e32 v233, v175
	v_mov_b32_e32 v234, v230
	v_mov_b32_e32 v164, v231
	v_mov_b32_e32 v231, 1
	v_mov_b32_e32 v230, 0x358637bd
	s_and_b64 vcc, exec, s[78:79]
	s_cbranch_vccnz .LBB0_261
	s_branch .LBB0_262

;     __device__ __forceinline__ unsigned a_off(const Unit& u, const Gemm& g) const { return (unsigned)u.pm * (unsigned)(BM * 2) * (unsigned)g.K; }
;     __device__ __forceinline__ unsigned b_off(const Unit& u, const Gemm& g) const { return (unsigned)u.pn * (unsigned)(BM * 2) * (unsigned)g.K; }
;     __device__ __forceinline__ bool next(int i, Unit& u) const { return so.next(i, u); }
; template <class Epi, class Sched, bool ALIGN_EPI = false, bool SP2 = false, bool FP8 = false>
; __device__ __forceinline__ void gemm_phase(LAS unsigned char* lds, const Gemm g, const Sched& S, const Epi& E, int wbase) {
;     ...
;     for (int i = 0; i < 2; ++i) { int R, C; stage_rc(tid * 16 + i * 8192, R, C); const int Rb = Epi::PERM ? ((R & ~31) + perm32(R & 31)) : R;
;         voffA[i] = (unsigned)(R * K + C) * 2u; voffB[i] = (unsigned)(Rb * K + C) * 2u; }
;     const unsigned kstep = (unsigned)(BK * 2);
;     const unsigned hstep = (unsigned)HALF * (unsigned)K * 2u;
;     typedef __amdgpu_buffer_rsrc_t rsrc_t;
;     const rsrc_t rA0 = __builtin_amdgcn_make_buffer_rsrc((void*)g.A, 0, 0xffffffff, 0x00020000), rB0 = __builtin_amdgcn_make_buffer_rsrc((void*)g.Bt, 0, 0xffffffff, 0x00020000);
;     rsrc_t rA1 = rA0, rB1 = rB0;
;     if constexpr (Sched::TWO) { rA1 = __builtin_amdgcn_make_buffer_rsrc((void*)S.A1, 0, 0xffffffff, 0x00020000); rB1 = __builtin_amdgcn_make_buffer_rsrc((void*)S.Bt1, 0, 0xffffffff, 0x00020000); }
;     const unsigned ldsw = (unsigned)wid * 1024u;
;     const int aoff = lds_byte(wr * 64 + fr, fq * 8), boff = lds_byte(wc * 32 + fr, fq * 8);
;     ...
;     Unit cur, nxt; int ui = 0;
;     if (!S.next(0, cur)) return;
;     f32x4 acc[2][2][4][2];
;     ...
;     PG8_ZERO_ACC();
;     v8i_t At[4], B0[2], B1[2];
;     unsigned cA = S.a_off(cur, g), cB = S.b_off(cur, g); rsrc_t rAc = (Sched::TWO && cur.part) ? rA1 : rA0, rBc = (Sched::TWO && cur.part) ? rB1 : rB0;
;     S.a_ready(cur);
;     if constexpr (SP2) {
;         PG8_STAGE(PG8_SB(0, 0), rBc, cB, voffB); PG8_STAGE(PG8_SB(0, 1), rBc, cB + hstep, voffB); PG8_STAGE(PG8_SA(0, 0), rAc, cA, voffA); PG8_STAGE(PG8_SA(0, 1), rAc, cA + hstep, voffA);
;         if (wr == 1) PG8_BAR;
;         PG8_WAIT_V(2); PG8_BAR;
;         PG8_STAGE(PG8_SB(1, 0), rBc, cB + kstep, voffB); PG8_STAGE(PG8_SA(1, 0), rAc, cA + kstep, voffA); PG8_STAGE(PG8_SB(1, 1), rBc, cB + hstep + kstep, voffB);
;         PG8_WAIT_V(6); PG8_BAR;
.LBB0_345:
	v_readlane_b32 s6, v255, 11
	s_cmp_eq_u32 s6, 0
	s_cselect_b32 s6, 0, 0x200000
	s_lshl_b32 s20, s95, 6
	s_add_u32 s14, s2, 0x1f800000
	s_addc_u32 s15, s3, 0
	s_add_u32 s2, s2, s6
	s_addc_u32 s3, s3, 0
	s_add_u32 s62, s2, 0x17200000
	s_addc_u32 s63, s3, 0
	s_add_i32 s56, s41, 0x18000
	s_or_b32 s2, s28, 0x80
	s_mov_b32 s6, s38
	s_mov_b32 s7, s39
	s_mov_b32 m0, s56
	s_add_i32 s57, s41, 0x1a000
	s_waitcnt vmcnt(2)
	s_barrier
	buffer_load_dwordx4 v165, s[4:7], s2 offen lds
	s_mov_b32 m0, s57
	s_add_i32 s58, s41, 0x8000
	buffer_load_dwordx4 v167, s[4:7], s2 offen lds
	s_or_b32 s2, s29, 0x80
	s_mov_b32 m0, s58
	s_add_i32 s59, s41, 0xa000
	buffer_load_dwordx4 v164, s[36:39], s2 offen lds
	s_mov_b32 m0, s59
	s_add_i32 s65, s41, 0x1c000
	buffer_load_dwordx4 v166, s[36:39], s2 offen lds
	s_bitset1_b32 s19, 7
	s_mov_b32 m0, s65
	s_add_i32 s76, s41, 0x1e000
	buffer_load_dwordx4 v165, s[4:7], s19 offen lds
	s_mov_b32 m0, s76
	s_ashr_i32 s3, s12, 31
	buffer_load_dwordx4 v167, s[4:7], s19 offen lds
	v_bfe_u32 v169, v4, 4, 2
	s_lshr_b32 s3, s3, 26
	v_and_b32_e32 v168, 15, v4
	s_add_i32 s3, s12, s3
	v_lshlrev_b32_e32 v5, 4, v169
	v_lshlrev_b32_e32 v4, 2, v4
	s_and_b32 s2, s13, 3
	s_ashr_i32 s82, s3, 6
	v_lshl_or_b32 v5, v168, 6, v5
	s_lshl_b32 s3, s18, 13
	v_and_b32_e32 v4, 32, v4
	s_lshl_b32 s48, s18, 6
	v_bitop3_b32 v6, v5, s3, v4 bitop3:0xde
	s_lshl_b32 s3, s2, 12
	s_cmp_gt_i32 s12, 63
	s_cselect_b64 s[66:67], -1, 0
	s_add_i32 s12, s82, -2
	s_add_i32 s13, s41, 0xc000
	s_waitcnt vmcnt(6)
	s_cmpk_lt_u32 s16, 0x100
	s_mov_b32 s21, s40
	v_bitop3_b32 v4, v5, s3, v4 bitop3:0xde
	s_cselect_b64 s[78:79], -1, 0
	s_lshl_b32 s2, s2, 6
	v_mov_b32_e32 v1, v0
	v_mov_b32_e32 v2, v0
	v_mov_b32_e32 v3, v0
	s_mov_b32 s77, 0
	s_add_i32 s83, s41, 0xe000
	v_add_u32_e32 v170, 0, v4
	v_add_u32_e32 v171, 0, v6
	s_lshl_b64 s[22:23], s[20:21], 2
	s_lshl_b32 s24, s2, 1
	s_barrier
	s_mov_b32 s100, 0
	s_branch .LBB0_348

;     __device__ __forceinline__ unsigned a_off(const Unit& u, const Gemm& g) const { return (unsigned)u.pm * (unsigned)(BM * 2) * (unsigned)g.K; }
;     __device__ __forceinline__ unsigned b_off(const Unit& u, const Gemm& g) const { return (unsigned)u.pn * (unsigned)(BM * 2) * (unsigned)g.K; }
;     __device__ __forceinline__ bool next(int i, Unit& u) const { return so.next(i, u); }
;     __device__ __forceinline__ unsigned a_off(const Unit& u, const Gemm& g) const { return (unsigned)u.pm * (unsigned)(BM * 2) * (unsigned)g.K; }
;     __device__ __forceinline__ bool next(int i, Unit& u) const { const bool ok = so.next(i >> 1, u); u.part = i & 1; return ok; }
;     __device__ __forceinline__ unsigned a_off(const Unit& u, const Gemm& g) const { return (unsigned)u.pm * (unsigned)(BM * 2) * (unsigned)g.K; }
;     __device__ __forceinline__ unsigned b_off(const Unit& u, const Gemm& g) const { return (unsigned)u.pn * (unsigned)(BM * 2) * (unsigned)g.K; }
; template <class Epi, class Sched, bool ALIGN_EPI = false, bool SP2 = false, bool FP8 = false>
; __device__ __forceinline__ void gemm_phase(LAS unsigned char* lds, const Gemm g, const Sched& S, const Epi& E, int wbase) {
;     ...
;         const bool has_next = S.next(ui + 1, nxt);
;         const unsigned nA = has_next ? S.a_off(nxt, g) : cA, nB = has_next ? S.b_off(nxt, g) : cB;
;         const rsrc_t rAn = (Sched::TWO && has_next) ? (nxt.part ? rA1 : rA0) : rAc, rBn = (Sched::TWO && has_next) ? (nxt.part ? rB1 : rB0) : rBc;
;         float pre_[8] = {0.f, 0.f, 0.f, 0.f, 0.f, 0.f, 0.f, 0.f};
;         if constexpr (Epi::HAS_PRE) E.pre_load(pre_, cur, wr);
;         for (int t = 0; t < nt; t += 2) {
;             const bool last = (t == nt - 2);
;             const unsigned a1 = cA + (unsigned)(t + 1) * kstep;
;             const unsigned a2 = last ? nA : cA + (unsigned)(t + 2) * kstep, b2 = last ? nB : cB + (unsigned)(t + 2) * kstep; const rsrc_t rA2 = (Sched::TWO && last) ? rAn : rAc, rB2 = (Sched::TWO && last) ? rBn : rBc;
;             const unsigned a3 = a2 + kstep, b3 = b2 + kstep;
;             if (last && has_next) S.a_ready(nxt);
;             if constexpr (SP2) {
;             PG8_LDB(B0, 0, 0); PG8_LDB(B1, 0, 1); PG8_SCHED; PG8_LDA(At, 0, 0); PG8_STAGE(PG8_SA(1, 1), rAc, a1 + hstep, voffA);
;             PG8_WAIT_V(8); PG8_WAIT_L(0); PG8_BAR; PG8_MMA(0, 0, At, B0); PG8_MMA(0, 1, At, B1); PG8_BAR; PG8_SCHED;
.LBB0_350:
	s_lshl_b32 s20, s19, 19
	s_andn2_b64 vcc, exec, s[66:67]
	s_lshl_b32 s21, s18, 19
	s_cbranch_vccnz .LBB0_430
	s_and_b64 s[2:3], s[26:27], exec
	v_mov_b64_e32 v[6:7], v[2:3]
	v_mov_b64_e32 v[18:19], v[2:3]
	v_mov_b64_e32 v[22:23], v[2:3]
	v_mov_b64_e32 v[34:35], v[2:3]
	v_mov_b64_e32 v[38:39], v[2:3]
	v_mov_b64_e32 v[50:51], v[2:3]
	v_mov_b64_e32 v[54:55], v[2:3]
	v_mov_b64_e32 v[10:11], v[2:3]
	v_mov_b64_e32 v[14:15], v[2:3]
	v_mov_b64_e32 v[26:27], v[2:3]
	v_mov_b64_e32 v[30:31], v[2:3]
	v_mov_b64_e32 v[42:43], v[2:3]
	v_mov_b64_e32 v[46:47], v[2:3]
	v_mov_b64_e32 v[58:59], v[2:3]
	s_waitcnt vmcnt(37)
	v_mov_b64_e32 v[62:63], v[2:3]
	s_waitcnt vmcnt(36)
	v_mov_b64_e32 v[66:67], v[2:3]
	s_waitcnt vmcnt(35)
	v_mov_b64_e32 v[70:71], v[2:3]
	s_waitcnt vmcnt(32)
	v_mov_b64_e32 v[82:83], v[2:3]
	s_waitcnt vmcnt(31)
	v_mov_b64_e32 v[86:87], v[2:3]
	s_waitcnt vmcnt(28)
	v_mov_b64_e32 v[98:99], v[2:3]
	s_waitcnt vmcnt(27)
	v_mov_b64_e32 v[102:103], v[2:3]
	s_waitcnt vmcnt(24)
	v_mov_b64_e32 v[114:115], v[2:3]
	s_waitcnt vmcnt(23)
	v_mov_b64_e32 v[118:119], v[2:3]
	v_mov_b64_e32 v[74:75], v[2:3]
	v_mov_b64_e32 v[78:79], v[2:3]
	v_mov_b64_e32 v[90:91], v[2:3]
	v_mov_b64_e32 v[94:95], v[2:3]
	v_mov_b64_e32 v[106:107], v[2:3]
	v_mov_b64_e32 v[110:111], v[2:3]
	s_waitcnt vmcnt(22)
	v_mov_b64_e32 v[122:123], v[2:3]
	v_mov_b64_e32 v[126:127], v[2:3]
	s_cselect_b32 s2, s20, s29
	s_cselect_b32 s3, s21, s28
	s_add_i32 s16, s29, 0x80
	s_addk_i32 s28, 0x100
	s_mov_b32 s29, 0
	v_mov_b64_e32 v[4:5], v[0:1]
	v_mov_b64_e32 v[16:17], v[0:1]
	v_mov_b64_e32 v[20:21], v[0:1]
	v_mov_b64_e32 v[32:33], v[0:1]
	v_mov_b64_e32 v[36:37], v[0:1]
	v_mov_b64_e32 v[48:49], v[0:1]
	v_mov_b64_e32 v[52:53], v[0:1]
	v_mov_b64_e32 v[8:9], v[0:1]
	v_mov_b64_e32 v[12:13], v[0:1]
	v_mov_b64_e32 v[24:25], v[0:1]
	v_mov_b64_e32 v[28:29], v[0:1]
	v_mov_b64_e32 v[40:41], v[0:1]
	v_mov_b64_e32 v[44:45], v[0:1]
	v_mov_b64_e32 v[56:57], v[0:1]
	v_mov_b64_e32 v[60:61], v[0:1]
	v_mov_b64_e32 v[64:65], v[0:1]
	v_mov_b64_e32 v[68:69], v[0:1]
	v_mov_b64_e32 v[80:81], v[0:1]
	v_mov_b64_e32 v[84:85], v[0:1]
	v_mov_b64_e32 v[96:97], v[0:1]
	v_mov_b64_e32 v[100:101], v[0:1]
	v_mov_b64_e32 v[112:113], v[0:1]
	v_mov_b64_e32 v[116:117], v[0:1]
	v_mov_b64_e32 v[72:73], v[0:1]
	v_mov_b64_e32 v[76:77], v[0:1]
	v_mov_b64_e32 v[88:89], v[0:1]
	v_mov_b64_e32 v[92:93], v[0:1]
	v_mov_b64_e32 v[104:105], v[0:1]
	v_mov_b64_e32 v[108:109], v[0:1]
	v_mov_b64_e32 v[120:121], v[0:1]
	v_mov_b64_e32 v[124:125], v[0:1]
	s_cmp_eq_u32 s100, 1
	s_cbranch_scc0 .LBB0_352
	v_add_u32_e32 v140, 0x10000, v170
	v_add_u32_e32 v156, 0x14000, v170
	ds_read_b128 v[128:131], v140
	ds_read_b128 v[132:135], v140 offset:1024
	ds_read_b128 v[136:139], v140 offset:2048
	ds_read_b128 v[140:143], v140 offset:3072
	ds_read_b128 v[144:147], v156
	ds_read_b128 v[148:151], v156 offset:1024
	ds_read_b128 v[152:155], v156 offset:2048
	ds_read_b128 v[156:159], v156 offset:3072
	s_add_i32 s6, s16, 0x80
	s_cmp_eq_u32 s12, s29
	s_cselect_b32 s46, s2, s6
	s_cselect_b32 s31, s3, s28
	s_or_b32 s30, s46, 0x80
	s_add_i32 s6, s33, s16
	s_mov_b32 m0, s13
	ds_read_b128 v[160:163], v171
	ds_read_b128 v[172:175], v171 offset:1024
	ds_read_b128 v[176:179], v171 offset:2048
	ds_read_b128 v[180:183], v171 offset:3072
	ds_read_b128 v[184:187], v171 offset:4096
	ds_read_b128 v[188:191], v171 offset:5120
	ds_read_b128 v[194:197], v171 offset:6144
	ds_read_b128 v[198:201], v171 offset:7168
	buffer_load_dwordx4 v164, s[36:39], s6 offen lds
	s_mov_b32 m0, s83
	s_nop 0
	buffer_load_dwordx4 v166, s[36:39], s6 offen lds
	s_waitcnt vmcnt(32)
	s_waitcnt lgkmcnt(0)
	s_barrier
	s_setprio 1
	s_waitcnt lgkmcnt(7)
	v_mfma_f32_16x16x32_bf16 v[124:127], v[128:131], v[160:163], v[124:127]
	v_mfma_f32_16x16x32_bf16 v[120:123], v[136:139], v[160:163], v[120:123]
	s_waitcnt lgkmcnt(5)
	v_mfma_f32_16x16x32_bf16 v[108:111], v[128:131], v[176:179], v[108:111]
	v_mfma_f32_16x16x32_bf16 v[104:107], v[136:139], v[176:179], v[104:107]
	s_waitcnt lgkmcnt(3)
	v_mfma_f32_16x16x32_bf16 v[92:95], v[128:131], v[184:187], v[92:95]
	v_mfma_f32_16x16x32_bf16 v[88:91], v[136:139], v[184:187], v[88:91]
	s_waitcnt lgkmcnt(1)
	v_mfma_f32_16x16x32_bf16 v[76:79], v[128:131], v[194:197], v[76:79]
	v_mfma_f32_16x16x32_bf16 v[72:75], v[136:139], v[194:197], v[72:75]
	v_mfma_f32_16x16x32_bf16 v[124:127], v[132:135], v[172:175], v[124:127]
	v_mfma_f32_16x16x32_bf16 v[120:123], v[140:143], v[172:175], v[120:123]
	v_mfma_f32_16x16x32_bf16 v[108:111], v[132:135], v[180:183], v[108:111]
	v_mfma_f32_16x16x32_bf16 v[104:107], v[140:143], v[180:183], v[104:107]
	v_mfma_f32_16x16x32_bf16 v[92:95], v[132:135], v[188:191], v[92:95]
	v_mfma_f32_16x16x32_bf16 v[88:91], v[140:143], v[188:191], v[88:91]
	s_waitcnt lgkmcnt(0)
	v_mfma_f32_16x16x32_bf16 v[76:79], v[132:135], v[198:201], v[76:79]
	v_mfma_f32_16x16x32_bf16 v[72:75], v[140:143], v[198:201], v[72:75]
	s_setprio 0
	s_setprio 1
	v_mfma_f32_16x16x32_bf16 v[116:119], v[144:147], v[160:163], v[116:119]
	v_mfma_f32_16x16x32_bf16 v[112:115], v[152:155], v[160:163], v[112:115]
	v_mfma_f32_16x16x32_bf16 v[100:103], v[144:147], v[176:179], v[100:103]
	v_mfma_f32_16x16x32_bf16 v[96:99], v[152:155], v[176:179], v[96:99]
	v_mfma_f32_16x16x32_bf16 v[84:87], v[144:147], v[184:187], v[84:87]
	v_mfma_f32_16x16x32_bf16 v[80:83], v[152:155], v[184:187], v[80:83]
	v_mfma_f32_16x16x32_bf16 v[68:71], v[144:147], v[194:197], v[68:71]
	v_mfma_f32_16x16x32_bf16 v[64:67], v[152:155], v[194:197], v[64:67]
	v_mfma_f32_16x16x32_bf16 v[116:119], v[148:151], v[172:175], v[116:119]
	v_mfma_f32_16x16x32_bf16 v[112:115], v[156:159], v[172:175], v[112:115]
	v_mfma_f32_16x16x32_bf16 v[100:103], v[148:151], v[180:183], v[100:103]
	v_mfma_f32_16x16x32_bf16 v[96:99], v[156:159], v[180:183], v[96:99]
	v_mfma_f32_16x16x32_bf16 v[84:87], v[148:151], v[188:191], v[84:87]
	v_mfma_f32_16x16x32_bf16 v[80:83], v[156:159], v[188:191], v[80:83]
	v_mfma_f32_16x16x32_bf16 v[68:71], v[148:151], v[198:201], v[68:71]
	v_mfma_f32_16x16x32_bf16 v[64:67], v[156:159], v[198:201], v[64:67]
	s_setprio 0
	s_barrier
; #define PG8_STAGE(bufoff, rs_, soff_, voff) do { _Pragma("unroll") for (int _i = 0; _i < 2; ++_i) \
;         __builtin_amdgcn_raw_ptr_buffer_load_lds(rs_, (LAS void*)(lds + (bufoff) + ldsw + _i * 8192), 16, (int)(voff)[_i], (int)(soff_), 0, 0); } while (0)
; #define PG8_LDA(dst, b, h) do { _Pragma("unroll") for (int m = 0; m < 4; ++m) dst[m] = PG8_LD2(lds + PG8_SA(b, h) + aoff + m * 2048); } while (0)
; #define PG8_LDB(dst, b, h) do { _Pragma("unroll") for (int n = 0; n < 2; ++n) dst[n] = PG8_LD2(lds + PG8_SB(b, h) + boff + n * 2048); } while (0)
; #define PG8_WAIT_V(n) asm volatile("s_waitcnt vmcnt(" #n ")" ::: "memory")
; #define PG8_WAIT_L(n) asm volatile("s_waitcnt lgkmcnt(" #n ")" ::: "memory")
; #define PG8_BAR __builtin_amdgcn_s_barrier()
; #define PG8_SCHED __builtin_amdgcn_sched_barrier(0)
; template <class Epi, class Sched, bool ALIGN_EPI = false, bool SP2 = false, bool FP8 = false>
; __device__ __forceinline__ void gemm_phase(LAS unsigned char* lds, const Gemm g, const Sched& S, const Epi& E, int wbase) {
;     ...
;             PG8_LDA(At, 0, 1); PG8_STAGE(PG8_SB(0, 0), rB2, b2, voffB); PG8_STAGE(PG8_SB(0, 1), rB2, b2 + hstep, voffB); PG8_STAGE(PG8_SA(0, 0), rA2, a2, voffA);
;             PG8_WAIT_V(8); PG8_WAIT_L(0); PG8_BAR; PG8_MMA(1, 0, At, B0); PG8_MMA(1, 1, At, B1); PG8_BAR; PG8_SCHED;
;             PG8_LDB(B0, 1, 0); PG8_LDB(B1, 1, 1); PG8_SCHED; PG8_LDA(At, 1, 0); PG8_STAGE(PG8_SA(0, 1), rA2, a2 + hstep, voffA);
;             PG8_WAIT_V(8); PG8_WAIT_L(0); PG8_BAR; PG8_MMA(0, 0, At, B0); PG8_MMA(0, 1, At, B1); PG8_BAR; PG8_SCHED;
	s_mov_b32 m0, s42
	s_mov_b32 s6, s38
	s_mov_b32 s7, s39
	ds_read_b128 v[160:163], v171 offset:16384
	ds_read_b128 v[172:175], v171 offset:17408
	ds_read_b128 v[176:179], v171 offset:18432
	ds_read_b128 v[180:183], v171 offset:19456
	ds_read_b128 v[184:187], v171 offset:20480
	ds_read_b128 v[188:191], v171 offset:21504
	ds_read_b128 v[194:197], v171 offset:22528
	ds_read_b128 v[198:201], v171 offset:23552
	buffer_load_dwordx4 v165, s[4:7], s31 offen lds
	s_mov_b32 m0, s43
	s_add_i32 s47, s31, s33
	buffer_load_dwordx4 v167, s[4:7], s31 offen lds
	s_mov_b32 m0, s44
	s_nop 0
	buffer_load_dwordx4 v165, s[4:7], s47 offen lds
	s_mov_b32 m0, s45
	s_nop 0
	buffer_load_dwordx4 v167, s[4:7], s47 offen lds
	s_mov_b32 m0, s41
	s_nop 0
	buffer_load_dwordx4 v164, s[36:39], s46 offen lds
	s_mov_b32 m0, s52
	s_nop 0
	buffer_load_dwordx4 v166, s[36:39], s46 offen lds
	s_waitcnt vmcnt(32)
	s_waitcnt lgkmcnt(0)
	s_barrier
	s_setprio 1
	s_waitcnt lgkmcnt(7)
	v_mfma_f32_16x16x32_bf16 v[60:63], v[128:131], v[160:163], v[60:63]
	v_mfma_f32_16x16x32_bf16 v[56:59], v[136:139], v[160:163], v[56:59]
	s_waitcnt lgkmcnt(5)
	v_mfma_f32_16x16x32_bf16 v[44:47], v[128:131], v[176:179], v[44:47]
	v_mfma_f32_16x16x32_bf16 v[40:43], v[136:139], v[176:179], v[40:43]
	s_waitcnt lgkmcnt(3)
	v_mfma_f32_16x16x32_bf16 v[28:31], v[128:131], v[184:187], v[28:31]
	v_mfma_f32_16x16x32_bf16 v[24:27], v[136:139], v[184:187], v[24:27]
	s_waitcnt lgkmcnt(1)
	v_mfma_f32_16x16x32_bf16 v[12:15], v[128:131], v[194:197], v[12:15]
	v_mfma_f32_16x16x32_bf16 v[8:11], v[136:139], v[194:197], v[8:11]
	v_mfma_f32_16x16x32_bf16 v[60:63], v[132:135], v[172:175], v[60:63]
	v_mfma_f32_16x16x32_bf16 v[56:59], v[140:143], v[172:175], v[56:59]
	v_mfma_f32_16x16x32_bf16 v[44:47], v[132:135], v[180:183], v[44:47]
	v_mfma_f32_16x16x32_bf16 v[40:43], v[140:143], v[180:183], v[40:43]
	v_mfma_f32_16x16x32_bf16 v[28:31], v[132:135], v[188:191], v[28:31]
	v_mfma_f32_16x16x32_bf16 v[24:27], v[140:143], v[188:191], v[24:27]
	s_waitcnt lgkmcnt(0)
	v_mfma_f32_16x16x32_bf16 v[12:15], v[132:135], v[198:201], v[12:15]
	v_mfma_f32_16x16x32_bf16 v[8:11], v[140:143], v[198:201], v[8:11]
	s_setprio 0
	s_setprio 1
	v_mfma_f32_16x16x32_bf16 v[52:55], v[144:147], v[160:163], v[52:55]
	v_mfma_f32_16x16x32_bf16 v[48:51], v[152:155], v[160:163], v[48:51]
	v_mfma_f32_16x16x32_bf16 v[36:39], v[144:147], v[176:179], v[36:39]
	v_mfma_f32_16x16x32_bf16 v[32:35], v[152:155], v[176:179], v[32:35]
	v_mfma_f32_16x16x32_bf16 v[20:23], v[144:147], v[184:187], v[20:23]
	v_mfma_f32_16x16x32_bf16 v[16:19], v[152:155], v[184:187], v[16:19]
	v_mfma_f32_16x16x32_bf16 v[4:7], v[144:147], v[194:197], v[4:7]
	v_mfma_f32_16x16x32_bf16 v[0:3], v[152:155], v[194:197], v[0:3]
	v_mfma_f32_16x16x32_bf16 v[52:55], v[148:151], v[172:175], v[52:55]
	v_mfma_f32_16x16x32_bf16 v[48:51], v[156:159], v[172:175], v[48:51]
	v_mfma_f32_16x16x32_bf16 v[36:39], v[148:151], v[180:183], v[36:39]
	v_mfma_f32_16x16x32_bf16 v[32:35], v[156:159], v[180:183], v[32:35]
	v_mfma_f32_16x16x32_bf16 v[20:23], v[148:151], v[188:191], v[20:23]
	v_mfma_f32_16x16x32_bf16 v[16:19], v[156:159], v[188:191], v[16:19]
	v_mfma_f32_16x16x32_bf16 v[4:7], v[148:151], v[198:201], v[4:7]
	v_mfma_f32_16x16x32_bf16 v[0:3], v[156:159], v[198:201], v[0:3]
	s_setprio 0
	s_barrier
	v_add_u32_e32 v140, 0x18000, v170
	v_add_u32_e32 v156, 0x1c000, v170
	ds_read_b128 v[128:131], v140
	ds_read_b128 v[132:135], v140 offset:1024
	ds_read_b128 v[136:139], v140 offset:2048
	ds_read_b128 v[140:143], v140 offset:3072
	ds_read_b128 v[144:147], v156
	ds_read_b128 v[148:151], v156 offset:1024
	ds_read_b128 v[152:155], v156 offset:2048
	ds_read_b128 v[156:159], v156 offset:3072
	s_add_i32 s46, s46, s33
	s_mov_b32 m0, s53
	ds_read_b128 v[160:163], v171 offset:32768
	ds_read_b128 v[172:175], v171 offset:33792
	ds_read_b128 v[176:179], v171 offset:34816
	ds_read_b128 v[180:183], v171 offset:35840
	ds_read_b128 v[184:187], v171 offset:36864
	ds_read_b128 v[188:191], v171 offset:37888
	ds_read_b128 v[194:197], v171 offset:38912
	ds_read_b128 v[198:201], v171 offset:39936
	buffer_load_dwordx4 v164, s[36:39], s46 offen lds
	s_mov_b32 m0, s1
	s_nop 0
	buffer_load_dwordx4 v166, s[36:39], s46 offen lds
	s_waitcnt vmcnt(8)
	s_waitcnt lgkmcnt(0)
	s_barrier
; #define PG8_STAGE(bufoff, rs_, soff_, voff) do { _Pragma("unroll") for (int _i = 0; _i < 2; ++_i) \
;         __builtin_amdgcn_raw_ptr_buffer_load_lds(rs_, (LAS void*)(lds + (bufoff) + ldsw + _i * 8192), 16, (int)(voff)[_i], (int)(soff_), 0, 0); } while (0)
; #define PG8_LDA(dst, b, h) do { _Pragma("unroll") for (int m = 0; m < 4; ++m) dst[m] = PG8_LD2(lds + PG8_SA(b, h) + aoff + m * 2048); } while (0)
; #define PG8_WAIT_V(n) asm volatile("s_waitcnt vmcnt(" #n ")" ::: "memory")
; #define PG8_WAIT_L(n) asm volatile("s_waitcnt lgkmcnt(" #n ")" ::: "memory")
; #define PG8_BAR __builtin_amdgcn_s_barrier()
; #define PG8_SCHED __builtin_amdgcn_sched_barrier(0)
; template <class Epi, class Sched, bool ALIGN_EPI = false, bool SP2 = false, bool FP8 = false>
; __device__ __forceinline__ void gemm_phase(LAS unsigned char* lds, const Gemm g, const Sched& S, const Epi& E, int wbase) {
;     ...
;             PG8_WAIT_V(8); PG8_WAIT_L(0); PG8_BAR; PG8_MMA(0, 0, At, B0); PG8_MMA(0, 1, At, B1); PG8_BAR; PG8_SCHED;
;             PG8_LDA(At, 1, 1); PG8_STAGE(PG8_SB(1, 0), rB2, b3, voffB); PG8_STAGE(PG8_SB(1, 1), rB2, b3 + hstep, voffB); PG8_STAGE(PG8_SA(1, 0), rA2, a3, voffA);
;             PG8_WAIT_V(8); PG8_WAIT_L(0); PG8_BAR; PG8_MMA(1, 0, At, B0); PG8_MMA(1, 1, At, B1); PG8_BAR; PG8_SCHED;
	s_setprio 1
	s_waitcnt lgkmcnt(7)
	v_mfma_f32_16x16x32_bf16 v[124:127], v[128:131], v[160:163], v[124:127]
	v_mfma_f32_16x16x32_bf16 v[120:123], v[136:139], v[160:163], v[120:123]
	s_waitcnt lgkmcnt(5)
	v_mfma_f32_16x16x32_bf16 v[108:111], v[128:131], v[176:179], v[108:111]
	v_mfma_f32_16x16x32_bf16 v[104:107], v[136:139], v[176:179], v[104:107]
	s_waitcnt lgkmcnt(3)
	v_mfma_f32_16x16x32_bf16 v[92:95], v[128:131], v[184:187], v[92:95]
	v_mfma_f32_16x16x32_bf16 v[88:91], v[136:139], v[184:187], v[88:91]
	s_waitcnt lgkmcnt(1)
	v_mfma_f32_16x16x32_bf16 v[76:79], v[128:131], v[194:197], v[76:79]
	v_mfma_f32_16x16x32_bf16 v[72:75], v[136:139], v[194:197], v[72:75]
	v_mfma_f32_16x16x32_bf16 v[124:127], v[132:135], v[172:175], v[124:127]
	v_mfma_f32_16x16x32_bf16 v[120:123], v[140:143], v[172:175], v[120:123]
	v_mfma_f32_16x16x32_bf16 v[108:111], v[132:135], v[180:183], v[108:111]
	v_mfma_f32_16x16x32_bf16 v[104:107], v[140:143], v[180:183], v[104:107]
	v_mfma_f32_16x16x32_bf16 v[92:95], v[132:135], v[188:191], v[92:95]
	v_mfma_f32_16x16x32_bf16 v[88:91], v[140:143], v[188:191], v[88:91]
	s_waitcnt lgkmcnt(0)
	v_mfma_f32_16x16x32_bf16 v[76:79], v[132:135], v[198:201], v[76:79]
	v_mfma_f32_16x16x32_bf16 v[72:75], v[140:143], v[198:201], v[72:75]
	s_setprio 0
	s_setprio 1
	v_mfma_f32_16x16x32_bf16 v[116:119], v[144:147], v[160:163], v[116:119]
	v_mfma_f32_16x16x32_bf16 v[112:115], v[152:155], v[160:163], v[112:115]
	v_mfma_f32_16x16x32_bf16 v[100:103], v[144:147], v[176:179], v[100:103]
	v_mfma_f32_16x16x32_bf16 v[96:99], v[152:155], v[176:179], v[96:99]
	v_mfma_f32_16x16x32_bf16 v[84:87], v[144:147], v[184:187], v[84:87]
	v_mfma_f32_16x16x32_bf16 v[80:83], v[152:155], v[184:187], v[80:83]
	v_mfma_f32_16x16x32_bf16 v[68:71], v[144:147], v[194:197], v[68:71]
	v_mfma_f32_16x16x32_bf16 v[64:67], v[152:155], v[194:197], v[64:67]
	v_mfma_f32_16x16x32_bf16 v[116:119], v[148:151], v[172:175], v[116:119]
	v_mfma_f32_16x16x32_bf16 v[112:115], v[156:159], v[172:175], v[112:115]
	v_mfma_f32_16x16x32_bf16 v[100:103], v[148:151], v[180:183], v[100:103]
	v_mfma_f32_16x16x32_bf16 v[96:99], v[156:159], v[180:183], v[96:99]
	v_mfma_f32_16x16x32_bf16 v[84:87], v[148:151], v[188:191], v[84:87]
	v_mfma_f32_16x16x32_bf16 v[80:83], v[156:159], v[188:191], v[80:83]
	v_mfma_f32_16x16x32_bf16 v[68:71], v[148:151], v[198:201], v[68:71]
	v_mfma_f32_16x16x32_bf16 v[64:67], v[156:159], v[198:201], v[64:67]
	s_setprio 0
	s_barrier
	s_mov_b32 m0, s56
	s_bitset1_b32 s31, 7
	ds_read_b128 v[160:163], v171 offset:49152
	ds_read_b128 v[172:175], v171 offset:50176
	ds_read_b128 v[176:179], v171 offset:51200
	ds_read_b128 v[180:183], v171 offset:52224
	ds_read_b128 v[184:187], v171 offset:53248
	ds_read_b128 v[188:191], v171 offset:54272
	ds_read_b128 v[194:197], v171 offset:55296
	ds_read_b128 v[198:201], v171 offset:56320
	buffer_load_dwordx4 v165, s[4:7], s31 offen lds
	s_mov_b32 m0, s57
	s_nop 0
	buffer_load_dwordx4 v167, s[4:7], s31 offen lds
	s_add_i32 s31, s31, s33
	s_mov_b32 m0, s65
	s_nop 0
	buffer_load_dwordx4 v165, s[4:7], s31 offen lds
	s_mov_b32 m0, s76
	s_nop 0
	buffer_load_dwordx4 v167, s[4:7], s31 offen lds
	s_mov_b32 m0, s58
	s_nop 0
	buffer_load_dwordx4 v164, s[36:39], s30 offen lds
	s_mov_b32 m0, s59
	s_nop 0
	buffer_load_dwordx4 v166, s[36:39], s30 offen lds
	s_waitcnt vmcnt(8)
	s_waitcnt lgkmcnt(0)
	s_barrier
	s_setprio 1
	s_waitcnt lgkmcnt(7)
	v_mfma_f32_16x16x32_bf16 v[60:63], v[128:131], v[160:163], v[60:63]
	v_mfma_f32_16x16x32_bf16 v[56:59], v[136:139], v[160:163], v[56:59]
	s_waitcnt lgkmcnt(5)
	v_mfma_f32_16x16x32_bf16 v[44:47], v[128:131], v[176:179], v[44:47]
	v_mfma_f32_16x16x32_bf16 v[40:43], v[136:139], v[176:179], v[40:43]
	s_waitcnt lgkmcnt(3)
	v_mfma_f32_16x16x32_bf16 v[28:31], v[128:131], v[184:187], v[28:31]
	v_mfma_f32_16x16x32_bf16 v[24:27], v[136:139], v[184:187], v[24:27]
	s_waitcnt lgkmcnt(1)
	v_mfma_f32_16x16x32_bf16 v[12:15], v[128:131], v[194:197], v[12:15]
	v_mfma_f32_16x16x32_bf16 v[8:11], v[136:139], v[194:197], v[8:11]
	v_mfma_f32_16x16x32_bf16 v[60:63], v[132:135], v[172:175], v[60:63]
	v_mfma_f32_16x16x32_bf16 v[56:59], v[140:143], v[172:175], v[56:59]
	v_mfma_f32_16x16x32_bf16 v[44:47], v[132:135], v[180:183], v[44:47]
	v_mfma_f32_16x16x32_bf16 v[40:43], v[140:143], v[180:183], v[40:43]
	v_mfma_f32_16x16x32_bf16 v[28:31], v[132:135], v[188:191], v[28:31]
	v_mfma_f32_16x16x32_bf16 v[24:27], v[140:143], v[188:191], v[24:27]
	s_waitcnt lgkmcnt(0)
	v_mfma_f32_16x16x32_bf16 v[12:15], v[132:135], v[198:201], v[12:15]
	v_mfma_f32_16x16x32_bf16 v[8:11], v[140:143], v[198:201], v[8:11]
	s_setprio 0
	s_setprio 1
	v_mfma_f32_16x16x32_bf16 v[52:55], v[144:147], v[160:163], v[52:55]
	v_mfma_f32_16x16x32_bf16 v[48:51], v[152:155], v[160:163], v[48:51]
	v_mfma_f32_16x16x32_bf16 v[36:39], v[144:147], v[176:179], v[36:39]
	v_mfma_f32_16x16x32_bf16 v[32:35], v[152:155], v[176:179], v[32:35]
	v_mfma_f32_16x16x32_bf16 v[20:23], v[144:147], v[184:187], v[20:23]
	v_mfma_f32_16x16x32_bf16 v[16:19], v[152:155], v[184:187], v[16:19]
	v_mfma_f32_16x16x32_bf16 v[4:7], v[144:147], v[194:197], v[4:7]
	v_mfma_f32_16x16x32_bf16 v[0:3], v[152:155], v[194:197], v[0:3]
	v_mfma_f32_16x16x32_bf16 v[52:55], v[148:151], v[172:175], v[52:55]
	v_mfma_f32_16x16x32_bf16 v[48:51], v[156:159], v[172:175], v[48:51]
	v_mfma_f32_16x16x32_bf16 v[36:39], v[148:151], v[180:183], v[36:39]
	v_mfma_f32_16x16x32_bf16 v[32:35], v[156:159], v[180:183], v[32:35]
	v_mfma_f32_16x16x32_bf16 v[20:23], v[148:151], v[188:191], v[20:23]
	v_mfma_f32_16x16x32_bf16 v[16:19], v[156:159], v[188:191], v[16:19]
	v_mfma_f32_16x16x32_bf16 v[4:7], v[148:151], v[198:201], v[4:7]
	v_mfma_f32_16x16x32_bf16 v[0:3], v[156:159], v[198:201], v[0:3]
	s_setprio 0
	s_barrier
	s_add_i32 s29, s29, 2
	s_addk_i32 s16, 0x100
	s_addk_i32 s28, 0x100
	s_cmp_ge_i32 s29, s82
	s_cbranch_scc0 .LBB0_352
	s_branch .Lpeel_after_352

; #define PG8_BAR __builtin_amdgcn_s_barrier()
; template <class Epi, class Sched, bool ALIGN_EPI = false, bool SP2 = false, bool FP8 = false>
; __device__ __forceinline__ void gemm_phase(LAS unsigned char* lds, const Gemm g, const Sched& S, const Epi& E, int wbase) {
;     ...
;         }
;         if constexpr (ALIGN_EPI) { if (wr == 0) PG8_BAR; }
.Lpeel_after_352:
	s_mov_b32 s100, 1
	s_and_b64 vcc, exec, s[78:79]
	s_cbranch_vccz .LBB0_355

;     __device__ __forceinline__ unsigned a_off(const Unit& u, const Gemm& g) const { return (unsigned)u.pm * (unsigned)(BM * 2) * (unsigned)g.K; }
;     __device__ __forceinline__ unsigned b_off(const Unit& u, const Gemm& g) const { return (unsigned)u.pn * (unsigned)(BM * 2) * (unsigned)g.K; }
;     __device__ __forceinline__ bool next(int i, Unit& u) const { return so.next(i, u); }
; template <class Epi, class Sched, bool ALIGN_EPI = false, bool SP2 = false, bool FP8 = false>
; __device__ __forceinline__ void gemm_phase(LAS unsigned char* lds, const Gemm g, const Sched& S, const Epi& E, int wbase) {
;     ...
;     for (int i = 0; i < 2; ++i) { int R, C; stage_rc(tid * 16 + i * 8192, R, C); const int Rb = Epi::PERM ? ((R & ~31) + perm32(R & 31)) : R;
;         voffA[i] = (unsigned)(R * K + C) * 2u; voffB[i] = (unsigned)(Rb * K + C) * 2u; }
;     const unsigned kstep = (unsigned)(BK * 2);
;     const unsigned hstep = (unsigned)HALF * (unsigned)K * 2u;
;     typedef __amdgpu_buffer_rsrc_t rsrc_t;
;     const rsrc_t rA0 = __builtin_amdgcn_make_buffer_rsrc((void*)g.A, 0, 0xffffffff, 0x00020000), rB0 = __builtin_amdgcn_make_buffer_rsrc((void*)g.Bt, 0, 0xffffffff, 0x00020000);
;     rsrc_t rA1 = rA0, rB1 = rB0;
;     if constexpr (Sched::TWO) { rA1 = __builtin_amdgcn_make_buffer_rsrc((void*)S.A1, 0, 0xffffffff, 0x00020000); rB1 = __builtin_amdgcn_make_buffer_rsrc((void*)S.Bt1, 0, 0xffffffff, 0x00020000); }
;     const unsigned ldsw = (unsigned)wid * 1024u;
;     const int aoff = lds_byte(wr * 64 + fr, fq * 8), boff = lds_byte(wc * 32 + fr, fq * 8);
;     ...
;     Unit cur, nxt; int ui = 0;
;     if (!S.next(0, cur)) return;
;     f32x4 acc[2][2][4][2];
;     ...
;     PG8_ZERO_ACC();
;     v8i_t At[4], B0[2], B1[2];
;     unsigned cA = S.a_off(cur, g), cB = S.b_off(cur, g); rsrc_t rAc = (Sched::TWO && cur.part) ? rA1 : rA0, rBc = (Sched::TWO && cur.part) ? rB1 : rB0;
;     S.a_ready(cur);
;     if constexpr (SP2) {
;         PG8_STAGE(PG8_SB(0, 0), rBc, cB, voffB); PG8_STAGE(PG8_SB(0, 1), rBc, cB + hstep, voffB); PG8_STAGE(PG8_SA(0, 0), rAc, cA, voffA); PG8_STAGE(PG8_SA(0, 1), rAc, cA + hstep, voffA);
;         if (wr == 1) PG8_BAR;
;         PG8_WAIT_V(2); PG8_BAR;
;         PG8_STAGE(PG8_SB(1, 0), rBc, cB + kstep, voffB); PG8_STAGE(PG8_SA(1, 0), rAc, cA + kstep, voffA); PG8_STAGE(PG8_SB(1, 1), rBc, cB + hstep + kstep, voffB);
;         PG8_WAIT_V(6); PG8_BAR;
.LBB0_439:
	s_add_u32 s8, s8, 0x17800000
	s_addc_u32 s9, s9, 0
	s_add_i32 s28, s20, 0x18000
	s_or_b32 s16, s54, 0x80
	s_mov_b32 s6, s38
	s_mov_b32 s7, s39
	s_mov_b32 m0, s28
	s_add_i32 s29, s20, 0x1a000
	s_waitcnt vmcnt(2)
	s_barrier
	buffer_load_dwordx4 v133, s[4:7], s16 offen lds
	s_mov_b32 m0, s29
	s_add_i32 s30, s20, 0x8000
	buffer_load_dwordx4 v135, s[4:7], s16 offen lds
	s_or_b32 s16, s55, 0x80
	s_mov_b32 m0, s30
	s_add_i32 s31, s20, 0xa000
	buffer_load_dwordx4 v132, s[36:39], s16 offen lds
	s_mov_b32 m0, s31
	s_add_i32 s33, s20, 0x1c000
	buffer_load_dwordx4 v134, s[36:39], s16 offen lds
	s_bitset1_b32 s13, 7
	s_mov_b32 m0, s33
	s_add_i32 s34, s20, 0x1e000
	buffer_load_dwordx4 v133, s[4:7], s13 offen lds
	s_mov_b32 m0, s34
	v_bfe_u32 v137, v4, 4, 2
	buffer_load_dwordx4 v135, s[4:7], s13 offen lds
	s_ashr_i32 s6, s10, 31
	s_lshr_b32 s6, s6, 26
	v_and_b32_e32 v136, 15, v4
	s_add_i32 s6, s10, s6
	v_lshlrev_b32_e32 v5, 4, v137
	v_lshlrev_b32_e32 v4, 2, v4
	s_ashr_i32 s35, s6, 6
	v_lshl_or_b32 v5, v136, 6, v5
	s_lshl_b32 s6, s14, 13
	v_and_b32_e32 v4, 32, v4
	v_bitop3_b32 v6, v5, s6, v4 bitop3:0xde
	s_lshl_b32 s6, s11, 5
	s_and_b32 s6, s6, 0x60
	s_lshl_b32 s41, s14, 6
	s_lshl_b32 s7, s6, 7
	s_cmp_gt_i32 s10, 63
	s_waitcnt vmcnt(6)
	s_cselect_b64 s[10:11], -1, 0
	s_add_i32 s42, s35, -2
	s_add_i32 s43, s20, 0xc000
	v_bitop3_b32 v4, v5, s7, v4 bitop3:0xde
	s_cmpk_lt_u32 s12, 0x100
	v_mov_b32_e32 v1, v0
	v_mov_b32_e32 v2, v0
	v_mov_b32_e32 v3, v0
	s_cselect_b64 s[12:13], -1, 0
	s_add_i32 s44, s20, 0xe000
	s_mov_b32 s45, 0
	v_add_u32_e32 v138, 0, v4
	v_add_u32_e32 v139, 0, v6
	s_lshl_b32 s14, s6, 1
	s_barrier
	s_mov_b32 s100, 0
	s_branch .LBB0_442

;     __device__ __forceinline__ unsigned a_off(const Unit& u, const Gemm& g) const { return (unsigned)u.pm * (unsigned)(BM * 2) * (unsigned)g.K; }
;     __device__ __forceinline__ unsigned b_off(const Unit& u, const Gemm& g) const { return (unsigned)u.pn * (unsigned)(BM * 2) * (unsigned)g.K; }
;     __device__ __forceinline__ bool next(int i, Unit& u) const { return so.next(i, u); }
;     __device__ __forceinline__ unsigned a_off(const Unit& u, const Gemm& g) const { return (unsigned)u.pm * (unsigned)(BM * 2) * (unsigned)g.K; }
;     __device__ __forceinline__ bool next(int i, Unit& u) const { const bool ok = so.next(i >> 1, u); u.part = i & 1; return ok; }
;     __device__ __forceinline__ unsigned a_off(const Unit& u, const Gemm& g) const { return (unsigned)u.pm * (unsigned)(BM * 2) * (unsigned)g.K; }
;     __device__ __forceinline__ unsigned b_off(const Unit& u, const Gemm& g) const { return (unsigned)u.pn * (unsigned)(BM * 2) * (unsigned)g.K; }
; template <class Epi, class Sched, bool ALIGN_EPI = false, bool SP2 = false, bool FP8 = false>
; __device__ __forceinline__ void gemm_phase(LAS unsigned char* lds, const Gemm g, const Sched& S, const Epi& E, int wbase) {
;     ...
;         const bool has_next = S.next(ui + 1, nxt);
;         const unsigned nA = has_next ? S.a_off(nxt, g) : cA, nB = has_next ? S.b_off(nxt, g) : cB;
;         const rsrc_t rAn = (Sched::TWO && has_next) ? (nxt.part ? rA1 : rA0) : rAc, rBn = (Sched::TWO && has_next) ? (nxt.part ? rB1 : rB0) : rBc;
;         float pre_[8] = {0.f, 0.f, 0.f, 0.f, 0.f, 0.f, 0.f, 0.f};
;         if constexpr (Epi::HAS_PRE) E.pre_load(pre_, cur, wr);
;         for (int t = 0; t < nt; t += 2) {
;             const bool last = (t == nt - 2);
;             const unsigned a1 = cA + (unsigned)(t + 1) * kstep;
;             const unsigned a2 = last ? nA : cA + (unsigned)(t + 2) * kstep, b2 = last ? nB : cB + (unsigned)(t + 2) * kstep; const rsrc_t rA2 = (Sched::TWO && last) ? rAn : rAc, rB2 = (Sched::TWO && last) ? rBn : rBc;
;             const unsigned a3 = a2 + kstep, b3 = b2 + kstep;
;             if (last && has_next) S.a_ready(nxt);
;             if constexpr (SP2) {
;             PG8_LDB(B0, 0, 0); PG8_LDB(B1, 0, 1); PG8_SCHED; PG8_LDA(At, 0, 0); PG8_STAGE(PG8_SA(1, 1), rAc, a1 + hstep, voffA);
;             PG8_WAIT_V(8); PG8_WAIT_L(0); PG8_BAR; PG8_MMA(0, 0, At, B0); PG8_MMA(0, 1, At, B1); PG8_BAR; PG8_SCHED;
.LBB0_448:
	s_lshl_b32 s48, s47, 17
	s_andn2_b64 vcc, exec, s[10:11]
	s_lshl_b32 s52, s46, 17
	s_cbranch_vccnz .LBB0_456
	s_and_b64 s[6:7], s[16:17], exec
	v_mov_b64_e32 v[6:7], v[2:3]
	v_mov_b64_e32 v[18:19], v[2:3]
	v_mov_b64_e32 v[22:23], v[2:3]
	v_mov_b64_e32 v[34:35], v[2:3]
	v_mov_b64_e32 v[38:39], v[2:3]
	v_mov_b64_e32 v[50:51], v[2:3]
	v_mov_b64_e32 v[54:55], v[2:3]
	v_mov_b64_e32 v[10:11], v[2:3]
	v_mov_b64_e32 v[14:15], v[2:3]
	v_mov_b64_e32 v[26:27], v[2:3]
	v_mov_b64_e32 v[30:31], v[2:3]
	v_mov_b64_e32 v[42:43], v[2:3]
	v_mov_b64_e32 v[46:47], v[2:3]
	v_mov_b64_e32 v[58:59], v[2:3]
	s_waitcnt vmcnt(37)
	v_mov_b64_e32 v[62:63], v[2:3]
	s_waitcnt vmcnt(36)
	v_mov_b64_e32 v[66:67], v[2:3]
	s_waitcnt vmcnt(35)
	v_mov_b64_e32 v[70:71], v[2:3]
	s_waitcnt vmcnt(32)
	v_mov_b64_e32 v[82:83], v[2:3]
	s_waitcnt vmcnt(31)
	v_mov_b64_e32 v[86:87], v[2:3]
	s_waitcnt vmcnt(28)
	v_mov_b64_e32 v[98:99], v[2:3]
	s_waitcnt vmcnt(27)
	v_mov_b64_e32 v[102:103], v[2:3]
	s_waitcnt vmcnt(24)
	v_mov_b64_e32 v[114:115], v[2:3]
	s_waitcnt vmcnt(23)
	v_mov_b64_e32 v[118:119], v[2:3]
	v_mov_b64_e32 v[74:75], v[2:3]
	v_mov_b64_e32 v[78:79], v[2:3]
	v_mov_b64_e32 v[90:91], v[2:3]
	v_mov_b64_e32 v[94:95], v[2:3]
	v_mov_b64_e32 v[106:107], v[2:3]
	v_mov_b64_e32 v[110:111], v[2:3]
	s_waitcnt vmcnt(22)
	v_mov_b64_e32 v[122:123], v[2:3]
	v_mov_b64_e32 v[126:127], v[2:3]
	s_cselect_b32 s56, s48, s55
	s_cselect_b32 s57, s52, s54
	s_add_i32 s58, s55, 0x80
	s_add_i32 s59, s54, 0x100
	s_mov_b32 s60, 0
	v_mov_b64_e32 v[4:5], v[0:1]
	v_mov_b64_e32 v[16:17], v[0:1]
	v_mov_b64_e32 v[20:21], v[0:1]
	v_mov_b64_e32 v[32:33], v[0:1]
	v_mov_b64_e32 v[36:37], v[0:1]
	v_mov_b64_e32 v[48:49], v[0:1]
	v_mov_b64_e32 v[52:53], v[0:1]
	v_mov_b64_e32 v[8:9], v[0:1]
	v_mov_b64_e32 v[12:13], v[0:1]
	v_mov_b64_e32 v[24:25], v[0:1]
	v_mov_b64_e32 v[28:29], v[0:1]
	v_mov_b64_e32 v[40:41], v[0:1]
	v_mov_b64_e32 v[44:45], v[0:1]
	v_mov_b64_e32 v[56:57], v[0:1]
	v_mov_b64_e32 v[60:61], v[0:1]
	v_mov_b64_e32 v[64:65], v[0:1]
	v_mov_b64_e32 v[68:69], v[0:1]
	v_mov_b64_e32 v[80:81], v[0:1]
	v_mov_b64_e32 v[84:85], v[0:1]
	v_mov_b64_e32 v[96:97], v[0:1]
	v_mov_b64_e32 v[100:101], v[0:1]
	v_mov_b64_e32 v[112:113], v[0:1]
	v_mov_b64_e32 v[116:117], v[0:1]
	v_mov_b64_e32 v[72:73], v[0:1]
	v_mov_b64_e32 v[76:77], v[0:1]
	v_mov_b64_e32 v[88:89], v[0:1]
	v_mov_b64_e32 v[92:93], v[0:1]
	v_mov_b64_e32 v[104:105], v[0:1]
	v_mov_b64_e32 v[108:109], v[0:1]
	v_mov_b64_e32 v[120:121], v[0:1]
	v_mov_b64_e32 v[124:125], v[0:1]
	s_cmp_eq_u32 s100, 1
	s_cbranch_scc0 .LBB0_450
	v_add_u32_e32 v148, 0x10000, v138
	v_add_u32_e32 v164, 0x14000, v138
	ds_read_b128 v[128:131], v148
	ds_read_b128 v[140:143], v148 offset:1024
	ds_read_b128 v[144:147], v148 offset:2048
	ds_read_b128 v[148:151], v148 offset:3072
	ds_read_b128 v[152:155], v164
	ds_read_b128 v[156:159], v164 offset:1024
	ds_read_b128 v[160:163], v164 offset:2048
	ds_read_b128 v[164:167], v164 offset:3072
	s_add_i32 s6, s58, 0x80
	s_cmp_eq_u32 s42, s60
	s_cselect_b32 s61, s56, s6
	s_cselect_b32 s55, s57, s59
	s_or_b32 s54, s61, 0x80
	s_add_i32 s6, s19, s58
	s_mov_b32 m0, s43
	ds_read_b128 v[168:171], v139
	ds_read_b128 v[172:175], v139 offset:1024
	ds_read_b128 v[176:179], v139 offset:2048
	ds_read_b128 v[180:183], v139 offset:3072
	ds_read_b128 v[184:187], v139 offset:4096
	ds_read_b128 v[188:191], v139 offset:5120
	ds_read_b128 v[194:197], v139 offset:6144
	ds_read_b128 v[198:201], v139 offset:7168
	buffer_load_dwordx4 v132, s[36:39], s6 offen lds
	s_mov_b32 m0, s44
	s_nop 0
	buffer_load_dwordx4 v134, s[36:39], s6 offen lds
	s_waitcnt vmcnt(24)
	s_waitcnt lgkmcnt(0)
	s_barrier
	s_setprio 1
	s_waitcnt lgkmcnt(7)
	v_mfma_f32_16x16x32_bf16 v[124:127], v[128:131], v[168:171], v[124:127]
	v_mfma_f32_16x16x32_bf16 v[120:123], v[144:147], v[168:171], v[120:123]
	s_waitcnt lgkmcnt(5)
	v_mfma_f32_16x16x32_bf16 v[108:111], v[128:131], v[176:179], v[108:111]
	v_mfma_f32_16x16x32_bf16 v[104:107], v[144:147], v[176:179], v[104:107]
	s_waitcnt lgkmcnt(3)
	v_mfma_f32_16x16x32_bf16 v[92:95], v[128:131], v[184:187], v[92:95]
	v_mfma_f32_16x16x32_bf16 v[88:91], v[144:147], v[184:187], v[88:91]
	s_waitcnt lgkmcnt(1)
	v_mfma_f32_16x16x32_bf16 v[76:79], v[128:131], v[194:197], v[76:79]
	v_mfma_f32_16x16x32_bf16 v[72:75], v[144:147], v[194:197], v[72:75]
	v_mfma_f32_16x16x32_bf16 v[124:127], v[140:143], v[172:175], v[124:127]
	v_mfma_f32_16x16x32_bf16 v[120:123], v[148:151], v[172:175], v[120:123]
	v_mfma_f32_16x16x32_bf16 v[108:111], v[140:143], v[180:183], v[108:111]
	v_mfma_f32_16x16x32_bf16 v[104:107], v[148:151], v[180:183], v[104:107]
	v_mfma_f32_16x16x32_bf16 v[92:95], v[140:143], v[188:191], v[92:95]
	v_mfma_f32_16x16x32_bf16 v[88:91], v[148:151], v[188:191], v[88:91]
	s_waitcnt lgkmcnt(0)
	v_mfma_f32_16x16x32_bf16 v[76:79], v[140:143], v[198:201], v[76:79]
	v_mfma_f32_16x16x32_bf16 v[72:75], v[148:151], v[198:201], v[72:75]
	s_setprio 0
	s_setprio 1
	v_mfma_f32_16x16x32_bf16 v[116:119], v[152:155], v[168:171], v[116:119]
	v_mfma_f32_16x16x32_bf16 v[112:115], v[160:163], v[168:171], v[112:115]
	v_mfma_f32_16x16x32_bf16 v[100:103], v[152:155], v[176:179], v[100:103]
	v_mfma_f32_16x16x32_bf16 v[96:99], v[160:163], v[176:179], v[96:99]
	v_mfma_f32_16x16x32_bf16 v[84:87], v[152:155], v[184:187], v[84:87]
	v_mfma_f32_16x16x32_bf16 v[80:83], v[160:163], v[184:187], v[80:83]
	v_mfma_f32_16x16x32_bf16 v[68:71], v[152:155], v[194:197], v[68:71]
	v_mfma_f32_16x16x32_bf16 v[64:67], v[160:163], v[194:197], v[64:67]
	v_mfma_f32_16x16x32_bf16 v[116:119], v[156:159], v[172:175], v[116:119]
	v_mfma_f32_16x16x32_bf16 v[112:115], v[164:167], v[172:175], v[112:115]
	v_mfma_f32_16x16x32_bf16 v[100:103], v[156:159], v[180:183], v[100:103]
	v_mfma_f32_16x16x32_bf16 v[96:99], v[164:167], v[180:183], v[96:99]
	v_mfma_f32_16x16x32_bf16 v[84:87], v[156:159], v[188:191], v[84:87]
	v_mfma_f32_16x16x32_bf16 v[80:83], v[164:167], v[188:191], v[80:83]
	v_mfma_f32_16x16x32_bf16 v[68:71], v[156:159], v[198:201], v[68:71]
	v_mfma_f32_16x16x32_bf16 v[64:67], v[164:167], v[198:201], v[64:67]
	s_setprio 0
	s_barrier
; #define PG8_STAGE(bufoff, rs_, soff_, voff) do { _Pragma("unroll") for (int _i = 0; _i < 2; ++_i) \
;         __builtin_amdgcn_raw_ptr_buffer_load_lds(rs_, (LAS void*)(lds + (bufoff) + ldsw + _i * 8192), 16, (int)(voff)[_i], (int)(soff_), 0, 0); } while (0)
; #define PG8_LDA(dst, b, h) do { _Pragma("unroll") for (int m = 0; m < 4; ++m) dst[m] = PG8_LD2(lds + PG8_SA(b, h) + aoff + m * 2048); } while (0)
; #define PG8_LDB(dst, b, h) do { _Pragma("unroll") for (int n = 0; n < 2; ++n) dst[n] = PG8_LD2(lds + PG8_SB(b, h) + boff + n * 2048); } while (0)
; #define PG8_WAIT_V(n) asm volatile("s_waitcnt vmcnt(" #n ")" ::: "memory")
; #define PG8_WAIT_L(n) asm volatile("s_waitcnt lgkmcnt(" #n ")" ::: "memory")
; #define PG8_BAR __builtin_amdgcn_s_barrier()
; #define PG8_SCHED __builtin_amdgcn_sched_barrier(0)
; template <class Epi, class Sched, bool ALIGN_EPI = false, bool SP2 = false, bool FP8 = false>
; __device__ __forceinline__ void gemm_phase(LAS unsigned char* lds, const Gemm g, const Sched& S, const Epi& E, int wbase) {
;     ...
;             PG8_LDA(At, 0, 1); PG8_STAGE(PG8_SB(0, 0), rB2, b2, voffB); PG8_STAGE(PG8_SB(0, 1), rB2, b2 + hstep, voffB); PG8_STAGE(PG8_SA(0, 0), rA2, a2, voffA);
;             PG8_WAIT_V(8); PG8_WAIT_L(0); PG8_BAR; PG8_MMA(1, 0, At, B0); PG8_MMA(1, 1, At, B1); PG8_BAR; PG8_SCHED;
;             PG8_LDB(B0, 1, 0); PG8_LDB(B1, 1, 1); PG8_SCHED; PG8_LDA(At, 1, 0); PG8_STAGE(PG8_SA(0, 1), rA2, a2 + hstep, voffA);
;             PG8_WAIT_V(8); PG8_WAIT_L(0); PG8_BAR; PG8_MMA(0, 0, At, B0); PG8_MMA(0, 1, At, B1); PG8_BAR; PG8_SCHED;
	s_mov_b32 m0, s21
	s_mov_b32 s6, s38
	s_mov_b32 s7, s39
	ds_read_b128 v[168:171], v139 offset:16384
	ds_read_b128 v[172:175], v139 offset:17408
	ds_read_b128 v[176:179], v139 offset:18432
	ds_read_b128 v[180:183], v139 offset:19456
	ds_read_b128 v[184:187], v139 offset:20480
	ds_read_b128 v[188:191], v139 offset:21504
	ds_read_b128 v[194:197], v139 offset:22528
	ds_read_b128 v[198:201], v139 offset:23552
	buffer_load_dwordx4 v133, s[4:7], s55 offen lds
	s_mov_b32 m0, s22
	s_add_i32 s62, s55, s19
	buffer_load_dwordx4 v135, s[4:7], s55 offen lds
	s_mov_b32 m0, s23
	s_nop 0
	buffer_load_dwordx4 v133, s[4:7], s62 offen lds
	s_mov_b32 m0, s24
	s_nop 0
	buffer_load_dwordx4 v135, s[4:7], s62 offen lds
	s_mov_b32 m0, s20
	s_nop 0
	buffer_load_dwordx4 v132, s[36:39], s61 offen lds
	s_mov_b32 m0, s25
	s_nop 0
	buffer_load_dwordx4 v134, s[36:39], s61 offen lds
	s_waitcnt vmcnt(24)
	s_waitcnt lgkmcnt(0)
	s_barrier
	s_setprio 1
	s_waitcnt lgkmcnt(7)
	v_mfma_f32_16x16x32_bf16 v[60:63], v[128:131], v[168:171], v[60:63]
	v_mfma_f32_16x16x32_bf16 v[56:59], v[144:147], v[168:171], v[56:59]
	s_waitcnt lgkmcnt(5)
	v_mfma_f32_16x16x32_bf16 v[44:47], v[128:131], v[176:179], v[44:47]
	v_mfma_f32_16x16x32_bf16 v[40:43], v[144:147], v[176:179], v[40:43]
	s_waitcnt lgkmcnt(3)
	v_mfma_f32_16x16x32_bf16 v[28:31], v[128:131], v[184:187], v[28:31]
	v_mfma_f32_16x16x32_bf16 v[24:27], v[144:147], v[184:187], v[24:27]
	s_waitcnt lgkmcnt(1)
	v_mfma_f32_16x16x32_bf16 v[12:15], v[128:131], v[194:197], v[12:15]
	v_mfma_f32_16x16x32_bf16 v[8:11], v[144:147], v[194:197], v[8:11]
	v_mfma_f32_16x16x32_bf16 v[60:63], v[140:143], v[172:175], v[60:63]
	v_mfma_f32_16x16x32_bf16 v[56:59], v[148:151], v[172:175], v[56:59]
	v_mfma_f32_16x16x32_bf16 v[44:47], v[140:143], v[180:183], v[44:47]
	v_mfma_f32_16x16x32_bf16 v[40:43], v[148:151], v[180:183], v[40:43]
	v_mfma_f32_16x16x32_bf16 v[28:31], v[140:143], v[188:191], v[28:31]
	v_mfma_f32_16x16x32_bf16 v[24:27], v[148:151], v[188:191], v[24:27]
	s_waitcnt lgkmcnt(0)
	v_mfma_f32_16x16x32_bf16 v[12:15], v[140:143], v[198:201], v[12:15]
	v_mfma_f32_16x16x32_bf16 v[8:11], v[148:151], v[198:201], v[8:11]
	s_setprio 0
	s_setprio 1
	v_mfma_f32_16x16x32_bf16 v[52:55], v[152:155], v[168:171], v[52:55]
	v_mfma_f32_16x16x32_bf16 v[48:51], v[160:163], v[168:171], v[48:51]
	v_mfma_f32_16x16x32_bf16 v[36:39], v[152:155], v[176:179], v[36:39]
	v_mfma_f32_16x16x32_bf16 v[32:35], v[160:163], v[176:179], v[32:35]
	v_mfma_f32_16x16x32_bf16 v[20:23], v[152:155], v[184:187], v[20:23]
	v_mfma_f32_16x16x32_bf16 v[16:19], v[160:163], v[184:187], v[16:19]
	v_mfma_f32_16x16x32_bf16 v[4:7], v[152:155], v[194:197], v[4:7]
	v_mfma_f32_16x16x32_bf16 v[0:3], v[160:163], v[194:197], v[0:3]
	v_mfma_f32_16x16x32_bf16 v[52:55], v[156:159], v[172:175], v[52:55]
	v_mfma_f32_16x16x32_bf16 v[48:51], v[164:167], v[172:175], v[48:51]
	v_mfma_f32_16x16x32_bf16 v[36:39], v[156:159], v[180:183], v[36:39]
	v_mfma_f32_16x16x32_bf16 v[32:35], v[164:167], v[180:183], v[32:35]
	v_mfma_f32_16x16x32_bf16 v[20:23], v[156:159], v[188:191], v[20:23]
	v_mfma_f32_16x16x32_bf16 v[16:19], v[164:167], v[188:191], v[16:19]
	v_mfma_f32_16x16x32_bf16 v[4:7], v[156:159], v[198:201], v[4:7]
	v_mfma_f32_16x16x32_bf16 v[0:3], v[164:167], v[198:201], v[0:3]
	s_setprio 0
	s_barrier
	v_add_u32_e32 v148, 0x18000, v138
	v_add_u32_e32 v164, 0x1c000, v138
	ds_read_b128 v[128:131], v148
	ds_read_b128 v[140:143], v148 offset:1024
	ds_read_b128 v[144:147], v148 offset:2048
	ds_read_b128 v[148:151], v148 offset:3072
	ds_read_b128 v[152:155], v164
	ds_read_b128 v[156:159], v164 offset:1024
	ds_read_b128 v[160:163], v164 offset:2048
	ds_read_b128 v[164:167], v164 offset:3072
	s_add_i32 s61, s61, s19
	s_mov_b32 m0, s26
	ds_read_b128 v[168:171], v139 offset:32768
	ds_read_b128 v[172:175], v139 offset:33792
	ds_read_b128 v[176:179], v139 offset:34816
	ds_read_b128 v[180:183], v139 offset:35840
	ds_read_b128 v[184:187], v139 offset:36864
	ds_read_b128 v[188:191], v139 offset:37888
	ds_read_b128 v[194:197], v139 offset:38912
	ds_read_b128 v[198:201], v139 offset:39936
	buffer_load_dwordx4 v132, s[36:39], s61 offen lds
	s_mov_b32 m0, s27
	s_nop 0
	buffer_load_dwordx4 v134, s[36:39], s61 offen lds
	s_waitcnt vmcnt(8)
	s_waitcnt lgkmcnt(0)
	s_barrier
; #define PG8_STAGE(bufoff, rs_, soff_, voff) do { _Pragma("unroll") for (int _i = 0; _i < 2; ++_i) \
;         __builtin_amdgcn_raw_ptr_buffer_load_lds(rs_, (LAS void*)(lds + (bufoff) + ldsw + _i * 8192), 16, (int)(voff)[_i], (int)(soff_), 0, 0); } while (0)
; #define PG8_LDA(dst, b, h) do { _Pragma("unroll") for (int m = 0; m < 4; ++m) dst[m] = PG8_LD2(lds + PG8_SA(b, h) + aoff + m * 2048); } while (0)
; #define PG8_WAIT_V(n) asm volatile("s_waitcnt vmcnt(" #n ")" ::: "memory")
; #define PG8_WAIT_L(n) asm volatile("s_waitcnt lgkmcnt(" #n ")" ::: "memory")
; #define PG8_BAR __builtin_amdgcn_s_barrier()
; #define PG8_SCHED __builtin_amdgcn_sched_barrier(0)
; template <class Epi, class Sched, bool ALIGN_EPI = false, bool SP2 = false, bool FP8 = false>
; __device__ __forceinline__ void gemm_phase(LAS unsigned char* lds, const Gemm g, const Sched& S, const Epi& E, int wbase) {
;     ...
;             PG8_WAIT_V(8); PG8_WAIT_L(0); PG8_BAR; PG8_MMA(0, 0, At, B0); PG8_MMA(0, 1, At, B1); PG8_BAR; PG8_SCHED;
;             PG8_LDA(At, 1, 1); PG8_STAGE(PG8_SB(1, 0), rB2, b3, voffB); PG8_STAGE(PG8_SB(1, 1), rB2, b3 + hstep, voffB); PG8_STAGE(PG8_SA(1, 0), rA2, a3, voffA);
;             PG8_WAIT_V(8); PG8_WAIT_L(0); PG8_BAR; PG8_MMA(1, 0, At, B0); PG8_MMA(1, 1, At, B1); PG8_BAR; PG8_SCHED;
	s_setprio 1
	s_waitcnt lgkmcnt(7)
	v_mfma_f32_16x16x32_bf16 v[124:127], v[128:131], v[168:171], v[124:127]
	v_mfma_f32_16x16x32_bf16 v[120:123], v[144:147], v[168:171], v[120:123]
	s_waitcnt lgkmcnt(5)
	v_mfma_f32_16x16x32_bf16 v[108:111], v[128:131], v[176:179], v[108:111]
	v_mfma_f32_16x16x32_bf16 v[104:107], v[144:147], v[176:179], v[104:107]
	s_waitcnt lgkmcnt(3)
	v_mfma_f32_16x16x32_bf16 v[92:95], v[128:131], v[184:187], v[92:95]
	v_mfma_f32_16x16x32_bf16 v[88:91], v[144:147], v[184:187], v[88:91]
	s_waitcnt lgkmcnt(1)
	v_mfma_f32_16x16x32_bf16 v[76:79], v[128:131], v[194:197], v[76:79]
	v_mfma_f32_16x16x32_bf16 v[72:75], v[144:147], v[194:197], v[72:75]
	v_mfma_f32_16x16x32_bf16 v[124:127], v[140:143], v[172:175], v[124:127]
	v_mfma_f32_16x16x32_bf16 v[120:123], v[148:151], v[172:175], v[120:123]
	v_mfma_f32_16x16x32_bf16 v[108:111], v[140:143], v[180:183], v[108:111]
	v_mfma_f32_16x16x32_bf16 v[104:107], v[148:151], v[180:183], v[104:107]
	v_mfma_f32_16x16x32_bf16 v[92:95], v[140:143], v[188:191], v[92:95]
	v_mfma_f32_16x16x32_bf16 v[88:91], v[148:151], v[188:191], v[88:91]
	s_waitcnt lgkmcnt(0)
	v_mfma_f32_16x16x32_bf16 v[76:79], v[140:143], v[198:201], v[76:79]
	v_mfma_f32_16x16x32_bf16 v[72:75], v[148:151], v[198:201], v[72:75]
	s_setprio 0
	s_setprio 1
	v_mfma_f32_16x16x32_bf16 v[116:119], v[152:155], v[168:171], v[116:119]
	v_mfma_f32_16x16x32_bf16 v[112:115], v[160:163], v[168:171], v[112:115]
	v_mfma_f32_16x16x32_bf16 v[100:103], v[152:155], v[176:179], v[100:103]
	v_mfma_f32_16x16x32_bf16 v[96:99], v[160:163], v[176:179], v[96:99]
	v_mfma_f32_16x16x32_bf16 v[84:87], v[152:155], v[184:187], v[84:87]
	v_mfma_f32_16x16x32_bf16 v[80:83], v[160:163], v[184:187], v[80:83]
	v_mfma_f32_16x16x32_bf16 v[68:71], v[152:155], v[194:197], v[68:71]
	v_mfma_f32_16x16x32_bf16 v[64:67], v[160:163], v[194:197], v[64:67]
	v_mfma_f32_16x16x32_bf16 v[116:119], v[156:159], v[172:175], v[116:119]
	v_mfma_f32_16x16x32_bf16 v[112:115], v[164:167], v[172:175], v[112:115]
	v_mfma_f32_16x16x32_bf16 v[100:103], v[156:159], v[180:183], v[100:103]
	v_mfma_f32_16x16x32_bf16 v[96:99], v[164:167], v[180:183], v[96:99]
	v_mfma_f32_16x16x32_bf16 v[84:87], v[156:159], v[188:191], v[84:87]
	v_mfma_f32_16x16x32_bf16 v[80:83], v[164:167], v[188:191], v[80:83]
	v_mfma_f32_16x16x32_bf16 v[68:71], v[156:159], v[198:201], v[68:71]
	v_mfma_f32_16x16x32_bf16 v[64:67], v[164:167], v[198:201], v[64:67]
	s_setprio 0
	s_barrier
	s_mov_b32 m0, s28
	s_bitset1_b32 s55, 7
	ds_read_b128 v[168:171], v139 offset:49152
	ds_read_b128 v[172:175], v139 offset:50176
	ds_read_b128 v[176:179], v139 offset:51200
	ds_read_b128 v[180:183], v139 offset:52224
	ds_read_b128 v[184:187], v139 offset:53248
	ds_read_b128 v[188:191], v139 offset:54272
	ds_read_b128 v[194:197], v139 offset:55296
	ds_read_b128 v[198:201], v139 offset:56320
	buffer_load_dwordx4 v133, s[4:7], s55 offen lds
	s_mov_b32 m0, s29
	s_nop 0
	buffer_load_dwordx4 v135, s[4:7], s55 offen lds
	s_add_i32 s55, s55, s19
	s_mov_b32 m0, s33
	s_nop 0
	buffer_load_dwordx4 v133, s[4:7], s55 offen lds
	s_mov_b32 m0, s34
	s_nop 0
	buffer_load_dwordx4 v135, s[4:7], s55 offen lds
	s_mov_b32 m0, s30
	s_nop 0
	buffer_load_dwordx4 v132, s[36:39], s54 offen lds
	s_mov_b32 m0, s31
	s_nop 0
	buffer_load_dwordx4 v134, s[36:39], s54 offen lds
	s_waitcnt vmcnt(8)
	s_waitcnt lgkmcnt(0)
	s_barrier
	s_setprio 1
	s_waitcnt lgkmcnt(7)
	v_mfma_f32_16x16x32_bf16 v[60:63], v[128:131], v[168:171], v[60:63]
	v_mfma_f32_16x16x32_bf16 v[56:59], v[144:147], v[168:171], v[56:59]
	s_waitcnt lgkmcnt(5)
	v_mfma_f32_16x16x32_bf16 v[44:47], v[128:131], v[176:179], v[44:47]
	v_mfma_f32_16x16x32_bf16 v[40:43], v[144:147], v[176:179], v[40:43]
	s_waitcnt lgkmcnt(3)
	v_mfma_f32_16x16x32_bf16 v[28:31], v[128:131], v[184:187], v[28:31]
	v_mfma_f32_16x16x32_bf16 v[24:27], v[144:147], v[184:187], v[24:27]
	s_waitcnt lgkmcnt(1)
	v_mfma_f32_16x16x32_bf16 v[12:15], v[128:131], v[194:197], v[12:15]
	v_mfma_f32_16x16x32_bf16 v[8:11], v[144:147], v[194:197], v[8:11]
	v_mfma_f32_16x16x32_bf16 v[60:63], v[140:143], v[172:175], v[60:63]
	v_mfma_f32_16x16x32_bf16 v[56:59], v[148:151], v[172:175], v[56:59]
	v_mfma_f32_16x16x32_bf16 v[44:47], v[140:143], v[180:183], v[44:47]
	v_mfma_f32_16x16x32_bf16 v[40:43], v[148:151], v[180:183], v[40:43]
	v_mfma_f32_16x16x32_bf16 v[28:31], v[140:143], v[188:191], v[28:31]
	v_mfma_f32_16x16x32_bf16 v[24:27], v[148:151], v[188:191], v[24:27]
	s_waitcnt lgkmcnt(0)
	v_mfma_f32_16x16x32_bf16 v[12:15], v[140:143], v[198:201], v[12:15]
	v_mfma_f32_16x16x32_bf16 v[8:11], v[148:151], v[198:201], v[8:11]
	s_setprio 0
	s_setprio 1
	v_mfma_f32_16x16x32_bf16 v[52:55], v[152:155], v[168:171], v[52:55]
	v_mfma_f32_16x16x32_bf16 v[48:51], v[160:163], v[168:171], v[48:51]
	v_mfma_f32_16x16x32_bf16 v[36:39], v[152:155], v[176:179], v[36:39]
	v_mfma_f32_16x16x32_bf16 v[32:35], v[160:163], v[176:179], v[32:35]
	v_mfma_f32_16x16x32_bf16 v[20:23], v[152:155], v[184:187], v[20:23]
	v_mfma_f32_16x16x32_bf16 v[16:19], v[160:163], v[184:187], v[16:19]
	v_mfma_f32_16x16x32_bf16 v[4:7], v[152:155], v[194:197], v[4:7]
	v_mfma_f32_16x16x32_bf16 v[0:3], v[160:163], v[194:197], v[0:3]
	v_mfma_f32_16x16x32_bf16 v[52:55], v[156:159], v[172:175], v[52:55]
	v_mfma_f32_16x16x32_bf16 v[48:51], v[164:167], v[172:175], v[48:51]
	v_mfma_f32_16x16x32_bf16 v[36:39], v[156:159], v[180:183], v[36:39]
	v_mfma_f32_16x16x32_bf16 v[32:35], v[164:167], v[180:183], v[32:35]
	v_mfma_f32_16x16x32_bf16 v[20:23], v[156:159], v[188:191], v[20:23]
	v_mfma_f32_16x16x32_bf16 v[16:19], v[164:167], v[188:191], v[16:19]
	v_mfma_f32_16x16x32_bf16 v[4:7], v[156:159], v[198:201], v[4:7]
	v_mfma_f32_16x16x32_bf16 v[0:3], v[164:167], v[198:201], v[0:3]
	s_setprio 0
	s_barrier
	s_add_i32 s60, s60, 2
	s_addk_i32 s58, 0x100
	s_addk_i32 s59, 0x100
	s_cmp_ge_i32 s60, s35
	s_cbranch_scc0 .LBB0_450
	s_branch .Lpeel_after_450

; #define PG8_BAR __builtin_amdgcn_s_barrier()
; template <class Epi, class Sched, bool ALIGN_EPI = false, bool SP2 = false, bool FP8 = false>
; __device__ __forceinline__ void gemm_phase(LAS unsigned char* lds, const Gemm g, const Sched& S, const Epi& E, int wbase) {
;     ...
;         }
;         if constexpr (ALIGN_EPI) { if (wr == 0) PG8_BAR; }
.Lpeel_after_450:
	s_mov_b32 s100, 1
	s_and_b64 vcc, exec, s[12:13]
	s_cbranch_vccz .LBB0_453

;     __device__ __forceinline__ unsigned a_off(const Unit& u, const Gemm& g) const { return (unsigned)u.pm * (unsigned)(BM * 2) * (unsigned)g.K; }
;     __device__ __forceinline__ unsigned b_off(const Unit& u, const Gemm& g) const { return (unsigned)u.pn * (unsigned)(BM * 2) * (unsigned)g.K; }
;     __device__ __forceinline__ bool next(int i, Unit& u) const { return so.next(i, u); }
; template <class Epi, class Sched, bool ALIGN_EPI = false, bool SP2 = false, bool FP8 = false>
; __device__ __forceinline__ void gemm_phase(LAS unsigned char* lds, const Gemm g, const Sched& S, const Epi& E, int wbase) {
;     ...
;     for (int i = 0; i < 2; ++i) { int R, C; stage_rc(tid * 16 + i * 8192, R, C); const int Rb = Epi::PERM ? ((R & ~31) + perm32(R & 31)) : R;
;         voffA[i] = (unsigned)(R * K + C) * 2u; voffB[i] = (unsigned)(Rb * K + C) * 2u; }
;     const unsigned kstep = (unsigned)(BK * 2);
;     const unsigned hstep = (unsigned)HALF * (unsigned)K * 2u;
;     typedef __amdgpu_buffer_rsrc_t rsrc_t;
;     const rsrc_t rA0 = __builtin_amdgcn_make_buffer_rsrc((void*)g.A, 0, 0xffffffff, 0x00020000), rB0 = __builtin_amdgcn_make_buffer_rsrc((void*)g.Bt, 0, 0xffffffff, 0x00020000);
;     rsrc_t rA1 = rA0, rB1 = rB0;
;     if constexpr (Sched::TWO) { rA1 = __builtin_amdgcn_make_buffer_rsrc((void*)S.A1, 0, 0xffffffff, 0x00020000); rB1 = __builtin_amdgcn_make_buffer_rsrc((void*)S.Bt1, 0, 0xffffffff, 0x00020000); }
;     const unsigned ldsw = (unsigned)wid * 1024u;
;     const int aoff = lds_byte(wr * 64 + fr, fq * 8), boff = lds_byte(wc * 32 + fr, fq * 8);
;     ...
;     Unit cur, nxt; int ui = 0;
;     if (!S.next(0, cur)) return;
;     f32x4 acc[2][2][4][2];
;     ...
;     PG8_ZERO_ACC();
;     v8i_t At[4], B0[2], B1[2];
;     unsigned cA = S.a_off(cur, g), cB = S.b_off(cur, g); rsrc_t rAc = (Sched::TWO && cur.part) ? rA1 : rA0, rBc = (Sched::TWO && cur.part) ? rB1 : rB0;
;     S.a_ready(cur);
;     if constexpr (SP2) {
;         PG8_STAGE(PG8_SB(0, 0), rBc, cB, voffB); PG8_STAGE(PG8_SB(0, 1), rBc, cB + hstep, voffB); PG8_STAGE(PG8_SA(0, 0), rAc, cA, voffA); PG8_STAGE(PG8_SA(0, 1), rAc, cA + hstep, voffA);
;         if (wr == 1) PG8_BAR;
;         PG8_WAIT_V(2); PG8_BAR;
;         PG8_STAGE(PG8_SB(1, 0), rBc, cB + kstep, voffB); PG8_STAGE(PG8_SA(1, 0), rAc, cA + kstep, voffA); PG8_STAGE(PG8_SB(1, 1), rBc, cB + hstep + kstep, voffB);
;         PG8_WAIT_V(6); PG8_BAR;
.LBB0_802:
	s_add_u32 s8, s10, 0x1f800000
	s_addc_u32 s9, s11, 0
	s_add_u32 s82, s10, 0x39800000
	s_addc_u32 s18, s11, 0
	s_add_u32 s2, s10, s2
	s_addc_u32 s6, s11, 0
	s_add_u32 s83, s2, 0x3500000
	s_addc_u32 s2, s6, 0
	s_add_u32 s24, s10, 0x3d800000
	s_addc_u32 s25, s11, 0
	s_add_i32 s84, s47, 0x18000
	s_or_b32 s10, s3, 0x80
	s_mov_b32 s6, s38
	s_mov_b32 s7, s39
	s_mov_b32 m0, s84
	s_add_i32 s85, s47, 0x1a000
	s_waitcnt vmcnt(2)
	s_barrier
	buffer_load_dwordx4 v235, s[4:7], s10 offen lds
	s_mov_b32 m0, s85
	s_add_i32 s94, s47, 0x8000
	buffer_load_dwordx4 v237, s[4:7], s10 offen lds
	s_or_b32 s10, s16, 0x80
	s_mov_b32 m0, s94
	s_add_i32 s95, s47, 0xa000
	buffer_load_dwordx4 v192, s[36:39], s10 offen lds
	s_mov_b32 m0, s95
	s_add_i32 s96, s47, 0x1c000
	buffer_load_dwordx4 v236, s[36:39], s10 offen lds
	s_bitset1_b32 s17, 7
	s_mov_b32 m0, s96
	s_add_i32 s97, s47, 0x1e000
	buffer_load_dwordx4 v235, s[4:7], s17 offen lds
	s_mov_b32 m0, s97
	v_bfe_u32 v239, v4, 4, 2
	buffer_load_dwordx4 v237, s[4:7], s17 offen lds
	s_ashr_i32 s6, s13, 31
	s_lshr_b32 s6, s6, 26
	v_and_b32_e32 v238, 15, v4
	s_add_i32 s6, s13, s6
	v_lshlrev_b32_e32 v5, 4, v239
	v_lshlrev_b32_e32 v4, 2, v4
	s_ashr_i32 s60, s6, 6
	v_lshl_or_b32 v5, v238, 6, v5
	s_lshl_b32 s6, s15, 13
	v_and_b32_e32 v4, 32, v4
	v_bitop3_b32 v6, v5, s6, v4 bitop3:0xde
	s_lshl_b32 s6, s14, 5
	s_and_b32 s10, s6, 0x60
	s_and_b32 s42, s18, 0xffff
	s_and_b32 s43, s2, 0xffff
	s_lshl_b32 s2, s15, 6
	s_lshl_b32 s6, s10, 7
	s_cmp_gt_i32 s13, 63
	v_mov_b32_e32 v2, v0
	v_mov_b32_e32 v3, v0
	v_bitop3_b32 v4, v5, s6, v4 bitop3:0xde
	s_waitcnt vmcnt(6)
	s_cselect_b64 s[6:7], -1, 0
	s_add_i32 s41, s60, -2
	s_add_i32 s61, s47, 0xc000
	v_mov_b32_e32 v1, v0
	s_cmpk_lt_u32 s12, 0x100
	v_add_u32_e32 v240, 0, v4
	v_add_u32_e32 v241, 0, v6
	v_mov_b64_e32 v[6:7], v[2:3]
	v_mov_b64_e32 v[10:11], v[2:3]
	v_mov_b64_e32 v[14:15], v[2:3]
	v_mov_b64_e32 v[18:19], v[2:3]
	v_mov_b64_e32 v[22:23], v[2:3]
	v_mov_b64_e32 v[26:27], v[2:3]
	v_mov_b64_e32 v[30:31], v[2:3]
	v_mov_b64_e32 v[34:35], v[2:3]
	v_mov_b64_e32 v[38:39], v[2:3]
	v_mov_b64_e32 v[42:43], v[2:3]
	v_mov_b64_e32 v[46:47], v[2:3]
	v_mov_b64_e32 v[50:51], v[2:3]
	v_mov_b64_e32 v[54:55], v[2:3]
	v_mov_b64_e32 v[58:59], v[2:3]
	s_waitcnt vmcnt(37)
	v_mov_b64_e32 v[62:63], v[2:3]
	s_waitcnt vmcnt(36)
	v_mov_b64_e32 v[66:67], v[2:3]
	s_waitcnt vmcnt(35)
	v_mov_b64_e32 v[70:71], v[2:3]
	s_waitcnt vmcnt(34)
	v_mov_b64_e32 v[74:75], v[2:3]
	s_waitcnt vmcnt(33)
	v_mov_b64_e32 v[78:79], v[2:3]
	s_waitcnt vmcnt(32)
	v_mov_b64_e32 v[82:83], v[2:3]
	s_waitcnt vmcnt(31)
	v_mov_b64_e32 v[86:87], v[2:3]
	s_waitcnt vmcnt(30)
	v_mov_b64_e32 v[90:91], v[2:3]
	s_waitcnt vmcnt(29)
	v_mov_b64_e32 v[94:95], v[2:3]
	s_waitcnt vmcnt(28)
	v_mov_b64_e32 v[98:99], v[2:3]
	s_waitcnt vmcnt(27)
	v_mov_b64_e32 v[102:103], v[2:3]
	s_waitcnt vmcnt(26)
	v_mov_b64_e32 v[106:107], v[2:3]
	s_waitcnt vmcnt(25)
	v_mov_b64_e32 v[110:111], v[2:3]
	s_waitcnt vmcnt(24)
	v_mov_b64_e32 v[114:115], v[2:3]
	s_waitcnt vmcnt(23)
	v_mov_b64_e32 v[118:119], v[2:3]
	s_waitcnt vmcnt(22)
	v_mov_b64_e32 v[122:123], v[2:3]
	v_mov_b64_e32 v[126:127], v[2:3]
	s_cselect_b64 s[26:27], -1, 0
	s_add_i32 s62, s47, 0xe000
	s_mov_b32 s92, 0
	v_writelane_b32 v255, s10, 46
	s_lshl_b32 s28, s10, 1
	v_mov_b64_e32 v[4:5], v[0:1]
	v_mov_b64_e32 v[8:9], v[0:1]
	v_mov_b64_e32 v[12:13], v[0:1]
	v_mov_b64_e32 v[16:17], v[0:1]
	v_mov_b64_e32 v[20:21], v[0:1]
	v_mov_b64_e32 v[24:25], v[0:1]
	v_mov_b64_e32 v[28:29], v[0:1]
	v_mov_b64_e32 v[32:33], v[0:1]
	v_mov_b64_e32 v[36:37], v[0:1]
	v_mov_b64_e32 v[40:41], v[0:1]
	v_mov_b64_e32 v[44:45], v[0:1]
	v_mov_b64_e32 v[48:49], v[0:1]
	v_mov_b64_e32 v[52:53], v[0:1]
	v_mov_b64_e32 v[56:57], v[0:1]
	v_mov_b64_e32 v[60:61], v[0:1]
	v_mov_b64_e32 v[64:65], v[0:1]
	v_mov_b64_e32 v[68:69], v[0:1]
	v_mov_b64_e32 v[72:73], v[0:1]
	v_mov_b64_e32 v[76:77], v[0:1]
	v_mov_b64_e32 v[80:81], v[0:1]
	v_mov_b64_e32 v[84:85], v[0:1]
	v_mov_b64_e32 v[88:89], v[0:1]
	v_mov_b64_e32 v[92:93], v[0:1]
	v_mov_b64_e32 v[96:97], v[0:1]
	v_mov_b64_e32 v[100:101], v[0:1]
	v_mov_b64_e32 v[104:105], v[0:1]
	v_mov_b64_e32 v[108:109], v[0:1]
	v_mov_b64_e32 v[112:113], v[0:1]
	v_mov_b64_e32 v[116:117], v[0:1]
	v_mov_b64_e32 v[120:121], v[0:1]
	v_mov_b64_e32 v[124:125], v[0:1]
	s_mov_b64 s[58:59], s[4:5]
	s_mov_b64 s[30:31], s[38:39]
	s_mov_b64 s[12:13], s[36:37]
	s_mov_b64 s[14:15], s[38:39]
	s_mov_b32 s63, 0
	s_barrier
	s_mov_b32 s100, 0
	s_branch .LBB0_805

;     __device__ __forceinline__ unsigned a_off(const Unit& u, const Gemm& g) const { return (unsigned)u.pm * (unsigned)(BM * 2) * (unsigned)g.K; }
;     __device__ __forceinline__ unsigned b_off(const Unit& u, const Gemm& g) const { return (unsigned)u.pn * (unsigned)(BM * 2) * (unsigned)g.K; }
;     __device__ __forceinline__ bool next(int i, Unit& u) const { return so.next(i, u); }
;     __device__ __forceinline__ unsigned a_off(const Unit& u, const Gemm& g) const { return (unsigned)u.pm * (unsigned)(BM * 2) * (unsigned)g.K; }
;     __device__ __forceinline__ bool next(int i, Unit& u) const { const bool ok = so.next(i >> 1, u); u.part = i & 1; return ok; }
;     __device__ __forceinline__ unsigned a_off(const Unit& u, const Gemm& g) const { return (unsigned)u.pm * (unsigned)(BM * 2) * (unsigned)g.K; }
;     __device__ __forceinline__ unsigned b_off(const Unit& u, const Gemm& g) const { return (unsigned)u.pn * (unsigned)(BM * 2) * (unsigned)g.K; }
; template <class Epi, class Sched, bool ALIGN_EPI = false, bool SP2 = false, bool FP8 = false>
; __device__ __forceinline__ void gemm_phase(LAS unsigned char* lds, const Gemm g, const Sched& S, const Epi& E, int wbase) {
;     ...
;         const bool has_next = S.next(ui + 1, nxt);
;         const unsigned nA = has_next ? S.a_off(nxt, g) : cA, nB = has_next ? S.b_off(nxt, g) : cB;
;         const rsrc_t rAn = (Sched::TWO && has_next) ? (nxt.part ? rA1 : rA0) : rAc, rBn = (Sched::TWO && has_next) ? (nxt.part ? rB1 : rB0) : rBc;
;         float pre_[8] = {0.f, 0.f, 0.f, 0.f, 0.f, 0.f, 0.f, 0.f};
;         if constexpr (Epi::HAS_PRE) E.pre_load(pre_, cur, wr);
;         for (int t = 0; t < nt; t += 2) {
;             const bool last = (t == nt - 2);
;             const unsigned a1 = cA + (unsigned)(t + 1) * kstep;
;             const unsigned a2 = last ? nA : cA + (unsigned)(t + 2) * kstep, b2 = last ? nB : cB + (unsigned)(t + 2) * kstep; const rsrc_t rA2 = (Sched::TWO && last) ? rAn : rAc, rB2 = (Sched::TWO && last) ? rBn : rBc;
;             const unsigned a3 = a2 + kstep, b3 = b2 + kstep;
;             if (last && has_next) S.a_ready(nxt);
;             if constexpr (SP2) {
;             PG8_LDB(B0, 0, 0); PG8_LDB(B1, 0, 1); PG8_SCHED; PG8_LDA(At, 0, 0); PG8_STAGE(PG8_SA(1, 1), rAc, a1 + hstep, voffA);
;             PG8_WAIT_V(8); PG8_WAIT_L(0); PG8_BAR; PG8_MMA(0, 0, At, B0); PG8_MMA(0, 1, At, B1); PG8_BAR; PG8_SCHED;
.LBB0_811:
	s_and_b32 s66, s63, 1
	s_lshl_b32 s88, s80, 18
	s_lshl_b32 s89, s81, 18
	s_cmp_eq_u32 s66, 0
	s_cselect_b32 s53, 0x20000, 0x20000
	s_cselect_b32 s52, -1, -1
	s_cselect_b32 s35, s37, s42
	s_cselect_b32 s34, s36, s82
	s_cselect_b32 s11, s5, s43
	s_cselect_b32 s10, s4, s83
	s_andn2_b64 vcc, exec, s[6:7]
	s_cbranch_vccnz .LBB0_815
	s_and_b64 s[18:19], s[44:45], exec
	v_mov_b32_e32 v222, 1
	v_mov_b32_e32 v193, 0x358637bd
	s_cselect_b32 s67, s88, s16
	s_cselect_b32 vcc_lo, s89, s3
	s_add_i32 vcc_hi, s16, 0x80
	s_addk_i32 s3, 0x100
	s_mov_b32 s78, 0
	s_cmp_eq_u32 s100, 1
	s_cbranch_scc0 .LBB0_813
	s_add_i32 s20, vcc_hi, 0x80
	v_add_u32_e32 v140, 0x10000, v240
	v_add_u32_e32 v156, 0x14000, v240
	s_cmp_eq_u32 s41, s78
	ds_read_b128 v[128:131], v140
	ds_read_b128 v[132:135], v140 offset:1024
	ds_read_b128 v[136:139], v140 offset:2048
	ds_read_b128 v[140:143], v140 offset:3072
	ds_read_b128 v[144:147], v156
	ds_read_b128 v[148:151], v156 offset:1024
	ds_read_b128 v[152:155], v156 offset:2048
	ds_read_b128 v[156:159], v156 offset:3072
	s_cselect_b64 s[16:17], -1, 0
	s_and_b64 s[18:19], s[16:17], exec
	s_cselect_b32 s68, s67, s20
	s_cselect_b32 s54, vcc_lo, s3
	s_and_b64 s[20:21], s[44:45], s[16:17]
	s_and_b64 s[16:17], s[20:21], exec
	s_cselect_b32 s18, s52, s14
	s_cselect_b32 s19, s53, s15
	s_cselect_b32 s17, s35, s13
	s_cselect_b32 s16, s34, s12
	s_or_b32 s55, s68, 0x80
	s_and_b64 s[20:21], s[20:21], exec
	s_cselect_b32 s23, s53, s31
	s_cselect_b32 s22, s52, s30
	s_cselect_b32 s21, s11, s59
	s_cselect_b32 s20, s10, s58
	s_add_i32 s69, s46, vcc_hi
	s_mov_b32 m0, s61
	ds_read_b128 v[160:163], v241
	ds_read_b128 v[164:167], v241 offset:1024
	ds_read_b128 v[168:171], v241 offset:2048
	ds_read_b128 v[172:175], v241 offset:3072
	ds_read_b128 v[176:179], v241 offset:4096
	ds_read_b128 v[180:183], v241 offset:5120
	ds_read_b128 v[184:187], v241 offset:6144
	ds_read_b128 v[188:191], v241 offset:7168
	buffer_load_dwordx4 v192, s[12:15], s69 offen lds
	s_mov_b32 m0, s62
	s_nop 0
	buffer_load_dwordx4 v236, s[12:15], s69 offen lds
	s_waitcnt vmcnt(24)
	s_waitcnt lgkmcnt(0)
	s_barrier
	s_setprio 1
	s_waitcnt lgkmcnt(6)
	v_mfma_scale_f32_16x16x128_f8f6f4 v[124:127], v[128:135], v[160:167], v[124:127], v224, v224 op_sel_hi:[0,0,0]
	v_mfma_scale_f32_16x16x128_f8f6f4 v[120:123], v[136:143], v[160:167], v[120:123], v224, v224 op_sel_hi:[0,0,0]
	s_waitcnt lgkmcnt(4)
	v_mfma_scale_f32_16x16x128_f8f6f4 v[116:119], v[128:135], v[168:175], v[116:119], v224, v224 op_sel_hi:[0,0,0]
	v_mfma_scale_f32_16x16x128_f8f6f4 v[112:115], v[136:143], v[168:175], v[112:115], v224, v224 op_sel_hi:[0,0,0]
	s_waitcnt lgkmcnt(2)
	v_mfma_scale_f32_16x16x128_f8f6f4 v[108:111], v[128:135], v[176:183], v[108:111], v224, v224 op_sel_hi:[0,0,0]
	v_mfma_scale_f32_16x16x128_f8f6f4 v[104:107], v[136:143], v[176:183], v[104:107], v224, v224 op_sel_hi:[0,0,0]
	s_waitcnt lgkmcnt(0)
	v_mfma_scale_f32_16x16x128_f8f6f4 v[100:103], v[128:135], v[184:191], v[100:103], v224, v224 op_sel_hi:[0,0,0]
	v_mfma_scale_f32_16x16x128_f8f6f4 v[96:99], v[136:143], v[184:191], v[96:99], v224, v224 op_sel_hi:[0,0,0]
	s_setprio 0
	s_setprio 1
	v_mfma_scale_f32_16x16x128_f8f6f4 v[194:197], v[144:151], v[160:167], v[92:95], v224, v224 op_sel_hi:[0,0,0]
	v_mfma_scale_f32_16x16x128_f8f6f4 v[160:163], v[152:159], v[160:167], v[88:91], v224, v224 op_sel_hi:[0,0,0]
	v_mfma_scale_f32_16x16x128_f8f6f4 v[164:167], v[144:151], v[168:175], v[84:87], v224, v224 op_sel_hi:[0,0,0]
	v_mfma_scale_f32_16x16x128_f8f6f4 v[168:171], v[152:159], v[168:175], v[80:83], v224, v224 op_sel_hi:[0,0,0]
	v_mfma_scale_f32_16x16x128_f8f6f4 v[172:175], v[144:151], v[176:183], v[76:79], v224, v224 op_sel_hi:[0,0,0]
	v_mfma_scale_f32_16x16x128_f8f6f4 v[176:179], v[152:159], v[176:183], v[72:75], v224, v224 op_sel_hi:[0,0,0]
	v_mfma_scale_f32_16x16x128_f8f6f4 v[180:183], v[144:151], v[184:191], v[68:71], v224, v224 op_sel_hi:[0,0,0]
	v_mfma_scale_f32_16x16x128_f8f6f4 v[184:187], v[152:159], v[184:191], v[64:67], v224, v224 op_sel_hi:[0,0,0]
	s_setprio 0
	s_barrier
	s_mov_b32 m0, s48
	s_nop 3
	ds_read_b128 v[64:67], v241 offset:16384
	ds_read_b128 v[68:71], v241 offset:17408
	ds_read_b128 v[72:75], v241 offset:18432
	ds_read_b128 v[76:79], v241 offset:19456
	ds_read_b128 v[80:83], v241 offset:20480
	ds_read_b128 v[84:87], v241 offset:21504
	ds_read_b128 v[88:91], v241 offset:22528
	ds_read_b128 v[92:95], v241 offset:23552
	buffer_load_dwordx4 v235, s[20:23], s54 offen lds
	s_mov_b32 m0, s56
	s_add_i32 s69, s54, s46
	buffer_load_dwordx4 v237, s[20:23], s54 offen lds
	s_mov_b32 m0, s57
	s_nop 0
	buffer_load_dwordx4 v235, s[20:23], s69 offen lds
	s_mov_b32 m0, s65
	s_nop 0
	buffer_load_dwordx4 v237, s[20:23], s69 offen lds
	s_mov_b32 m0, s47
	s_nop 0
	buffer_load_dwordx4 v192, s[16:19], s68 offen lds
	s_mov_b32 m0, s76
	s_nop 0
	buffer_load_dwordx4 v236, s[16:19], s68 offen lds
	s_waitcnt vmcnt(24)
	s_waitcnt lgkmcnt(0)
	s_barrier
; #define PG8_STAGE(bufoff, rs_, soff_, voff) do { _Pragma("unroll") for (int _i = 0; _i < 2; ++_i) \
;         __builtin_amdgcn_raw_ptr_buffer_load_lds(rs_, (LAS void*)(lds + (bufoff) + ldsw + _i * 8192), 16, (int)(voff)[_i], (int)(soff_), 0, 0); } while (0)
; #define PG8_LDA(dst, b, h) do { _Pragma("unroll") for (int m = 0; m < 4; ++m) dst[m] = PG8_LD2(lds + PG8_SA(b, h) + aoff + m * 2048); } while (0)
; #define PG8_LDB(dst, b, h) do { _Pragma("unroll") for (int n = 0; n < 2; ++n) dst[n] = PG8_LD2(lds + PG8_SB(b, h) + boff + n * 2048); } while (0)
; #define PG8_WAIT_V(n) asm volatile("s_waitcnt vmcnt(" #n ")" ::: "memory")
; #define PG8_WAIT_L(n) asm volatile("s_waitcnt lgkmcnt(" #n ")" ::: "memory")
; #define PG8_BAR __builtin_amdgcn_s_barrier()
; #define PG8_SCHED __builtin_amdgcn_sched_barrier(0)
; template <class Epi, class Sched, bool ALIGN_EPI = false, bool SP2 = false, bool FP8 = false>
; __device__ __forceinline__ void gemm_phase(LAS unsigned char* lds, const Gemm g, const Sched& S, const Epi& E, int wbase) {
;     ...
;             PG8_WAIT_V(8); PG8_WAIT_L(0); PG8_BAR; PG8_MMA(0, 0, At, B0); PG8_MMA(0, 1, At, B1); PG8_BAR; PG8_SCHED;
;             PG8_LDA(At, 0, 1); PG8_STAGE(PG8_SB(0, 0), rB2, b2, voffB); PG8_STAGE(PG8_SB(0, 1), rB2, b2 + hstep, voffB); PG8_STAGE(PG8_SA(0, 0), rA2, a2, voffA);
;             PG8_WAIT_V(8); PG8_WAIT_L(0); PG8_BAR; PG8_MMA(1, 0, At, B0); PG8_MMA(1, 1, At, B1); PG8_BAR; PG8_SCHED;
;             PG8_LDB(B0, 1, 0); PG8_LDB(B1, 1, 1); PG8_SCHED; PG8_LDA(At, 1, 0); PG8_STAGE(PG8_SA(0, 1), rA2, a2 + hstep, voffA);
;             PG8_WAIT_V(8); PG8_WAIT_L(0); PG8_BAR; PG8_MMA(0, 0, At, B0); PG8_MMA(0, 1, At, B1); PG8_BAR; PG8_SCHED;
	s_setprio 1
	s_waitcnt lgkmcnt(6)
	v_mfma_scale_f32_16x16x128_f8f6f4 v[60:63], v[128:135], v[64:71], v[60:63], v224, v224 op_sel_hi:[0,0,0]
	v_mfma_scale_f32_16x16x128_f8f6f4 v[56:59], v[136:143], v[64:71], v[56:59], v224, v224 op_sel_hi:[0,0,0]
	s_waitcnt lgkmcnt(4)
	v_mfma_scale_f32_16x16x128_f8f6f4 v[52:55], v[128:135], v[72:79], v[52:55], v224, v224 op_sel_hi:[0,0,0]
	v_mfma_scale_f32_16x16x128_f8f6f4 v[48:51], v[136:143], v[72:79], v[48:51], v224, v224 op_sel_hi:[0,0,0]
	s_waitcnt lgkmcnt(2)
	v_mfma_scale_f32_16x16x128_f8f6f4 v[188:191], v[128:135], v[80:87], v[44:47], v224, v224 op_sel_hi:[0,0,0]
	v_mfma_scale_f32_16x16x128_f8f6f4 v[198:201], v[136:143], v[80:87], v[40:43], v224, v224 op_sel_hi:[0,0,0]
	s_waitcnt lgkmcnt(0)
	v_mfma_scale_f32_16x16x128_f8f6f4 v[202:205], v[128:135], v[88:95], v[36:39], v224, v224 op_sel_hi:[0,0,0]
	v_mfma_scale_f32_16x16x128_f8f6f4 v[206:209], v[136:143], v[88:95], v[32:35], v224, v224 op_sel_hi:[0,0,0]
	s_setprio 0
	s_setprio 1
	v_mfma_scale_f32_16x16x128_f8f6f4 v[210:213], v[144:151], v[64:71], v[28:31], v224, v224 op_sel_hi:[0,0,0]
	v_mfma_scale_f32_16x16x128_f8f6f4 v[214:217], v[152:159], v[64:71], v[24:27], v224, v224 op_sel_hi:[0,0,0]
	v_mfma_scale_f32_16x16x128_f8f6f4 v[218:221], v[144:151], v[72:79], v[20:23], v224, v224 op_sel_hi:[0,0,0]
	v_mfma_scale_f32_16x16x128_f8f6f4 v[226:229], v[152:159], v[72:79], v[16:19], v224, v224 op_sel_hi:[0,0,0]
	v_mfma_scale_f32_16x16x128_f8f6f4 v[242:245], v[144:151], v[80:87], v[12:15], v224, v224 op_sel_hi:[0,0,0]
	v_mfma_scale_f32_16x16x128_f8f6f4 v[246:249], v[152:159], v[80:87], v[8:11], v224, v224 op_sel_hi:[0,0,0]
	v_mfma_scale_f32_16x16x128_f8f6f4 v[250:253], v[144:151], v[88:95], v[4:7], v224, v224 op_sel_hi:[0,0,0]
	v_mfma_scale_f32_16x16x128_f8f6f4 v[230:233], v[152:159], v[88:95], v[0:3], v224, v224 op_sel_hi:[0,0,0]
	s_setprio 0
	s_barrier
	s_nop 1
	v_add_u32_e32 v12, 0x18000, v240
	v_add_u32_e32 v16, 0x1c000, v240
	s_nop 0
	ds_read_b128 v[0:3], v12
	ds_read_b128 v[4:7], v12 offset:1024
	ds_read_b128 v[8:11], v12 offset:2048
	ds_read_b128 v[12:15], v12 offset:3072
	ds_read_b128 v[128:131], v16
	ds_read_b128 v[132:135], v16 offset:1024
	ds_read_b128 v[136:139], v16 offset:2048
	ds_read_b128 v[140:143], v16 offset:3072
	s_add_i32 s68, s68, s46
	s_mov_b32 m0, s77
	ds_read_b128 v[16:19], v241 offset:32768
	ds_read_b128 v[20:23], v241 offset:33792
	ds_read_b128 v[24:27], v241 offset:34816
	ds_read_b128 v[28:31], v241 offset:35840
	ds_read_b128 v[32:35], v241 offset:36864
	ds_read_b128 v[36:39], v241 offset:37888
	ds_read_b128 v[40:43], v241 offset:38912
	ds_read_b128 v[44:47], v241 offset:39936
	buffer_load_dwordx4 v192, s[16:19], s68 offen lds
	s_mov_b32 m0, s79
	s_nop 0
	buffer_load_dwordx4 v236, s[16:19], s68 offen lds
	s_waitcnt vmcnt(8)
	s_waitcnt lgkmcnt(0)
	s_barrier
	s_setprio 1
	s_waitcnt lgkmcnt(6)
	v_mfma_scale_f32_16x16x128_f8f6f4 v[124:127], v[0:7], v[16:23], v[124:127], v224, v224 op_sel_hi:[0,0,0]
	v_mfma_scale_f32_16x16x128_f8f6f4 v[120:123], v[8:15], v[16:23], v[120:123], v224, v224 op_sel_hi:[0,0,0]
	s_waitcnt lgkmcnt(4)
	v_mfma_scale_f32_16x16x128_f8f6f4 v[116:119], v[0:7], v[24:31], v[116:119], v224, v224 op_sel_hi:[0,0,0]
	v_mfma_scale_f32_16x16x128_f8f6f4 v[112:115], v[8:15], v[24:31], v[112:115], v224, v224 op_sel_hi:[0,0,0]
	s_waitcnt lgkmcnt(2)
	v_mfma_scale_f32_16x16x128_f8f6f4 v[108:111], v[0:7], v[32:39], v[108:111], v224, v224 op_sel_hi:[0,0,0]
	v_mfma_scale_f32_16x16x128_f8f6f4 v[104:107], v[8:15], v[32:39], v[104:107], v224, v224 op_sel_hi:[0,0,0]
	s_waitcnt lgkmcnt(0)
	v_mfma_scale_f32_16x16x128_f8f6f4 v[100:103], v[0:7], v[40:47], v[100:103], v224, v224 op_sel_hi:[0,0,0]
	v_mfma_scale_f32_16x16x128_f8f6f4 v[96:99], v[8:15], v[40:47], v[96:99], v224, v224 op_sel_hi:[0,0,0]
	s_setprio 0
	s_setprio 1
	v_mfma_scale_f32_16x16x128_f8f6f4 v[92:95], v[128:135], v[16:23], v[194:197], v224, v224 op_sel_hi:[0,0,0]
	v_mfma_scale_f32_16x16x128_f8f6f4 v[88:91], v[136:143], v[16:23], v[160:163], v224, v224 op_sel_hi:[0,0,0]
	v_mfma_scale_f32_16x16x128_f8f6f4 v[84:87], v[128:135], v[24:31], v[164:167], v224, v224 op_sel_hi:[0,0,0]
	v_mfma_scale_f32_16x16x128_f8f6f4 v[80:83], v[136:143], v[24:31], v[168:171], v224, v224 op_sel_hi:[0,0,0]
	v_mfma_scale_f32_16x16x128_f8f6f4 v[76:79], v[128:135], v[32:39], v[172:175], v224, v224 op_sel_hi:[0,0,0]
	v_mfma_scale_f32_16x16x128_f8f6f4 v[72:75], v[136:143], v[32:39], v[176:179], v224, v224 op_sel_hi:[0,0,0]
	v_mfma_scale_f32_16x16x128_f8f6f4 v[68:71], v[128:135], v[40:47], v[180:183], v224, v224 op_sel_hi:[0,0,0]
	v_mfma_scale_f32_16x16x128_f8f6f4 v[64:67], v[136:143], v[40:47], v[184:187], v224, v224 op_sel_hi:[0,0,0]
	s_setprio 0
	s_barrier
; #define PG8_STAGE(bufoff, rs_, soff_, voff) do { _Pragma("unroll") for (int _i = 0; _i < 2; ++_i) \
;         __builtin_amdgcn_raw_ptr_buffer_load_lds(rs_, (LAS void*)(lds + (bufoff) + ldsw + _i * 8192), 16, (int)(voff)[_i], (int)(soff_), 0, 0); } while (0)
; #define PG8_LDA(dst, b, h) do { _Pragma("unroll") for (int m = 0; m < 4; ++m) dst[m] = PG8_LD2(lds + PG8_SA(b, h) + aoff + m * 2048); } while (0)
; #define PG8_WAIT_V(n) asm volatile("s_waitcnt vmcnt(" #n ")" ::: "memory")
; #define PG8_WAIT_L(n) asm volatile("s_waitcnt lgkmcnt(" #n ")" ::: "memory")
; #define PG8_BAR __builtin_amdgcn_s_barrier()
; #define PG8_SCHED __builtin_amdgcn_sched_barrier(0)
; template <class Epi, class Sched, bool ALIGN_EPI = false, bool SP2 = false, bool FP8 = false>
; __device__ __forceinline__ void gemm_phase(LAS unsigned char* lds, const Gemm g, const Sched& S, const Epi& E, int wbase) {
;     ...
;         for (int t = 0; t < nt; t += 2) {
;     ...
;             PG8_LDA(At, 1, 1); PG8_STAGE(PG8_SB(1, 0), rB2, b3, voffB); PG8_STAGE(PG8_SB(1, 1), rB2, b3 + hstep, voffB); PG8_STAGE(PG8_SA(1, 0), rA2, a3, voffA);
;             PG8_WAIT_V(8); PG8_WAIT_L(0); PG8_BAR; PG8_MMA(1, 0, At, B0); PG8_MMA(1, 1, At, B1); PG8_BAR; PG8_SCHED;
	s_mov_b32 m0, s84
	s_bitset1_b32 s54, 7
	ds_read_b128 v[16:19], v241 offset:49152
	ds_read_b128 v[20:23], v241 offset:50176
	ds_read_b128 v[144:147], v241 offset:51200
	ds_read_b128 v[148:151], v241 offset:52224
	ds_read_b128 v[152:155], v241 offset:53248
	ds_read_b128 v[156:159], v241 offset:54272
	ds_read_b128 v[160:163], v241 offset:55296
	ds_read_b128 v[164:167], v241 offset:56320
	buffer_load_dwordx4 v235, s[20:23], s54 offen lds
	s_mov_b32 m0, s85
	s_nop 0
	buffer_load_dwordx4 v237, s[20:23], s54 offen lds
	s_add_i32 s54, s54, s46
	s_mov_b32 m0, s96
	s_nop 0
	buffer_load_dwordx4 v235, s[20:23], s54 offen lds
	s_mov_b32 m0, s97
	s_nop 0
	buffer_load_dwordx4 v237, s[20:23], s54 offen lds
	s_mov_b32 m0, s94
	s_nop 0
	buffer_load_dwordx4 v192, s[16:19], s55 offen lds
	s_mov_b32 m0, s95
	s_nop 0
	buffer_load_dwordx4 v236, s[16:19], s55 offen lds
	s_waitcnt vmcnt(8)
	s_waitcnt lgkmcnt(0)
	s_barrier
	s_setprio 1
	s_waitcnt lgkmcnt(6)
	v_mfma_scale_f32_16x16x128_f8f6f4 v[60:63], v[0:7], v[16:23], v[60:63], v224, v224 op_sel_hi:[0,0,0]
	v_mfma_scale_f32_16x16x128_f8f6f4 v[56:59], v[8:15], v[16:23], v[56:59], v224, v224 op_sel_hi:[0,0,0]
	s_waitcnt lgkmcnt(4)
	v_mfma_scale_f32_16x16x128_f8f6f4 v[52:55], v[0:7], v[144:151], v[52:55], v224, v224 op_sel_hi:[0,0,0]
	v_mfma_scale_f32_16x16x128_f8f6f4 v[48:51], v[8:15], v[144:151], v[48:51], v224, v224 op_sel_hi:[0,0,0]
	s_waitcnt lgkmcnt(2)
	v_mfma_scale_f32_16x16x128_f8f6f4 v[44:47], v[0:7], v[152:159], v[188:191], v224, v224 op_sel_hi:[0,0,0]
	v_mfma_scale_f32_16x16x128_f8f6f4 v[40:43], v[8:15], v[152:159], v[198:201], v224, v224 op_sel_hi:[0,0,0]
	s_waitcnt lgkmcnt(0)
	v_mfma_scale_f32_16x16x128_f8f6f4 v[36:39], v[0:7], v[160:167], v[202:205], v224, v224 op_sel_hi:[0,0,0]
	v_mfma_scale_f32_16x16x128_f8f6f4 v[32:35], v[8:15], v[160:167], v[206:209], v224, v224 op_sel_hi:[0,0,0]
	s_setprio 0
	s_setprio 1
	v_mfma_scale_f32_16x16x128_f8f6f4 v[28:31], v[128:135], v[16:23], v[210:213], v224, v224 op_sel_hi:[0,0,0]
	v_mfma_scale_f32_16x16x128_f8f6f4 v[24:27], v[136:143], v[16:23], v[214:217], v224, v224 op_sel_hi:[0,0,0]
	v_mfma_scale_f32_16x16x128_f8f6f4 v[20:23], v[128:135], v[144:151], v[218:221], v224, v224 op_sel_hi:[0,0,0]
	v_mfma_scale_f32_16x16x128_f8f6f4 v[16:19], v[136:143], v[144:151], v[226:229], v224, v224 op_sel_hi:[0,0,0]
	v_mfma_scale_f32_16x16x128_f8f6f4 v[12:15], v[128:135], v[152:159], v[242:245], v224, v224 op_sel_hi:[0,0,0]
	v_mfma_scale_f32_16x16x128_f8f6f4 v[8:11], v[136:143], v[152:159], v[246:249], v224, v224 op_sel_hi:[0,0,0]
	v_mfma_scale_f32_16x16x128_f8f6f4 v[4:7], v[128:135], v[160:167], v[250:253], v224, v224 op_sel_hi:[0,0,0]
	v_mfma_scale_f32_16x16x128_f8f6f4 v[0:3], v[136:143], v[160:167], v[230:233], v224, v224 op_sel_hi:[0,0,0]
	s_setprio 0
	s_barrier
	s_add_i32 s78, s78, 2
	s_addk_i32 vcc_hi, 0x100
	s_addk_i32 s3, 0x100
	s_cmp_ge_i32 s78, s60
	s_cbranch_scc0 .LBB0_813
	s_branch .Lpeel_after_813

; #define PG8_BAR __builtin_amdgcn_s_barrier()
; template <class Epi, class Sched, bool ALIGN_EPI = false, bool SP2 = false, bool FP8 = false>
; __device__ __forceinline__ void gemm_phase(LAS unsigned char* lds, const Gemm g, const Sched& S, const Epi& E, int wbase) {
;     ...
;         }
;         if constexpr (ALIGN_EPI) { if (wr == 0) PG8_BAR; }
;         { int fr_ = fr, fq_ = fq; asm volatile("" : "+v"(fr_), "+v"(fq_));
;           if constexpr (Epi::HAS_PRE) E(acc, cur, wr, wc, fr_, fq_, pre_); else E(acc, cur, wr, wc, fr_, fq_); } S.done(cur);
.Lpeel_after_813:
	s_mov_b32 s100, 1
	v_readlane_b32 s68, v255, 22
	v_readlane_b32 s54, v255, 25
	v_readlane_b32 s69, v255, 23
	v_readlane_b32 s55, v255, 26
	v_mov_b32_e32 v230, v193
	v_mov_b32_e32 v231, v222

;     __device__ __forceinline__ unsigned a_off(const Unit& u, const Gemm& g) const { return (unsigned)u.pm * (unsigned)(BM * 2) * (unsigned)g.K; }
;     __device__ __forceinline__ unsigned b_off(const Unit& u, const Gemm& g) const { return (unsigned)u.pn * (unsigned)(BM * 2) * (unsigned)g.K; }
;     __device__ __forceinline__ bool next(int i, Unit& u) const { return so.next(i, u); }
; template <class Epi, class Sched, bool ALIGN_EPI = false, bool SP2 = false, bool FP8 = false>
; __device__ __forceinline__ void gemm_phase(LAS unsigned char* lds, const Gemm g, const Sched& S, const Epi& E, int wbase) {
;     ...
;     for (int i = 0; i < 2; ++i) { int R, C; stage_rc(tid * 16 + i * 8192, R, C); const int Rb = Epi::PERM ? ((R & ~31) + perm32(R & 31)) : R;
;         voffA[i] = (unsigned)(R * K + C) * 2u; voffB[i] = (unsigned)(Rb * K + C) * 2u; }
;     const unsigned kstep = (unsigned)(BK * 2);
;     const unsigned hstep = (unsigned)HALF * (unsigned)K * 2u;
;     typedef __amdgpu_buffer_rsrc_t rsrc_t;
;     const rsrc_t rA0 = __builtin_amdgcn_make_buffer_rsrc((void*)g.A, 0, 0xffffffff, 0x00020000), rB0 = __builtin_amdgcn_make_buffer_rsrc((void*)g.Bt, 0, 0xffffffff, 0x00020000);
;     rsrc_t rA1 = rA0, rB1 = rB0;
;     if constexpr (Sched::TWO) { rA1 = __builtin_amdgcn_make_buffer_rsrc((void*)S.A1, 0, 0xffffffff, 0x00020000); rB1 = __builtin_amdgcn_make_buffer_rsrc((void*)S.Bt1, 0, 0xffffffff, 0x00020000); }
;     const unsigned ldsw = (unsigned)wid * 1024u;
;     const int aoff = lds_byte(wr * 64 + fr, fq * 8), boff = lds_byte(wc * 32 + fr, fq * 8);
;     ...
;     Unit cur, nxt; int ui = 0;
;     if (!S.next(0, cur)) return;
;     f32x4 acc[2][2][4][2];
;     ...
;     PG8_ZERO_ACC();
;     v8i_t At[4], B0[2], B1[2];
;     unsigned cA = S.a_off(cur, g), cB = S.b_off(cur, g); rsrc_t rAc = (Sched::TWO && cur.part) ? rA1 : rA0, rBc = (Sched::TWO && cur.part) ? rB1 : rB0;
;     S.a_ready(cur);
;     if constexpr (SP2) {
;         PG8_STAGE(PG8_SB(0, 0), rBc, cB, voffB); PG8_STAGE(PG8_SB(0, 1), rBc, cB + hstep, voffB); PG8_STAGE(PG8_SA(0, 0), rAc, cA, voffA); PG8_STAGE(PG8_SA(0, 1), rAc, cA + hstep, voffA);
;         if (wr == 1) PG8_BAR;
;         PG8_WAIT_V(2); PG8_BAR;
;         PG8_STAGE(PG8_SB(1, 0), rBc, cB + kstep, voffB); PG8_STAGE(PG8_SA(1, 0), rAc, cA + kstep, voffA); PG8_STAGE(PG8_SB(1, 1), rBc, cB + hstep + kstep, voffB);
;         PG8_WAIT_V(6); PG8_BAR;
.LBB0_836:
	s_add_u32 s8, s10, 0x1f800000
	s_addc_u32 s9, s11, 0
	s_add_u32 s61, s10, 0x39800000
	s_addc_u32 s17, s11, 0
	s_add_u32 s6, s10, s14
	s_addc_u32 s7, s11, 0
	s_add_u32 s62, s6, 0x3500000
	s_addc_u32 s14, s7, 0
	s_add_u32 s24, s10, 0x3d800000
	s_addc_u32 s25, s11, 0
	s_add_i32 s63, s42, 0x18000
	s_or_b32 s10, s18, 0x80
	s_mov_b32 s6, s38
	s_mov_b32 s7, s39
	s_mov_b32 m0, s63
	s_add_i32 s65, s42, 0x1a000
	s_waitcnt vmcnt(2)
	s_barrier
	buffer_load_dwordx4 v222, s[4:7], s10 offen lds
	s_mov_b32 m0, s65
	s_add_i32 s76, s42, 0x8000
	buffer_load_dwordx4 v235, s[4:7], s10 offen lds
	s_or_b32 s10, s19, 0x80
	s_mov_b32 m0, s76
	s_add_i32 s77, s42, 0xa000
	buffer_load_dwordx4 v192, s[36:39], s10 offen lds
	s_mov_b32 m0, s77
	s_add_i32 s79, s42, 0x1c000
	buffer_load_dwordx4 v223, s[36:39], s10 offen lds
	s_bitset1_b32 s16, 7
	s_mov_b32 m0, s79
	s_add_i32 s80, s42, 0x1e000
	buffer_load_dwordx4 v222, s[4:7], s16 offen lds
	s_mov_b32 m0, s80
	s_lshl_b32 s2, s2, 5
	buffer_load_dwordx4 v235, s[4:7], s16 offen lds
	s_ashr_i32 s6, s13, 31
	s_lshr_b32 s6, s6, 26
	v_bfe_u32 v237, v4, 4, 2
	s_add_i32 s6, s13, s6
	s_and_b32 s10, s2, 0x60
	v_and_b32_e32 v236, 15, v4
	s_ashr_i32 s81, s6, 6
	s_and_b32 s82, s17, 0xffff
	s_and_b32 s83, s14, 0xffff
	s_lshl_b32 s84, s15, 6
	v_lshlrev_b32_e32 v5, 4, v237
	s_lshl_b32 s6, s15, 13
	v_lshlrev_b32_e32 v4, 2, v4
	s_lshl_b32 s2, s10, 7
	v_lshl_or_b32 v5, v236, 6, v5
	v_and_b32_e32 v4, 32, v4
	s_cmp_gt_i32 s13, 63
	v_mov_b32_e32 v2, v0
	v_mov_b32_e32 v3, v0
	v_bitop3_b32 v6, v5, s6, v4 bitop3:0xde
	v_bitop3_b32 v4, v5, s2, v4 bitop3:0xde
	s_waitcnt vmcnt(6)
	s_cselect_b64 s[6:7], -1, 0
	s_add_i32 s88, s81, -2
	s_add_i32 s89, s42, 0xc000
	v_mov_b32_e32 v1, v0
	s_cmpk_lt_u32 s12, 0x100
	v_add_u32_e32 v238, 0, v4
	v_add_u32_e32 v239, 0, v6
	v_mov_b64_e32 v[6:7], v[2:3]
	v_mov_b64_e32 v[10:11], v[2:3]
	v_mov_b64_e32 v[14:15], v[2:3]
	v_mov_b64_e32 v[18:19], v[2:3]
	v_mov_b64_e32 v[22:23], v[2:3]
	v_mov_b64_e32 v[26:27], v[2:3]
	v_mov_b64_e32 v[30:31], v[2:3]
	v_mov_b64_e32 v[34:35], v[2:3]
	v_mov_b64_e32 v[38:39], v[2:3]
	v_mov_b64_e32 v[42:43], v[2:3]
	v_mov_b64_e32 v[46:47], v[2:3]
	v_mov_b64_e32 v[50:51], v[2:3]
	v_mov_b64_e32 v[54:55], v[2:3]
	v_mov_b64_e32 v[58:59], v[2:3]
	s_waitcnt vmcnt(37)
	v_mov_b64_e32 v[62:63], v[2:3]
	s_waitcnt vmcnt(36)
	v_mov_b64_e32 v[66:67], v[2:3]
	s_waitcnt vmcnt(35)
	v_mov_b64_e32 v[70:71], v[2:3]
	s_waitcnt vmcnt(34)
	v_mov_b64_e32 v[74:75], v[2:3]
	s_waitcnt vmcnt(33)
	v_mov_b64_e32 v[78:79], v[2:3]
	s_waitcnt vmcnt(32)
	v_mov_b64_e32 v[82:83], v[2:3]
	s_waitcnt vmcnt(31)
	v_mov_b64_e32 v[86:87], v[2:3]
	s_waitcnt vmcnt(30)
	v_mov_b64_e32 v[90:91], v[2:3]
	s_waitcnt vmcnt(29)
	v_mov_b64_e32 v[94:95], v[2:3]
	s_waitcnt vmcnt(28)
	v_mov_b64_e32 v[98:99], v[2:3]
	s_waitcnt vmcnt(27)
	v_mov_b64_e32 v[102:103], v[2:3]
	s_waitcnt vmcnt(26)
	v_mov_b64_e32 v[106:107], v[2:3]
	s_waitcnt vmcnt(25)
	v_mov_b64_e32 v[110:111], v[2:3]
	s_waitcnt vmcnt(24)
	v_mov_b64_e32 v[114:115], v[2:3]
	s_waitcnt vmcnt(23)
	v_mov_b64_e32 v[118:119], v[2:3]
	s_waitcnt vmcnt(22)
	v_mov_b64_e32 v[122:123], v[2:3]
	v_mov_b64_e32 v[126:127], v[2:3]
	s_cselect_b64 s[26:27], -1, 0
	s_add_i32 s92, s42, 0xe000
	s_mov_b32 s66, 0
	v_writelane_b32 v255, s10, 46
	s_lshl_b32 s28, s10, 1
	v_mov_b64_e32 v[4:5], v[0:1]
	v_mov_b64_e32 v[8:9], v[0:1]
	v_mov_b64_e32 v[12:13], v[0:1]
	v_mov_b64_e32 v[16:17], v[0:1]
	v_mov_b64_e32 v[20:21], v[0:1]
	v_mov_b64_e32 v[24:25], v[0:1]
	v_mov_b64_e32 v[28:29], v[0:1]
	v_mov_b64_e32 v[32:33], v[0:1]
	v_mov_b64_e32 v[36:37], v[0:1]
	v_mov_b64_e32 v[40:41], v[0:1]
	v_mov_b64_e32 v[44:45], v[0:1]
	v_mov_b64_e32 v[48:49], v[0:1]
	v_mov_b64_e32 v[52:53], v[0:1]
	v_mov_b64_e32 v[56:57], v[0:1]
	v_mov_b64_e32 v[60:61], v[0:1]
	v_mov_b64_e32 v[64:65], v[0:1]
	v_mov_b64_e32 v[68:69], v[0:1]
	v_mov_b64_e32 v[72:73], v[0:1]
	v_mov_b64_e32 v[76:77], v[0:1]
	v_mov_b64_e32 v[80:81], v[0:1]
	v_mov_b64_e32 v[84:85], v[0:1]
	v_mov_b64_e32 v[88:89], v[0:1]
	v_mov_b64_e32 v[92:93], v[0:1]
	v_mov_b64_e32 v[96:97], v[0:1]
	v_mov_b64_e32 v[100:101], v[0:1]
	v_mov_b64_e32 v[104:105], v[0:1]
	v_mov_b64_e32 v[108:109], v[0:1]
	v_mov_b64_e32 v[112:113], v[0:1]
	v_mov_b64_e32 v[116:117], v[0:1]
	v_mov_b64_e32 v[120:121], v[0:1]
	v_mov_b64_e32 v[124:125], v[0:1]
	s_mov_b64 s[10:11], s[4:5]
	s_mov_b64 s[52:53], s[38:39]
	s_mov_b64 s[12:13], s[36:37]
	s_mov_b64 s[14:15], s[38:39]
	s_mov_b32 s93, 0
	s_barrier
	s_mov_b32 s100, 0
	s_branch .LBB0_839

;     __device__ __forceinline__ unsigned a_off(const Unit& u, const Gemm& g) const { return (unsigned)u.pm * (unsigned)(BM * 2) * (unsigned)g.K; }
;     __device__ __forceinline__ unsigned b_off(const Unit& u, const Gemm& g) const { return (unsigned)u.pn * (unsigned)(BM * 2) * (unsigned)g.K; }
;     __device__ __forceinline__ bool next(int i, Unit& u) const { return so.next(i, u); }
;     __device__ __forceinline__ unsigned a_off(const Unit& u, const Gemm& g) const { return (unsigned)u.pm * (unsigned)(BM * 2) * (unsigned)g.K; }
;     __device__ __forceinline__ bool next(int i, Unit& u) const { const bool ok = so.next(i >> 1, u); u.part = i & 1; return ok; }
; template <class Epi, class Sched, bool ALIGN_EPI = false, bool SP2 = false, bool FP8 = false>
; __device__ __forceinline__ void gemm_phase(LAS unsigned char* lds, const Gemm g, const Sched& S, const Epi& E, int wbase) {
;     ...
;         const bool has_next = S.next(ui + 1, nxt);
;         const unsigned nA = has_next ? S.a_off(nxt, g) : cA, nB = has_next ? S.b_off(nxt, g) : cB;
;         const rsrc_t rAn = (Sched::TWO && has_next) ? (nxt.part ? rA1 : rA0) : rAc, rBn = (Sched::TWO && has_next) ? (nxt.part ? rB1 : rB0) : rBc;
;         float pre_[8] = {0.f, 0.f, 0.f, 0.f, 0.f, 0.f, 0.f, 0.f};
;         if constexpr (Epi::HAS_PRE) E.pre_load(pre_, cur, wr);
;         for (int t = 0; t < nt; t += 2) {
;             const bool last = (t == nt - 2);
;             const unsigned a1 = cA + (unsigned)(t + 1) * kstep;
;             const unsigned a2 = last ? nA : cA + (unsigned)(t + 2) * kstep, b2 = last ? nB : cB + (unsigned)(t + 2) * kstep; const rsrc_t rA2 = (Sched::TWO && last) ? rAn : rAc, rB2 = (Sched::TWO && last) ? rBn : rBc;
;             const unsigned a3 = a2 + kstep, b3 = b2 + kstep;
;             if (last && has_next) S.a_ready(nxt);
;             if constexpr (SP2) {
;             PG8_LDB(B0, 0, 0); PG8_LDB(B1, 0, 1); PG8_SCHED; PG8_LDA(At, 0, 0); PG8_STAGE(PG8_SA(1, 1), rAc, a1 + hstep, voffA);
;             PG8_WAIT_V(8); PG8_WAIT_L(0); PG8_BAR; PG8_MMA(0, 0, At, B0); PG8_MMA(0, 1, At, B1); PG8_BAR; PG8_SCHED;
;             PG8_LDA(At, 0, 1); PG8_STAGE(PG8_SB(0, 0), rB2, b2, voffB); PG8_STAGE(PG8_SB(0, 1), rB2, b2 + hstep, voffB); PG8_STAGE(PG8_SA(0, 0), rA2, a2, voffA);
;             PG8_WAIT_V(8); PG8_WAIT_L(0); PG8_BAR; PG8_MMA(1, 0, At, B0); PG8_MMA(1, 1, At, B1); PG8_BAR; PG8_SCHED;
.LBB0_845:
	s_and_b32 s2, s93, 1
	s_lshl_b32 s96, s94, 19
	s_lshl_b32 s97, s95, 19
	s_cmp_eq_u32 s2, 0
	s_cselect_b32 s31, 0x20000, 0x20000
	s_cselect_b32 s30, -1, -1
	s_cselect_b32 s35, s37, s82
	s_cselect_b32 s34, s36, s61
	s_cselect_b32 s45, s5, s83
	s_cselect_b32 s44, s4, s62
	s_andn2_b64 vcc, exec, s[6:7]
	s_cbranch_vccnz .LBB0_849
	s_and_b64 s[16:17], s[58:59], exec
	s_cselect_b32 s67, s96, s19
	s_cselect_b32 s78, s97, s18
	s_add_i32 vcc_lo, s19, 0x80
	s_add_i32 vcc_hi, s18, 0x100
	s_mov_b32 s85, 0
	s_cmp_eq_u32 s100, 1
	s_cbranch_scc0 .LBB0_847
	s_add_i32 s20, vcc_lo, 0x80
	v_add_u32_e32 v140, 0x10000, v238
	v_add_u32_e32 v156, 0x14000, v238
	s_cmp_eq_u32 s88, s85
	ds_read_b128 v[128:131], v140
	ds_read_b128 v[132:135], v140 offset:1024
	ds_read_b128 v[136:139], v140 offset:2048
	ds_read_b128 v[140:143], v140 offset:3072
	ds_read_b128 v[144:147], v156
	ds_read_b128 v[148:151], v156 offset:1024
	ds_read_b128 v[152:155], v156 offset:2048
	ds_read_b128 v[156:159], v156 offset:3072
	s_cselect_b64 s[16:17], -1, 0
	s_and_b64 s[18:19], s[16:17], exec
	s_cselect_b32 s68, s67, s20
	s_cselect_b32 s54, s78, vcc_hi
	s_and_b64 s[20:21], s[58:59], s[16:17]
	s_and_b64 s[16:17], s[20:21], exec
	s_cselect_b32 s18, s30, s14
	s_cselect_b32 s19, s31, s15
	s_cselect_b32 s17, s35, s13
	s_cselect_b32 s16, s34, s12
	s_or_b32 s55, s68, 0x80
	s_and_b64 s[20:21], s[20:21], exec
	s_cselect_b32 s23, s31, s53
	s_cselect_b32 s22, s30, s52
	s_cselect_b32 s21, s45, s11
	s_cselect_b32 s20, s44, s10
	s_add_i32 s69, s41, vcc_lo
	s_mov_b32 m0, s89
	ds_read_b128 v[160:163], v239
	ds_read_b128 v[164:167], v239 offset:1024
	ds_read_b128 v[168:171], v239 offset:2048
	ds_read_b128 v[172:175], v239 offset:3072
	ds_read_b128 v[176:179], v239 offset:4096
	ds_read_b128 v[180:183], v239 offset:5120
	ds_read_b128 v[184:187], v239 offset:6144
	ds_read_b128 v[188:191], v239 offset:7168
	buffer_load_dwordx4 v192, s[12:15], s69 offen lds
	s_mov_b32 m0, s92
	s_nop 0
	buffer_load_dwordx4 v223, s[12:15], s69 offen lds
	s_waitcnt vmcnt(24)
	s_waitcnt lgkmcnt(0)
	s_barrier
	s_setprio 1
	s_waitcnt lgkmcnt(7)
	v_mfma_f32_16x16x32_bf16 v[124:127], v[128:131], v[160:163], v[124:127]
	v_mfma_f32_16x16x32_bf16 v[120:123], v[136:139], v[160:163], v[120:123]
	s_waitcnt lgkmcnt(5)
	v_mfma_f32_16x16x32_bf16 v[116:119], v[128:131], v[168:171], v[116:119]
	v_mfma_f32_16x16x32_bf16 v[112:115], v[136:139], v[168:171], v[112:115]
	s_waitcnt lgkmcnt(3)
	v_mfma_f32_16x16x32_bf16 v[108:111], v[128:131], v[176:179], v[108:111]
	v_mfma_f32_16x16x32_bf16 v[104:107], v[136:139], v[176:179], v[104:107]
	s_waitcnt lgkmcnt(1)
	v_mfma_f32_16x16x32_bf16 v[100:103], v[128:131], v[184:187], v[100:103]
	v_mfma_f32_16x16x32_bf16 v[96:99], v[136:139], v[184:187], v[96:99]
	v_mfma_f32_16x16x32_bf16 v[124:127], v[132:135], v[164:167], v[124:127]
	v_mfma_f32_16x16x32_bf16 v[120:123], v[140:143], v[164:167], v[120:123]
	v_mfma_f32_16x16x32_bf16 v[116:119], v[132:135], v[172:175], v[116:119]
	v_mfma_f32_16x16x32_bf16 v[112:115], v[140:143], v[172:175], v[112:115]
	v_mfma_f32_16x16x32_bf16 v[108:111], v[132:135], v[180:183], v[108:111]
	v_mfma_f32_16x16x32_bf16 v[104:107], v[140:143], v[180:183], v[104:107]
	s_waitcnt lgkmcnt(0)
	v_mfma_f32_16x16x32_bf16 v[100:103], v[132:135], v[188:191], v[100:103]
	v_mfma_f32_16x16x32_bf16 v[96:99], v[140:143], v[188:191], v[96:99]
	s_setprio 0
	s_setprio 1
	v_mfma_f32_16x16x32_bf16 v[92:95], v[144:147], v[160:163], v[92:95]
	v_mfma_f32_16x16x32_bf16 v[88:91], v[152:155], v[160:163], v[88:91]
	v_mfma_f32_16x16x32_bf16 v[84:87], v[144:147], v[168:171], v[84:87]
	v_mfma_f32_16x16x32_bf16 v[80:83], v[152:155], v[168:171], v[80:83]
	v_mfma_f32_16x16x32_bf16 v[76:79], v[144:147], v[176:179], v[76:79]
	v_mfma_f32_16x16x32_bf16 v[72:75], v[152:155], v[176:179], v[72:75]
	v_mfma_f32_16x16x32_bf16 v[68:71], v[144:147], v[184:187], v[68:71]
	v_mfma_f32_16x16x32_bf16 v[64:67], v[152:155], v[184:187], v[64:67]
	v_mfma_f32_16x16x32_bf16 v[92:95], v[148:151], v[164:167], v[92:95]
	v_mfma_f32_16x16x32_bf16 v[88:91], v[156:159], v[164:167], v[88:91]
	v_mfma_f32_16x16x32_bf16 v[84:87], v[148:151], v[172:175], v[84:87]
	v_mfma_f32_16x16x32_bf16 v[80:83], v[156:159], v[172:175], v[80:83]
	v_mfma_f32_16x16x32_bf16 v[76:79], v[148:151], v[180:183], v[76:79]
	v_mfma_f32_16x16x32_bf16 v[72:75], v[156:159], v[180:183], v[72:75]
	v_mfma_f32_16x16x32_bf16 v[68:71], v[148:151], v[188:191], v[68:71]
	v_mfma_f32_16x16x32_bf16 v[64:67], v[156:159], v[188:191], v[64:67]
	s_setprio 0
	s_barrier
	s_mov_b32 m0, s43
	ds_read_b128 v[160:163], v239 offset:16384
	ds_read_b128 v[164:167], v239 offset:17408
	ds_read_b128 v[168:171], v239 offset:18432
	ds_read_b128 v[172:175], v239 offset:19456
	ds_read_b128 v[176:179], v239 offset:20480
	ds_read_b128 v[180:183], v239 offset:21504
	ds_read_b128 v[184:187], v239 offset:22528
	ds_read_b128 v[188:191], v239 offset:23552
	buffer_load_dwordx4 v222, s[20:23], s54 offen lds
	s_mov_b32 m0, s46
	s_add_i32 s69, s54, s41
	buffer_load_dwordx4 v235, s[20:23], s54 offen lds
	s_mov_b32 m0, s47
	s_nop 0
	buffer_load_dwordx4 v222, s[20:23], s69 offen lds
	s_mov_b32 m0, s48
	s_nop 0
	buffer_load_dwordx4 v235, s[20:23], s69 offen lds
	s_mov_b32 m0, s42
	s_nop 0
	buffer_load_dwordx4 v192, s[16:19], s68 offen lds
	s_mov_b32 m0, s56
	s_nop 0
	buffer_load_dwordx4 v223, s[16:19], s68 offen lds
	s_waitcnt vmcnt(24)
	s_waitcnt lgkmcnt(0)
	s_barrier
; #define PG8_STAGE(bufoff, rs_, soff_, voff) do { _Pragma("unroll") for (int _i = 0; _i < 2; ++_i) \
;         __builtin_amdgcn_raw_ptr_buffer_load_lds(rs_, (LAS void*)(lds + (bufoff) + ldsw + _i * 8192), 16, (int)(voff)[_i], (int)(soff_), 0, 0); } while (0)
; #define PG8_LDA(dst, b, h) do { _Pragma("unroll") for (int m = 0; m < 4; ++m) dst[m] = PG8_LD2(lds + PG8_SA(b, h) + aoff + m * 2048); } while (0)
; #define PG8_LDB(dst, b, h) do { _Pragma("unroll") for (int n = 0; n < 2; ++n) dst[n] = PG8_LD2(lds + PG8_SB(b, h) + boff + n * 2048); } while (0)
; #define PG8_WAIT_V(n) asm volatile("s_waitcnt vmcnt(" #n ")" ::: "memory")
; #define PG8_WAIT_L(n) asm volatile("s_waitcnt lgkmcnt(" #n ")" ::: "memory")
; #define PG8_BAR __builtin_amdgcn_s_barrier()
; #define PG8_SCHED __builtin_amdgcn_sched_barrier(0)
; template <class Epi, class Sched, bool ALIGN_EPI = false, bool SP2 = false, bool FP8 = false>
; __device__ __forceinline__ void gemm_phase(LAS unsigned char* lds, const Gemm g, const Sched& S, const Epi& E, int wbase) {
;     ...
;             PG8_WAIT_V(8); PG8_WAIT_L(0); PG8_BAR; PG8_MMA(1, 0, At, B0); PG8_MMA(1, 1, At, B1); PG8_BAR; PG8_SCHED;
;             PG8_LDB(B0, 1, 0); PG8_LDB(B1, 1, 1); PG8_SCHED; PG8_LDA(At, 1, 0); PG8_STAGE(PG8_SA(0, 1), rA2, a2 + hstep, voffA);
;             PG8_WAIT_V(8); PG8_WAIT_L(0); PG8_BAR; PG8_MMA(0, 0, At, B0); PG8_MMA(0, 1, At, B1); PG8_BAR; PG8_SCHED;
	s_setprio 1
	s_waitcnt lgkmcnt(7)
	v_mfma_f32_16x16x32_bf16 v[60:63], v[128:131], v[160:163], v[60:63]
	v_mfma_f32_16x16x32_bf16 v[56:59], v[136:139], v[160:163], v[56:59]
	s_waitcnt lgkmcnt(5)
	v_mfma_f32_16x16x32_bf16 v[52:55], v[128:131], v[168:171], v[52:55]
	v_mfma_f32_16x16x32_bf16 v[48:51], v[136:139], v[168:171], v[48:51]
	s_waitcnt lgkmcnt(3)
	v_mfma_f32_16x16x32_bf16 v[44:47], v[128:131], v[176:179], v[44:47]
	v_mfma_f32_16x16x32_bf16 v[40:43], v[136:139], v[176:179], v[40:43]
	s_waitcnt lgkmcnt(1)
	v_mfma_f32_16x16x32_bf16 v[36:39], v[128:131], v[184:187], v[36:39]
	v_mfma_f32_16x16x32_bf16 v[32:35], v[136:139], v[184:187], v[32:35]
	v_mfma_f32_16x16x32_bf16 v[60:63], v[132:135], v[164:167], v[60:63]
	v_mfma_f32_16x16x32_bf16 v[56:59], v[140:143], v[164:167], v[56:59]
	v_mfma_f32_16x16x32_bf16 v[52:55], v[132:135], v[172:175], v[52:55]
	v_mfma_f32_16x16x32_bf16 v[48:51], v[140:143], v[172:175], v[48:51]
	v_mfma_f32_16x16x32_bf16 v[44:47], v[132:135], v[180:183], v[44:47]
	v_mfma_f32_16x16x32_bf16 v[40:43], v[140:143], v[180:183], v[40:43]
	s_waitcnt lgkmcnt(0)
	v_mfma_f32_16x16x32_bf16 v[36:39], v[132:135], v[188:191], v[36:39]
	v_mfma_f32_16x16x32_bf16 v[32:35], v[140:143], v[188:191], v[32:35]
	s_setprio 0
	s_setprio 1
	v_mfma_f32_16x16x32_bf16 v[28:31], v[144:147], v[160:163], v[28:31]
	v_mfma_f32_16x16x32_bf16 v[24:27], v[152:155], v[160:163], v[24:27]
	v_mfma_f32_16x16x32_bf16 v[20:23], v[144:147], v[168:171], v[20:23]
	v_mfma_f32_16x16x32_bf16 v[16:19], v[152:155], v[168:171], v[16:19]
	v_mfma_f32_16x16x32_bf16 v[12:15], v[144:147], v[176:179], v[12:15]
	v_mfma_f32_16x16x32_bf16 v[8:11], v[152:155], v[176:179], v[8:11]
	v_mfma_f32_16x16x32_bf16 v[4:7], v[144:147], v[184:187], v[4:7]
	v_mfma_f32_16x16x32_bf16 v[0:3], v[152:155], v[184:187], v[0:3]
	v_mfma_f32_16x16x32_bf16 v[28:31], v[148:151], v[164:167], v[28:31]
	v_mfma_f32_16x16x32_bf16 v[24:27], v[156:159], v[164:167], v[24:27]
	v_mfma_f32_16x16x32_bf16 v[20:23], v[148:151], v[172:175], v[20:23]
	v_mfma_f32_16x16x32_bf16 v[16:19], v[156:159], v[172:175], v[16:19]
	v_mfma_f32_16x16x32_bf16 v[12:15], v[148:151], v[180:183], v[12:15]
	v_mfma_f32_16x16x32_bf16 v[8:11], v[156:159], v[180:183], v[8:11]
	v_mfma_f32_16x16x32_bf16 v[4:7], v[148:151], v[188:191], v[4:7]
	v_mfma_f32_16x16x32_bf16 v[0:3], v[156:159], v[188:191], v[0:3]
	s_setprio 0
	s_barrier
	v_add_u32_e32 v140, 0x18000, v238
	v_add_u32_e32 v156, 0x1c000, v238
	ds_read_b128 v[128:131], v140
	ds_read_b128 v[132:135], v140 offset:1024
	ds_read_b128 v[136:139], v140 offset:2048
	ds_read_b128 v[140:143], v140 offset:3072
	ds_read_b128 v[144:147], v156
	ds_read_b128 v[148:151], v156 offset:1024
	ds_read_b128 v[152:155], v156 offset:2048
	ds_read_b128 v[156:159], v156 offset:3072
	s_add_i32 s68, s68, s41
	s_mov_b32 m0, s57
	ds_read_b128 v[160:163], v239 offset:32768
	ds_read_b128 v[164:167], v239 offset:33792
	ds_read_b128 v[168:171], v239 offset:34816
	ds_read_b128 v[172:175], v239 offset:35840
	ds_read_b128 v[176:179], v239 offset:36864
	ds_read_b128 v[180:183], v239 offset:37888
	ds_read_b128 v[184:187], v239 offset:38912
	ds_read_b128 v[188:191], v239 offset:39936
	buffer_load_dwordx4 v192, s[16:19], s68 offen lds
	s_mov_b32 m0, s60
	s_nop 0
	buffer_load_dwordx4 v223, s[16:19], s68 offen lds
	s_waitcnt vmcnt(8)
	s_waitcnt lgkmcnt(0)
	s_barrier
	s_setprio 1
	s_waitcnt lgkmcnt(7)
	v_mfma_f32_16x16x32_bf16 v[124:127], v[128:131], v[160:163], v[124:127]
	v_mfma_f32_16x16x32_bf16 v[120:123], v[136:139], v[160:163], v[120:123]
	s_waitcnt lgkmcnt(5)
	v_mfma_f32_16x16x32_bf16 v[116:119], v[128:131], v[168:171], v[116:119]
	v_mfma_f32_16x16x32_bf16 v[112:115], v[136:139], v[168:171], v[112:115]
	s_waitcnt lgkmcnt(3)
	v_mfma_f32_16x16x32_bf16 v[108:111], v[128:131], v[176:179], v[108:111]
	v_mfma_f32_16x16x32_bf16 v[104:107], v[136:139], v[176:179], v[104:107]
	s_waitcnt lgkmcnt(1)
	v_mfma_f32_16x16x32_bf16 v[100:103], v[128:131], v[184:187], v[100:103]
	v_mfma_f32_16x16x32_bf16 v[96:99], v[136:139], v[184:187], v[96:99]
	v_mfma_f32_16x16x32_bf16 v[124:127], v[132:135], v[164:167], v[124:127]
	v_mfma_f32_16x16x32_bf16 v[120:123], v[140:143], v[164:167], v[120:123]
	v_mfma_f32_16x16x32_bf16 v[116:119], v[132:135], v[172:175], v[116:119]
	v_mfma_f32_16x16x32_bf16 v[112:115], v[140:143], v[172:175], v[112:115]
	v_mfma_f32_16x16x32_bf16 v[108:111], v[132:135], v[180:183], v[108:111]
	v_mfma_f32_16x16x32_bf16 v[104:107], v[140:143], v[180:183], v[104:107]
	s_waitcnt lgkmcnt(0)
	v_mfma_f32_16x16x32_bf16 v[100:103], v[132:135], v[188:191], v[100:103]
	v_mfma_f32_16x16x32_bf16 v[96:99], v[140:143], v[188:191], v[96:99]
	s_setprio 0
	s_setprio 1
	v_mfma_f32_16x16x32_bf16 v[92:95], v[144:147], v[160:163], v[92:95]
	v_mfma_f32_16x16x32_bf16 v[88:91], v[152:155], v[160:163], v[88:91]
	v_mfma_f32_16x16x32_bf16 v[84:87], v[144:147], v[168:171], v[84:87]
	v_mfma_f32_16x16x32_bf16 v[80:83], v[152:155], v[168:171], v[80:83]
	v_mfma_f32_16x16x32_bf16 v[76:79], v[144:147], v[176:179], v[76:79]
	v_mfma_f32_16x16x32_bf16 v[72:75], v[152:155], v[176:179], v[72:75]
	v_mfma_f32_16x16x32_bf16 v[68:71], v[144:147], v[184:187], v[68:71]
	v_mfma_f32_16x16x32_bf16 v[64:67], v[152:155], v[184:187], v[64:67]
	v_mfma_f32_16x16x32_bf16 v[92:95], v[148:151], v[164:167], v[92:95]
	v_mfma_f32_16x16x32_bf16 v[88:91], v[156:159], v[164:167], v[88:91]
	v_mfma_f32_16x16x32_bf16 v[84:87], v[148:151], v[172:175], v[84:87]
	v_mfma_f32_16x16x32_bf16 v[80:83], v[156:159], v[172:175], v[80:83]
	v_mfma_f32_16x16x32_bf16 v[76:79], v[148:151], v[180:183], v[76:79]
	v_mfma_f32_16x16x32_bf16 v[72:75], v[156:159], v[180:183], v[72:75]
	v_mfma_f32_16x16x32_bf16 v[68:71], v[148:151], v[188:191], v[68:71]
	v_mfma_f32_16x16x32_bf16 v[64:67], v[156:159], v[188:191], v[64:67]
	s_setprio 0
	s_barrier
; #define PG8_STAGE(bufoff, rs_, soff_, voff) do { _Pragma("unroll") for (int _i = 0; _i < 2; ++_i) \
;         __builtin_amdgcn_raw_ptr_buffer_load_lds(rs_, (LAS void*)(lds + (bufoff) + ldsw + _i * 8192), 16, (int)(voff)[_i], (int)(soff_), 0, 0); } while (0)
; #define PG8_LDA(dst, b, h) do { _Pragma("unroll") for (int m = 0; m < 4; ++m) dst[m] = PG8_LD2(lds + PG8_SA(b, h) + aoff + m * 2048); } while (0)
; #define PG8_WAIT_V(n) asm volatile("s_waitcnt vmcnt(" #n ")" ::: "memory")
; #define PG8_WAIT_L(n) asm volatile("s_waitcnt lgkmcnt(" #n ")" ::: "memory")
; #define PG8_BAR __builtin_amdgcn_s_barrier()
; #define PG8_SCHED __builtin_amdgcn_sched_barrier(0)
; template <class Epi, class Sched, bool ALIGN_EPI = false, bool SP2 = false, bool FP8 = false>
; __device__ __forceinline__ void gemm_phase(LAS unsigned char* lds, const Gemm g, const Sched& S, const Epi& E, int wbase) {
;     ...
;         for (int t = 0; t < nt; t += 2) {
;             const bool last = (t == nt - 2);
;             const unsigned a1 = cA + (unsigned)(t + 1) * kstep;
;             const unsigned a2 = last ? nA : cA + (unsigned)(t + 2) * kstep, b2 = last ? nB : cB + (unsigned)(t + 2) * kstep; const rsrc_t rA2 = (Sched::TWO && last) ? rAn : rAc, rB2 = (Sched::TWO && last) ? rBn : rBc;
;             const unsigned a3 = a2 + kstep, b3 = b2 + kstep;
;     ...
;             PG8_LDA(At, 1, 1); PG8_STAGE(PG8_SB(1, 0), rB2, b3, voffB); PG8_STAGE(PG8_SB(1, 1), rB2, b3 + hstep, voffB); PG8_STAGE(PG8_SA(1, 0), rA2, a3, voffA);
;             PG8_WAIT_V(8); PG8_WAIT_L(0); PG8_BAR; PG8_MMA(1, 0, At, B0); PG8_MMA(1, 1, At, B1); PG8_BAR; PG8_SCHED;
	s_mov_b32 m0, s63
	s_bitset1_b32 s54, 7
	ds_read_b128 v[160:163], v239 offset:49152
	ds_read_b128 v[164:167], v239 offset:50176
	ds_read_b128 v[168:171], v239 offset:51200
	ds_read_b128 v[172:175], v239 offset:52224
	ds_read_b128 v[176:179], v239 offset:53248
	ds_read_b128 v[180:183], v239 offset:54272
	ds_read_b128 v[184:187], v239 offset:55296
	ds_read_b128 v[188:191], v239 offset:56320
	buffer_load_dwordx4 v222, s[20:23], s54 offen lds
	s_mov_b32 m0, s65
	s_nop 0
	buffer_load_dwordx4 v235, s[20:23], s54 offen lds
	s_add_i32 s54, s54, s41
	s_mov_b32 m0, s79
	s_nop 0
	buffer_load_dwordx4 v222, s[20:23], s54 offen lds
	s_mov_b32 m0, s80
	s_nop 0
	buffer_load_dwordx4 v235, s[20:23], s54 offen lds
	s_mov_b32 m0, s76
	s_nop 0
	buffer_load_dwordx4 v192, s[16:19], s55 offen lds
	s_mov_b32 m0, s77
	s_nop 0
	buffer_load_dwordx4 v223, s[16:19], s55 offen lds
	s_waitcnt vmcnt(8)
	s_waitcnt lgkmcnt(0)
	s_barrier
	s_setprio 1
	s_waitcnt lgkmcnt(7)
	v_mfma_f32_16x16x32_bf16 v[60:63], v[128:131], v[160:163], v[60:63]
	v_mfma_f32_16x16x32_bf16 v[56:59], v[136:139], v[160:163], v[56:59]
	s_waitcnt lgkmcnt(5)
	v_mfma_f32_16x16x32_bf16 v[52:55], v[128:131], v[168:171], v[52:55]
	v_mfma_f32_16x16x32_bf16 v[48:51], v[136:139], v[168:171], v[48:51]
	s_waitcnt lgkmcnt(3)
	v_mfma_f32_16x16x32_bf16 v[44:47], v[128:131], v[176:179], v[44:47]
	v_mfma_f32_16x16x32_bf16 v[40:43], v[136:139], v[176:179], v[40:43]
	s_waitcnt lgkmcnt(1)
	v_mfma_f32_16x16x32_bf16 v[36:39], v[128:131], v[184:187], v[36:39]
	v_mfma_f32_16x16x32_bf16 v[32:35], v[136:139], v[184:187], v[32:35]
	v_mfma_f32_16x16x32_bf16 v[60:63], v[132:135], v[164:167], v[60:63]
	v_mfma_f32_16x16x32_bf16 v[56:59], v[140:143], v[164:167], v[56:59]
	v_mfma_f32_16x16x32_bf16 v[52:55], v[132:135], v[172:175], v[52:55]
	v_mfma_f32_16x16x32_bf16 v[48:51], v[140:143], v[172:175], v[48:51]
	v_mfma_f32_16x16x32_bf16 v[44:47], v[132:135], v[180:183], v[44:47]
	v_mfma_f32_16x16x32_bf16 v[40:43], v[140:143], v[180:183], v[40:43]
	s_waitcnt lgkmcnt(0)
	v_mfma_f32_16x16x32_bf16 v[36:39], v[132:135], v[188:191], v[36:39]
	v_mfma_f32_16x16x32_bf16 v[32:35], v[140:143], v[188:191], v[32:35]
	s_setprio 0
	s_setprio 1
	v_mfma_f32_16x16x32_bf16 v[28:31], v[144:147], v[160:163], v[28:31]
	v_mfma_f32_16x16x32_bf16 v[24:27], v[152:155], v[160:163], v[24:27]
	v_mfma_f32_16x16x32_bf16 v[20:23], v[144:147], v[168:171], v[20:23]
	v_mfma_f32_16x16x32_bf16 v[16:19], v[152:155], v[168:171], v[16:19]
	v_mfma_f32_16x16x32_bf16 v[12:15], v[144:147], v[176:179], v[12:15]
	v_mfma_f32_16x16x32_bf16 v[8:11], v[152:155], v[176:179], v[8:11]
	v_mfma_f32_16x16x32_bf16 v[4:7], v[144:147], v[184:187], v[4:7]
	v_mfma_f32_16x16x32_bf16 v[0:3], v[152:155], v[184:187], v[0:3]
	v_mfma_f32_16x16x32_bf16 v[28:31], v[148:151], v[164:167], v[28:31]
	v_mfma_f32_16x16x32_bf16 v[24:27], v[156:159], v[164:167], v[24:27]
	v_mfma_f32_16x16x32_bf16 v[20:23], v[148:151], v[172:175], v[20:23]
	v_mfma_f32_16x16x32_bf16 v[16:19], v[156:159], v[172:175], v[16:19]
	v_mfma_f32_16x16x32_bf16 v[12:15], v[148:151], v[180:183], v[12:15]
	v_mfma_f32_16x16x32_bf16 v[8:11], v[156:159], v[180:183], v[8:11]
	v_mfma_f32_16x16x32_bf16 v[4:7], v[148:151], v[188:191], v[4:7]
	v_mfma_f32_16x16x32_bf16 v[0:3], v[156:159], v[188:191], v[0:3]
	s_setprio 0
	s_barrier
	s_add_i32 s85, s85, 2
	s_addk_i32 vcc_lo, 0x100
	s_addk_i32 vcc_hi, 0x100
	s_cmp_ge_i32 s85, s81
	s_cbranch_scc0 .LBB0_847
	s_branch .Lpeel_after_847

; #define PG8_BAR __builtin_amdgcn_s_barrier()
; template <class Epi, class Sched, bool ALIGN_EPI = false, bool SP2 = false, bool FP8 = false>
; __device__ __forceinline__ void gemm_phase(LAS unsigned char* lds, const Gemm g, const Sched& S, const Epi& E, int wbase) {
;     ...
;         }
;         if constexpr (ALIGN_EPI) { if (wr == 0) PG8_BAR; }
;         { int fr_ = fr, fq_ = fq; asm volatile("" : "+v"(fr_), "+v"(fq_));
;           if constexpr (Epi::HAS_PRE) E(acc, cur, wr, wc, fr_, fq_, pre_); else E(acc, cur, wr, wc, fr_, fq_); } S.done(cur);
;         if (!has_next) break;
.Lpeel_after_847:
	s_mov_b32 s100, 1
	v_readlane_b32 s68, v255, 22
	v_readlane_b32 s54, v255, 25
	v_readlane_b32 s69, v255, 23
	v_readlane_b32 s55, v255, 26

;     __device__ __forceinline__ unsigned a_off(const Unit& u, const Gemm& g) const { return (unsigned)u.pm * (unsigned)(BM * 2) * (unsigned)g.K; }
;     __device__ __forceinline__ unsigned b_off(const Unit& u, const Gemm& g) const { return (unsigned)u.pn * (unsigned)(BM * 2) * (unsigned)g.K; }
;     __device__ __forceinline__ bool next(int i, Unit& u) const { return so.next(i, u); }
; template <class Epi, class Sched, bool ALIGN_EPI = false, bool SP2 = false, bool FP8 = false>
; __device__ __forceinline__ void gemm_phase(LAS unsigned char* lds, const Gemm g, const Sched& S, const Epi& E, int wbase) {
;     ...
;     for (int i = 0; i < 2; ++i) { int R, C; stage_rc(tid * 16 + i * 8192, R, C); const int Rb = Epi::PERM ? ((R & ~31) + perm32(R & 31)) : R;
;         voffA[i] = (unsigned)(R * K + C) * 2u; voffB[i] = (unsigned)(Rb * K + C) * 2u; }
;     const unsigned kstep = (unsigned)(BK * 2);
;     const unsigned hstep = (unsigned)HALF * (unsigned)K * 2u;
;     typedef __amdgpu_buffer_rsrc_t rsrc_t;
;     const rsrc_t rA0 = __builtin_amdgcn_make_buffer_rsrc((void*)g.A, 0, 0xffffffff, 0x00020000), rB0 = __builtin_amdgcn_make_buffer_rsrc((void*)g.Bt, 0, 0xffffffff, 0x00020000);
;     rsrc_t rA1 = rA0, rB1 = rB0;
;     if constexpr (Sched::TWO) { rA1 = __builtin_amdgcn_make_buffer_rsrc((void*)S.A1, 0, 0xffffffff, 0x00020000); rB1 = __builtin_amdgcn_make_buffer_rsrc((void*)S.Bt1, 0, 0xffffffff, 0x00020000); }
;     const unsigned ldsw = (unsigned)wid * 1024u;
;     const int aoff = lds_byte(wr * 64 + fr, fq * 8), boff = lds_byte(wc * 32 + fr, fq * 8);
;     ...
;     Unit cur, nxt; int ui = 0;
;     if (!S.next(0, cur)) return;
;     f32x4 acc[2][2][4][2];
;     ...
;     PG8_ZERO_ACC();
;     v8i_t At[4], B0[2], B1[2];
;     unsigned cA = S.a_off(cur, g), cB = S.b_off(cur, g); rsrc_t rAc = (Sched::TWO && cur.part) ? rA1 : rA0, rBc = (Sched::TWO && cur.part) ? rB1 : rB0;
;     S.a_ready(cur);
;     if constexpr (SP2) {
;         PG8_STAGE(PG8_SB(0, 0), rBc, cB, voffB); PG8_STAGE(PG8_SB(0, 1), rBc, cB + hstep, voffB); PG8_STAGE(PG8_SA(0, 0), rAc, cA, voffA); PG8_STAGE(PG8_SA(0, 1), rAc, cA + hstep, voffA);
;         if (wr == 1) PG8_BAR;
;         PG8_WAIT_V(2); PG8_BAR;
;         PG8_STAGE(PG8_SB(1, 0), rBc, cB + kstep, voffB); PG8_STAGE(PG8_SA(1, 0), rAc, cA + kstep, voffA); PG8_STAGE(PG8_SB(1, 1), rBc, cB + hstep + kstep, voffB);
;         PG8_WAIT_V(6); PG8_BAR;
.LBB0_915:
	v_readlane_b32 s8, v255, 10
	s_cmp_eq_u32 s8, 0
	s_mov_b32 s8, 0x13200000
	s_cselect_b32 s8, s8, 0x1b800000
	s_add_u32 s8, s2, s8
	s_addc_u32 s9, s3, 0
	v_readlane_b32 s14, v255, 11
	s_cmp_eq_u32 s14, 1
	s_cselect_b32 s14, 0, 0x200000
	s_add_u32 s14, s2, s14
	s_addc_u32 s15, s3, 0
	s_add_u32 s16, s14, 0x17200000
	s_addc_u32 s17, s15, 0
	s_add_u32 s18, s2, 0xb200000
	s_addc_u32 s19, s3, 0
	s_add_i32 s45, s31, 0x18000
	s_or_b32 s2, s5, 0x80
	s_mov_b32 s14, s38
	s_mov_b32 s15, s39
	s_mov_b32 m0, s45
	s_add_i32 s46, s31, 0x1a000
	s_waitcnt vmcnt(2)
	s_barrier
	buffer_load_dwordx4 v223, s[12:15], s2 offen lds
	s_mov_b32 m0, s46
	s_add_i32 s47, s31, 0x8000
	buffer_load_dwordx4 v157, s[12:15], s2 offen lds
	s_or_b32 s2, s4, 0x80
	s_mov_b32 m0, s47
	s_add_i32 s48, s31, 0xa000
	buffer_load_dwordx4 v222, s[36:39], s2 offen lds
	s_mov_b32 m0, s48
	s_add_i32 s52, s31, 0x1c000
	buffer_load_dwordx4 v156, s[36:39], s2 offen lds
	s_bitset1_b32 s23, 7
	s_mov_b32 m0, s52
	s_add_i32 s53, s31, 0x1e000
	buffer_load_dwordx4 v223, s[12:15], s23 offen lds
	s_mov_b32 m0, s53
	s_ashr_i32 s2, s21, 31
	buffer_load_dwordx4 v157, s[12:15], s23 offen lds
	v_bfe_u32 v225, v4, 4, 2
	s_lshr_b32 s2, s2, 26
	v_and_b32_e32 v158, 15, v4
	s_add_i32 s2, s21, s2
	v_lshlrev_b32_e32 v5, 4, v225
	v_lshlrev_b32_e32 v4, 2, v4
	s_and_b32 s57, s20, 3
	s_ashr_i32 s58, s2, 6
	v_lshl_or_b32 v5, v158, 6, v5
	s_lshl_b32 s2, s22, 13
	v_and_b32_e32 v4, 32, v4
	s_lshl_b32 s59, s22, 6
	v_bitop3_b32 v6, v5, s2, v4 bitop3:0xde
	s_lshl_b32 s20, s57, 5
	s_lshl_b32 s2, s57, 12
	s_cmp_gt_i32 s21, 63
	s_cselect_b64 s[22:23], -1, 0
	s_add_i32 s60, s58, -2
	s_add_i32 s61, s31, 0xc000
	s_cmpk_lt_u32 s11, 0x100
	v_bitop3_b32 v4, v5, s2, v4 bitop3:0xde
	s_waitcnt vmcnt(6)
	s_cselect_b64 s[24:25], -1, 0
	s_add_i32 s62, s31, 0xe000
	s_lshl_b32 s2, s57, 6
	s_add_u32 s63, s8, s2
	v_mov_b32_e32 v1, v0
	v_mov_b32_e32 v2, v0
	v_mov_b32_e32 v3, v0
	s_mov_b32 s56, 0
	s_mov_b32 s21, s40
	s_addc_u32 s65, s9, 0
	v_add_u32_e32 v160, 0, v4
	v_add_u32_e32 v161, 0, v6
	s_barrier
	s_mov_b32 s100, 0
	s_branch .LBB0_918

;     __device__ __forceinline__ unsigned a_off(const Unit& u, const Gemm& g) const { return (unsigned)u.pm * (unsigned)(BM * 2) * (unsigned)g.K; }
;     __device__ __forceinline__ unsigned b_off(const Unit& u, const Gemm& g) const { return (unsigned)u.pn * (unsigned)(BM * 2) * (unsigned)g.K; }
;     __device__ __forceinline__ bool next(int i, Unit& u) const { return so.next(i, u); }
;     __device__ __forceinline__ unsigned a_off(const Unit& u, const Gemm& g) const { return (unsigned)u.pm * (unsigned)(BM * 2) * (unsigned)g.K; }
;     __device__ __forceinline__ bool next(int i, Unit& u) const { const bool ok = so.next(i >> 1, u); u.part = i & 1; return ok; }
;     __device__ __forceinline__ unsigned a_off(const Unit& u, const Gemm& g) const { return (unsigned)u.pm * (unsigned)(BM * 2) * (unsigned)g.K; }
;     __device__ __forceinline__ unsigned b_off(const Unit& u, const Gemm& g) const { return (unsigned)u.pn * (unsigned)(BM * 2) * (unsigned)g.K; }
; template <class Epi, class Sched, bool ALIGN_EPI = false, bool SP2 = false, bool FP8 = false>
; __device__ __forceinline__ void gemm_phase(LAS unsigned char* lds, const Gemm g, const Sched& S, const Epi& E, int wbase) {
;     ...
;         const bool has_next = S.next(ui + 1, nxt);
;         const unsigned nA = has_next ? S.a_off(nxt, g) : cA, nB = has_next ? S.b_off(nxt, g) : cB;
;         const rsrc_t rAn = (Sched::TWO && has_next) ? (nxt.part ? rA1 : rA0) : rAc, rBn = (Sched::TWO && has_next) ? (nxt.part ? rB1 : rB0) : rBc;
;         float pre_[8] = {0.f, 0.f, 0.f, 0.f, 0.f, 0.f, 0.f, 0.f};
;         if constexpr (Epi::HAS_PRE) E.pre_load(pre_, cur, wr);
;         for (int t = 0; t < nt; t += 2) {
;             const bool last = (t == nt - 2);
;             const unsigned a1 = cA + (unsigned)(t + 1) * kstep;
;             const unsigned a2 = last ? nA : cA + (unsigned)(t + 2) * kstep, b2 = last ? nB : cB + (unsigned)(t + 2) * kstep; const rsrc_t rA2 = (Sched::TWO && last) ? rAn : rAc, rB2 = (Sched::TWO && last) ? rBn : rBc;
;             const unsigned a3 = a2 + kstep, b3 = b2 + kstep;
;             if (last && has_next) S.a_ready(nxt);
;             if constexpr (SP2) {
;             PG8_LDB(B0, 0, 0); PG8_LDB(B1, 0, 1); PG8_SCHED; PG8_LDA(At, 0, 0); PG8_STAGE(PG8_SA(1, 1), rAc, a1 + hstep, voffA);
;             PG8_WAIT_V(8); PG8_WAIT_L(0); PG8_BAR; PG8_MMA(0, 0, At, B0); PG8_MMA(0, 1, At, B1); PG8_BAR; PG8_SCHED;
.LBB0_924:
	s_lshl_b32 s79, s77, 18
	s_andn2_b64 vcc, exec, s[22:23]
	s_lshl_b32 s80, s76, 18
	s_cbranch_vccnz .LBB0_928
	s_and_b64 s[2:3], s[26:27], exec
	v_mov_b64_e32 v[6:7], v[2:3]
	v_mov_b64_e32 v[18:19], v[2:3]
	v_mov_b64_e32 v[22:23], v[2:3]
	v_mov_b64_e32 v[34:35], v[2:3]
	v_mov_b64_e32 v[38:39], v[2:3]
	v_mov_b64_e32 v[50:51], v[2:3]
	v_mov_b64_e32 v[54:55], v[2:3]
	v_mov_b64_e32 v[10:11], v[2:3]
	v_mov_b64_e32 v[14:15], v[2:3]
	v_mov_b64_e32 v[26:27], v[2:3]
	v_mov_b64_e32 v[30:31], v[2:3]
	v_mov_b64_e32 v[42:43], v[2:3]
	v_mov_b64_e32 v[46:47], v[2:3]
	v_mov_b64_e32 v[58:59], v[2:3]
	s_waitcnt vmcnt(37)
	v_mov_b64_e32 v[62:63], v[2:3]
	s_waitcnt vmcnt(36)
	v_mov_b64_e32 v[66:67], v[2:3]
	s_waitcnt vmcnt(35)
	v_mov_b64_e32 v[70:71], v[2:3]
	s_waitcnt vmcnt(32)
	v_mov_b64_e32 v[82:83], v[2:3]
	s_waitcnt vmcnt(31)
	v_mov_b64_e32 v[86:87], v[2:3]
	s_waitcnt vmcnt(28)
	v_mov_b64_e32 v[98:99], v[2:3]
	s_waitcnt vmcnt(27)
	v_mov_b64_e32 v[102:103], v[2:3]
	s_waitcnt vmcnt(24)
	v_mov_b64_e32 v[114:115], v[2:3]
	s_waitcnt vmcnt(23)
	v_mov_b64_e32 v[118:119], v[2:3]
	v_mov_b64_e32 v[74:75], v[2:3]
	v_mov_b64_e32 v[78:79], v[2:3]
	v_mov_b64_e32 v[90:91], v[2:3]
	v_mov_b64_e32 v[94:95], v[2:3]
	v_mov_b64_e32 v[106:107], v[2:3]
	v_mov_b64_e32 v[110:111], v[2:3]
	v_mov_b64_e32 v[126:127], v[2:3]
	v_mov_b64_e32 v[130:131], v[2:3]
	v_mov_b32_e32 v159, v233
	s_cselect_b32 s2, s79, s4
	s_cselect_b32 s3, s80, s5
	s_addk_i32 s4, 0x80
	s_addk_i32 s5, 0x100
	s_mov_b32 s11, 0
	v_mov_b64_e32 v[4:5], v[0:1]
	v_mov_b64_e32 v[16:17], v[0:1]
	v_mov_b64_e32 v[20:21], v[0:1]
	v_mov_b64_e32 v[32:33], v[0:1]
	v_mov_b64_e32 v[36:37], v[0:1]
	v_mov_b64_e32 v[48:49], v[0:1]
	v_mov_b64_e32 v[52:53], v[0:1]
	v_mov_b64_e32 v[8:9], v[0:1]
	v_mov_b64_e32 v[12:13], v[0:1]
	v_mov_b64_e32 v[24:25], v[0:1]
	v_mov_b64_e32 v[28:29], v[0:1]
	v_mov_b64_e32 v[40:41], v[0:1]
	v_mov_b64_e32 v[44:45], v[0:1]
	v_mov_b64_e32 v[56:57], v[0:1]
	v_mov_b64_e32 v[60:61], v[0:1]
	v_mov_b64_e32 v[64:65], v[0:1]
	v_mov_b64_e32 v[68:69], v[0:1]
	v_mov_b64_e32 v[80:81], v[0:1]
	v_mov_b64_e32 v[84:85], v[0:1]
	v_mov_b64_e32 v[96:97], v[0:1]
	v_mov_b64_e32 v[100:101], v[0:1]
	v_mov_b64_e32 v[112:113], v[0:1]
	v_mov_b64_e32 v[116:117], v[0:1]
	v_mov_b64_e32 v[72:73], v[0:1]
	v_mov_b64_e32 v[76:77], v[0:1]
	v_mov_b64_e32 v[88:89], v[0:1]
	v_mov_b64_e32 v[92:93], v[0:1]
	v_mov_b64_e32 v[104:105], v[0:1]
	v_mov_b64_e32 v[108:109], v[0:1]
	v_mov_b64_e32 v[124:125], v[0:1]
	v_mov_b64_e32 v[128:129], v[0:1]
	s_nop 0
	s_cmp_eq_u32 s100, 1
	s_cbranch_scc0 .LBB0_926
	v_add_u32_e32 v120, 0x10000, v160
	ds_read_b128 v[132:135], v120
	ds_read_b128 v[136:139], v120 offset:1024
	ds_read_b128 v[140:143], v120 offset:2048
	ds_read_b128 v[144:147], v120 offset:3072
	v_add_u32_e32 v120, 0x14000, v160
	ds_read_b128 v[162:165], v120
	ds_read_b128 v[166:169], v120 offset:1024
	ds_read_b128 v[170:173], v120 offset:2048
	ds_read_b128 v[174:177], v120 offset:3072
	s_add_i32 s14, s4, 0x80
	s_cmp_eq_u32 s60, s11
	s_cselect_b32 s66, s2, s14
	s_cselect_b32 s55, s3, s5
	s_or_b32 s54, s66, 0x80
	s_add_i32 s14, s30, s4
	s_mov_b32 m0, s61
	ds_read_b128 v[178:181], v161
	ds_read_b128 v[182:185], v161 offset:1024
	ds_read_b128 v[194:197], v161 offset:2048
	ds_read_b128 v[198:201], v161 offset:3072
	ds_read_b128 v[202:205], v161 offset:4096
	ds_read_b128 v[206:209], v161 offset:5120
	ds_read_b128 v[210:213], v161 offset:6144
	ds_read_b128 v[214:217], v161 offset:7168
	buffer_load_dwordx4 v222, s[36:39], s14 offen lds
	s_mov_b32 m0, s62
	s_nop 0
	buffer_load_dwordx4 v156, s[36:39], s14 offen lds
	s_waitcnt vmcnt(32)
	s_waitcnt lgkmcnt(0)
	s_barrier
	s_setprio 1
	s_waitcnt lgkmcnt(6)
	v_mfma_scale_f32_16x16x128_f8f6f4 v[124:127], v[140:147], v[178:185], v[124:127], v224, v224 op_sel_hi:[0,0,0]
	s_waitcnt lgkmcnt(4)
	v_mfma_scale_f32_16x16x128_f8f6f4 v[108:111], v[132:139], v[194:201], v[108:111], v224, v224 op_sel_hi:[0,0,0]
	v_mfma_scale_f32_16x16x128_f8f6f4 v[104:107], v[140:147], v[194:201], v[104:107], v224, v224 op_sel_hi:[0,0,0]
	v_mfma_scale_f32_16x16x128_f8f6f4 v[120:123], v[132:139], v[178:185], v[128:131], v224, v224 op_sel_hi:[0,0,0]
	s_waitcnt lgkmcnt(2)
	v_mfma_scale_f32_16x16x128_f8f6f4 v[148:151], v[132:139], v[202:209], v[92:95], v224, v224 op_sel_hi:[0,0,0]
	v_mfma_scale_f32_16x16x128_f8f6f4 v[186:189], v[140:147], v[202:209], v[88:91], v224, v224 op_sel_hi:[0,0,0]
	s_waitcnt lgkmcnt(0)
	v_mfma_scale_f32_16x16x128_f8f6f4 v[218:221], v[132:139], v[210:217], v[76:79], v224, v224 op_sel_hi:[0,0,0]
	v_mfma_scale_f32_16x16x128_f8f6f4 v[226:229], v[140:147], v[210:217], v[72:75], v224, v224 op_sel_hi:[0,0,0]
	s_setprio 0
	s_setprio 1
	v_mfma_scale_f32_16x16x128_f8f6f4 v[116:119], v[162:169], v[178:185], v[116:119], v224, v224 op_sel_hi:[0,0,0]
	v_mfma_scale_f32_16x16x128_f8f6f4 v[112:115], v[170:177], v[178:185], v[112:115], v224, v224 op_sel_hi:[0,0,0]
	v_mfma_scale_f32_16x16x128_f8f6f4 v[100:103], v[162:169], v[194:201], v[100:103], v224, v224 op_sel_hi:[0,0,0]
	v_mfma_scale_f32_16x16x128_f8f6f4 v[96:99], v[170:177], v[194:201], v[96:99], v224, v224 op_sel_hi:[0,0,0]
	v_mfma_scale_f32_16x16x128_f8f6f4 v[178:181], v[162:169], v[202:209], v[84:87], v224, v224 op_sel_hi:[0,0,0]
	v_mfma_scale_f32_16x16x128_f8f6f4 v[182:185], v[170:177], v[202:209], v[80:83], v224, v224 op_sel_hi:[0,0,0]
	v_mfma_scale_f32_16x16x128_f8f6f4 v[194:197], v[162:169], v[210:217], v[68:71], v224, v224 op_sel_hi:[0,0,0]
	v_mfma_scale_f32_16x16x128_f8f6f4 v[198:201], v[170:177], v[210:217], v[64:67], v224, v224 op_sel_hi:[0,0,0]
	s_setprio 0
	s_barrier
; #define PG8_STAGE(bufoff, rs_, soff_, voff) do { _Pragma("unroll") for (int _i = 0; _i < 2; ++_i) \
;         __builtin_amdgcn_raw_ptr_buffer_load_lds(rs_, (LAS void*)(lds + (bufoff) + ldsw + _i * 8192), 16, (int)(voff)[_i], (int)(soff_), 0, 0); } while (0)
; #define PG8_LDA(dst, b, h) do { _Pragma("unroll") for (int m = 0; m < 4; ++m) dst[m] = PG8_LD2(lds + PG8_SA(b, h) + aoff + m * 2048); } while (0)
; #define PG8_LDB(dst, b, h) do { _Pragma("unroll") for (int n = 0; n < 2; ++n) dst[n] = PG8_LD2(lds + PG8_SB(b, h) + boff + n * 2048); } while (0)
; #define PG8_WAIT_V(n) asm volatile("s_waitcnt vmcnt(" #n ")" ::: "memory")
; #define PG8_WAIT_L(n) asm volatile("s_waitcnt lgkmcnt(" #n ")" ::: "memory")
; #define PG8_BAR __builtin_amdgcn_s_barrier()
; #define PG8_SCHED __builtin_amdgcn_sched_barrier(0)
; template <class Epi, class Sched, bool ALIGN_EPI = false, bool SP2 = false, bool FP8 = false>
; __device__ __forceinline__ void gemm_phase(LAS unsigned char* lds, const Gemm g, const Sched& S, const Epi& E, int wbase) {
;     ...
;             PG8_LDA(At, 0, 1); PG8_STAGE(PG8_SB(0, 0), rB2, b2, voffB); PG8_STAGE(PG8_SB(0, 1), rB2, b2 + hstep, voffB); PG8_STAGE(PG8_SA(0, 0), rA2, a2, voffA);
;             PG8_WAIT_V(8); PG8_WAIT_L(0); PG8_BAR; PG8_MMA(1, 0, At, B0); PG8_MMA(1, 1, At, B1); PG8_BAR; PG8_SCHED;
;             PG8_LDB(B0, 1, 0); PG8_LDB(B1, 1, 1); PG8_SCHED; PG8_LDA(At, 1, 0); PG8_STAGE(PG8_SA(0, 1), rA2, a2 + hstep, voffA);
;             PG8_WAIT_V(8); PG8_WAIT_L(0); PG8_BAR; PG8_MMA(0, 0, At, B0); PG8_MMA(0, 1, At, B1); PG8_BAR; PG8_SCHED;
	s_mov_b32 m0, s33
	s_mov_b32 s14, s38
	s_mov_b32 s15, s39
	s_nop 1
	ds_read_b128 v[64:67], v161 offset:16384
	ds_read_b128 v[68:71], v161 offset:17408
	ds_read_b128 v[72:75], v161 offset:18432
	ds_read_b128 v[76:79], v161 offset:19456
	ds_read_b128 v[80:83], v161 offset:20480
	ds_read_b128 v[84:87], v161 offset:21504
	ds_read_b128 v[88:91], v161 offset:22528
	ds_read_b128 v[92:95], v161 offset:23552
	buffer_load_dwordx4 v223, s[12:15], s55 offen lds
	s_mov_b32 m0, s34
	s_add_i32 s67, s55, s30
	buffer_load_dwordx4 v157, s[12:15], s55 offen lds
	s_mov_b32 m0, s35
	s_nop 0
	buffer_load_dwordx4 v223, s[12:15], s67 offen lds
	s_mov_b32 m0, s41
	s_nop 0
	buffer_load_dwordx4 v157, s[12:15], s67 offen lds
	s_mov_b32 m0, s31
	s_nop 0
	buffer_load_dwordx4 v222, s[36:39], s66 offen lds
	s_mov_b32 m0, s42
	s_nop 0
	buffer_load_dwordx4 v156, s[36:39], s66 offen lds
	s_waitcnt vmcnt(32)
	s_waitcnt lgkmcnt(0)
	s_barrier
	s_setprio 1
	s_waitcnt lgkmcnt(6)
	v_mfma_scale_f32_16x16x128_f8f6f4 v[60:63], v[132:139], v[64:71], v[60:63], v224, v224 op_sel_hi:[0,0,0]
	v_mfma_scale_f32_16x16x128_f8f6f4 v[56:59], v[140:147], v[64:71], v[56:59], v224, v224 op_sel_hi:[0,0,0]
	s_waitcnt lgkmcnt(4)
	v_mfma_scale_f32_16x16x128_f8f6f4 v[202:205], v[132:139], v[72:79], v[44:47], v224, v224 op_sel_hi:[0,0,0]
	v_mfma_scale_f32_16x16x128_f8f6f4 v[206:209], v[140:147], v[72:79], v[40:43], v224, v224 op_sel_hi:[0,0,0]
	s_waitcnt lgkmcnt(2)
	v_mfma_scale_f32_16x16x128_f8f6f4 v[210:213], v[132:139], v[80:87], v[28:31], v224, v224 op_sel_hi:[0,0,0]
	v_mfma_scale_f32_16x16x128_f8f6f4 v[214:217], v[140:147], v[80:87], v[24:27], v224, v224 op_sel_hi:[0,0,0]
	s_waitcnt lgkmcnt(0)
	v_mfma_scale_f32_16x16x128_f8f6f4 v[230:233], v[132:139], v[88:95], v[12:15], v224, v224 op_sel_hi:[0,0,0]
	v_mfma_scale_f32_16x16x128_f8f6f4 v[234:237], v[140:147], v[88:95], v[8:11], v224, v224 op_sel_hi:[0,0,0]
	s_setprio 0
	s_setprio 1
	v_mfma_scale_f32_16x16x128_f8f6f4 v[52:55], v[162:169], v[64:71], v[52:55], v224, v224 op_sel_hi:[0,0,0]
	v_mfma_scale_f32_16x16x128_f8f6f4 v[48:51], v[170:177], v[64:71], v[48:51], v224, v224 op_sel_hi:[0,0,0]
	v_mfma_scale_f32_16x16x128_f8f6f4 v[238:241], v[162:169], v[72:79], v[36:39], v224, v224 op_sel_hi:[0,0,0]
	v_mfma_scale_f32_16x16x128_f8f6f4 v[242:245], v[170:177], v[72:79], v[32:35], v224, v224 op_sel_hi:[0,0,0]
	v_mfma_scale_f32_16x16x128_f8f6f4 v[246:249], v[162:169], v[80:87], v[20:23], v224, v224 op_sel_hi:[0,0,0]
	v_mfma_scale_f32_16x16x128_f8f6f4 v[250:253], v[170:177], v[80:87], v[16:19], v224, v224 op_sel_hi:[0,0,0]
	v_mfma_scale_f32_16x16x128_f8f6f4 v[190:193], v[162:169], v[88:95], v[4:7], v224, v224 op_sel_hi:[0,0,0]
	v_mfma_scale_f32_16x16x128_f8f6f4 v[152:155], v[170:177], v[88:95], v[0:3], v224, v224 op_sel_hi:[0,0,0]
	s_setprio 0
	s_barrier
	v_add_u32_e32 v8, 0x18000, v160
	s_nop 3
	ds_read_b128 v[0:3], v8
	ds_read_b128 v[4:7], v8 offset:1024
	ds_read_b128 v[16:19], v8 offset:2048
	ds_read_b128 v[20:23], v8 offset:3072
	v_add_u32_e32 v8, 0x1c000, v160
	ds_read_b128 v[132:135], v8
	ds_read_b128 v[136:139], v8 offset:1024
	ds_read_b128 v[140:143], v8 offset:2048
	ds_read_b128 v[144:147], v8 offset:3072
	s_add_i32 s66, s66, s30
	s_mov_b32 m0, s43
	ds_read_b128 v[8:11], v161 offset:32768
	ds_read_b128 v[12:15], v161 offset:33792
	ds_read_b128 v[24:27], v161 offset:34816
	ds_read_b128 v[28:31], v161 offset:35840
	ds_read_b128 v[32:35], v161 offset:36864
	ds_read_b128 v[36:39], v161 offset:37888
	ds_read_b128 v[40:43], v161 offset:38912
	ds_read_b128 v[44:47], v161 offset:39936
	buffer_load_dwordx4 v222, s[36:39], s66 offen lds
	s_mov_b32 m0, s44
	s_nop 0
	buffer_load_dwordx4 v156, s[36:39], s66 offen lds
	s_waitcnt vmcnt(8)
	s_waitcnt lgkmcnt(0)
	s_barrier
; #define PG8_STAGE(bufoff, rs_, soff_, voff) do { _Pragma("unroll") for (int _i = 0; _i < 2; ++_i) \
;         __builtin_amdgcn_raw_ptr_buffer_load_lds(rs_, (LAS void*)(lds + (bufoff) + ldsw + _i * 8192), 16, (int)(voff)[_i], (int)(soff_), 0, 0); } while (0)
; #define PG8_LDA(dst, b, h) do { _Pragma("unroll") for (int m = 0; m < 4; ++m) dst[m] = PG8_LD2(lds + PG8_SA(b, h) + aoff + m * 2048); } while (0)
; #define PG8_WAIT_V(n) asm volatile("s_waitcnt vmcnt(" #n ")" ::: "memory")
; #define PG8_WAIT_L(n) asm volatile("s_waitcnt lgkmcnt(" #n ")" ::: "memory")
; #define PG8_BAR __builtin_amdgcn_s_barrier()
; #define PG8_SCHED __builtin_amdgcn_sched_barrier(0)
; template <class Epi, class Sched, bool ALIGN_EPI = false, bool SP2 = false, bool FP8 = false>
; __device__ __forceinline__ void gemm_phase(LAS unsigned char* lds, const Gemm g, const Sched& S, const Epi& E, int wbase) {
;     ...
;             PG8_WAIT_V(8); PG8_WAIT_L(0); PG8_BAR; PG8_MMA(0, 0, At, B0); PG8_MMA(0, 1, At, B1); PG8_BAR; PG8_SCHED;
;             PG8_LDA(At, 1, 1); PG8_STAGE(PG8_SB(1, 0), rB2, b3, voffB); PG8_STAGE(PG8_SB(1, 1), rB2, b3 + hstep, voffB); PG8_STAGE(PG8_SA(1, 0), rA2, a3, voffA);
;             PG8_WAIT_V(8); PG8_WAIT_L(0); PG8_BAR; PG8_MMA(1, 0, At, B0); PG8_MMA(1, 1, At, B1); PG8_BAR; PG8_SCHED;
	s_setprio 1
	s_waitcnt lgkmcnt(6)
	v_mfma_scale_f32_16x16x128_f8f6f4 v[128:131], v[0:7], v[8:15], v[120:123], v224, v224 op_sel_hi:[0,0,0]
	v_mfma_scale_f32_16x16x128_f8f6f4 v[124:127], v[16:23], v[8:15], v[124:127], v224, v224 op_sel_hi:[0,0,0]
	s_waitcnt lgkmcnt(4)
	v_mfma_scale_f32_16x16x128_f8f6f4 v[108:111], v[0:7], v[24:31], v[108:111], v224, v224 op_sel_hi:[0,0,0]
	v_mfma_scale_f32_16x16x128_f8f6f4 v[104:107], v[16:23], v[24:31], v[104:107], v224, v224 op_sel_hi:[0,0,0]
	s_waitcnt lgkmcnt(2)
	v_mfma_scale_f32_16x16x128_f8f6f4 v[92:95], v[0:7], v[32:39], v[148:151], v224, v224 op_sel_hi:[0,0,0]
	v_mfma_scale_f32_16x16x128_f8f6f4 v[88:91], v[16:23], v[32:39], v[186:189], v224, v224 op_sel_hi:[0,0,0]
	s_waitcnt lgkmcnt(0)
	v_mfma_scale_f32_16x16x128_f8f6f4 v[76:79], v[0:7], v[40:47], v[218:221], v224, v224 op_sel_hi:[0,0,0]
	v_mfma_scale_f32_16x16x128_f8f6f4 v[72:75], v[16:23], v[40:47], v[226:229], v224, v224 op_sel_hi:[0,0,0]
	s_setprio 0
	s_setprio 1
	v_mfma_scale_f32_16x16x128_f8f6f4 v[116:119], v[132:139], v[8:15], v[116:119], v224, v224 op_sel_hi:[0,0,0]
	v_mfma_scale_f32_16x16x128_f8f6f4 v[112:115], v[140:147], v[8:15], v[112:115], v224, v224 op_sel_hi:[0,0,0]
	v_mfma_scale_f32_16x16x128_f8f6f4 v[100:103], v[132:139], v[24:31], v[100:103], v224, v224 op_sel_hi:[0,0,0]
	v_mfma_scale_f32_16x16x128_f8f6f4 v[96:99], v[140:147], v[24:31], v[96:99], v224, v224 op_sel_hi:[0,0,0]
	v_mfma_scale_f32_16x16x128_f8f6f4 v[84:87], v[132:139], v[32:39], v[178:181], v224, v224 op_sel_hi:[0,0,0]
	v_mfma_scale_f32_16x16x128_f8f6f4 v[80:83], v[140:147], v[32:39], v[182:185], v224, v224 op_sel_hi:[0,0,0]
	v_mfma_scale_f32_16x16x128_f8f6f4 v[68:71], v[132:139], v[40:47], v[194:197], v224, v224 op_sel_hi:[0,0,0]
	v_mfma_scale_f32_16x16x128_f8f6f4 v[64:67], v[140:147], v[40:47], v[198:201], v224, v224 op_sel_hi:[0,0,0]
	s_setprio 0
	s_barrier
	s_mov_b32 m0, s45
	s_bitset1_b32 s55, 7
	ds_read_b128 v[32:35], v161 offset:49152
	ds_read_b128 v[36:39], v161 offset:50176
	ds_read_b128 v[162:165], v161 offset:51200
	ds_read_b128 v[166:169], v161 offset:52224
	ds_read_b128 v[170:173], v161 offset:53248
	ds_read_b128 v[174:177], v161 offset:54272
	ds_read_b128 v[178:181], v161 offset:55296
	ds_read_b128 v[182:185], v161 offset:56320
	buffer_load_dwordx4 v223, s[12:15], s55 offen lds
	s_mov_b32 m0, s46
	s_nop 0
	buffer_load_dwordx4 v157, s[12:15], s55 offen lds
	s_add_i32 s55, s55, s30
	s_mov_b32 m0, s52
	s_nop 0
	buffer_load_dwordx4 v223, s[12:15], s55 offen lds
	s_mov_b32 m0, s53
	s_nop 0
	buffer_load_dwordx4 v157, s[12:15], s55 offen lds
	s_mov_b32 m0, s47
	s_nop 0
	buffer_load_dwordx4 v222, s[36:39], s54 offen lds
	s_mov_b32 m0, s48
	s_nop 0
	buffer_load_dwordx4 v156, s[36:39], s54 offen lds
	s_waitcnt vmcnt(8)
	s_waitcnt lgkmcnt(0)
	s_barrier
	s_setprio 1
	s_waitcnt lgkmcnt(6)
	v_mfma_scale_f32_16x16x128_f8f6f4 v[60:63], v[0:7], v[32:39], v[60:63], v224, v224 op_sel_hi:[0,0,0]
	v_mfma_scale_f32_16x16x128_f8f6f4 v[56:59], v[16:23], v[32:39], v[56:59], v224, v224 op_sel_hi:[0,0,0]
	s_waitcnt lgkmcnt(4)
	v_mfma_scale_f32_16x16x128_f8f6f4 v[44:47], v[0:7], v[162:169], v[202:205], v224, v224 op_sel_hi:[0,0,0]
	v_mfma_scale_f32_16x16x128_f8f6f4 v[40:43], v[16:23], v[162:169], v[206:209], v224, v224 op_sel_hi:[0,0,0]
	s_waitcnt lgkmcnt(2)
	v_mfma_scale_f32_16x16x128_f8f6f4 v[28:31], v[0:7], v[170:177], v[210:213], v224, v224 op_sel_hi:[0,0,0]
	v_mfma_scale_f32_16x16x128_f8f6f4 v[24:27], v[16:23], v[170:177], v[214:217], v224, v224 op_sel_hi:[0,0,0]
	s_waitcnt lgkmcnt(0)
	v_mfma_scale_f32_16x16x128_f8f6f4 v[12:15], v[0:7], v[178:185], v[230:233], v224, v224 op_sel_hi:[0,0,0]
	v_mfma_scale_f32_16x16x128_f8f6f4 v[8:11], v[16:23], v[178:185], v[234:237], v224, v224 op_sel_hi:[0,0,0]
	s_setprio 0
	s_setprio 1
	v_mfma_scale_f32_16x16x128_f8f6f4 v[52:55], v[132:139], v[32:39], v[52:55], v224, v224 op_sel_hi:[0,0,0]
	v_mfma_scale_f32_16x16x128_f8f6f4 v[48:51], v[140:147], v[32:39], v[48:51], v224, v224 op_sel_hi:[0,0,0]
	v_mfma_scale_f32_16x16x128_f8f6f4 v[36:39], v[132:139], v[162:169], v[238:241], v224, v224 op_sel_hi:[0,0,0]
	v_mfma_scale_f32_16x16x128_f8f6f4 v[32:35], v[140:147], v[162:169], v[242:245], v224, v224 op_sel_hi:[0,0,0]
	v_mfma_scale_f32_16x16x128_f8f6f4 v[20:23], v[132:139], v[170:177], v[246:249], v224, v224 op_sel_hi:[0,0,0]
	v_mfma_scale_f32_16x16x128_f8f6f4 v[16:19], v[140:147], v[170:177], v[250:253], v224, v224 op_sel_hi:[0,0,0]
	v_mfma_scale_f32_16x16x128_f8f6f4 v[4:7], v[132:139], v[178:185], v[190:193], v224, v224 op_sel_hi:[0,0,0]
	v_mfma_scale_f32_16x16x128_f8f6f4 v[0:3], v[140:147], v[178:185], v[152:155], v224, v224 op_sel_hi:[0,0,0]
	s_setprio 0
	s_barrier
	s_add_i32 s11, s11, 2
	s_addk_i32 s4, 0x100
	s_addk_i32 s5, 0x100
	s_cmp_ge_i32 s11, s58
	s_cbranch_scc0 .LBB0_926
	s_branch .Lpeel_after_926

; #define PG8_BAR __builtin_amdgcn_s_barrier()
; #define PG8_ZERO_ACC() do { float z_; asm volatile("v_mov_b32 %0, 0" : "=v"(z_)); _Pragma("unroll") for (int a = 0; a < 2; ++a) _Pragma("unroll") for (int b = 0; b < 2; ++b) _Pragma("unroll") for (int m = 0; m < 4; ++m) \
;         _Pragma("unroll") for (int n = 0; n < 2; ++n) acc[a][b][m][n] = (f32x4){z_, z_, z_, z_}; } while (0)
; template <class Epi, class Sched, bool ALIGN_EPI = false, bool SP2 = false, bool FP8 = false>
; __device__ __forceinline__ void gemm_phase(LAS unsigned char* lds, const Gemm g, const Sched& S, const Epi& E, int wbase) {
;     ...
;         }
;         if constexpr (ALIGN_EPI) { if (wr == 0) PG8_BAR; }
;         { int fr_ = fr, fq_ = fq; asm volatile("" : "+v"(fr_), "+v"(fq_));
;           if constexpr (Epi::HAS_PRE) E(acc, cur, wr, wc, fr_, fq_, pre_); else E(acc, cur, wr, wc, fr_, fq_); } S.done(cur);
;         if (!has_next) break;
;         if (E.reset(cur)) PG8_ZERO_ACC();
.Lpeel_after_926:
	s_mov_b32 s100, 1
	v_mov_b32_e32 v230, 0x358637bd
	v_mov_b32_e32 v233, v159
	v_mov_b32_e32 v231, 1
	v_mov_b32_e32 v234, 0xff61b1e6
	s_and_b64 vcc, exec, s[24:25]
	s_cbranch_vccnz .LBB0_929
	s_branch .LBB0_930

;     __device__ __forceinline__ unsigned a_off(const Unit& u, const Gemm& g) const { return (unsigned)u.pm * (unsigned)(BM * 2) * (unsigned)g.K; }
;     __device__ __forceinline__ unsigned b_off(const Unit& u, const Gemm& g) const { return (unsigned)u.pn * (unsigned)(BM * 2) * (unsigned)g.K; }
;     __device__ __forceinline__ bool next(int i, Unit& u) const { return so.next(i, u); }
; template <class Epi, class Sched, bool ALIGN_EPI = false, bool SP2 = false, bool FP8 = false>
; __device__ __forceinline__ void gemm_phase(LAS unsigned char* lds, const Gemm g, const Sched& S, const Epi& E, int wbase) {
;     ...
;     for (int i = 0; i < 2; ++i) { int R, C; stage_rc(tid * 16 + i * 8192, R, C); const int Rb = Epi::PERM ? ((R & ~31) + perm32(R & 31)) : R;
;         voffA[i] = (unsigned)(R * K + C) * 2u; voffB[i] = (unsigned)(Rb * K + C) * 2u; }
;     const unsigned kstep = (unsigned)(BK * 2);
;     const unsigned hstep = (unsigned)HALF * (unsigned)K * 2u;
;     typedef __amdgpu_buffer_rsrc_t rsrc_t;
;     const rsrc_t rA0 = __builtin_amdgcn_make_buffer_rsrc((void*)g.A, 0, 0xffffffff, 0x00020000), rB0 = __builtin_amdgcn_make_buffer_rsrc((void*)g.Bt, 0, 0xffffffff, 0x00020000);
;     rsrc_t rA1 = rA0, rB1 = rB0;
;     if constexpr (Sched::TWO) { rA1 = __builtin_amdgcn_make_buffer_rsrc((void*)S.A1, 0, 0xffffffff, 0x00020000); rB1 = __builtin_amdgcn_make_buffer_rsrc((void*)S.Bt1, 0, 0xffffffff, 0x00020000); }
;     const unsigned ldsw = (unsigned)wid * 1024u;
;     const int aoff = lds_byte(wr * 64 + fr, fq * 8), boff = lds_byte(wc * 32 + fr, fq * 8);
;     ...
;     Unit cur, nxt; int ui = 0;
;     if (!S.next(0, cur)) return;
;     f32x4 acc[2][2][4][2];
;     ...
;     PG8_ZERO_ACC();
;     v8i_t At[4], B0[2], B1[2];
;     unsigned cA = S.a_off(cur, g), cB = S.b_off(cur, g); rsrc_t rAc = (Sched::TWO && cur.part) ? rA1 : rA0, rBc = (Sched::TWO && cur.part) ? rB1 : rB0;
;     S.a_ready(cur);
;     if constexpr (SP2) {
;         PG8_STAGE(PG8_SB(0, 0), rBc, cB, voffB); PG8_STAGE(PG8_SB(0, 1), rBc, cB + hstep, voffB); PG8_STAGE(PG8_SA(0, 0), rAc, cA, voffA); PG8_STAGE(PG8_SA(0, 1), rAc, cA + hstep, voffA);
;         if (wr == 1) PG8_BAR;
;         PG8_WAIT_V(2); PG8_BAR;
;         PG8_STAGE(PG8_SB(1, 0), rBc, cB + kstep, voffB); PG8_STAGE(PG8_SA(1, 0), rAc, cA + kstep, voffA); PG8_STAGE(PG8_SB(1, 1), rBc, cB + hstep + kstep, voffB);
;         PG8_WAIT_V(6); PG8_BAR;
.LBB0_993:
	v_readlane_b32 s8, v255, 10
	s_cmp_eq_u32 s8, 0
	s_mov_b32 s8, 0x13200000
	s_cselect_b32 s14, s8, 0x1b800000
	v_readlane_b32 s8, v255, 11
	s_cmp_eq_u32 s8, 1
	s_cselect_b32 s15, 0, 0x200000
	s_cmp_eq_u32 s95, 2
	s_cselect_b64 s[8:9], -1, 0
	s_add_u32 s16, s2, s14
	s_addc_u32 s17, s3, 0
	s_add_u32 s14, s2, s15
	s_addc_u32 s15, s3, 0
	s_add_u32 s18, s14, 0x17200000
	s_addc_u32 s19, s15, 0
	s_add_u32 s20, s2, 0xb200000
	s_addc_u32 s21, s3, 0
	s_add_i32 s47, s34, 0x18000
	s_or_b32 s2, s5, 0x80
	s_mov_b32 s14, s38
	s_mov_b32 s15, s39
	s_mov_b32 m0, s47
	s_add_i32 s48, s34, 0x1a000
	s_waitcnt vmcnt(2)
	s_barrier
	buffer_load_dwordx4 v175, s[12:15], s2 offen lds
	s_mov_b32 m0, s48
	s_add_i32 s52, s34, 0x8000
	buffer_load_dwordx4 v177, s[12:15], s2 offen lds
	s_or_b32 s2, s4, 0x80
	s_mov_b32 m0, s52
	s_add_i32 s53, s34, 0xa000
	buffer_load_dwordx4 v174, s[36:39], s2 offen lds
	s_mov_b32 m0, s53
	s_add_i32 s56, s34, 0x1c000
	buffer_load_dwordx4 v176, s[36:39], s2 offen lds
	s_bitset1_b32 s25, 7
	s_mov_b32 m0, s56
	s_add_i32 s57, s34, 0x1e000
	buffer_load_dwordx4 v175, s[12:15], s25 offen lds
	s_mov_b32 m0, s57
	s_ashr_i32 s2, s23, 31
	buffer_load_dwordx4 v177, s[12:15], s25 offen lds
	v_bfe_u32 v179, v4, 4, 2
	s_lshr_b32 s2, s2, 26
	v_and_b32_e32 v178, 15, v4
	s_add_i32 s2, s23, s2
	v_lshlrev_b32_e32 v5, 4, v179
	v_lshlrev_b32_e32 v4, 2, v4
	s_and_b32 s59, s22, 3
	s_ashr_i32 s60, s2, 6
	v_lshl_or_b32 v5, v178, 6, v5
	s_lshl_b32 s2, s24, 13
	v_and_b32_e32 v4, 32, v4
	s_lshl_b32 s61, s24, 6
	v_bitop3_b32 v6, v5, s2, v4 bitop3:0xde
	s_lshl_b32 s22, s59, 5
	s_lshl_b32 s2, s59, 12
	s_cmp_gt_i32 s23, 63
	s_cselect_b64 s[24:25], -1, 0
	s_add_i32 s62, s60, -2
	s_add_i32 s63, s34, 0xc000
	s_cmpk_lt_u32 s11, 0x100
	v_bitop3_b32 v4, v5, s2, v4 bitop3:0xde
	s_waitcnt vmcnt(6)
	s_cselect_b64 s[26:27], -1, 0
	s_add_i32 s65, s34, 0xe000
	s_lshl_b32 s2, s59, 6
	s_add_u32 s76, s16, s2
	v_mov_b32_e32 v1, v0
	v_mov_b32_e32 v2, v0
	v_mov_b32_e32 v3, v0
	s_mov_b32 s58, 0
	s_mov_b32 s23, s40
	s_addc_u32 s77, s17, 0
	v_add_u32_e32 v180, 0, v4
	v_add_u32_e32 v181, 0, v6
	s_barrier
	s_mov_b32 s100, 0
	s_branch .LBB0_996

;     __device__ __forceinline__ unsigned a_off(const Unit& u, const Gemm& g) const { return (unsigned)u.pm * (unsigned)(BM * 2) * (unsigned)g.K; }
;     __device__ __forceinline__ unsigned b_off(const Unit& u, const Gemm& g) const { return (unsigned)u.pn * (unsigned)(BM * 2) * (unsigned)g.K; }
;     __device__ __forceinline__ bool next(int i, Unit& u) const { return so.next(i, u); }
;     __device__ __forceinline__ unsigned a_off(const Unit& u, const Gemm& g) const { return (unsigned)u.pm * (unsigned)(BM * 2) * (unsigned)g.K; }
;     __device__ __forceinline__ bool next(int i, Unit& u) const { const bool ok = so.next(i >> 1, u); u.part = i & 1; return ok; }
;     __device__ __forceinline__ unsigned a_off(const Unit& u, const Gemm& g) const { return (unsigned)u.pm * (unsigned)(BM * 2) * (unsigned)g.K; }
;     __device__ __forceinline__ unsigned b_off(const Unit& u, const Gemm& g) const { return (unsigned)u.pn * (unsigned)(BM * 2) * (unsigned)g.K; }
; template <class Epi, class Sched, bool ALIGN_EPI = false, bool SP2 = false, bool FP8 = false>
; __device__ __forceinline__ void gemm_phase(LAS unsigned char* lds, const Gemm g, const Sched& S, const Epi& E, int wbase) {
;     ...
;         const bool has_next = S.next(ui + 1, nxt);
;         const unsigned nA = has_next ? S.a_off(nxt, g) : cA, nB = has_next ? S.b_off(nxt, g) : cB;
;         const rsrc_t rAn = (Sched::TWO && has_next) ? (nxt.part ? rA1 : rA0) : rAc, rBn = (Sched::TWO && has_next) ? (nxt.part ? rB1 : rB0) : rBc;
;         float pre_[8] = {0.f, 0.f, 0.f, 0.f, 0.f, 0.f, 0.f, 0.f};
;         if constexpr (Epi::HAS_PRE) E.pre_load(pre_, cur, wr);
;         for (int t = 0; t < nt; t += 2) {
;             const bool last = (t == nt - 2);
;             const unsigned a1 = cA + (unsigned)(t + 1) * kstep;
;             const unsigned a2 = last ? nA : cA + (unsigned)(t + 2) * kstep, b2 = last ? nB : cB + (unsigned)(t + 2) * kstep; const rsrc_t rA2 = (Sched::TWO && last) ? rAn : rAc, rB2 = (Sched::TWO && last) ? rBn : rBc;
;             const unsigned a3 = a2 + kstep, b3 = b2 + kstep;
;             if (last && has_next) S.a_ready(nxt);
;             if constexpr (SP2) {
;             PG8_LDB(B0, 0, 0); PG8_LDB(B1, 0, 1); PG8_SCHED; PG8_LDA(At, 0, 0); PG8_STAGE(PG8_SA(1, 1), rAc, a1 + hstep, voffA);
;             PG8_WAIT_V(8); PG8_WAIT_L(0); PG8_BAR; PG8_MMA(0, 0, At, B0); PG8_MMA(0, 1, At, B1); PG8_BAR; PG8_SCHED;
.LBB0_1002:
	s_lshl_b32 s81, s80, 19
	s_andn2_b64 vcc, exec, s[24:25]
	s_lshl_b32 s82, s79, 19
	s_cbranch_vccnz .LBB0_1058
	s_and_b64 s[2:3], s[28:29], exec
	v_mov_b64_e32 v[6:7], v[2:3]
	v_mov_b64_e32 v[18:19], v[2:3]
	v_mov_b64_e32 v[22:23], v[2:3]
	v_mov_b64_e32 v[34:35], v[2:3]
	v_mov_b64_e32 v[38:39], v[2:3]
	v_mov_b64_e32 v[50:51], v[2:3]
	v_mov_b64_e32 v[54:55], v[2:3]
	v_mov_b64_e32 v[10:11], v[2:3]
	v_mov_b64_e32 v[14:15], v[2:3]
	v_mov_b64_e32 v[26:27], v[2:3]
	v_mov_b64_e32 v[30:31], v[2:3]
	v_mov_b64_e32 v[42:43], v[2:3]
	v_mov_b64_e32 v[46:47], v[2:3]
	v_mov_b64_e32 v[58:59], v[2:3]
	s_waitcnt vmcnt(37)
	v_mov_b64_e32 v[62:63], v[2:3]
	s_waitcnt vmcnt(36)
	v_mov_b64_e32 v[66:67], v[2:3]
	s_waitcnt vmcnt(35)
	v_mov_b64_e32 v[70:71], v[2:3]
	s_waitcnt vmcnt(32)
	v_mov_b64_e32 v[82:83], v[2:3]
	s_waitcnt vmcnt(31)
	v_mov_b64_e32 v[86:87], v[2:3]
	s_waitcnt vmcnt(27)
	v_mov_b64_e32 v[102:103], v[2:3]
	s_waitcnt vmcnt(26)
	v_mov_b64_e32 v[106:107], v[2:3]
	v_mov_b64_e32 v[126:127], v[2:3]
	v_mov_b64_e32 v[130:131], v[2:3]
	v_mov_b64_e32 v[74:75], v[2:3]
	v_mov_b64_e32 v[78:79], v[2:3]
	v_mov_b64_e32 v[90:91], v[2:3]
	v_mov_b64_e32 v[94:95], v[2:3]
	s_waitcnt vmcnt(24)
	v_mov_b64_e32 v[114:115], v[2:3]
	s_waitcnt vmcnt(23)
	v_mov_b64_e32 v[118:119], v[2:3]
	v_mov_b64_e32 v[142:143], v[2:3]
	v_mov_b64_e32 v[150:151], v[2:3]
	s_cselect_b32 s2, s81, s4
	s_cselect_b32 s3, s82, s5
	s_addk_i32 s4, 0x80
	s_addk_i32 s5, 0x100
	s_mov_b32 s11, 0
	v_mov_b64_e32 v[4:5], v[0:1]
	v_mov_b64_e32 v[16:17], v[0:1]
	v_mov_b64_e32 v[20:21], v[0:1]
	v_mov_b64_e32 v[32:33], v[0:1]
	v_mov_b64_e32 v[36:37], v[0:1]
	v_mov_b64_e32 v[48:49], v[0:1]
	v_mov_b64_e32 v[52:53], v[0:1]
	v_mov_b64_e32 v[8:9], v[0:1]
	v_mov_b64_e32 v[12:13], v[0:1]
	v_mov_b64_e32 v[24:25], v[0:1]
	v_mov_b64_e32 v[28:29], v[0:1]
	v_mov_b64_e32 v[40:41], v[0:1]
	v_mov_b64_e32 v[44:45], v[0:1]
	v_mov_b64_e32 v[56:57], v[0:1]
	v_mov_b64_e32 v[60:61], v[0:1]
	v_mov_b64_e32 v[64:65], v[0:1]
	v_mov_b64_e32 v[68:69], v[0:1]
	v_mov_b64_e32 v[80:81], v[0:1]
	v_mov_b64_e32 v[84:85], v[0:1]
	v_mov_b64_e32 v[100:101], v[0:1]
	v_mov_b64_e32 v[104:105], v[0:1]
	v_mov_b64_e32 v[124:125], v[0:1]
	v_mov_b64_e32 v[128:129], v[0:1]
	v_mov_b64_e32 v[72:73], v[0:1]
	v_mov_b64_e32 v[76:77], v[0:1]
	v_mov_b64_e32 v[88:89], v[0:1]
	v_mov_b64_e32 v[92:93], v[0:1]
	v_mov_b64_e32 v[112:113], v[0:1]
	v_mov_b64_e32 v[116:117], v[0:1]
	v_mov_b64_e32 v[140:141], v[0:1]
	v_mov_b64_e32 v[148:149], v[0:1]
	s_nop 0
	s_cmp_eq_u32 s100, 1
	s_cbranch_scc0 .LBB0_1004
	v_add_u32_e32 v132, 0x10000, v180
	v_add_u32_e32 v156, 0x14000, v180
	ds_read_b128 v[96:99], v132
	ds_read_b128 v[108:111], v132 offset:1024
	ds_read_b128 v[120:123], v132 offset:2048
	ds_read_b128 v[132:135], v132 offset:3072
	ds_read_b128 v[136:139], v156
	ds_read_b128 v[144:147], v156 offset:1024
	ds_read_b128 v[152:155], v156 offset:2048
	ds_read_b128 v[156:159], v156 offset:3072
	s_add_i32 s14, s4, 0x80
	s_cmp_eq_u32 s62, s11
	s_cselect_b32 s66, s2, s14
	s_cselect_b32 s55, s3, s5
	s_or_b32 s54, s66, 0x80
	s_add_i32 s14, s33, s4
	s_mov_b32 m0, s63
	ds_read_b128 v[160:163], v181
	ds_read_b128 v[164:167], v181 offset:1024
	ds_read_b128 v[168:171], v181 offset:2048
	ds_read_b128 v[182:185], v181 offset:3072
	ds_read_b128 v[186:189], v181 offset:4096
	ds_read_b128 v[190:193], v181 offset:5120
	ds_read_b128 v[194:197], v181 offset:6144
	ds_read_b128 v[198:201], v181 offset:7168
	buffer_load_dwordx4 v174, s[36:39], s14 offen lds
	s_mov_b32 m0, s65
	s_nop 0
	buffer_load_dwordx4 v176, s[36:39], s14 offen lds
	s_waitcnt vmcnt(32)
	s_waitcnt lgkmcnt(0)
	s_barrier
	s_setprio 1
	s_waitcnt lgkmcnt(7)
	v_mfma_f32_16x16x32_bf16 v[148:151], v[96:99], v[160:163], v[148:151]
	v_mfma_f32_16x16x32_bf16 v[140:143], v[120:123], v[160:163], v[140:143]
	s_waitcnt lgkmcnt(5)
	v_mfma_f32_16x16x32_bf16 v[116:119], v[96:99], v[168:171], v[116:119]
	v_mfma_f32_16x16x32_bf16 v[112:115], v[120:123], v[168:171], v[112:115]
	s_waitcnt lgkmcnt(3)
	v_mfma_f32_16x16x32_bf16 v[92:95], v[96:99], v[186:189], v[92:95]
	v_mfma_f32_16x16x32_bf16 v[88:91], v[120:123], v[186:189], v[88:91]
	s_waitcnt lgkmcnt(1)
	v_mfma_f32_16x16x32_bf16 v[76:79], v[96:99], v[194:197], v[76:79]
	v_mfma_f32_16x16x32_bf16 v[72:75], v[120:123], v[194:197], v[72:75]
	v_mfma_f32_16x16x32_bf16 v[148:151], v[108:111], v[164:167], v[148:151]
	v_mfma_f32_16x16x32_bf16 v[140:143], v[132:135], v[164:167], v[140:143]
	v_mfma_f32_16x16x32_bf16 v[116:119], v[108:111], v[182:185], v[116:119]
	v_mfma_f32_16x16x32_bf16 v[112:115], v[132:135], v[182:185], v[112:115]
	v_mfma_f32_16x16x32_bf16 v[92:95], v[108:111], v[190:193], v[92:95]
	v_mfma_f32_16x16x32_bf16 v[88:91], v[132:135], v[190:193], v[88:91]
	s_waitcnt lgkmcnt(0)
	v_mfma_f32_16x16x32_bf16 v[76:79], v[108:111], v[198:201], v[76:79]
	v_mfma_f32_16x16x32_bf16 v[72:75], v[132:135], v[198:201], v[72:75]
	s_setprio 0
	s_setprio 1
	v_mfma_f32_16x16x32_bf16 v[128:131], v[136:139], v[160:163], v[128:131]
	v_mfma_f32_16x16x32_bf16 v[124:127], v[152:155], v[160:163], v[124:127]
	v_mfma_f32_16x16x32_bf16 v[104:107], v[136:139], v[168:171], v[104:107]
	v_mfma_f32_16x16x32_bf16 v[100:103], v[152:155], v[168:171], v[100:103]
	v_mfma_f32_16x16x32_bf16 v[84:87], v[136:139], v[186:189], v[84:87]
	v_mfma_f32_16x16x32_bf16 v[80:83], v[152:155], v[186:189], v[80:83]
	v_mfma_f32_16x16x32_bf16 v[68:71], v[136:139], v[194:197], v[68:71]
	v_mfma_f32_16x16x32_bf16 v[64:67], v[152:155], v[194:197], v[64:67]
	v_mfma_f32_16x16x32_bf16 v[128:131], v[144:147], v[164:167], v[128:131]
	v_mfma_f32_16x16x32_bf16 v[124:127], v[156:159], v[164:167], v[124:127]
	v_mfma_f32_16x16x32_bf16 v[104:107], v[144:147], v[182:185], v[104:107]
	v_mfma_f32_16x16x32_bf16 v[100:103], v[156:159], v[182:185], v[100:103]
	v_mfma_f32_16x16x32_bf16 v[84:87], v[144:147], v[190:193], v[84:87]
	v_mfma_f32_16x16x32_bf16 v[80:83], v[156:159], v[190:193], v[80:83]
	v_mfma_f32_16x16x32_bf16 v[68:71], v[144:147], v[198:201], v[68:71]
	v_mfma_f32_16x16x32_bf16 v[64:67], v[156:159], v[198:201], v[64:67]
	s_setprio 0
	s_barrier
; #define PG8_STAGE(bufoff, rs_, soff_, voff) do { _Pragma("unroll") for (int _i = 0; _i < 2; ++_i) \
;         __builtin_amdgcn_raw_ptr_buffer_load_lds(rs_, (LAS void*)(lds + (bufoff) + ldsw + _i * 8192), 16, (int)(voff)[_i], (int)(soff_), 0, 0); } while (0)
; #define PG8_LDA(dst, b, h) do { _Pragma("unroll") for (int m = 0; m < 4; ++m) dst[m] = PG8_LD2(lds + PG8_SA(b, h) + aoff + m * 2048); } while (0)
; #define PG8_LDB(dst, b, h) do { _Pragma("unroll") for (int n = 0; n < 2; ++n) dst[n] = PG8_LD2(lds + PG8_SB(b, h) + boff + n * 2048); } while (0)
; #define PG8_WAIT_V(n) asm volatile("s_waitcnt vmcnt(" #n ")" ::: "memory")
; #define PG8_WAIT_L(n) asm volatile("s_waitcnt lgkmcnt(" #n ")" ::: "memory")
; #define PG8_BAR __builtin_amdgcn_s_barrier()
; #define PG8_SCHED __builtin_amdgcn_sched_barrier(0)
; template <class Epi, class Sched, bool ALIGN_EPI = false, bool SP2 = false, bool FP8 = false>
; __device__ __forceinline__ void gemm_phase(LAS unsigned char* lds, const Gemm g, const Sched& S, const Epi& E, int wbase) {
;     ...
;             PG8_LDA(At, 0, 1); PG8_STAGE(PG8_SB(0, 0), rB2, b2, voffB); PG8_STAGE(PG8_SB(0, 1), rB2, b2 + hstep, voffB); PG8_STAGE(PG8_SA(0, 0), rA2, a2, voffA);
;             PG8_WAIT_V(8); PG8_WAIT_L(0); PG8_BAR; PG8_MMA(1, 0, At, B0); PG8_MMA(1, 1, At, B1); PG8_BAR; PG8_SCHED;
;             PG8_LDB(B0, 1, 0); PG8_LDB(B1, 1, 1); PG8_SCHED; PG8_LDA(At, 1, 0); PG8_STAGE(PG8_SA(0, 1), rA2, a2 + hstep, voffA);
;             PG8_WAIT_V(8); PG8_WAIT_L(0); PG8_BAR; PG8_MMA(0, 0, At, B0); PG8_MMA(0, 1, At, B1); PG8_BAR; PG8_SCHED;
	s_mov_b32 m0, s35
	s_mov_b32 s14, s38
	s_mov_b32 s15, s39
	ds_read_b128 v[160:163], v181 offset:16384
	ds_read_b128 v[164:167], v181 offset:17408
	ds_read_b128 v[168:171], v181 offset:18432
	ds_read_b128 v[182:185], v181 offset:19456
	ds_read_b128 v[186:189], v181 offset:20480
	ds_read_b128 v[190:193], v181 offset:21504
	ds_read_b128 v[194:197], v181 offset:22528
	ds_read_b128 v[198:201], v181 offset:23552
	buffer_load_dwordx4 v175, s[12:15], s55 offen lds
	s_mov_b32 m0, s41
	s_add_i32 s67, s55, s33
	buffer_load_dwordx4 v177, s[12:15], s55 offen lds
	s_mov_b32 m0, s42
	s_nop 0
	buffer_load_dwordx4 v175, s[12:15], s67 offen lds
	s_mov_b32 m0, s43
	s_nop 0
	buffer_load_dwordx4 v177, s[12:15], s67 offen lds
	s_mov_b32 m0, s34
	s_nop 0
	buffer_load_dwordx4 v174, s[36:39], s66 offen lds
	s_mov_b32 m0, s44
	s_nop 0
	buffer_load_dwordx4 v176, s[36:39], s66 offen lds
	s_waitcnt vmcnt(32)
	s_waitcnt lgkmcnt(0)
	s_barrier
	s_setprio 1
	s_waitcnt lgkmcnt(7)
	v_mfma_f32_16x16x32_bf16 v[60:63], v[96:99], v[160:163], v[60:63]
	v_mfma_f32_16x16x32_bf16 v[56:59], v[120:123], v[160:163], v[56:59]
	s_waitcnt lgkmcnt(5)
	v_mfma_f32_16x16x32_bf16 v[44:47], v[96:99], v[168:171], v[44:47]
	v_mfma_f32_16x16x32_bf16 v[40:43], v[120:123], v[168:171], v[40:43]
	s_waitcnt lgkmcnt(3)
	v_mfma_f32_16x16x32_bf16 v[28:31], v[96:99], v[186:189], v[28:31]
	v_mfma_f32_16x16x32_bf16 v[24:27], v[120:123], v[186:189], v[24:27]
	s_waitcnt lgkmcnt(1)
	v_mfma_f32_16x16x32_bf16 v[12:15], v[96:99], v[194:197], v[12:15]
	v_mfma_f32_16x16x32_bf16 v[8:11], v[120:123], v[194:197], v[8:11]
	v_mfma_f32_16x16x32_bf16 v[60:63], v[108:111], v[164:167], v[60:63]
	v_mfma_f32_16x16x32_bf16 v[56:59], v[132:135], v[164:167], v[56:59]
	v_mfma_f32_16x16x32_bf16 v[44:47], v[108:111], v[182:185], v[44:47]
	v_mfma_f32_16x16x32_bf16 v[40:43], v[132:135], v[182:185], v[40:43]
	v_mfma_f32_16x16x32_bf16 v[28:31], v[108:111], v[190:193], v[28:31]
	v_mfma_f32_16x16x32_bf16 v[24:27], v[132:135], v[190:193], v[24:27]
	s_waitcnt lgkmcnt(0)
	v_mfma_f32_16x16x32_bf16 v[12:15], v[108:111], v[198:201], v[12:15]
	v_mfma_f32_16x16x32_bf16 v[8:11], v[132:135], v[198:201], v[8:11]
	s_setprio 0
	s_setprio 1
	v_mfma_f32_16x16x32_bf16 v[52:55], v[136:139], v[160:163], v[52:55]
	v_mfma_f32_16x16x32_bf16 v[48:51], v[152:155], v[160:163], v[48:51]
	v_mfma_f32_16x16x32_bf16 v[36:39], v[136:139], v[168:171], v[36:39]
	v_mfma_f32_16x16x32_bf16 v[32:35], v[152:155], v[168:171], v[32:35]
	v_mfma_f32_16x16x32_bf16 v[20:23], v[136:139], v[186:189], v[20:23]
	v_mfma_f32_16x16x32_bf16 v[16:19], v[152:155], v[186:189], v[16:19]
	v_mfma_f32_16x16x32_bf16 v[4:7], v[136:139], v[194:197], v[4:7]
	v_mfma_f32_16x16x32_bf16 v[0:3], v[152:155], v[194:197], v[0:3]
	v_mfma_f32_16x16x32_bf16 v[52:55], v[144:147], v[164:167], v[52:55]
	v_mfma_f32_16x16x32_bf16 v[48:51], v[156:159], v[164:167], v[48:51]
	v_mfma_f32_16x16x32_bf16 v[36:39], v[144:147], v[182:185], v[36:39]
	v_mfma_f32_16x16x32_bf16 v[32:35], v[156:159], v[182:185], v[32:35]
	v_mfma_f32_16x16x32_bf16 v[20:23], v[144:147], v[190:193], v[20:23]
	v_mfma_f32_16x16x32_bf16 v[16:19], v[156:159], v[190:193], v[16:19]
	v_mfma_f32_16x16x32_bf16 v[4:7], v[144:147], v[198:201], v[4:7]
	v_mfma_f32_16x16x32_bf16 v[0:3], v[156:159], v[198:201], v[0:3]
	s_setprio 0
	s_barrier
	v_add_u32_e32 v132, 0x18000, v180
	v_add_u32_e32 v156, 0x1c000, v180
	ds_read_b128 v[96:99], v132
	ds_read_b128 v[108:111], v132 offset:1024
	ds_read_b128 v[120:123], v132 offset:2048
	ds_read_b128 v[132:135], v132 offset:3072
	ds_read_b128 v[136:139], v156
	ds_read_b128 v[144:147], v156 offset:1024
	ds_read_b128 v[152:155], v156 offset:2048
	ds_read_b128 v[156:159], v156 offset:3072
	s_add_i32 s66, s66, s33
	s_mov_b32 m0, s45
	ds_read_b128 v[160:163], v181 offset:32768
	ds_read_b128 v[164:167], v181 offset:33792
	ds_read_b128 v[168:171], v181 offset:34816
	ds_read_b128 v[182:185], v181 offset:35840
	ds_read_b128 v[186:189], v181 offset:36864
	ds_read_b128 v[190:193], v181 offset:37888
	ds_read_b128 v[194:197], v181 offset:38912
	ds_read_b128 v[198:201], v181 offset:39936
	buffer_load_dwordx4 v174, s[36:39], s66 offen lds
	s_mov_b32 m0, s46
	s_nop 0
	buffer_load_dwordx4 v176, s[36:39], s66 offen lds
	s_waitcnt vmcnt(8)
	s_waitcnt lgkmcnt(0)
	s_barrier
; #define PG8_STAGE(bufoff, rs_, soff_, voff) do { _Pragma("unroll") for (int _i = 0; _i < 2; ++_i) \
;         __builtin_amdgcn_raw_ptr_buffer_load_lds(rs_, (LAS void*)(lds + (bufoff) + ldsw + _i * 8192), 16, (int)(voff)[_i], (int)(soff_), 0, 0); } while (0)
; #define PG8_LDA(dst, b, h) do { _Pragma("unroll") for (int m = 0; m < 4; ++m) dst[m] = PG8_LD2(lds + PG8_SA(b, h) + aoff + m * 2048); } while (0)
; #define PG8_WAIT_V(n) asm volatile("s_waitcnt vmcnt(" #n ")" ::: "memory")
; #define PG8_WAIT_L(n) asm volatile("s_waitcnt lgkmcnt(" #n ")" ::: "memory")
; #define PG8_BAR __builtin_amdgcn_s_barrier()
; #define PG8_SCHED __builtin_amdgcn_sched_barrier(0)
; template <class Epi, class Sched, bool ALIGN_EPI = false, bool SP2 = false, bool FP8 = false>
; __device__ __forceinline__ void gemm_phase(LAS unsigned char* lds, const Gemm g, const Sched& S, const Epi& E, int wbase) {
;     ...
;             PG8_WAIT_V(8); PG8_WAIT_L(0); PG8_BAR; PG8_MMA(0, 0, At, B0); PG8_MMA(0, 1, At, B1); PG8_BAR; PG8_SCHED;
;             PG8_LDA(At, 1, 1); PG8_STAGE(PG8_SB(1, 0), rB2, b3, voffB); PG8_STAGE(PG8_SB(1, 1), rB2, b3 + hstep, voffB); PG8_STAGE(PG8_SA(1, 0), rA2, a3, voffA);
;             PG8_WAIT_V(8); PG8_WAIT_L(0); PG8_BAR; PG8_MMA(1, 0, At, B0); PG8_MMA(1, 1, At, B1); PG8_BAR; PG8_SCHED;
	s_setprio 1
	s_waitcnt lgkmcnt(7)
	v_mfma_f32_16x16x32_bf16 v[148:151], v[96:99], v[160:163], v[148:151]
	v_mfma_f32_16x16x32_bf16 v[140:143], v[120:123], v[160:163], v[140:143]
	s_waitcnt lgkmcnt(5)
	v_mfma_f32_16x16x32_bf16 v[116:119], v[96:99], v[168:171], v[116:119]
	v_mfma_f32_16x16x32_bf16 v[112:115], v[120:123], v[168:171], v[112:115]
	s_waitcnt lgkmcnt(3)
	v_mfma_f32_16x16x32_bf16 v[92:95], v[96:99], v[186:189], v[92:95]
	v_mfma_f32_16x16x32_bf16 v[88:91], v[120:123], v[186:189], v[88:91]
	s_waitcnt lgkmcnt(1)
	v_mfma_f32_16x16x32_bf16 v[76:79], v[96:99], v[194:197], v[76:79]
	v_mfma_f32_16x16x32_bf16 v[72:75], v[120:123], v[194:197], v[72:75]
	v_mfma_f32_16x16x32_bf16 v[148:151], v[108:111], v[164:167], v[148:151]
	v_mfma_f32_16x16x32_bf16 v[140:143], v[132:135], v[164:167], v[140:143]
	v_mfma_f32_16x16x32_bf16 v[116:119], v[108:111], v[182:185], v[116:119]
	v_mfma_f32_16x16x32_bf16 v[112:115], v[132:135], v[182:185], v[112:115]
	v_mfma_f32_16x16x32_bf16 v[92:95], v[108:111], v[190:193], v[92:95]
	v_mfma_f32_16x16x32_bf16 v[88:91], v[132:135], v[190:193], v[88:91]
	s_waitcnt lgkmcnt(0)
	v_mfma_f32_16x16x32_bf16 v[76:79], v[108:111], v[198:201], v[76:79]
	v_mfma_f32_16x16x32_bf16 v[72:75], v[132:135], v[198:201], v[72:75]
	s_setprio 0
	s_setprio 1
	v_mfma_f32_16x16x32_bf16 v[128:131], v[136:139], v[160:163], v[128:131]
	v_mfma_f32_16x16x32_bf16 v[124:127], v[152:155], v[160:163], v[124:127]
	v_mfma_f32_16x16x32_bf16 v[104:107], v[136:139], v[168:171], v[104:107]
	v_mfma_f32_16x16x32_bf16 v[100:103], v[152:155], v[168:171], v[100:103]
	v_mfma_f32_16x16x32_bf16 v[84:87], v[136:139], v[186:189], v[84:87]
	v_mfma_f32_16x16x32_bf16 v[80:83], v[152:155], v[186:189], v[80:83]
	v_mfma_f32_16x16x32_bf16 v[68:71], v[136:139], v[194:197], v[68:71]
	v_mfma_f32_16x16x32_bf16 v[64:67], v[152:155], v[194:197], v[64:67]
	v_mfma_f32_16x16x32_bf16 v[128:131], v[144:147], v[164:167], v[128:131]
	v_mfma_f32_16x16x32_bf16 v[124:127], v[156:159], v[164:167], v[124:127]
	v_mfma_f32_16x16x32_bf16 v[104:107], v[144:147], v[182:185], v[104:107]
	v_mfma_f32_16x16x32_bf16 v[100:103], v[156:159], v[182:185], v[100:103]
	v_mfma_f32_16x16x32_bf16 v[84:87], v[144:147], v[190:193], v[84:87]
	v_mfma_f32_16x16x32_bf16 v[80:83], v[156:159], v[190:193], v[80:83]
	v_mfma_f32_16x16x32_bf16 v[68:71], v[144:147], v[198:201], v[68:71]
	v_mfma_f32_16x16x32_bf16 v[64:67], v[156:159], v[198:201], v[64:67]
	s_setprio 0
	s_barrier
	s_mov_b32 m0, s47
	s_bitset1_b32 s55, 7
	ds_read_b128 v[160:163], v181 offset:49152
	ds_read_b128 v[164:167], v181 offset:50176
	ds_read_b128 v[168:171], v181 offset:51200
	ds_read_b128 v[182:185], v181 offset:52224
	ds_read_b128 v[186:189], v181 offset:53248
	ds_read_b128 v[190:193], v181 offset:54272
	ds_read_b128 v[194:197], v181 offset:55296
	ds_read_b128 v[198:201], v181 offset:56320
	buffer_load_dwordx4 v175, s[12:15], s55 offen lds
	s_mov_b32 m0, s48
	s_nop 0
	buffer_load_dwordx4 v177, s[12:15], s55 offen lds
	s_add_i32 s55, s55, s33
	s_mov_b32 m0, s56
	s_nop 0
	buffer_load_dwordx4 v175, s[12:15], s55 offen lds
	s_mov_b32 m0, s57
	s_nop 0
	buffer_load_dwordx4 v177, s[12:15], s55 offen lds
	s_mov_b32 m0, s52
	s_nop 0
	buffer_load_dwordx4 v174, s[36:39], s54 offen lds
	s_mov_b32 m0, s53
	s_nop 0
	buffer_load_dwordx4 v176, s[36:39], s54 offen lds
	s_waitcnt vmcnt(8)
	s_waitcnt lgkmcnt(0)
	s_barrier
	s_setprio 1
	s_waitcnt lgkmcnt(7)
	v_mfma_f32_16x16x32_bf16 v[60:63], v[96:99], v[160:163], v[60:63]
	v_mfma_f32_16x16x32_bf16 v[56:59], v[120:123], v[160:163], v[56:59]
	s_waitcnt lgkmcnt(5)
	v_mfma_f32_16x16x32_bf16 v[44:47], v[96:99], v[168:171], v[44:47]
	v_mfma_f32_16x16x32_bf16 v[40:43], v[120:123], v[168:171], v[40:43]
	s_waitcnt lgkmcnt(3)
	v_mfma_f32_16x16x32_bf16 v[28:31], v[96:99], v[186:189], v[28:31]
	v_mfma_f32_16x16x32_bf16 v[24:27], v[120:123], v[186:189], v[24:27]
	s_waitcnt lgkmcnt(1)
	v_mfma_f32_16x16x32_bf16 v[12:15], v[96:99], v[194:197], v[12:15]
	v_mfma_f32_16x16x32_bf16 v[8:11], v[120:123], v[194:197], v[8:11]
	v_mfma_f32_16x16x32_bf16 v[60:63], v[108:111], v[164:167], v[60:63]
	v_mfma_f32_16x16x32_bf16 v[56:59], v[132:135], v[164:167], v[56:59]
	v_mfma_f32_16x16x32_bf16 v[44:47], v[108:111], v[182:185], v[44:47]
	v_mfma_f32_16x16x32_bf16 v[40:43], v[132:135], v[182:185], v[40:43]
	v_mfma_f32_16x16x32_bf16 v[28:31], v[108:111], v[190:193], v[28:31]
	v_mfma_f32_16x16x32_bf16 v[24:27], v[132:135], v[190:193], v[24:27]
	s_waitcnt lgkmcnt(0)
	v_mfma_f32_16x16x32_bf16 v[12:15], v[108:111], v[198:201], v[12:15]
	v_mfma_f32_16x16x32_bf16 v[8:11], v[132:135], v[198:201], v[8:11]
	s_setprio 0
	s_setprio 1
	v_mfma_f32_16x16x32_bf16 v[52:55], v[136:139], v[160:163], v[52:55]
	v_mfma_f32_16x16x32_bf16 v[48:51], v[152:155], v[160:163], v[48:51]
	v_mfma_f32_16x16x32_bf16 v[36:39], v[136:139], v[168:171], v[36:39]
	v_mfma_f32_16x16x32_bf16 v[32:35], v[152:155], v[168:171], v[32:35]
	v_mfma_f32_16x16x32_bf16 v[20:23], v[136:139], v[186:189], v[20:23]
	v_mfma_f32_16x16x32_bf16 v[16:19], v[152:155], v[186:189], v[16:19]
	v_mfma_f32_16x16x32_bf16 v[4:7], v[136:139], v[194:197], v[4:7]
	v_mfma_f32_16x16x32_bf16 v[0:3], v[152:155], v[194:197], v[0:3]
	v_mfma_f32_16x16x32_bf16 v[52:55], v[144:147], v[164:167], v[52:55]
	v_mfma_f32_16x16x32_bf16 v[48:51], v[156:159], v[164:167], v[48:51]
	v_mfma_f32_16x16x32_bf16 v[36:39], v[144:147], v[182:185], v[36:39]
	v_mfma_f32_16x16x32_bf16 v[32:35], v[156:159], v[182:185], v[32:35]
	v_mfma_f32_16x16x32_bf16 v[20:23], v[144:147], v[190:193], v[20:23]
	v_mfma_f32_16x16x32_bf16 v[16:19], v[156:159], v[190:193], v[16:19]
	v_mfma_f32_16x16x32_bf16 v[4:7], v[144:147], v[198:201], v[4:7]
	v_mfma_f32_16x16x32_bf16 v[0:3], v[156:159], v[198:201], v[0:3]
	s_setprio 0
	s_barrier
	s_add_i32 s11, s11, 2
	s_addk_i32 s4, 0x100
	s_addk_i32 s5, 0x100
	s_cmp_ge_i32 s11, s60
	s_cbranch_scc0 .LBB0_1004
	s_branch .Lpeel_after_1004

; #define PG8_BAR __builtin_amdgcn_s_barrier()
; #define PG8_ZERO_ACC() do { float z_; asm volatile("v_mov_b32 %0, 0" : "=v"(z_)); _Pragma("unroll") for (int a = 0; a < 2; ++a) _Pragma("unroll") for (int b = 0; b < 2; ++b) _Pragma("unroll") for (int m = 0; m < 4; ++m) \
;         _Pragma("unroll") for (int n = 0; n < 2; ++n) acc[a][b][m][n] = (f32x4){z_, z_, z_, z_}; } while (0)
; template <class Epi, class Sched, bool ALIGN_EPI = false, bool SP2 = false, bool FP8 = false>
; __device__ __forceinline__ void gemm_phase(LAS unsigned char* lds, const Gemm g, const Sched& S, const Epi& E, int wbase) {
;     ...
;         }
;         if constexpr (ALIGN_EPI) { if (wr == 0) PG8_BAR; }
;         { int fr_ = fr, fq_ = fq; asm volatile("" : "+v"(fr_), "+v"(fq_));
;           if constexpr (Epi::HAS_PRE) E(acc, cur, wr, wc, fr_, fq_, pre_); else E(acc, cur, wr, wc, fr_, fq_); } S.done(cur);
;         if (!has_next) break;
;         if (E.reset(cur)) PG8_ZERO_ACC();
.Lpeel_after_1004:
	s_mov_b32 s100, 1
	s_and_b64 vcc, exec, s[26:27]
	s_cbranch_vccz .LBB0_1007

;     __device__ __forceinline__ bool next(int i, Unit& u) const { return so.next(i, u); }
;     __device__ __forceinline__ unsigned a_off(const Unit& u, const Gemm& g) const { return (unsigned)u.pm * (unsigned)(BM * 2) * (unsigned)g.K; }
;     __device__ __forceinline__ void setup(int G_, int c_) { so.setup(G_, c_); }
;     __device__ __forceinline__ bool next(int i, Unit& u) const { const bool ok = so.next(i >> 1, u); u.part = i & 1; return ok; }
;     __device__ __forceinline__ unsigned a_off(const Unit& u, const Gemm& g) const { return (unsigned)u.pm * (unsigned)(BM * 2) * (unsigned)g.K; }
;     __device__ __forceinline__ unsigned b_off(const Unit& u, const Gemm& g) const { return (unsigned)u.pn * (unsigned)(BM * 2) * (unsigned)g.K; }
;     __host__ __device__ bool next(int i, Unit& u) const {
;         const int L = i * G + c; if (L >= nwg) return false;
;         int wgid = L; { const int q = nwg / NXCD, r = nwg % NXCD, xcd = wgid % NXCD, off = wgid / NXCD; wgid = (xcd < r ? xcd * (q + 1) : r * (q + 1) + (xcd - r) * q) + off; }
;         const int nig = WGM * nN, gid = wgid / nig, fm = gid * WGM, gsz = (nM - fm) < WGM ? (nM - fm) : WGM;
;         u.pm = fm + ((wgid % nig) % gsz); u.pn = (wgid % nig) / gsz; u.part = 0; return true;
;     }
;     __device__ __forceinline__ unsigned a_off(const Unit& u, const Gemm& g) const { return (unsigned)u.pm * (unsigned)(BM * 2) * (unsigned)g.K; }
;     __device__ __forceinline__ unsigned b_off(const Unit& u, const Gemm& g) const { return (unsigned)u.pn * (unsigned)(BM * 2) * (unsigned)g.K; }
;     __device__ __forceinline__ void setup(int G_, int c_) {
; #pragma unroll
;         for (int e = 0; e < 9; ++e) ts[e] = __builtin_amdgcn_readfirstlane(__hip_atomic_load(meta + e, __ATOMIC_RELAXED, __HIP_MEMORY_SCOPE_AGENT));
;         so.init(ts[8] * BM, N, G_, c_);
.LBB0_1312:
	s_or_b64 exec, exec, s[10:11]
	s_mov_b64 s[2:3], s[88:89]
	s_waitcnt lgkmcnt(0)
	s_barrier
	s_mov_b32 s100, 0
	s_load_dwordx2 s[2:3], s[2:3], 0xf8
	v_readlane_b32 s4, v255, 4
	s_mov_b32 s1, s4
	s_mov_b32 s22, s92
	v_mov_b32_e32 v1, 0x177f0000
	s_waitcnt lgkmcnt(0)
	global_load_dword v0, v1, s[2:3] sc1
	global_load_dword v33, v1, s[2:3] offset:4 sc1
	global_load_dword v34, v1, s[2:3] offset:8 sc1
	global_load_dword v35, v1, s[2:3] offset:12 sc1
	global_load_dword v36, v1, s[2:3] offset:16 sc1
	global_load_dword v37, v1, s[2:3] offset:20 sc1
	global_load_dword v38, v1, s[2:3] offset:24 sc1
	global_load_dword v39, v1, s[2:3] offset:28 sc1
	global_load_dword v40, v1, s[2:3] offset:32 sc1
	s_mov_b32 s4, s38
	s_movk_i32 s16, 0x200
	v_readlane_b32 s5, v255, 5
	s_waitcnt vmcnt(0)
	v_readfirstlane_b32 s23, v33
	v_readfirstlane_b32 s24, v34
	v_readfirstlane_b32 s25, v35
	v_readfirstlane_b32 s26, v36
	v_readfirstlane_b32 s27, v37
	v_readfirstlane_b32 s28, v38
	v_readfirstlane_b32 s29, v39
	v_readfirstlane_b32 s30, v40
	v_mbcnt_lo_u32_b32 v0, s4, 0
	v_mbcnt_hi_u32_b32 v0, s4, v0
	s_mul_i32 s31, s30, 28
	v_add_u32_e32 v1, s93, v0
	s_cmp_lt_i32 s22, s31
	v_readfirstlane_b32 s15, v1
	s_cbranch_scc0 .LBB0_1372
	s_ashr_i32 s4, s31, 31
	s_lshr_b32 s4, s4, 29
	s_add_i32 s4, s31, s4
	s_ashr_i32 s33, s4, 3
	s_and_b32 s4, s4, -8
	s_sub_i32 s34, s31, s4
	s_ashr_i32 s4, s22, 31
	s_lshr_b32 s4, s4, 29
	s_add_i32 s7, s22, s4
	s_and_b32 s4, s7, -8
	s_sub_i32 s8, s22, s4
	s_add_i32 s35, s33, 1
	s_cmp_ge_i32 s8, s34
	s_mov_b64 s[4:5], -1
	s_cbranch_scc0 .LBB0_1315
	s_sub_i32 s5, s8, s34
	s_mul_i32 s4, s35, s34
	s_mul_i32 s5, s5, s33
	s_add_i32 s6, s4, s5
	s_mov_b64 s[4:5], 0

; __device__ __forceinline__ int lane_id() { unsigned ones = ~0u; asm volatile("" : "+s"(ones)); return (int)__builtin_amdgcn_mbcnt_hi(ones, __builtin_amdgcn_mbcnt_lo(ones, 0u)); }
;     __device__ __forceinline__ unsigned a_off(const Unit& u, const Gemm& g) const { return (unsigned)u.pm * (unsigned)(BM * 2) * (unsigned)g.K; }
;     __device__ __forceinline__ unsigned b_off(const Unit& u, const Gemm& g) const { return (unsigned)u.pn * (unsigned)(BM * 2) * (unsigned)g.K; }
; #define PG8_WAIT_V(n) asm volatile("s_waitcnt vmcnt(" #n ")" ::: "memory")
;     __device__ __forceinline__ void pre_load(float (&pre)[8], const Unit& u, int wr) const { const int fr = lane_id() & 15;
; #pragma unroll
;         for (int ai = 0; ai < 2; ++ai)
; #pragma unroll
;             for (int m = 0; m < 4; ++m) { const unsigned o4 = (unsigned)EPI_ROWS(ai, m) * 4u; asm volatile("global_load_dword %0, %1, %2" : "=v"(pre[ai * 4 + m]) : "v"(o4), "s"(sgw) : "memory"); } }
; template <class Epi, class Sched, bool ALIGN_EPI = false, bool SP2 = false, bool FP8 = false>
; __device__ __forceinline__ void gemm_phase(LAS unsigned char* lds, const Gemm g, const Sched& S, const Epi& E, int wbase) {
;     ...
;         const bool has_next = S.next(ui + 1, nxt);
;         const unsigned nA = has_next ? S.a_off(nxt, g) : cA, nB = has_next ? S.b_off(nxt, g) : cB;
;         const rsrc_t rAn = (Sched::TWO && has_next) ? (nxt.part ? rA1 : rA0) : rAc, rBn = (Sched::TWO && has_next) ? (nxt.part ? rB1 : rB0) : rBc;
;         float pre_[8] = {0.f, 0.f, 0.f, 0.f, 0.f, 0.f, 0.f, 0.f};
;         if constexpr (Epi::HAS_PRE) E.pre_load(pre_, cur, wr);
;         for (int t = 0; t < nt; t += 2) {
;             const bool last = (t == nt - 2);
;             const unsigned a1 = cA + (unsigned)(t + 1) * kstep;
;             const unsigned a2 = last ? nA : cA + (unsigned)(t + 2) * kstep, b2 = last ? nB : cB + (unsigned)(t + 2) * kstep; const rsrc_t rA2 = (Sched::TWO && last) ? rAn : rAc, rB2 = (Sched::TWO && last) ? rBn : rBc;
;             const unsigned a3 = a2 + kstep, b3 = b2 + kstep;
;             if (last && has_next) S.a_ready(nxt);
;             if constexpr (SP2) {
;             PG8_LDB(B0, 0, 0); PG8_LDB(B1, 0, 1); PG8_SCHED; PG8_LDA(At, 0, 0); PG8_STAGE(PG8_SA(1, 1), rAc, a1 + hstep, voffA);
;             PG8_WAIT_V(8); PG8_WAIT_L(0); PG8_BAR; PG8_MMA(0, 0, At, B0); PG8_MMA(0, 1, At, B1); PG8_BAR; PG8_SCHED;
.LBB0_1346:
	s_mov_b32 s21, -1
	s_lshl_b32 s82, s81, 18
	v_mbcnt_lo_u32_b32 v1, s21, 0
	v_mbcnt_hi_u32_b32 v1, s21, v1
	v_lshlrev_b32_e32 v1, 2, v1
	v_and_or_b32 v1, v1, 60, s63
	v_lshl_add_u32 v1, s84, 10, v1
	global_load_dword v209, v1, s[12:13]
	v_or_b32_e32 v2, 64, v1
	global_load_dword v208, v2, s[12:13]
	v_or_b32_e32 v2, 0x80, v1
	global_load_dword v207, v2, s[12:13]
	v_or_b32_e32 v2, 0xc0, v1
	global_load_dword v205, v2, s[12:13]
	v_add_u32_e32 v2, 0x200, v1
	global_load_dword v204, v2, s[12:13]
	v_add_u32_e32 v2, 0x240, v1
	global_load_dword v203, v2, s[12:13]
	v_add_u32_e32 v2, 0x280, v1
	global_load_dword v202, v2, s[12:13]
	v_add_u32_e32 v1, 0x2c0, v1
	global_load_dword v206, v1, s[12:13]
	s_andn2_b64 vcc, exec, s[16:17]
	s_cbranch_vccnz .LBB0_1366
	s_and_b64 s[6:7], s[6:7], exec
	v_mov_b64_e32 v[70:71], v[66:67]
	v_mov_b64_e32 v[86:87], v[66:67]
	v_mov_b64_e32 v[82:83], v[66:67]
	v_mov_b64_e32 v[102:103], v[66:67]
	v_mov_b64_e32 v[98:99], v[66:67]
	v_mov_b64_e32 v[118:119], v[66:67]
	v_mov_b64_e32 v[114:115], v[66:67]
	v_mov_b64_e32 v[78:79], v[66:67]
	v_mov_b64_e32 v[74:75], v[66:67]
	v_mov_b64_e32 v[94:95], v[66:67]
	v_mov_b64_e32 v[90:91], v[66:67]
	v_mov_b64_e32 v[110:111], v[66:67]
	v_mov_b64_e32 v[106:107], v[66:67]
	v_mov_b64_e32 v[126:127], v[66:67]
	v_mov_b64_e32 v[122:123], v[66:67]
	v_mov_b64_e32 v[134:135], v[66:67]
	v_mov_b64_e32 v[130:131], v[66:67]
	v_mov_b64_e32 v[150:151], v[66:67]
	v_mov_b64_e32 v[146:147], v[66:67]
	v_mov_b64_e32 v[166:167], v[66:67]
	v_mov_b64_e32 v[162:163], v[66:67]
	v_mov_b64_e32 v[182:183], v[66:67]
	v_mov_b64_e32 v[178:179], v[66:67]
	v_mov_b64_e32 v[142:143], v[66:67]
	v_mov_b64_e32 v[138:139], v[66:67]
	v_mov_b64_e32 v[158:159], v[66:67]
	v_mov_b64_e32 v[154:155], v[66:67]
	v_mov_b64_e32 v[174:175], v[66:67]
	v_mov_b64_e32 v[170:171], v[66:67]
	v_mov_b64_e32 v[190:191], v[66:67]
	v_mov_b64_e32 v[186:187], v[66:67]
	s_cselect_b32 s66, s82, s20
	s_add_i32 s67, s20, 0x80
	v_add_u32_e32 v210, 0x100, v0
	s_mov_b32 s85, 0
	v_mov_b64_e32 v[68:69], v[64:65]
	v_mov_b64_e32 v[84:85], v[64:65]
	v_mov_b64_e32 v[80:81], v[64:65]
	v_mov_b64_e32 v[100:101], v[64:65]
	v_mov_b64_e32 v[96:97], v[64:65]
	v_mov_b64_e32 v[116:117], v[64:65]
	v_mov_b64_e32 v[112:113], v[64:65]
	v_mov_b64_e32 v[76:77], v[64:65]
	v_mov_b64_e32 v[72:73], v[64:65]
	v_mov_b64_e32 v[92:93], v[64:65]
	v_mov_b64_e32 v[88:89], v[64:65]
	v_mov_b64_e32 v[108:109], v[64:65]
	v_mov_b64_e32 v[104:105], v[64:65]
	v_mov_b64_e32 v[124:125], v[64:65]
	v_mov_b64_e32 v[120:121], v[64:65]
	v_mov_b64_e32 v[132:133], v[64:65]
	v_mov_b64_e32 v[128:129], v[64:65]
	v_mov_b64_e32 v[148:149], v[64:65]
	v_mov_b64_e32 v[144:145], v[64:65]
	v_mov_b64_e32 v[164:165], v[64:65]
	v_mov_b64_e32 v[160:161], v[64:65]
	v_mov_b64_e32 v[180:181], v[64:65]
	v_mov_b64_e32 v[176:177], v[64:65]
	v_mov_b64_e32 v[140:141], v[64:65]
	v_mov_b64_e32 v[136:137], v[64:65]
	v_mov_b64_e32 v[156:157], v[64:65]
	v_mov_b64_e32 v[152:153], v[64:65]
	v_mov_b64_e32 v[172:173], v[64:65]
	v_mov_b64_e32 v[168:169], v[64:65]
	v_mov_b64_e32 v[188:189], v[64:65]
	v_mov_b64_e32 v[184:185], v[64:65]
	s_cmp_eq_u32 s100, 1
	s_cbranch_scc0 .LBB0_1348
	v_add_u32_e32 v12, 0x10000, v199
	v_add_u32_e32 v28, 0x14000, v199
	ds_read_b128 v[0:3], v12
	ds_read_b128 v[4:7], v12 offset:1024
	ds_read_b128 v[8:11], v12 offset:2048
	ds_read_b128 v[12:15], v12 offset:3072
	ds_read_b128 v[16:19], v28
	ds_read_b128 v[20:23], v28 offset:1024
	ds_read_b128 v[24:27], v28 offset:2048
	ds_read_b128 v[28:31], v28 offset:3072
	s_add_i32 s6, s67, 0x80
	s_cmp_eq_u32 s65, s85
	s_cselect_b32 s54, s66, s6
	s_cselect_b64 vcc, -1, 0
	v_cndmask_b32_e32 v211, v210, v201, vcc
	s_or_b32 s78, s54, 0x80
	s_add_i32 s6, s41, s67
	s_mov_b32 m0, s76
	ds_read_b128 v[32:35], v200
	ds_read_b128 v[36:39], v200 offset:1024
	ds_read_b128 v[40:43], v200 offset:2048
	ds_read_b128 v[44:47], v200 offset:3072
	ds_read_b128 v[48:51], v200 offset:4096
	ds_read_b128 v[52:55], v200 offset:5120
	ds_read_b128 v[56:59], v200 offset:6144
	ds_read_b128 v[60:63], v200 offset:7168
	v_readfirstlane_b32 s55, v211
	s_add_i32 s20, s55, s41
	buffer_load_dwordx4 v192, s[36:39], s6 offen lds
	s_mov_b32 m0, s77
	s_nop 0
	buffer_load_dwordx4 v195, s[36:39], s6 offen lds
	s_waitcnt vmcnt(24)
	s_waitcnt lgkmcnt(0)
	s_barrier
	s_setprio 1
	s_waitcnt lgkmcnt(6)
	v_mfma_scale_f32_16x16x128_f8f6f4 v[184:187], v[0:7], v[32:39], v[184:187], v224, v224 op_sel_hi:[0,0,0]
	v_mfma_scale_f32_16x16x128_f8f6f4 v[188:191], v[8:15], v[32:39], v[188:191], v224, v224 op_sel_hi:[0,0,0]
	s_waitcnt lgkmcnt(4)
	v_mfma_scale_f32_16x16x128_f8f6f4 v[168:171], v[0:7], v[40:47], v[168:171], v224, v224 op_sel_hi:[0,0,0]
	v_mfma_scale_f32_16x16x128_f8f6f4 v[172:175], v[8:15], v[40:47], v[172:175], v224, v224 op_sel_hi:[0,0,0]
	s_waitcnt lgkmcnt(2)
	v_mfma_scale_f32_16x16x128_f8f6f4 v[152:155], v[0:7], v[48:55], v[152:155], v224, v224 op_sel_hi:[0,0,0]
	v_mfma_scale_f32_16x16x128_f8f6f4 v[156:159], v[8:15], v[48:55], v[156:159], v224, v224 op_sel_hi:[0,0,0]
	s_waitcnt lgkmcnt(0)
	v_mfma_scale_f32_16x16x128_f8f6f4 v[136:139], v[0:7], v[56:63], v[136:139], v224, v224 op_sel_hi:[0,0,0]
	v_mfma_scale_f32_16x16x128_f8f6f4 v[140:143], v[8:15], v[56:63], v[140:143], v224, v224 op_sel_hi:[0,0,0]
	s_setprio 0
	s_setprio 1
	v_mfma_scale_f32_16x16x128_f8f6f4 v[176:179], v[16:23], v[32:39], v[176:179], v224, v224 op_sel_hi:[0,0,0]
	v_mfma_scale_f32_16x16x128_f8f6f4 v[180:183], v[24:31], v[32:39], v[180:183], v224, v224 op_sel_hi:[0,0,0]
	v_mfma_scale_f32_16x16x128_f8f6f4 v[160:163], v[16:23], v[40:47], v[160:163], v224, v224 op_sel_hi:[0,0,0]
	v_mfma_scale_f32_16x16x128_f8f6f4 v[164:167], v[24:31], v[40:47], v[164:167], v224, v224 op_sel_hi:[0,0,0]
	v_mfma_scale_f32_16x16x128_f8f6f4 v[144:147], v[16:23], v[48:55], v[144:147], v224, v224 op_sel_hi:[0,0,0]
	v_mfma_scale_f32_16x16x128_f8f6f4 v[148:151], v[24:31], v[48:55], v[148:151], v224, v224 op_sel_hi:[0,0,0]
	v_mfma_scale_f32_16x16x128_f8f6f4 v[128:131], v[16:23], v[56:63], v[128:131], v224, v224 op_sel_hi:[0,0,0]
	v_mfma_scale_f32_16x16x128_f8f6f4 v[132:135], v[24:31], v[56:63], v[132:135], v224, v224 op_sel_hi:[0,0,0]
	s_setprio 0
	s_barrier
; #define PG8_STAGE(bufoff, rs_, soff_, voff) do { _Pragma("unroll") for (int _i = 0; _i < 2; ++_i) \
;         __builtin_amdgcn_raw_ptr_buffer_load_lds(rs_, (LAS void*)(lds + (bufoff) + ldsw + _i * 8192), 16, (int)(voff)[_i], (int)(soff_), 0, 0); } while (0)
; #define PG8_LDA(dst, b, h) do { _Pragma("unroll") for (int m = 0; m < 4; ++m) dst[m] = PG8_LD2(lds + PG8_SA(b, h) + aoff + m * 2048); } while (0)
; #define PG8_LDB(dst, b, h) do { _Pragma("unroll") for (int n = 0; n < 2; ++n) dst[n] = PG8_LD2(lds + PG8_SB(b, h) + boff + n * 2048); } while (0)
; #define PG8_WAIT_V(n) asm volatile("s_waitcnt vmcnt(" #n ")" ::: "memory")
; #define PG8_WAIT_L(n) asm volatile("s_waitcnt lgkmcnt(" #n ")" ::: "memory")
; #define PG8_BAR __builtin_amdgcn_s_barrier()
; #define PG8_SCHED __builtin_amdgcn_sched_barrier(0)
; template <class Epi, class Sched, bool ALIGN_EPI = false, bool SP2 = false, bool FP8 = false>
; __device__ __forceinline__ void gemm_phase(LAS unsigned char* lds, const Gemm g, const Sched& S, const Epi& E, int wbase) {
;     ...
;             PG8_LDA(At, 0, 1); PG8_STAGE(PG8_SB(0, 0), rB2, b2, voffB); PG8_STAGE(PG8_SB(0, 1), rB2, b2 + hstep, voffB); PG8_STAGE(PG8_SA(0, 0), rA2, a2, voffA);
;             PG8_WAIT_V(8); PG8_WAIT_L(0); PG8_BAR; PG8_MMA(1, 0, At, B0); PG8_MMA(1, 1, At, B1); PG8_BAR; PG8_SCHED;
;             PG8_LDB(B0, 1, 0); PG8_LDB(B1, 1, 1); PG8_SCHED; PG8_LDA(At, 1, 0); PG8_STAGE(PG8_SA(0, 1), rA2, a2 + hstep, voffA);
;             PG8_WAIT_V(8); PG8_WAIT_L(0); PG8_BAR; PG8_MMA(0, 0, At, B0); PG8_MMA(0, 1, At, B1); PG8_BAR; PG8_SCHED;
	ds_read_b128 v[32:35], v200 offset:16384
	ds_read_b128 v[36:39], v200 offset:17408
	ds_read_b128 v[40:43], v200 offset:18432
	ds_read_b128 v[44:47], v200 offset:19456
	ds_read_b128 v[48:51], v200 offset:20480
	ds_read_b128 v[52:55], v200 offset:21504
	ds_read_b128 v[56:59], v200 offset:22528
	ds_read_b128 v[60:63], v200 offset:23552
	s_mov_b32 s6, s38
	s_mov_b32 s7, s39
	s_mov_b32 m0, s43
	s_nop 0
	buffer_load_dwordx4 v194, s[4:7], s55 offen lds
	s_mov_b32 m0, s44
	s_nop 0
	buffer_load_dwordx4 v196, s[4:7], s55 offen lds
	s_mov_b32 m0, s45
	s_nop 0
	buffer_load_dwordx4 v194, s[4:7], s20 offen lds
	s_mov_b32 m0, s46
	s_nop 0
	buffer_load_dwordx4 v196, s[4:7], s20 offen lds
	s_mov_b32 m0, s42
	s_nop 0
	buffer_load_dwordx4 v192, s[36:39], s54 offen lds
	s_mov_b32 m0, s47
	s_nop 0
	buffer_load_dwordx4 v195, s[36:39], s54 offen lds
	s_waitcnt vmcnt(24)
	s_waitcnt lgkmcnt(0)
	s_barrier
	s_setprio 1
	s_waitcnt lgkmcnt(6)
	v_mfma_scale_f32_16x16x128_f8f6f4 v[120:123], v[0:7], v[32:39], v[120:123], v224, v224 op_sel_hi:[0,0,0]
	v_mfma_scale_f32_16x16x128_f8f6f4 v[124:127], v[8:15], v[32:39], v[124:127], v224, v224 op_sel_hi:[0,0,0]
	s_waitcnt lgkmcnt(4)
	v_mfma_scale_f32_16x16x128_f8f6f4 v[104:107], v[0:7], v[40:47], v[104:107], v224, v224 op_sel_hi:[0,0,0]
	v_mfma_scale_f32_16x16x128_f8f6f4 v[108:111], v[8:15], v[40:47], v[108:111], v224, v224 op_sel_hi:[0,0,0]
	s_waitcnt lgkmcnt(2)
	v_mfma_scale_f32_16x16x128_f8f6f4 v[88:91], v[0:7], v[48:55], v[88:91], v224, v224 op_sel_hi:[0,0,0]
	v_mfma_scale_f32_16x16x128_f8f6f4 v[92:95], v[8:15], v[48:55], v[92:95], v224, v224 op_sel_hi:[0,0,0]
	s_waitcnt lgkmcnt(0)
	v_mfma_scale_f32_16x16x128_f8f6f4 v[72:75], v[0:7], v[56:63], v[72:75], v224, v224 op_sel_hi:[0,0,0]
	v_mfma_scale_f32_16x16x128_f8f6f4 v[76:79], v[8:15], v[56:63], v[76:79], v224, v224 op_sel_hi:[0,0,0]
	s_setprio 0
	s_setprio 1
	v_mfma_scale_f32_16x16x128_f8f6f4 v[112:115], v[16:23], v[32:39], v[112:115], v224, v224 op_sel_hi:[0,0,0]
	v_mfma_scale_f32_16x16x128_f8f6f4 v[116:119], v[24:31], v[32:39], v[116:119], v224, v224 op_sel_hi:[0,0,0]
	v_mfma_scale_f32_16x16x128_f8f6f4 v[96:99], v[16:23], v[40:47], v[96:99], v224, v224 op_sel_hi:[0,0,0]
	v_mfma_scale_f32_16x16x128_f8f6f4 v[100:103], v[24:31], v[40:47], v[100:103], v224, v224 op_sel_hi:[0,0,0]
	v_mfma_scale_f32_16x16x128_f8f6f4 v[80:83], v[16:23], v[48:55], v[80:83], v224, v224 op_sel_hi:[0,0,0]
	v_mfma_scale_f32_16x16x128_f8f6f4 v[84:87], v[24:31], v[48:55], v[84:87], v224, v224 op_sel_hi:[0,0,0]
	v_mfma_scale_f32_16x16x128_f8f6f4 v[68:71], v[16:23], v[56:63], v[68:71], v224, v224 op_sel_hi:[0,0,0]
	v_mfma_scale_f32_16x16x128_f8f6f4 v[64:67], v[24:31], v[56:63], v[64:67], v224, v224 op_sel_hi:[0,0,0]
	s_setprio 0
	s_barrier
	v_add_u32_e32 v12, 0x18000, v199
	v_add_u32_e32 v28, 0x1c000, v199
	ds_read_b128 v[0:3], v12
	ds_read_b128 v[4:7], v12 offset:1024
	ds_read_b128 v[8:11], v12 offset:2048
	ds_read_b128 v[12:15], v12 offset:3072
	ds_read_b128 v[16:19], v28
	ds_read_b128 v[20:23], v28 offset:1024
	ds_read_b128 v[24:27], v28 offset:2048
	ds_read_b128 v[28:31], v28 offset:3072
	s_add_i32 s54, s54, s41
	s_mov_b32 m0, s48
	ds_read_b128 v[32:35], v200 offset:32768
	ds_read_b128 v[36:39], v200 offset:33792
	ds_read_b128 v[40:43], v200 offset:34816
	ds_read_b128 v[44:47], v200 offset:35840
	ds_read_b128 v[48:51], v200 offset:36864
	ds_read_b128 v[52:55], v200 offset:37888
	ds_read_b128 v[56:59], v200 offset:38912
	ds_read_b128 v[60:63], v200 offset:39936
	buffer_load_dwordx4 v192, s[36:39], s54 offen lds
	s_mov_b32 m0, s52
	s_nop 0
	buffer_load_dwordx4 v195, s[36:39], s54 offen lds
	s_waitcnt vmcnt(8)
	s_waitcnt lgkmcnt(0)
	s_barrier
; #define PG8_STAGE(bufoff, rs_, soff_, voff) do { _Pragma("unroll") for (int _i = 0; _i < 2; ++_i) \
;         __builtin_amdgcn_raw_ptr_buffer_load_lds(rs_, (LAS void*)(lds + (bufoff) + ldsw + _i * 8192), 16, (int)(voff)[_i], (int)(soff_), 0, 0); } while (0)
; #define PG8_LDA(dst, b, h) do { _Pragma("unroll") for (int m = 0; m < 4; ++m) dst[m] = PG8_LD2(lds + PG8_SA(b, h) + aoff + m * 2048); } while (0)
; #define PG8_WAIT_V(n) asm volatile("s_waitcnt vmcnt(" #n ")" ::: "memory")
; #define PG8_WAIT_L(n) asm volatile("s_waitcnt lgkmcnt(" #n ")" ::: "memory")
; #define PG8_BAR __builtin_amdgcn_s_barrier()
; #define PG8_SCHED __builtin_amdgcn_sched_barrier(0)
; template <class Epi, class Sched, bool ALIGN_EPI = false, bool SP2 = false, bool FP8 = false>
; __device__ __forceinline__ void gemm_phase(LAS unsigned char* lds, const Gemm g, const Sched& S, const Epi& E, int wbase) {
;     ...
;             PG8_WAIT_V(8); PG8_WAIT_L(0); PG8_BAR; PG8_MMA(0, 0, At, B0); PG8_MMA(0, 1, At, B1); PG8_BAR; PG8_SCHED;
;             PG8_LDA(At, 1, 1); PG8_STAGE(PG8_SB(1, 0), rB2, b3, voffB); PG8_STAGE(PG8_SB(1, 1), rB2, b3 + hstep, voffB); PG8_STAGE(PG8_SA(1, 0), rA2, a3, voffA);
;             PG8_WAIT_V(8); PG8_WAIT_L(0); PG8_BAR; PG8_MMA(1, 0, At, B0); PG8_MMA(1, 1, At, B1); PG8_BAR; PG8_SCHED;
	s_setprio 1
	s_waitcnt lgkmcnt(6)
	v_mfma_scale_f32_16x16x128_f8f6f4 v[184:187], v[0:7], v[32:39], v[184:187], v224, v224 op_sel_hi:[0,0,0]
	v_mfma_scale_f32_16x16x128_f8f6f4 v[188:191], v[8:15], v[32:39], v[188:191], v224, v224 op_sel_hi:[0,0,0]
	s_waitcnt lgkmcnt(4)
	v_mfma_scale_f32_16x16x128_f8f6f4 v[168:171], v[0:7], v[40:47], v[168:171], v224, v224 op_sel_hi:[0,0,0]
	v_mfma_scale_f32_16x16x128_f8f6f4 v[172:175], v[8:15], v[40:47], v[172:175], v224, v224 op_sel_hi:[0,0,0]
	s_waitcnt lgkmcnt(2)
	v_mfma_scale_f32_16x16x128_f8f6f4 v[152:155], v[0:7], v[48:55], v[152:155], v224, v224 op_sel_hi:[0,0,0]
	v_mfma_scale_f32_16x16x128_f8f6f4 v[156:159], v[8:15], v[48:55], v[156:159], v224, v224 op_sel_hi:[0,0,0]
	s_waitcnt lgkmcnt(0)
	v_mfma_scale_f32_16x16x128_f8f6f4 v[136:139], v[0:7], v[56:63], v[136:139], v224, v224 op_sel_hi:[0,0,0]
	v_mfma_scale_f32_16x16x128_f8f6f4 v[140:143], v[8:15], v[56:63], v[140:143], v224, v224 op_sel_hi:[0,0,0]
	s_setprio 0
	s_setprio 1
	v_mfma_scale_f32_16x16x128_f8f6f4 v[176:179], v[16:23], v[32:39], v[176:179], v224, v224 op_sel_hi:[0,0,0]
	v_mfma_scale_f32_16x16x128_f8f6f4 v[180:183], v[24:31], v[32:39], v[180:183], v224, v224 op_sel_hi:[0,0,0]
	v_mfma_scale_f32_16x16x128_f8f6f4 v[160:163], v[16:23], v[40:47], v[160:163], v224, v224 op_sel_hi:[0,0,0]
	v_mfma_scale_f32_16x16x128_f8f6f4 v[164:167], v[24:31], v[40:47], v[164:167], v224, v224 op_sel_hi:[0,0,0]
	v_mfma_scale_f32_16x16x128_f8f6f4 v[144:147], v[16:23], v[48:55], v[144:147], v224, v224 op_sel_hi:[0,0,0]
	v_mfma_scale_f32_16x16x128_f8f6f4 v[148:151], v[24:31], v[48:55], v[148:151], v224, v224 op_sel_hi:[0,0,0]
	v_mfma_scale_f32_16x16x128_f8f6f4 v[128:131], v[16:23], v[56:63], v[128:131], v224, v224 op_sel_hi:[0,0,0]
	v_mfma_scale_f32_16x16x128_f8f6f4 v[132:135], v[24:31], v[56:63], v[132:135], v224, v224 op_sel_hi:[0,0,0]
	s_setprio 0
	s_barrier
	ds_read_b128 v[32:35], v200 offset:49152
	ds_read_b128 v[36:39], v200 offset:50176
	ds_read_b128 v[40:43], v200 offset:51200
	ds_read_b128 v[44:47], v200 offset:52224
	ds_read_b128 v[48:51], v200 offset:53248
	ds_read_b128 v[52:55], v200 offset:54272
	ds_read_b128 v[56:59], v200 offset:55296
	ds_read_b128 v[60:63], v200 offset:56320
	s_addk_i32 s55, 0x80
	s_addk_i32 s20, 0x80
	s_mov_b32 m0, s57
	s_nop 0
	buffer_load_dwordx4 v194, s[4:7], s55 offen lds
	s_mov_b32 m0, s58
	s_nop 0
	buffer_load_dwordx4 v196, s[4:7], s55 offen lds
	s_mov_b32 m0, s61
	s_nop 0
	buffer_load_dwordx4 v194, s[4:7], s20 offen lds
	s_mov_b32 m0, s62
	s_nop 0
	buffer_load_dwordx4 v196, s[4:7], s20 offen lds
	s_mov_b32 m0, s59
	s_nop 0
	buffer_load_dwordx4 v192, s[36:39], s78 offen lds
	s_mov_b32 m0, s60
	s_nop 0
	buffer_load_dwordx4 v195, s[36:39], s78 offen lds
	s_waitcnt vmcnt(8)
	s_waitcnt lgkmcnt(0)
	s_barrier
	s_setprio 1
	s_waitcnt lgkmcnt(6)
	v_mfma_scale_f32_16x16x128_f8f6f4 v[120:123], v[0:7], v[32:39], v[120:123], v224, v224 op_sel_hi:[0,0,0]
	v_mfma_scale_f32_16x16x128_f8f6f4 v[124:127], v[8:15], v[32:39], v[124:127], v224, v224 op_sel_hi:[0,0,0]
	s_waitcnt lgkmcnt(4)
	v_mfma_scale_f32_16x16x128_f8f6f4 v[104:107], v[0:7], v[40:47], v[104:107], v224, v224 op_sel_hi:[0,0,0]
	v_mfma_scale_f32_16x16x128_f8f6f4 v[108:111], v[8:15], v[40:47], v[108:111], v224, v224 op_sel_hi:[0,0,0]
	s_waitcnt lgkmcnt(2)
	v_mfma_scale_f32_16x16x128_f8f6f4 v[88:91], v[0:7], v[48:55], v[88:91], v224, v224 op_sel_hi:[0,0,0]
	v_mfma_scale_f32_16x16x128_f8f6f4 v[92:95], v[8:15], v[48:55], v[92:95], v224, v224 op_sel_hi:[0,0,0]
	s_waitcnt lgkmcnt(0)
	v_mfma_scale_f32_16x16x128_f8f6f4 v[72:75], v[0:7], v[56:63], v[72:75], v224, v224 op_sel_hi:[0,0,0]
	v_mfma_scale_f32_16x16x128_f8f6f4 v[76:79], v[8:15], v[56:63], v[76:79], v224, v224 op_sel_hi:[0,0,0]
	s_setprio 0
	s_setprio 1
	v_mfma_scale_f32_16x16x128_f8f6f4 v[112:115], v[16:23], v[32:39], v[112:115], v224, v224 op_sel_hi:[0,0,0]
	v_mfma_scale_f32_16x16x128_f8f6f4 v[116:119], v[24:31], v[32:39], v[116:119], v224, v224 op_sel_hi:[0,0,0]
	v_mfma_scale_f32_16x16x128_f8f6f4 v[96:99], v[16:23], v[40:47], v[96:99], v224, v224 op_sel_hi:[0,0,0]
	v_mfma_scale_f32_16x16x128_f8f6f4 v[100:103], v[24:31], v[40:47], v[100:103], v224, v224 op_sel_hi:[0,0,0]
	v_mfma_scale_f32_16x16x128_f8f6f4 v[80:83], v[16:23], v[48:55], v[80:83], v224, v224 op_sel_hi:[0,0,0]
	v_mfma_scale_f32_16x16x128_f8f6f4 v[84:87], v[24:31], v[48:55], v[84:87], v224, v224 op_sel_hi:[0,0,0]
	v_mfma_scale_f32_16x16x128_f8f6f4 v[68:71], v[16:23], v[56:63], v[68:71], v224, v224 op_sel_hi:[0,0,0]
	v_mfma_scale_f32_16x16x128_f8f6f4 v[64:67], v[24:31], v[56:63], v[64:67], v224, v224 op_sel_hi:[0,0,0]
	s_setprio 0
	s_barrier
	s_add_i32 s85, s85, 2
	s_addk_i32 s67, 0x100
	s_cmp_ge_i32 s85, s53
	v_add_u32_e32 v210, 0x100, v210
	s_cbranch_scc0 .LBB0_1348
	s_branch .Lmup_after

; #define PG8_BAR __builtin_amdgcn_s_barrier()
; #define PG8_ZERO_ACC() do { float z_; asm volatile("v_mov_b32 %0, 0" : "=v"(z_)); _Pragma("unroll") for (int a = 0; a < 2; ++a) _Pragma("unroll") for (int b = 0; b < 2; ++b) _Pragma("unroll") for (int m = 0; m < 4; ++m) \
;         _Pragma("unroll") for (int n = 0; n < 2; ++n) acc[a][b][m][n] = (f32x4){z_, z_, z_, z_}; } while (0)
; template <class Epi, class Sched, bool ALIGN_EPI = false, bool SP2 = false, bool FP8 = false>
; __device__ __forceinline__ void gemm_phase(LAS unsigned char* lds, const Gemm g, const Sched& S, const Epi& E, int wbase) {
;     ...
;         }
;         if constexpr (ALIGN_EPI) { if (wr == 0) PG8_BAR; }
;         { int fr_ = fr, fq_ = fq; asm volatile("" : "+v"(fr_), "+v"(fq_));
;           if constexpr (Epi::HAS_PRE) E(acc, cur, wr, wc, fr_, fq_, pre_); else E(acc, cur, wr, wc, fr_, fq_); } S.done(cur);
;         if (!has_next) break;
;         if (E.reset(cur)) PG8_ZERO_ACC();
.Lmup_after:
	s_mov_b32 s100, 1
	v_readlane_b32 s54, v255, 25
	v_readlane_b32 s55, v255, 26
	s_and_b64 vcc, exec, s[18:19]
	s_cbranch_vccnz .LBB0_1367
	s_branch .LBB0_1368

;     __device__ __forceinline__ unsigned a_off(const Unit& u, const Gemm& g) const { return (unsigned)u.pm * (unsigned)(BM * 2) * (unsigned)g.K; }
;     __device__ __forceinline__ unsigned b_off(const Unit& u, const Gemm& g) const { return (unsigned)u.pn * (unsigned)(BM * 2) * (unsigned)g.K; }
;     __device__ __forceinline__ bool next(int i, Unit& u) const { return so.next(i, u); }
; template <class Epi, class Sched, bool ALIGN_EPI = false, bool SP2 = false, bool FP8 = false>
; __device__ __forceinline__ void gemm_phase(LAS unsigned char* lds, const Gemm g, const Sched& S, const Epi& E, int wbase) {
;     ...
;     for (int i = 0; i < 2; ++i) { int R, C; stage_rc(tid * 16 + i * 8192, R, C); const int Rb = Epi::PERM ? ((R & ~31) + perm32(R & 31)) : R;
;         voffA[i] = (unsigned)(R * K + C) * 2u; voffB[i] = (unsigned)(Rb * K + C) * 2u; }
;     const unsigned kstep = (unsigned)(BK * 2);
;     const unsigned hstep = (unsigned)HALF * (unsigned)K * 2u;
;     typedef __amdgpu_buffer_rsrc_t rsrc_t;
;     const rsrc_t rA0 = __builtin_amdgcn_make_buffer_rsrc((void*)g.A, 0, 0xffffffff, 0x00020000), rB0 = __builtin_amdgcn_make_buffer_rsrc((void*)g.Bt, 0, 0xffffffff, 0x00020000);
;     rsrc_t rA1 = rA0, rB1 = rB0;
;     if constexpr (Sched::TWO) { rA1 = __builtin_amdgcn_make_buffer_rsrc((void*)S.A1, 0, 0xffffffff, 0x00020000); rB1 = __builtin_amdgcn_make_buffer_rsrc((void*)S.Bt1, 0, 0xffffffff, 0x00020000); }
;     const unsigned ldsw = (unsigned)wid * 1024u;
;     const int aoff = lds_byte(wr * 64 + fr, fq * 8), boff = lds_byte(wc * 32 + fr, fq * 8);
;     ...
;     Unit cur, nxt; int ui = 0;
;     if (!S.next(0, cur)) return;
;     f32x4 acc[2][2][4][2];
;     ...
;     PG8_ZERO_ACC();
;     v8i_t At[4], B0[2], B1[2];
;     unsigned cA = S.a_off(cur, g), cB = S.b_off(cur, g); rsrc_t rAc = (Sched::TWO && cur.part) ? rA1 : rA0, rBc = (Sched::TWO && cur.part) ? rB1 : rB0;
;     S.a_ready(cur);
;     if constexpr (SP2) {
;         PG8_STAGE(PG8_SB(0, 0), rBc, cB, voffB); PG8_STAGE(PG8_SB(0, 1), rBc, cB + hstep, voffB); PG8_STAGE(PG8_SA(0, 0), rAc, cA, voffA); PG8_STAGE(PG8_SA(0, 1), rAc, cA + hstep, voffA);
;         if (wr == 1) PG8_BAR;
;         PG8_WAIT_V(2); PG8_BAR;
;         PG8_STAGE(PG8_SB(1, 0), rBc, cB + kstep, voffB); PG8_STAGE(PG8_SA(1, 0), rAc, cA + kstep, voffA); PG8_STAGE(PG8_SB(1, 1), rBc, cB + hstep + kstep, voffB);
;         PG8_WAIT_V(6); PG8_BAR;
.LBB0_1621:
	v_readlane_b32 s6, v255, 11
	s_cmp_eq_u32 s6, 1
	s_cselect_b32 s6, 0, 0x200000
	s_add_u32 s8, s10, 0x1f800000
	s_addc_u32 s9, s11, 0
	s_add_u32 s6, s10, s6
	s_addc_u32 s7, s11, 0
	s_add_u32 s10, s6, 0x17200000
	s_addc_u32 s11, s7, 0
	s_add_i32 s31, s23, 0x18000
	s_or_b32 s18, s54, 0x80
	s_mov_b32 s6, s38
	s_mov_b32 s7, s39
	s_mov_b32 m0, s31
	s_add_i32 s33, s23, 0x1a000
	s_waitcnt vmcnt(2)
	s_barrier
	buffer_load_dwordx4 v141, s[4:7], s18 offen lds
	s_mov_b32 m0, s33
	s_add_i32 s34, s23, 0x8000
	buffer_load_dwordx4 v149, s[4:7], s18 offen lds
	s_or_b32 s18, s55, 0x80
	s_mov_b32 m0, s34
	s_add_i32 s35, s23, 0xa000
	buffer_load_dwordx4 v137, s[36:39], s18 offen lds
	s_mov_b32 m0, s35
	s_add_i32 s41, s23, 0x1c000
	buffer_load_dwordx4 v145, s[36:39], s18 offen lds
	s_bitset1_b32 s16, 7
	s_mov_b32 m0, s41
	s_add_i32 s42, s23, 0x1e000
	buffer_load_dwordx4 v141, s[4:7], s16 offen lds
	s_mov_b32 m0, s42
	v_bfe_u32 v157, v4, 4, 2
	buffer_load_dwordx4 v149, s[4:7], s16 offen lds
	s_ashr_i32 s6, s12, 31
	s_lshr_b32 s6, s6, 26
	v_and_b32_e32 v153, 15, v4
	s_add_i32 s6, s12, s6
	v_lshlrev_b32_e32 v5, 4, v157
	v_lshlrev_b32_e32 v4, 2, v4
	s_ashr_i32 s44, s6, 6
	v_lshl_or_b32 v5, v153, 6, v5
	s_lshl_b32 s6, s13, 13
	v_and_b32_e32 v4, 32, v4
	v_bitop3_b32 v6, v5, s6, v4 bitop3:0xde
	s_lshl_b32 s6, s15, 5
	s_and_b32 s6, s6, 0x60
	s_lshl_b32 s45, s13, 6
	s_lshl_b32 s7, s6, 7
	s_cmp_gt_i32 s12, 63
	s_waitcnt vmcnt(6)
	s_cselect_b64 s[12:13], -1, 0
	s_add_i32 s46, s44, -2
	s_add_i32 s47, s23, 0xc000
	v_bitop3_b32 v4, v5, s7, v4 bitop3:0xde
	s_cmpk_lt_u32 s14, 0x100
	v_mov_b32_e32 v1, v0
	v_mov_b32_e32 v2, v0
	v_mov_b32_e32 v3, v0
	s_mov_b32 s43, 0
	s_cselect_b64 s[14:15], -1, 0
	s_add_i32 s48, s23, 0xe000
	v_add_u32_e32 v161, 0, v4
	v_add_u32_e32 v162, 0, v6
	s_lshl_b32 s16, s6, 1
	s_barrier
	s_mov_b32 s100, 0
	s_branch .LBB0_1624

;     __device__ __forceinline__ unsigned a_off(const Unit& u, const Gemm& g) const { return (unsigned)u.pm * (unsigned)(BM * 2) * (unsigned)g.K; }
;     __device__ __forceinline__ unsigned b_off(const Unit& u, const Gemm& g) const { return (unsigned)u.pn * (unsigned)(BM * 2) * (unsigned)g.K; }
;     __device__ __forceinline__ bool next(int i, Unit& u) const { return so.next(i, u); }
;     __device__ __forceinline__ unsigned a_off(const Unit& u, const Gemm& g) const { return (unsigned)u.pm * (unsigned)(BM * 2) * (unsigned)g.K; }
;     __device__ __forceinline__ bool next(int i, Unit& u) const { const bool ok = so.next(i >> 1, u); u.part = i & 1; return ok; }
;     __device__ __forceinline__ unsigned a_off(const Unit& u, const Gemm& g) const { return (unsigned)u.pm * (unsigned)(BM * 2) * (unsigned)g.K; }
;     __device__ __forceinline__ unsigned b_off(const Unit& u, const Gemm& g) const { return (unsigned)u.pn * (unsigned)(BM * 2) * (unsigned)g.K; }
; template <class Epi, class Sched, bool ALIGN_EPI = false, bool SP2 = false, bool FP8 = false>
; __device__ __forceinline__ void gemm_phase(LAS unsigned char* lds, const Gemm g, const Sched& S, const Epi& E, int wbase) {
;     ...
;         const bool has_next = S.next(ui + 1, nxt);
;         const unsigned nA = has_next ? S.a_off(nxt, g) : cA, nB = has_next ? S.b_off(nxt, g) : cB;
;         const rsrc_t rAn = (Sched::TWO && has_next) ? (nxt.part ? rA1 : rA0) : rAc, rBn = (Sched::TWO && has_next) ? (nxt.part ? rB1 : rB0) : rBc;
;         float pre_[8] = {0.f, 0.f, 0.f, 0.f, 0.f, 0.f, 0.f, 0.f};
;         if constexpr (Epi::HAS_PRE) E.pre_load(pre_, cur, wr);
;         for (int t = 0; t < nt; t += 2) {
;             const bool last = (t == nt - 2);
;             const unsigned a1 = cA + (unsigned)(t + 1) * kstep;
;             const unsigned a2 = last ? nA : cA + (unsigned)(t + 2) * kstep, b2 = last ? nB : cB + (unsigned)(t + 2) * kstep; const rsrc_t rA2 = (Sched::TWO && last) ? rAn : rAc, rB2 = (Sched::TWO && last) ? rBn : rBc;
;             const unsigned a3 = a2 + kstep, b3 = b2 + kstep;
;             if (last && has_next) S.a_ready(nxt);
;             if constexpr (SP2) {
;             PG8_LDB(B0, 0, 0); PG8_LDB(B1, 0, 1); PG8_SCHED; PG8_LDA(At, 0, 0); PG8_STAGE(PG8_SA(1, 1), rAc, a1 + hstep, voffA);
;             PG8_WAIT_V(8); PG8_WAIT_L(0); PG8_BAR; PG8_MMA(0, 0, At, B0); PG8_MMA(0, 1, At, B1); PG8_BAR; PG8_SCHED;
.LBB0_1626:
	s_lshl_b32 s56, s53, 19
	s_andn2_b64 vcc, exec, s[12:13]
	s_lshl_b32 s57, s52, 19
	s_cbranch_vccnz .LBB0_1634
	s_and_b64 s[6:7], s[18:19], exec
	v_mov_b64_e32 v[6:7], v[2:3]
	v_mov_b64_e32 v[22:23], v[2:3]
	v_mov_b64_e32 v[18:19], v[2:3]
	v_mov_b64_e32 v[38:39], v[2:3]
	v_mov_b64_e32 v[34:35], v[2:3]
	v_mov_b64_e32 v[54:55], v[2:3]
	v_mov_b64_e32 v[50:51], v[2:3]
	v_mov_b64_e32 v[14:15], v[2:3]
	v_mov_b64_e32 v[10:11], v[2:3]
	v_mov_b64_e32 v[30:31], v[2:3]
	v_mov_b64_e32 v[26:27], v[2:3]
	v_mov_b64_e32 v[46:47], v[2:3]
	v_mov_b64_e32 v[42:43], v[2:3]
	s_waitcnt vmcnt(37)
	v_mov_b64_e32 v[62:63], v[2:3]
	v_mov_b64_e32 v[58:59], v[2:3]
	s_waitcnt vmcnt(35)
	v_mov_b64_e32 v[70:71], v[2:3]
	v_mov_b64_e32 v[66:67], v[2:3]
	s_waitcnt vmcnt(31)
	v_mov_b64_e32 v[86:87], v[2:3]
	v_mov_b64_e32 v[82:83], v[2:3]
	s_waitcnt vmcnt(27)
	v_mov_b64_e32 v[102:103], v[2:3]
	v_mov_b64_e32 v[98:99], v[2:3]
	s_waitcnt vmcnt(23)
	v_mov_b64_e32 v[118:119], v[2:3]
	v_mov_b64_e32 v[114:115], v[2:3]
	v_mov_b64_e32 v[78:79], v[2:3]
	v_mov_b64_e32 v[74:75], v[2:3]
	v_mov_b64_e32 v[94:95], v[2:3]
	v_mov_b64_e32 v[90:91], v[2:3]
	v_mov_b64_e32 v[110:111], v[2:3]
	v_mov_b64_e32 v[106:107], v[2:3]
	v_mov_b64_e32 v[126:127], v[2:3]
	s_waitcnt vmcnt(22)
	v_mov_b64_e32 v[122:123], v[2:3]
	s_cselect_b32 s59, s56, s55
	s_cselect_b32 s60, s57, s54
	s_add_i32 s61, s55, 0x80
	s_add_i32 s62, s54, 0x100
	s_mov_b32 s63, 0
	v_mov_b64_e32 v[4:5], v[0:1]
	v_mov_b64_e32 v[20:21], v[0:1]
	v_mov_b64_e32 v[16:17], v[0:1]
	v_mov_b64_e32 v[36:37], v[0:1]
	v_mov_b64_e32 v[32:33], v[0:1]
	v_mov_b64_e32 v[52:53], v[0:1]
	v_mov_b64_e32 v[48:49], v[0:1]
	v_mov_b64_e32 v[12:13], v[0:1]
	v_mov_b64_e32 v[8:9], v[0:1]
	v_mov_b64_e32 v[28:29], v[0:1]
	v_mov_b64_e32 v[24:25], v[0:1]
	v_mov_b64_e32 v[44:45], v[0:1]
	v_mov_b64_e32 v[40:41], v[0:1]
	v_mov_b64_e32 v[60:61], v[0:1]
	v_mov_b64_e32 v[56:57], v[0:1]
	v_mov_b64_e32 v[68:69], v[0:1]
	v_mov_b64_e32 v[64:65], v[0:1]
	v_mov_b64_e32 v[84:85], v[0:1]
	v_mov_b64_e32 v[80:81], v[0:1]
	v_mov_b64_e32 v[100:101], v[0:1]
	v_mov_b64_e32 v[96:97], v[0:1]
	v_mov_b64_e32 v[116:117], v[0:1]
	v_mov_b64_e32 v[112:113], v[0:1]
	v_mov_b64_e32 v[76:77], v[0:1]
	v_mov_b64_e32 v[72:73], v[0:1]
	v_mov_b64_e32 v[92:93], v[0:1]
	v_mov_b64_e32 v[88:89], v[0:1]
	v_mov_b64_e32 v[108:109], v[0:1]
	v_mov_b64_e32 v[104:105], v[0:1]
	v_mov_b64_e32 v[124:125], v[0:1]
	v_mov_b64_e32 v[120:121], v[0:1]
	s_cmp_eq_u32 s100, 1
	s_cbranch_scc0 .LBB0_1628
	v_add_u32_e32 v136, 0x10000, v161
	ds_read_b128 v[128:131], v136
	ds_read_b128 v[132:135], v136 offset:1024
	ds_read_b128 v[164:167], v136 offset:2048
	ds_read_b128 v[168:171], v136 offset:3072
	v_add_u32_e32 v136, 0x14000, v161
	ds_read_b128 v[172:175], v136
	ds_read_b128 v[176:179], v136 offset:1024
	ds_read_b128 v[180:183], v136 offset:2048
	ds_read_b128 v[184:187], v136 offset:3072
	s_add_i32 s6, s61, 0x80
	s_cmp_eq_u32 s46, s63
	s_cselect_b32 s65, s59, s6
	s_cselect_b32 s55, s60, s62
	s_or_b32 s54, s65, 0x80
	s_add_i32 s6, s22, s61
	s_mov_b32 m0, s47
	ds_read_b128 v[188:191], v162
	ds_read_b128 v[192:195], v162 offset:1024
	ds_read_b128 v[196:199], v162 offset:2048
	ds_read_b128 v[200:203], v162 offset:3072
	ds_read_b128 v[204:207], v162 offset:4096
	ds_read_b128 v[208:211], v162 offset:5120
	ds_read_b128 v[212:215], v162 offset:6144
	ds_read_b128 v[216:219], v162 offset:7168
	buffer_load_dwordx4 v137, s[36:39], s6 offen lds
	s_mov_b32 m0, s48
	s_nop 0
	buffer_load_dwordx4 v145, s[36:39], s6 offen lds
	s_waitcnt vmcnt(24)
	s_waitcnt lgkmcnt(0)
	s_barrier
	s_setprio 1
	s_waitcnt lgkmcnt(7)
	v_mfma_f32_16x16x32_bf16 v[120:123], v[128:131], v[188:191], v[120:123]
	v_mfma_f32_16x16x32_bf16 v[124:127], v[164:167], v[188:191], v[124:127]
	s_waitcnt lgkmcnt(5)
	v_mfma_f32_16x16x32_bf16 v[104:107], v[128:131], v[196:199], v[104:107]
	v_mfma_f32_16x16x32_bf16 v[108:111], v[164:167], v[196:199], v[108:111]
	s_waitcnt lgkmcnt(3)
	v_mfma_f32_16x16x32_bf16 v[88:91], v[128:131], v[204:207], v[88:91]
	v_mfma_f32_16x16x32_bf16 v[92:95], v[164:167], v[204:207], v[92:95]
	s_waitcnt lgkmcnt(1)
	v_mfma_f32_16x16x32_bf16 v[72:75], v[128:131], v[212:215], v[72:75]
	v_mfma_f32_16x16x32_bf16 v[76:79], v[164:167], v[212:215], v[76:79]
	v_mfma_f32_16x16x32_bf16 v[120:123], v[132:135], v[192:195], v[120:123]
	v_mfma_f32_16x16x32_bf16 v[124:127], v[168:171], v[192:195], v[124:127]
	v_mfma_f32_16x16x32_bf16 v[104:107], v[132:135], v[200:203], v[104:107]
	v_mfma_f32_16x16x32_bf16 v[108:111], v[168:171], v[200:203], v[108:111]
	v_mfma_f32_16x16x32_bf16 v[88:91], v[132:135], v[208:211], v[88:91]
	v_mfma_f32_16x16x32_bf16 v[92:95], v[168:171], v[208:211], v[92:95]
	s_waitcnt lgkmcnt(0)
	v_mfma_f32_16x16x32_bf16 v[72:75], v[132:135], v[216:219], v[72:75]
	v_mfma_f32_16x16x32_bf16 v[76:79], v[168:171], v[216:219], v[76:79]
	s_setprio 0
	s_setprio 1
	v_mfma_f32_16x16x32_bf16 v[112:115], v[172:175], v[188:191], v[112:115]
	v_mfma_f32_16x16x32_bf16 v[116:119], v[180:183], v[188:191], v[116:119]
	v_mfma_f32_16x16x32_bf16 v[96:99], v[172:175], v[196:199], v[96:99]
	v_mfma_f32_16x16x32_bf16 v[100:103], v[180:183], v[196:199], v[100:103]
	v_mfma_f32_16x16x32_bf16 v[80:83], v[172:175], v[204:207], v[80:83]
	v_mfma_f32_16x16x32_bf16 v[84:87], v[180:183], v[204:207], v[84:87]
	v_mfma_f32_16x16x32_bf16 v[64:67], v[172:175], v[212:215], v[64:67]
	v_mfma_f32_16x16x32_bf16 v[68:71], v[180:183], v[212:215], v[68:71]
	v_mfma_f32_16x16x32_bf16 v[112:115], v[176:179], v[192:195], v[112:115]
	v_mfma_f32_16x16x32_bf16 v[116:119], v[184:187], v[192:195], v[116:119]
	v_mfma_f32_16x16x32_bf16 v[96:99], v[176:179], v[200:203], v[96:99]
	v_mfma_f32_16x16x32_bf16 v[100:103], v[184:187], v[200:203], v[100:103]
	v_mfma_f32_16x16x32_bf16 v[80:83], v[176:179], v[208:211], v[80:83]
	v_mfma_f32_16x16x32_bf16 v[84:87], v[184:187], v[208:211], v[84:87]
	v_mfma_f32_16x16x32_bf16 v[64:67], v[176:179], v[216:219], v[64:67]
	v_mfma_f32_16x16x32_bf16 v[68:71], v[184:187], v[216:219], v[68:71]
	s_setprio 0
	s_barrier
; #define PG8_STAGE(bufoff, rs_, soff_, voff) do { _Pragma("unroll") for (int _i = 0; _i < 2; ++_i) \
;         __builtin_amdgcn_raw_ptr_buffer_load_lds(rs_, (LAS void*)(lds + (bufoff) + ldsw + _i * 8192), 16, (int)(voff)[_i], (int)(soff_), 0, 0); } while (0)
; #define PG8_LDA(dst, b, h) do { _Pragma("unroll") for (int m = 0; m < 4; ++m) dst[m] = PG8_LD2(lds + PG8_SA(b, h) + aoff + m * 2048); } while (0)
; #define PG8_LDB(dst, b, h) do { _Pragma("unroll") for (int n = 0; n < 2; ++n) dst[n] = PG8_LD2(lds + PG8_SB(b, h) + boff + n * 2048); } while (0)
; #define PG8_WAIT_V(n) asm volatile("s_waitcnt vmcnt(" #n ")" ::: "memory")
; #define PG8_WAIT_L(n) asm volatile("s_waitcnt lgkmcnt(" #n ")" ::: "memory")
; #define PG8_BAR __builtin_amdgcn_s_barrier()
; #define PG8_SCHED __builtin_amdgcn_sched_barrier(0)
; template <class Epi, class Sched, bool ALIGN_EPI = false, bool SP2 = false, bool FP8 = false>
; __device__ __forceinline__ void gemm_phase(LAS unsigned char* lds, const Gemm g, const Sched& S, const Epi& E, int wbase) {
;     ...
;             PG8_LDA(At, 0, 1); PG8_STAGE(PG8_SB(0, 0), rB2, b2, voffB); PG8_STAGE(PG8_SB(0, 1), rB2, b2 + hstep, voffB); PG8_STAGE(PG8_SA(0, 0), rA2, a2, voffA);
;             PG8_WAIT_V(8); PG8_WAIT_L(0); PG8_BAR; PG8_MMA(1, 0, At, B0); PG8_MMA(1, 1, At, B1); PG8_BAR; PG8_SCHED;
;             PG8_LDB(B0, 1, 0); PG8_LDB(B1, 1, 1); PG8_SCHED; PG8_LDA(At, 1, 0); PG8_STAGE(PG8_SA(0, 1), rA2, a2 + hstep, voffA);
;             PG8_WAIT_V(8); PG8_WAIT_L(0); PG8_BAR; PG8_MMA(0, 0, At, B0); PG8_MMA(0, 1, At, B1); PG8_BAR; PG8_SCHED;
	s_mov_b32 m0, s24
	s_mov_b32 s6, s38
	s_mov_b32 s7, s39
	ds_read_b128 v[188:191], v162 offset:16384
	ds_read_b128 v[192:195], v162 offset:17408
	ds_read_b128 v[196:199], v162 offset:18432
	ds_read_b128 v[200:203], v162 offset:19456
	ds_read_b128 v[204:207], v162 offset:20480
	ds_read_b128 v[208:211], v162 offset:21504
	ds_read_b128 v[212:215], v162 offset:22528
	ds_read_b128 v[216:219], v162 offset:23552
	buffer_load_dwordx4 v141, s[4:7], s55 offen lds
	s_mov_b32 m0, s25
	s_add_i32 s66, s55, s22
	buffer_load_dwordx4 v149, s[4:7], s55 offen lds
	s_mov_b32 m0, s26
	s_nop 0
	buffer_load_dwordx4 v141, s[4:7], s66 offen lds
	s_mov_b32 m0, s27
	s_nop 0
	buffer_load_dwordx4 v149, s[4:7], s66 offen lds
	s_mov_b32 m0, s23
	s_nop 0
	buffer_load_dwordx4 v137, s[36:39], s65 offen lds
	s_mov_b32 m0, s28
	s_nop 0
	buffer_load_dwordx4 v145, s[36:39], s65 offen lds
	s_waitcnt vmcnt(24)
	s_waitcnt lgkmcnt(0)
	s_barrier
	s_setprio 1
	s_waitcnt lgkmcnt(7)
	v_mfma_f32_16x16x32_bf16 v[56:59], v[128:131], v[188:191], v[56:59]
	v_mfma_f32_16x16x32_bf16 v[60:63], v[164:167], v[188:191], v[60:63]
	s_waitcnt lgkmcnt(5)
	v_mfma_f32_16x16x32_bf16 v[40:43], v[128:131], v[196:199], v[40:43]
	v_mfma_f32_16x16x32_bf16 v[44:47], v[164:167], v[196:199], v[44:47]
	s_waitcnt lgkmcnt(3)
	v_mfma_f32_16x16x32_bf16 v[24:27], v[128:131], v[204:207], v[24:27]
	v_mfma_f32_16x16x32_bf16 v[28:31], v[164:167], v[204:207], v[28:31]
	s_waitcnt lgkmcnt(1)
	v_mfma_f32_16x16x32_bf16 v[8:11], v[128:131], v[212:215], v[8:11]
	v_mfma_f32_16x16x32_bf16 v[12:15], v[164:167], v[212:215], v[12:15]
	v_mfma_f32_16x16x32_bf16 v[56:59], v[132:135], v[192:195], v[56:59]
	v_mfma_f32_16x16x32_bf16 v[60:63], v[168:171], v[192:195], v[60:63]
	v_mfma_f32_16x16x32_bf16 v[40:43], v[132:135], v[200:203], v[40:43]
	v_mfma_f32_16x16x32_bf16 v[44:47], v[168:171], v[200:203], v[44:47]
	v_mfma_f32_16x16x32_bf16 v[24:27], v[132:135], v[208:211], v[24:27]
	v_mfma_f32_16x16x32_bf16 v[28:31], v[168:171], v[208:211], v[28:31]
	s_waitcnt lgkmcnt(0)
	v_mfma_f32_16x16x32_bf16 v[8:11], v[132:135], v[216:219], v[8:11]
	v_mfma_f32_16x16x32_bf16 v[12:15], v[168:171], v[216:219], v[12:15]
	s_setprio 0
	s_setprio 1
	v_mfma_f32_16x16x32_bf16 v[48:51], v[172:175], v[188:191], v[48:51]
	v_mfma_f32_16x16x32_bf16 v[52:55], v[180:183], v[188:191], v[52:55]
	v_mfma_f32_16x16x32_bf16 v[32:35], v[172:175], v[196:199], v[32:35]
	v_mfma_f32_16x16x32_bf16 v[36:39], v[180:183], v[196:199], v[36:39]
	v_mfma_f32_16x16x32_bf16 v[16:19], v[172:175], v[204:207], v[16:19]
	v_mfma_f32_16x16x32_bf16 v[20:23], v[180:183], v[204:207], v[20:23]
	v_mfma_f32_16x16x32_bf16 v[4:7], v[172:175], v[212:215], v[4:7]
	v_mfma_f32_16x16x32_bf16 v[0:3], v[180:183], v[212:215], v[0:3]
	v_mfma_f32_16x16x32_bf16 v[48:51], v[176:179], v[192:195], v[48:51]
	v_mfma_f32_16x16x32_bf16 v[52:55], v[184:187], v[192:195], v[52:55]
	v_mfma_f32_16x16x32_bf16 v[32:35], v[176:179], v[200:203], v[32:35]
	v_mfma_f32_16x16x32_bf16 v[36:39], v[184:187], v[200:203], v[36:39]
	v_mfma_f32_16x16x32_bf16 v[16:19], v[176:179], v[208:211], v[16:19]
	v_mfma_f32_16x16x32_bf16 v[20:23], v[184:187], v[208:211], v[20:23]
	v_mfma_f32_16x16x32_bf16 v[4:7], v[176:179], v[216:219], v[4:7]
	v_mfma_f32_16x16x32_bf16 v[0:3], v[184:187], v[216:219], v[0:3]
	s_setprio 0
	s_barrier
	v_add_u32_e32 v136, 0x18000, v161
	ds_read_b128 v[128:131], v136
	ds_read_b128 v[132:135], v136 offset:1024
	ds_read_b128 v[164:167], v136 offset:2048
	ds_read_b128 v[168:171], v136 offset:3072
	v_add_u32_e32 v136, 0x1c000, v161
	ds_read_b128 v[172:175], v136
	ds_read_b128 v[176:179], v136 offset:1024
	ds_read_b128 v[180:183], v136 offset:2048
	ds_read_b128 v[184:187], v136 offset:3072
	s_add_i32 s65, s65, s22
	s_mov_b32 m0, s29
	ds_read_b128 v[188:191], v162 offset:32768
	ds_read_b128 v[192:195], v162 offset:33792
	ds_read_b128 v[196:199], v162 offset:34816
	ds_read_b128 v[200:203], v162 offset:35840
	ds_read_b128 v[204:207], v162 offset:36864
	ds_read_b128 v[208:211], v162 offset:37888
	ds_read_b128 v[212:215], v162 offset:38912
	ds_read_b128 v[216:219], v162 offset:39936
	buffer_load_dwordx4 v137, s[36:39], s65 offen lds
	s_mov_b32 m0, s30
	s_nop 0
	buffer_load_dwordx4 v145, s[36:39], s65 offen lds
	s_waitcnt vmcnt(8)
	s_waitcnt lgkmcnt(0)
	s_barrier
; #define PG8_STAGE(bufoff, rs_, soff_, voff) do { _Pragma("unroll") for (int _i = 0; _i < 2; ++_i) \
;         __builtin_amdgcn_raw_ptr_buffer_load_lds(rs_, (LAS void*)(lds + (bufoff) + ldsw + _i * 8192), 16, (int)(voff)[_i], (int)(soff_), 0, 0); } while (0)
; #define PG8_LDA(dst, b, h) do { _Pragma("unroll") for (int m = 0; m < 4; ++m) dst[m] = PG8_LD2(lds + PG8_SA(b, h) + aoff + m * 2048); } while (0)
; #define PG8_WAIT_V(n) asm volatile("s_waitcnt vmcnt(" #n ")" ::: "memory")
; #define PG8_WAIT_L(n) asm volatile("s_waitcnt lgkmcnt(" #n ")" ::: "memory")
; #define PG8_BAR __builtin_amdgcn_s_barrier()
; #define PG8_SCHED __builtin_amdgcn_sched_barrier(0)
; template <class Epi, class Sched, bool ALIGN_EPI = false, bool SP2 = false, bool FP8 = false>
; __device__ __forceinline__ void gemm_phase(LAS unsigned char* lds, const Gemm g, const Sched& S, const Epi& E, int wbase) {
;     ...
;             PG8_WAIT_V(8); PG8_WAIT_L(0); PG8_BAR; PG8_MMA(0, 0, At, B0); PG8_MMA(0, 1, At, B1); PG8_BAR; PG8_SCHED;
;             PG8_LDA(At, 1, 1); PG8_STAGE(PG8_SB(1, 0), rB2, b3, voffB); PG8_STAGE(PG8_SB(1, 1), rB2, b3 + hstep, voffB); PG8_STAGE(PG8_SA(1, 0), rA2, a3, voffA);
;             PG8_WAIT_V(8); PG8_WAIT_L(0); PG8_BAR; PG8_MMA(1, 0, At, B0); PG8_MMA(1, 1, At, B1); PG8_BAR; PG8_SCHED;
	s_setprio 1
	s_waitcnt lgkmcnt(7)
	v_mfma_f32_16x16x32_bf16 v[120:123], v[128:131], v[188:191], v[120:123]
	v_mfma_f32_16x16x32_bf16 v[124:127], v[164:167], v[188:191], v[124:127]
	s_waitcnt lgkmcnt(5)
	v_mfma_f32_16x16x32_bf16 v[104:107], v[128:131], v[196:199], v[104:107]
	v_mfma_f32_16x16x32_bf16 v[108:111], v[164:167], v[196:199], v[108:111]
	s_waitcnt lgkmcnt(3)
	v_mfma_f32_16x16x32_bf16 v[88:91], v[128:131], v[204:207], v[88:91]
	v_mfma_f32_16x16x32_bf16 v[92:95], v[164:167], v[204:207], v[92:95]
	s_waitcnt lgkmcnt(1)
	v_mfma_f32_16x16x32_bf16 v[72:75], v[128:131], v[212:215], v[72:75]
	v_mfma_f32_16x16x32_bf16 v[76:79], v[164:167], v[212:215], v[76:79]
	v_mfma_f32_16x16x32_bf16 v[120:123], v[132:135], v[192:195], v[120:123]
	v_mfma_f32_16x16x32_bf16 v[124:127], v[168:171], v[192:195], v[124:127]
	v_mfma_f32_16x16x32_bf16 v[104:107], v[132:135], v[200:203], v[104:107]
	v_mfma_f32_16x16x32_bf16 v[108:111], v[168:171], v[200:203], v[108:111]
	v_mfma_f32_16x16x32_bf16 v[88:91], v[132:135], v[208:211], v[88:91]
	v_mfma_f32_16x16x32_bf16 v[92:95], v[168:171], v[208:211], v[92:95]
	s_waitcnt lgkmcnt(0)
	v_mfma_f32_16x16x32_bf16 v[72:75], v[132:135], v[216:219], v[72:75]
	v_mfma_f32_16x16x32_bf16 v[76:79], v[168:171], v[216:219], v[76:79]
	s_setprio 0
	s_setprio 1
	v_mfma_f32_16x16x32_bf16 v[112:115], v[172:175], v[188:191], v[112:115]
	v_mfma_f32_16x16x32_bf16 v[116:119], v[180:183], v[188:191], v[116:119]
	v_mfma_f32_16x16x32_bf16 v[96:99], v[172:175], v[196:199], v[96:99]
	v_mfma_f32_16x16x32_bf16 v[100:103], v[180:183], v[196:199], v[100:103]
	v_mfma_f32_16x16x32_bf16 v[80:83], v[172:175], v[204:207], v[80:83]
	v_mfma_f32_16x16x32_bf16 v[84:87], v[180:183], v[204:207], v[84:87]
	v_mfma_f32_16x16x32_bf16 v[64:67], v[172:175], v[212:215], v[64:67]
	v_mfma_f32_16x16x32_bf16 v[68:71], v[180:183], v[212:215], v[68:71]
	v_mfma_f32_16x16x32_bf16 v[112:115], v[176:179], v[192:195], v[112:115]
	v_mfma_f32_16x16x32_bf16 v[116:119], v[184:187], v[192:195], v[116:119]
	v_mfma_f32_16x16x32_bf16 v[96:99], v[176:179], v[200:203], v[96:99]
	v_mfma_f32_16x16x32_bf16 v[100:103], v[184:187], v[200:203], v[100:103]
	v_mfma_f32_16x16x32_bf16 v[80:83], v[176:179], v[208:211], v[80:83]
	v_mfma_f32_16x16x32_bf16 v[84:87], v[184:187], v[208:211], v[84:87]
	v_mfma_f32_16x16x32_bf16 v[64:67], v[176:179], v[216:219], v[64:67]
	v_mfma_f32_16x16x32_bf16 v[68:71], v[184:187], v[216:219], v[68:71]
	s_setprio 0
	s_barrier
	s_mov_b32 m0, s31
	s_bitset1_b32 s55, 7
	ds_read_b128 v[188:191], v162 offset:49152
	ds_read_b128 v[192:195], v162 offset:50176
	ds_read_b128 v[196:199], v162 offset:51200
	ds_read_b128 v[200:203], v162 offset:52224
	ds_read_b128 v[204:207], v162 offset:53248
	ds_read_b128 v[208:211], v162 offset:54272
	ds_read_b128 v[212:215], v162 offset:55296
	ds_read_b128 v[216:219], v162 offset:56320
	buffer_load_dwordx4 v141, s[4:7], s55 offen lds
	s_mov_b32 m0, s33
	s_nop 0
	buffer_load_dwordx4 v149, s[4:7], s55 offen lds
	s_add_i32 s55, s55, s22
	s_mov_b32 m0, s41
	s_nop 0
	buffer_load_dwordx4 v141, s[4:7], s55 offen lds
	s_mov_b32 m0, s42
	s_nop 0
	buffer_load_dwordx4 v149, s[4:7], s55 offen lds
	s_mov_b32 m0, s34
	s_nop 0
	buffer_load_dwordx4 v137, s[36:39], s54 offen lds
	s_mov_b32 m0, s35
	s_nop 0
	buffer_load_dwordx4 v145, s[36:39], s54 offen lds
	s_waitcnt vmcnt(8)
	s_waitcnt lgkmcnt(0)
	s_barrier
	s_setprio 1
	s_waitcnt lgkmcnt(7)
	v_mfma_f32_16x16x32_bf16 v[56:59], v[128:131], v[188:191], v[56:59]
	v_mfma_f32_16x16x32_bf16 v[60:63], v[164:167], v[188:191], v[60:63]
	s_waitcnt lgkmcnt(5)
	v_mfma_f32_16x16x32_bf16 v[40:43], v[128:131], v[196:199], v[40:43]
	v_mfma_f32_16x16x32_bf16 v[44:47], v[164:167], v[196:199], v[44:47]
	s_waitcnt lgkmcnt(3)
	v_mfma_f32_16x16x32_bf16 v[24:27], v[128:131], v[204:207], v[24:27]
	v_mfma_f32_16x16x32_bf16 v[28:31], v[164:167], v[204:207], v[28:31]
	s_waitcnt lgkmcnt(1)
	v_mfma_f32_16x16x32_bf16 v[8:11], v[128:131], v[212:215], v[8:11]
	v_mfma_f32_16x16x32_bf16 v[12:15], v[164:167], v[212:215], v[12:15]
	v_mfma_f32_16x16x32_bf16 v[56:59], v[132:135], v[192:195], v[56:59]
	v_mfma_f32_16x16x32_bf16 v[60:63], v[168:171], v[192:195], v[60:63]
	v_mfma_f32_16x16x32_bf16 v[40:43], v[132:135], v[200:203], v[40:43]
	v_mfma_f32_16x16x32_bf16 v[44:47], v[168:171], v[200:203], v[44:47]
	v_mfma_f32_16x16x32_bf16 v[24:27], v[132:135], v[208:211], v[24:27]
	v_mfma_f32_16x16x32_bf16 v[28:31], v[168:171], v[208:211], v[28:31]
	s_waitcnt lgkmcnt(0)
	v_mfma_f32_16x16x32_bf16 v[8:11], v[132:135], v[216:219], v[8:11]
	v_mfma_f32_16x16x32_bf16 v[12:15], v[168:171], v[216:219], v[12:15]
	s_setprio 0
	s_setprio 1
	v_mfma_f32_16x16x32_bf16 v[48:51], v[172:175], v[188:191], v[48:51]
	v_mfma_f32_16x16x32_bf16 v[52:55], v[180:183], v[188:191], v[52:55]
	v_mfma_f32_16x16x32_bf16 v[32:35], v[172:175], v[196:199], v[32:35]
	v_mfma_f32_16x16x32_bf16 v[36:39], v[180:183], v[196:199], v[36:39]
	v_mfma_f32_16x16x32_bf16 v[16:19], v[172:175], v[204:207], v[16:19]
	v_mfma_f32_16x16x32_bf16 v[20:23], v[180:183], v[204:207], v[20:23]
	v_mfma_f32_16x16x32_bf16 v[4:7], v[172:175], v[212:215], v[4:7]
	v_mfma_f32_16x16x32_bf16 v[0:3], v[180:183], v[212:215], v[0:3]
	v_mfma_f32_16x16x32_bf16 v[48:51], v[176:179], v[192:195], v[48:51]
	v_mfma_f32_16x16x32_bf16 v[52:55], v[184:187], v[192:195], v[52:55]
	v_mfma_f32_16x16x32_bf16 v[32:35], v[176:179], v[200:203], v[32:35]
	v_mfma_f32_16x16x32_bf16 v[36:39], v[184:187], v[200:203], v[36:39]
	v_mfma_f32_16x16x32_bf16 v[16:19], v[176:179], v[208:211], v[16:19]
	v_mfma_f32_16x16x32_bf16 v[20:23], v[184:187], v[208:211], v[20:23]
	v_mfma_f32_16x16x32_bf16 v[4:7], v[176:179], v[216:219], v[4:7]
	v_mfma_f32_16x16x32_bf16 v[0:3], v[184:187], v[216:219], v[0:3]
	s_setprio 0
	s_barrier
	s_add_i32 s63, s63, 2
	s_addk_i32 s61, 0x100
	s_addk_i32 s62, 0x100
	s_cmp_ge_i32 s63, s44
	s_cbranch_scc0 .LBB0_1628
	s_branch .Lpeel_after_1628

; #define PG8_BAR __builtin_amdgcn_s_barrier()
; #define PG8_ZERO_ACC() do { float z_; asm volatile("v_mov_b32 %0, 0" : "=v"(z_)); _Pragma("unroll") for (int a = 0; a < 2; ++a) _Pragma("unroll") for (int b = 0; b < 2; ++b) _Pragma("unroll") for (int m = 0; m < 4; ++m) \
;         _Pragma("unroll") for (int n = 0; n < 2; ++n) acc[a][b][m][n] = (f32x4){z_, z_, z_, z_}; } while (0)
; template <class Epi, class Sched, bool ALIGN_EPI = false, bool SP2 = false, bool FP8 = false>
; __device__ __forceinline__ void gemm_phase(LAS unsigned char* lds, const Gemm g, const Sched& S, const Epi& E, int wbase) {
;     ...
;         }
;         if constexpr (ALIGN_EPI) { if (wr == 0) PG8_BAR; }
;         { int fr_ = fr, fq_ = fq; asm volatile("" : "+v"(fr_), "+v"(fq_));
;           if constexpr (Epi::HAS_PRE) E(acc, cur, wr, wc, fr_, fq_, pre_); else E(acc, cur, wr, wc, fr_, fq_); } S.done(cur);
;         if (!has_next) break;
;         if (E.reset(cur)) PG8_ZERO_ACC();
.Lpeel_after_1628:
	s_mov_b32 s100, 1
	s_and_b64 vcc, exec, s[14:15]
	s_cbranch_vccz .LBB0_1631

;     __device__ __forceinline__ unsigned a_off(const Unit& u, const Gemm& g) const { return (unsigned)u.pm * (unsigned)(BM * 2) * (unsigned)g.K; }
;     __device__ __forceinline__ unsigned b_off(const Unit& u, const Gemm& g) const { return (unsigned)u.pn * (unsigned)(BM * 2) * (unsigned)g.K; }
;     __device__ __forceinline__ bool next(int i, Unit& u) const { return so.next(i, u); }
; template <class Epi, class Sched, bool ALIGN_EPI = false, bool SP2 = false, bool FP8 = false>
; __device__ __forceinline__ void gemm_phase(LAS unsigned char* lds, const Gemm g, const Sched& S, const Epi& E, int wbase) {
;     ...
;     for (int i = 0; i < 2; ++i) { int R, C; stage_rc(tid * 16 + i * 8192, R, C); const int Rb = Epi::PERM ? ((R & ~31) + perm32(R & 31)) : R;
;         voffA[i] = (unsigned)(R * K + C) * 2u; voffB[i] = (unsigned)(Rb * K + C) * 2u; }
;     const unsigned kstep = (unsigned)(BK * 2);
;     const unsigned hstep = (unsigned)HALF * (unsigned)K * 2u;
;     typedef __amdgpu_buffer_rsrc_t rsrc_t;
;     const rsrc_t rA0 = __builtin_amdgcn_make_buffer_rsrc((void*)g.A, 0, 0xffffffff, 0x00020000), rB0 = __builtin_amdgcn_make_buffer_rsrc((void*)g.Bt, 0, 0xffffffff, 0x00020000);
;     rsrc_t rA1 = rA0, rB1 = rB0;
;     if constexpr (Sched::TWO) { rA1 = __builtin_amdgcn_make_buffer_rsrc((void*)S.A1, 0, 0xffffffff, 0x00020000); rB1 = __builtin_amdgcn_make_buffer_rsrc((void*)S.Bt1, 0, 0xffffffff, 0x00020000); }
;     const unsigned ldsw = (unsigned)wid * 1024u;
;     const int aoff = lds_byte(wr * 64 + fr, fq * 8), boff = lds_byte(wc * 32 + fr, fq * 8);
;     ...
;     Unit cur, nxt; int ui = 0;
;     if (!S.next(0, cur)) return;
;     f32x4 acc[2][2][4][2];
;     ...
;     PG8_ZERO_ACC();
;     v8i_t At[4], B0[2], B1[2];
;     unsigned cA = S.a_off(cur, g), cB = S.b_off(cur, g); rsrc_t rAc = (Sched::TWO && cur.part) ? rA1 : rA0, rBc = (Sched::TWO && cur.part) ? rB1 : rB0;
;     S.a_ready(cur);
;     if constexpr (SP2) {
;         PG8_STAGE(PG8_SB(0, 0), rBc, cB, voffB); PG8_STAGE(PG8_SB(0, 1), rBc, cB + hstep, voffB); PG8_STAGE(PG8_SA(0, 0), rAc, cA, voffA); PG8_STAGE(PG8_SA(0, 1), rAc, cA + hstep, voffA);
;         if (wr == 1) PG8_BAR;
;         PG8_WAIT_V(2); PG8_BAR;
;         PG8_STAGE(PG8_SB(1, 0), rBc, cB + kstep, voffB); PG8_STAGE(PG8_SA(1, 0), rAc, cA + kstep, voffA); PG8_STAGE(PG8_SB(1, 1), rBc, cB + hstep + kstep, voffB);
;         PG8_WAIT_V(6); PG8_BAR;
.LBB0_1690:
	s_add_u32 s8, s10, s1
	s_addc_u32 s9, s11, 0
	v_readlane_b32 s1, v255, 11
	s_cmp_eq_u32 s1, 0
	s_cselect_b32 s1, 0, 0x200000
	s_add_u32 s1, s10, s1
	s_addc_u32 s6, s11, 0
	s_add_u32 s10, s1, 0x17200000
	s_addc_u32 s11, s6, 0
	s_add_i32 s1, s26, 0x18000
	s_or_b32 s17, s54, 0x80
	s_mov_b32 s6, s38
	s_mov_b32 s7, s39
	s_mov_b32 m0, s1
	s_add_i32 s35, s26, 0x1a000
	s_waitcnt vmcnt(2)
	s_barrier
	buffer_load_dwordx4 v171, s[4:7], s17 offen lds
	s_mov_b32 m0, s35
	s_add_i32 s41, s26, 0x8000
	buffer_load_dwordx4 v173, s[4:7], s17 offen lds
	s_or_b32 s17, s55, 0x80
	s_mov_b32 m0, s41
	s_add_i32 s42, s26, 0xa000
	buffer_load_dwordx4 v170, s[36:39], s17 offen lds
	s_mov_b32 m0, s42
	s_add_i32 s43, s26, 0x1c000
	buffer_load_dwordx4 v172, s[36:39], s17 offen lds
	s_bitset1_b32 s16, 7
	s_mov_b32 m0, s43
	s_add_i32 s44, s26, 0x1e000
	buffer_load_dwordx4 v171, s[4:7], s16 offen lds
	s_mov_b32 m0, s44
	v_bfe_u32 v175, v4, 4, 2
	buffer_load_dwordx4 v173, s[4:7], s16 offen lds
	s_ashr_i32 s6, s14, 31
	s_lshr_b32 s6, s6, 26
	v_and_b32_e32 v174, 15, v4
	s_add_i32 s6, s14, s6
	v_lshlrev_b32_e32 v5, 4, v175
	v_lshlrev_b32_e32 v4, 2, v4
	s_and_b32 s46, s12, 3
	s_ashr_i32 s47, s6, 6
	v_lshl_or_b32 v5, v174, 6, v5
	s_lshl_b32 s6, s15, 13
	v_and_b32_e32 v4, 32, v4
	s_lshl_b32 s48, s15, 6
	v_bitop3_b32 v6, v5, s6, v4 bitop3:0xde
	s_lshl_b32 s12, s46, 5
	s_lshl_b32 s6, s46, 12
	s_cmp_gt_i32 s14, 63
	s_cselect_b64 s[14:15], -1, 0
	s_add_i32 s52, s47, -2
	s_add_i32 s53, s26, 0xc000
	s_cmpk_lt_u32 s13, 0x100
	v_bitop3_b32 v4, v5, s6, v4 bitop3:0xde
	s_waitcnt vmcnt(6)
	s_cselect_b64 s[16:17], -1, 0
	s_add_i32 s56, s26, 0xe000
	s_lshl_b32 s6, s46, 6
	s_add_u32 s57, s8, s6
	v_mov_b32_e32 v1, v0
	v_mov_b32_e32 v2, v0
	v_mov_b32_e32 v3, v0
	s_mov_b32 s45, 0
	s_mov_b32 s13, s40
	s_addc_u32 s58, s9, 0
	v_add_u32_e32 v176, 0, v4
	v_add_u32_e32 v177, 0, v6
	s_barrier
	s_mov_b32 s100, 0
	s_branch .LBB0_1693

;     __device__ __forceinline__ unsigned a_off(const Unit& u, const Gemm& g) const { return (unsigned)u.pm * (unsigned)(BM * 2) * (unsigned)g.K; }
;     __device__ __forceinline__ unsigned b_off(const Unit& u, const Gemm& g) const { return (unsigned)u.pn * (unsigned)(BM * 2) * (unsigned)g.K; }
;     __device__ __forceinline__ bool next(int i, Unit& u) const { return so.next(i, u); }
;     __device__ __forceinline__ unsigned a_off(const Unit& u, const Gemm& g) const { return (unsigned)u.pm * (unsigned)(BM * 2) * (unsigned)g.K; }
;     __device__ __forceinline__ bool next(int i, Unit& u) const { const bool ok = so.next(i >> 1, u); u.part = i & 1; return ok; }
;     __device__ __forceinline__ unsigned a_off(const Unit& u, const Gemm& g) const { return (unsigned)u.pm * (unsigned)(BM * 2) * (unsigned)g.K; }
;     __device__ __forceinline__ unsigned b_off(const Unit& u, const Gemm& g) const { return (unsigned)u.pn * (unsigned)(BM * 2) * (unsigned)g.K; }
; template <class Epi, class Sched, bool ALIGN_EPI = false, bool SP2 = false, bool FP8 = false>
; __device__ __forceinline__ void gemm_phase(LAS unsigned char* lds, const Gemm g, const Sched& S, const Epi& E, int wbase) {
;     ...
;         const bool has_next = S.next(ui + 1, nxt);
;         const unsigned nA = has_next ? S.a_off(nxt, g) : cA, nB = has_next ? S.b_off(nxt, g) : cB;
;         const rsrc_t rAn = (Sched::TWO && has_next) ? (nxt.part ? rA1 : rA0) : rAc, rBn = (Sched::TWO && has_next) ? (nxt.part ? rB1 : rB0) : rBc;
;         float pre_[8] = {0.f, 0.f, 0.f, 0.f, 0.f, 0.f, 0.f, 0.f};
;         if constexpr (Epi::HAS_PRE) E.pre_load(pre_, cur, wr);
;         for (int t = 0; t < nt; t += 2) {
;             const bool last = (t == nt - 2);
;             const unsigned a1 = cA + (unsigned)(t + 1) * kstep;
;             const unsigned a2 = last ? nA : cA + (unsigned)(t + 2) * kstep, b2 = last ? nB : cB + (unsigned)(t + 2) * kstep; const rsrc_t rA2 = (Sched::TWO && last) ? rAn : rAc, rB2 = (Sched::TWO && last) ? rBn : rBc;
;             const unsigned a3 = a2 + kstep, b3 = b2 + kstep;
;             if (last && has_next) S.a_ready(nxt);
;             if constexpr (SP2) {
;             PG8_LDB(B0, 0, 0); PG8_LDB(B1, 0, 1); PG8_SCHED; PG8_LDA(At, 0, 0); PG8_STAGE(PG8_SA(1, 1), rAc, a1 + hstep, voffA);
;             PG8_WAIT_V(8); PG8_WAIT_L(0); PG8_BAR; PG8_MMA(0, 0, At, B0); PG8_MMA(0, 1, At, B1); PG8_BAR; PG8_SCHED;
.LBB0_1699:
	s_mul_i32 s61, s60, 0x1c0000
	s_andn2_b64 vcc, exec, s[14:15]
	s_mul_i32 s62, s59, 0x1c0000
	s_cbranch_vccnz .LBB0_1703
	s_and_b64 s[6:7], s[18:19], exec
	v_mov_b64_e32 v[6:7], v[2:3]
	v_mov_b64_e32 v[18:19], v[2:3]
	v_mov_b64_e32 v[22:23], v[2:3]
	v_mov_b64_e32 v[34:35], v[2:3]
	v_mov_b64_e32 v[38:39], v[2:3]
	v_mov_b64_e32 v[50:51], v[2:3]
	v_mov_b64_e32 v[54:55], v[2:3]
	v_mov_b64_e32 v[10:11], v[2:3]
	v_mov_b64_e32 v[14:15], v[2:3]
	v_mov_b64_e32 v[26:27], v[2:3]
	v_mov_b64_e32 v[30:31], v[2:3]
	v_mov_b64_e32 v[42:43], v[2:3]
	v_mov_b64_e32 v[46:47], v[2:3]
	v_mov_b64_e32 v[58:59], v[2:3]
	s_waitcnt vmcnt(37)
	v_mov_b64_e32 v[62:63], v[2:3]
	s_waitcnt vmcnt(36)
	v_mov_b64_e32 v[66:67], v[2:3]
	s_waitcnt vmcnt(35)
	v_mov_b64_e32 v[70:71], v[2:3]
	s_waitcnt vmcnt(32)
	v_mov_b64_e32 v[82:83], v[2:3]
	s_waitcnt vmcnt(31)
	v_mov_b64_e32 v[86:87], v[2:3]
	s_waitcnt vmcnt(28)
	v_mov_b64_e32 v[98:99], v[2:3]
	s_waitcnt vmcnt(27)
	v_mov_b64_e32 v[102:103], v[2:3]
	s_waitcnt vmcnt(23)
	v_mov_b64_e32 v[118:119], v[2:3]
	s_waitcnt vmcnt(22)
	v_mov_b64_e32 v[122:123], v[2:3]
	v_mov_b64_e32 v[74:75], v[2:3]
	v_mov_b64_e32 v[78:79], v[2:3]
	v_mov_b64_e32 v[90:91], v[2:3]
	v_mov_b64_e32 v[94:95], v[2:3]
	v_mov_b64_e32 v[106:107], v[2:3]
	v_mov_b64_e32 v[110:111], v[2:3]
	v_mov_b64_e32 v[130:131], v[2:3]
	v_mov_b64_e32 v[134:135], v[2:3]
	s_cselect_b32 s21, s61, s55
	s_cselect_b32 s63, s62, s54
	s_add_i32 s65, s55, 0x80
	s_add_i32 s66, s54, 0x100
	s_mov_b32 s67, 0
	v_mov_b64_e32 v[4:5], v[0:1]
	v_mov_b64_e32 v[16:17], v[0:1]
	v_mov_b64_e32 v[20:21], v[0:1]
	v_mov_b64_e32 v[32:33], v[0:1]
	v_mov_b64_e32 v[36:37], v[0:1]
	v_mov_b64_e32 v[48:49], v[0:1]
	v_mov_b64_e32 v[52:53], v[0:1]
	v_mov_b64_e32 v[8:9], v[0:1]
	v_mov_b64_e32 v[12:13], v[0:1]
	v_mov_b64_e32 v[24:25], v[0:1]
	v_mov_b64_e32 v[28:29], v[0:1]
	v_mov_b64_e32 v[40:41], v[0:1]
	v_mov_b64_e32 v[44:45], v[0:1]
	v_mov_b64_e32 v[56:57], v[0:1]
	v_mov_b64_e32 v[60:61], v[0:1]
	v_mov_b64_e32 v[64:65], v[0:1]
	v_mov_b64_e32 v[68:69], v[0:1]
	v_mov_b64_e32 v[80:81], v[0:1]
	v_mov_b64_e32 v[84:85], v[0:1]
	v_mov_b64_e32 v[96:97], v[0:1]
	v_mov_b64_e32 v[100:101], v[0:1]
	v_mov_b64_e32 v[116:117], v[0:1]
	v_mov_b64_e32 v[120:121], v[0:1]
	v_mov_b64_e32 v[72:73], v[0:1]
	v_mov_b64_e32 v[76:77], v[0:1]
	v_mov_b64_e32 v[88:89], v[0:1]
	v_mov_b64_e32 v[92:93], v[0:1]
	v_mov_b64_e32 v[104:105], v[0:1]
	v_mov_b64_e32 v[108:109], v[0:1]
	v_mov_b64_e32 v[128:129], v[0:1]
	v_mov_b64_e32 v[132:133], v[0:1]
	s_cmp_eq_u32 s100, 1
	s_cbranch_scc0 .LBB0_1701
	v_add_u32_e32 v140, 0x10000, v176
	v_add_u32_e32 v156, 0x14000, v176
	ds_read_b128 v[112:115], v140
	ds_read_b128 v[124:127], v140 offset:1024
	ds_read_b128 v[136:139], v140 offset:2048
	ds_read_b128 v[140:143], v140 offset:3072
	ds_read_b128 v[144:147], v156
	ds_read_b128 v[148:151], v156 offset:1024
	ds_read_b128 v[152:155], v156 offset:2048
	ds_read_b128 v[156:159], v156 offset:3072
	s_add_i32 s6, s65, 0x80
	s_cmp_eq_u32 s52, s67
	s_cselect_b32 s68, s21, s6
	s_cselect_b32 s55, s63, s66
	s_or_b32 s54, s68, 0x80
	s_add_i32 s6, s25, s65
	s_mov_b32 m0, s53
	ds_read_b128 v[160:163], v177
	ds_read_b128 v[164:167], v177 offset:1024
	ds_read_b128 v[178:181], v177 offset:2048
	ds_read_b128 v[182:185], v177 offset:3072
	ds_read_b128 v[186:189], v177 offset:4096
	ds_read_b128 v[190:193], v177 offset:5120
	ds_read_b128 v[194:197], v177 offset:6144
	ds_read_b128 v[198:201], v177 offset:7168
	buffer_load_dwordx4 v170, s[36:39], s6 offen lds
	s_mov_b32 m0, s56
	s_nop 0
	buffer_load_dwordx4 v172, s[36:39], s6 offen lds
	s_waitcnt vmcnt(32)
	s_waitcnt lgkmcnt(0)
	s_barrier
	s_setprio 1
	s_waitcnt lgkmcnt(7)
	v_mfma_f32_16x16x32_bf16 v[132:135], v[112:115], v[160:163], v[132:135]
	v_mfma_f32_16x16x32_bf16 v[128:131], v[136:139], v[160:163], v[128:131]
	s_waitcnt lgkmcnt(5)
	v_mfma_f32_16x16x32_bf16 v[108:111], v[112:115], v[178:181], v[108:111]
	v_mfma_f32_16x16x32_bf16 v[104:107], v[136:139], v[178:181], v[104:107]
	s_waitcnt lgkmcnt(3)
	v_mfma_f32_16x16x32_bf16 v[92:95], v[112:115], v[186:189], v[92:95]
	v_mfma_f32_16x16x32_bf16 v[88:91], v[136:139], v[186:189], v[88:91]
	s_waitcnt lgkmcnt(1)
	v_mfma_f32_16x16x32_bf16 v[76:79], v[112:115], v[194:197], v[76:79]
	v_mfma_f32_16x16x32_bf16 v[72:75], v[136:139], v[194:197], v[72:75]
	v_mfma_f32_16x16x32_bf16 v[132:135], v[124:127], v[164:167], v[132:135]
	v_mfma_f32_16x16x32_bf16 v[128:131], v[140:143], v[164:167], v[128:131]
	v_mfma_f32_16x16x32_bf16 v[108:111], v[124:127], v[182:185], v[108:111]
	v_mfma_f32_16x16x32_bf16 v[104:107], v[140:143], v[182:185], v[104:107]
	v_mfma_f32_16x16x32_bf16 v[92:95], v[124:127], v[190:193], v[92:95]
	v_mfma_f32_16x16x32_bf16 v[88:91], v[140:143], v[190:193], v[88:91]
	s_waitcnt lgkmcnt(0)
	v_mfma_f32_16x16x32_bf16 v[76:79], v[124:127], v[198:201], v[76:79]
	v_mfma_f32_16x16x32_bf16 v[72:75], v[140:143], v[198:201], v[72:75]
	s_setprio 0
	s_setprio 1
	v_mfma_f32_16x16x32_bf16 v[120:123], v[144:147], v[160:163], v[120:123]
	v_mfma_f32_16x16x32_bf16 v[116:119], v[152:155], v[160:163], v[116:119]
	v_mfma_f32_16x16x32_bf16 v[100:103], v[144:147], v[178:181], v[100:103]
	v_mfma_f32_16x16x32_bf16 v[96:99], v[152:155], v[178:181], v[96:99]
	v_mfma_f32_16x16x32_bf16 v[84:87], v[144:147], v[186:189], v[84:87]
	v_mfma_f32_16x16x32_bf16 v[80:83], v[152:155], v[186:189], v[80:83]
	v_mfma_f32_16x16x32_bf16 v[68:71], v[144:147], v[194:197], v[68:71]
	v_mfma_f32_16x16x32_bf16 v[64:67], v[152:155], v[194:197], v[64:67]
	v_mfma_f32_16x16x32_bf16 v[120:123], v[148:151], v[164:167], v[120:123]
	v_mfma_f32_16x16x32_bf16 v[116:119], v[156:159], v[164:167], v[116:119]
	v_mfma_f32_16x16x32_bf16 v[100:103], v[148:151], v[182:185], v[100:103]
	v_mfma_f32_16x16x32_bf16 v[96:99], v[156:159], v[182:185], v[96:99]
	v_mfma_f32_16x16x32_bf16 v[84:87], v[148:151], v[190:193], v[84:87]
	v_mfma_f32_16x16x32_bf16 v[80:83], v[156:159], v[190:193], v[80:83]
	v_mfma_f32_16x16x32_bf16 v[68:71], v[148:151], v[198:201], v[68:71]
	v_mfma_f32_16x16x32_bf16 v[64:67], v[156:159], v[198:201], v[64:67]
	s_setprio 0
	s_barrier
; #define PG8_STAGE(bufoff, rs_, soff_, voff) do { _Pragma("unroll") for (int _i = 0; _i < 2; ++_i) \
;         __builtin_amdgcn_raw_ptr_buffer_load_lds(rs_, (LAS void*)(lds + (bufoff) + ldsw + _i * 8192), 16, (int)(voff)[_i], (int)(soff_), 0, 0); } while (0)
; #define PG8_LDA(dst, b, h) do { _Pragma("unroll") for (int m = 0; m < 4; ++m) dst[m] = PG8_LD2(lds + PG8_SA(b, h) + aoff + m * 2048); } while (0)
; #define PG8_LDB(dst, b, h) do { _Pragma("unroll") for (int n = 0; n < 2; ++n) dst[n] = PG8_LD2(lds + PG8_SB(b, h) + boff + n * 2048); } while (0)
; #define PG8_WAIT_V(n) asm volatile("s_waitcnt vmcnt(" #n ")" ::: "memory")
; #define PG8_WAIT_L(n) asm volatile("s_waitcnt lgkmcnt(" #n ")" ::: "memory")
; #define PG8_BAR __builtin_amdgcn_s_barrier()
; #define PG8_SCHED __builtin_amdgcn_sched_barrier(0)
; template <class Epi, class Sched, bool ALIGN_EPI = false, bool SP2 = false, bool FP8 = false>
; __device__ __forceinline__ void gemm_phase(LAS unsigned char* lds, const Gemm g, const Sched& S, const Epi& E, int wbase) {
;     ...
;             PG8_LDA(At, 0, 1); PG8_STAGE(PG8_SB(0, 0), rB2, b2, voffB); PG8_STAGE(PG8_SB(0, 1), rB2, b2 + hstep, voffB); PG8_STAGE(PG8_SA(0, 0), rA2, a2, voffA);
;             PG8_WAIT_V(8); PG8_WAIT_L(0); PG8_BAR; PG8_MMA(1, 0, At, B0); PG8_MMA(1, 1, At, B1); PG8_BAR; PG8_SCHED;
;             PG8_LDB(B0, 1, 0); PG8_LDB(B1, 1, 1); PG8_SCHED; PG8_LDA(At, 1, 0); PG8_STAGE(PG8_SA(0, 1), rA2, a2 + hstep, voffA);
;             PG8_WAIT_V(8); PG8_WAIT_L(0); PG8_BAR; PG8_MMA(0, 0, At, B0); PG8_MMA(0, 1, At, B1); PG8_BAR; PG8_SCHED;
	s_mov_b32 m0, s27
	s_mov_b32 s6, s38
	s_mov_b32 s7, s39
	ds_read_b128 v[160:163], v177 offset:16384
	ds_read_b128 v[164:167], v177 offset:17408
	ds_read_b128 v[178:181], v177 offset:18432
	ds_read_b128 v[182:185], v177 offset:19456
	ds_read_b128 v[186:189], v177 offset:20480
	ds_read_b128 v[190:193], v177 offset:21504
	ds_read_b128 v[194:197], v177 offset:22528
	ds_read_b128 v[198:201], v177 offset:23552
	buffer_load_dwordx4 v171, s[4:7], s55 offen lds
	s_mov_b32 m0, s28
	s_add_i32 s69, s55, s25
	buffer_load_dwordx4 v173, s[4:7], s55 offen lds
	s_mov_b32 m0, s29
	s_nop 0
	buffer_load_dwordx4 v171, s[4:7], s69 offen lds
	s_mov_b32 m0, s30
	s_nop 0
	buffer_load_dwordx4 v173, s[4:7], s69 offen lds
	s_mov_b32 m0, s26
	s_nop 0
	buffer_load_dwordx4 v170, s[36:39], s68 offen lds
	s_mov_b32 m0, s31
	s_nop 0
	buffer_load_dwordx4 v172, s[36:39], s68 offen lds
	s_waitcnt vmcnt(32)
	s_waitcnt lgkmcnt(0)
	s_barrier
	s_setprio 1
	s_waitcnt lgkmcnt(7)
	v_mfma_f32_16x16x32_bf16 v[60:63], v[112:115], v[160:163], v[60:63]
	v_mfma_f32_16x16x32_bf16 v[56:59], v[136:139], v[160:163], v[56:59]
	s_waitcnt lgkmcnt(5)
	v_mfma_f32_16x16x32_bf16 v[44:47], v[112:115], v[178:181], v[44:47]
	v_mfma_f32_16x16x32_bf16 v[40:43], v[136:139], v[178:181], v[40:43]
	s_waitcnt lgkmcnt(3)
	v_mfma_f32_16x16x32_bf16 v[28:31], v[112:115], v[186:189], v[28:31]
	v_mfma_f32_16x16x32_bf16 v[24:27], v[136:139], v[186:189], v[24:27]
	s_waitcnt lgkmcnt(1)
	v_mfma_f32_16x16x32_bf16 v[12:15], v[112:115], v[194:197], v[12:15]
	v_mfma_f32_16x16x32_bf16 v[8:11], v[136:139], v[194:197], v[8:11]
	v_mfma_f32_16x16x32_bf16 v[60:63], v[124:127], v[164:167], v[60:63]
	v_mfma_f32_16x16x32_bf16 v[56:59], v[140:143], v[164:167], v[56:59]
	v_mfma_f32_16x16x32_bf16 v[44:47], v[124:127], v[182:185], v[44:47]
	v_mfma_f32_16x16x32_bf16 v[40:43], v[140:143], v[182:185], v[40:43]
	v_mfma_f32_16x16x32_bf16 v[28:31], v[124:127], v[190:193], v[28:31]
	v_mfma_f32_16x16x32_bf16 v[24:27], v[140:143], v[190:193], v[24:27]
	s_waitcnt lgkmcnt(0)
	v_mfma_f32_16x16x32_bf16 v[12:15], v[124:127], v[198:201], v[12:15]
	v_mfma_f32_16x16x32_bf16 v[8:11], v[140:143], v[198:201], v[8:11]
	s_setprio 0
	s_setprio 1
	v_mfma_f32_16x16x32_bf16 v[52:55], v[144:147], v[160:163], v[52:55]
	v_mfma_f32_16x16x32_bf16 v[48:51], v[152:155], v[160:163], v[48:51]
	v_mfma_f32_16x16x32_bf16 v[36:39], v[144:147], v[178:181], v[36:39]
	v_mfma_f32_16x16x32_bf16 v[32:35], v[152:155], v[178:181], v[32:35]
	v_mfma_f32_16x16x32_bf16 v[20:23], v[144:147], v[186:189], v[20:23]
	v_mfma_f32_16x16x32_bf16 v[16:19], v[152:155], v[186:189], v[16:19]
	v_mfma_f32_16x16x32_bf16 v[4:7], v[144:147], v[194:197], v[4:7]
	v_mfma_f32_16x16x32_bf16 v[0:3], v[152:155], v[194:197], v[0:3]
	v_mfma_f32_16x16x32_bf16 v[52:55], v[148:151], v[164:167], v[52:55]
	v_mfma_f32_16x16x32_bf16 v[48:51], v[156:159], v[164:167], v[48:51]
	v_mfma_f32_16x16x32_bf16 v[36:39], v[148:151], v[182:185], v[36:39]
	v_mfma_f32_16x16x32_bf16 v[32:35], v[156:159], v[182:185], v[32:35]
	v_mfma_f32_16x16x32_bf16 v[20:23], v[148:151], v[190:193], v[20:23]
	v_mfma_f32_16x16x32_bf16 v[16:19], v[156:159], v[190:193], v[16:19]
	v_mfma_f32_16x16x32_bf16 v[4:7], v[148:151], v[198:201], v[4:7]
	v_mfma_f32_16x16x32_bf16 v[0:3], v[156:159], v[198:201], v[0:3]
	s_setprio 0
	s_barrier
	v_add_u32_e32 v140, 0x18000, v176
	v_add_u32_e32 v156, 0x1c000, v176
	ds_read_b128 v[112:115], v140
	ds_read_b128 v[124:127], v140 offset:1024
	ds_read_b128 v[136:139], v140 offset:2048
	ds_read_b128 v[140:143], v140 offset:3072
	ds_read_b128 v[144:147], v156
	ds_read_b128 v[148:151], v156 offset:1024
	ds_read_b128 v[152:155], v156 offset:2048
	ds_read_b128 v[156:159], v156 offset:3072
	s_add_i32 s68, s68, s25
	s_mov_b32 m0, s33
	ds_read_b128 v[160:163], v177 offset:32768
	ds_read_b128 v[164:167], v177 offset:33792
	ds_read_b128 v[178:181], v177 offset:34816
	ds_read_b128 v[182:185], v177 offset:35840
	ds_read_b128 v[186:189], v177 offset:36864
	ds_read_b128 v[190:193], v177 offset:37888
	ds_read_b128 v[194:197], v177 offset:38912
	ds_read_b128 v[198:201], v177 offset:39936
	buffer_load_dwordx4 v170, s[36:39], s68 offen lds
	s_mov_b32 m0, s34
	s_nop 0
	buffer_load_dwordx4 v172, s[36:39], s68 offen lds
	s_waitcnt vmcnt(8)
	s_waitcnt lgkmcnt(0)
	s_barrier
; #define PG8_STAGE(bufoff, rs_, soff_, voff) do { _Pragma("unroll") for (int _i = 0; _i < 2; ++_i) \
;         __builtin_amdgcn_raw_ptr_buffer_load_lds(rs_, (LAS void*)(lds + (bufoff) + ldsw + _i * 8192), 16, (int)(voff)[_i], (int)(soff_), 0, 0); } while (0)
; #define PG8_LDA(dst, b, h) do { _Pragma("unroll") for (int m = 0; m < 4; ++m) dst[m] = PG8_LD2(lds + PG8_SA(b, h) + aoff + m * 2048); } while (0)
; #define PG8_WAIT_V(n) asm volatile("s_waitcnt vmcnt(" #n ")" ::: "memory")
; #define PG8_WAIT_L(n) asm volatile("s_waitcnt lgkmcnt(" #n ")" ::: "memory")
; #define PG8_BAR __builtin_amdgcn_s_barrier()
; #define PG8_SCHED __builtin_amdgcn_sched_barrier(0)
; template <class Epi, class Sched, bool ALIGN_EPI = false, bool SP2 = false, bool FP8 = false>
; __device__ __forceinline__ void gemm_phase(LAS unsigned char* lds, const Gemm g, const Sched& S, const Epi& E, int wbase) {
;     ...
;             PG8_WAIT_V(8); PG8_WAIT_L(0); PG8_BAR; PG8_MMA(0, 0, At, B0); PG8_MMA(0, 1, At, B1); PG8_BAR; PG8_SCHED;
;             PG8_LDA(At, 1, 1); PG8_STAGE(PG8_SB(1, 0), rB2, b3, voffB); PG8_STAGE(PG8_SB(1, 1), rB2, b3 + hstep, voffB); PG8_STAGE(PG8_SA(1, 0), rA2, a3, voffA);
;             PG8_WAIT_V(8); PG8_WAIT_L(0); PG8_BAR; PG8_MMA(1, 0, At, B0); PG8_MMA(1, 1, At, B1); PG8_BAR; PG8_SCHED;
	s_setprio 1
	s_waitcnt lgkmcnt(7)
	v_mfma_f32_16x16x32_bf16 v[132:135], v[112:115], v[160:163], v[132:135]
	v_mfma_f32_16x16x32_bf16 v[128:131], v[136:139], v[160:163], v[128:131]
	s_waitcnt lgkmcnt(5)
	v_mfma_f32_16x16x32_bf16 v[108:111], v[112:115], v[178:181], v[108:111]
	v_mfma_f32_16x16x32_bf16 v[104:107], v[136:139], v[178:181], v[104:107]
	s_waitcnt lgkmcnt(3)
	v_mfma_f32_16x16x32_bf16 v[92:95], v[112:115], v[186:189], v[92:95]
	v_mfma_f32_16x16x32_bf16 v[88:91], v[136:139], v[186:189], v[88:91]
	s_waitcnt lgkmcnt(1)
	v_mfma_f32_16x16x32_bf16 v[76:79], v[112:115], v[194:197], v[76:79]
	v_mfma_f32_16x16x32_bf16 v[72:75], v[136:139], v[194:197], v[72:75]
	v_mfma_f32_16x16x32_bf16 v[132:135], v[124:127], v[164:167], v[132:135]
	v_mfma_f32_16x16x32_bf16 v[128:131], v[140:143], v[164:167], v[128:131]
	v_mfma_f32_16x16x32_bf16 v[108:111], v[124:127], v[182:185], v[108:111]
	v_mfma_f32_16x16x32_bf16 v[104:107], v[140:143], v[182:185], v[104:107]
	v_mfma_f32_16x16x32_bf16 v[92:95], v[124:127], v[190:193], v[92:95]
	v_mfma_f32_16x16x32_bf16 v[88:91], v[140:143], v[190:193], v[88:91]
	s_waitcnt lgkmcnt(0)
	v_mfma_f32_16x16x32_bf16 v[76:79], v[124:127], v[198:201], v[76:79]
	v_mfma_f32_16x16x32_bf16 v[72:75], v[140:143], v[198:201], v[72:75]
	s_setprio 0
	s_setprio 1
	v_mfma_f32_16x16x32_bf16 v[120:123], v[144:147], v[160:163], v[120:123]
	v_mfma_f32_16x16x32_bf16 v[116:119], v[152:155], v[160:163], v[116:119]
	v_mfma_f32_16x16x32_bf16 v[100:103], v[144:147], v[178:181], v[100:103]
	v_mfma_f32_16x16x32_bf16 v[96:99], v[152:155], v[178:181], v[96:99]
	v_mfma_f32_16x16x32_bf16 v[84:87], v[144:147], v[186:189], v[84:87]
	v_mfma_f32_16x16x32_bf16 v[80:83], v[152:155], v[186:189], v[80:83]
	v_mfma_f32_16x16x32_bf16 v[68:71], v[144:147], v[194:197], v[68:71]
	v_mfma_f32_16x16x32_bf16 v[64:67], v[152:155], v[194:197], v[64:67]
	v_mfma_f32_16x16x32_bf16 v[120:123], v[148:151], v[164:167], v[120:123]
	v_mfma_f32_16x16x32_bf16 v[116:119], v[156:159], v[164:167], v[116:119]
	v_mfma_f32_16x16x32_bf16 v[100:103], v[148:151], v[182:185], v[100:103]
	v_mfma_f32_16x16x32_bf16 v[96:99], v[156:159], v[182:185], v[96:99]
	v_mfma_f32_16x16x32_bf16 v[84:87], v[148:151], v[190:193], v[84:87]
	v_mfma_f32_16x16x32_bf16 v[80:83], v[156:159], v[190:193], v[80:83]
	v_mfma_f32_16x16x32_bf16 v[68:71], v[148:151], v[198:201], v[68:71]
	v_mfma_f32_16x16x32_bf16 v[64:67], v[156:159], v[198:201], v[64:67]
	s_setprio 0
	s_barrier
	s_mov_b32 m0, s1
	s_bitset1_b32 s55, 7
	ds_read_b128 v[160:163], v177 offset:49152
	ds_read_b128 v[164:167], v177 offset:50176
	ds_read_b128 v[178:181], v177 offset:51200
	ds_read_b128 v[182:185], v177 offset:52224
	ds_read_b128 v[186:189], v177 offset:53248
	ds_read_b128 v[190:193], v177 offset:54272
	ds_read_b128 v[194:197], v177 offset:55296
	ds_read_b128 v[198:201], v177 offset:56320
	buffer_load_dwordx4 v171, s[4:7], s55 offen lds
	s_mov_b32 m0, s35
	s_nop 0
	buffer_load_dwordx4 v173, s[4:7], s55 offen lds
	s_add_i32 s55, s55, s25
	s_mov_b32 m0, s43
	s_nop 0
	buffer_load_dwordx4 v171, s[4:7], s55 offen lds
	s_mov_b32 m0, s44
	s_nop 0
	buffer_load_dwordx4 v173, s[4:7], s55 offen lds
	s_mov_b32 m0, s41
	s_nop 0
	buffer_load_dwordx4 v170, s[36:39], s54 offen lds
	s_mov_b32 m0, s42
	s_nop 0
	buffer_load_dwordx4 v172, s[36:39], s54 offen lds
	s_waitcnt vmcnt(8)
	s_waitcnt lgkmcnt(0)
	s_barrier
	s_setprio 1
	s_waitcnt lgkmcnt(7)
	v_mfma_f32_16x16x32_bf16 v[60:63], v[112:115], v[160:163], v[60:63]
	v_mfma_f32_16x16x32_bf16 v[56:59], v[136:139], v[160:163], v[56:59]
	s_waitcnt lgkmcnt(5)
	v_mfma_f32_16x16x32_bf16 v[44:47], v[112:115], v[178:181], v[44:47]
	v_mfma_f32_16x16x32_bf16 v[40:43], v[136:139], v[178:181], v[40:43]
	s_waitcnt lgkmcnt(3)
	v_mfma_f32_16x16x32_bf16 v[28:31], v[112:115], v[186:189], v[28:31]
	v_mfma_f32_16x16x32_bf16 v[24:27], v[136:139], v[186:189], v[24:27]
	s_waitcnt lgkmcnt(1)
	v_mfma_f32_16x16x32_bf16 v[12:15], v[112:115], v[194:197], v[12:15]
	v_mfma_f32_16x16x32_bf16 v[8:11], v[136:139], v[194:197], v[8:11]
	v_mfma_f32_16x16x32_bf16 v[60:63], v[124:127], v[164:167], v[60:63]
	v_mfma_f32_16x16x32_bf16 v[56:59], v[140:143], v[164:167], v[56:59]
	v_mfma_f32_16x16x32_bf16 v[44:47], v[124:127], v[182:185], v[44:47]
	v_mfma_f32_16x16x32_bf16 v[40:43], v[140:143], v[182:185], v[40:43]
	v_mfma_f32_16x16x32_bf16 v[28:31], v[124:127], v[190:193], v[28:31]
	v_mfma_f32_16x16x32_bf16 v[24:27], v[140:143], v[190:193], v[24:27]
	s_waitcnt lgkmcnt(0)
	v_mfma_f32_16x16x32_bf16 v[12:15], v[124:127], v[198:201], v[12:15]
	v_mfma_f32_16x16x32_bf16 v[8:11], v[140:143], v[198:201], v[8:11]
	s_setprio 0
	s_setprio 1
	v_mfma_f32_16x16x32_bf16 v[52:55], v[144:147], v[160:163], v[52:55]
	v_mfma_f32_16x16x32_bf16 v[48:51], v[152:155], v[160:163], v[48:51]
	v_mfma_f32_16x16x32_bf16 v[36:39], v[144:147], v[178:181], v[36:39]
	v_mfma_f32_16x16x32_bf16 v[32:35], v[152:155], v[178:181], v[32:35]
	v_mfma_f32_16x16x32_bf16 v[20:23], v[144:147], v[186:189], v[20:23]
	v_mfma_f32_16x16x32_bf16 v[16:19], v[152:155], v[186:189], v[16:19]
	v_mfma_f32_16x16x32_bf16 v[4:7], v[144:147], v[194:197], v[4:7]
	v_mfma_f32_16x16x32_bf16 v[0:3], v[152:155], v[194:197], v[0:3]
	v_mfma_f32_16x16x32_bf16 v[52:55], v[148:151], v[164:167], v[52:55]
	v_mfma_f32_16x16x32_bf16 v[48:51], v[156:159], v[164:167], v[48:51]
	v_mfma_f32_16x16x32_bf16 v[36:39], v[148:151], v[182:185], v[36:39]
	v_mfma_f32_16x16x32_bf16 v[32:35], v[156:159], v[182:185], v[32:35]
	v_mfma_f32_16x16x32_bf16 v[20:23], v[148:151], v[190:193], v[20:23]
	v_mfma_f32_16x16x32_bf16 v[16:19], v[156:159], v[190:193], v[16:19]
	v_mfma_f32_16x16x32_bf16 v[4:7], v[148:151], v[198:201], v[4:7]
	v_mfma_f32_16x16x32_bf16 v[0:3], v[156:159], v[198:201], v[0:3]
	s_setprio 0
	s_barrier
	s_add_i32 s67, s67, 2
	s_addk_i32 s65, 0x100
	s_addk_i32 s66, 0x100
	s_cmp_ge_i32 s67, s47
	s_cbranch_scc0 .LBB0_1701
	s_branch .Lpeel_after_1701

; #define PG8_BAR __builtin_amdgcn_s_barrier()
; #define PG8_ZERO_ACC() do { float z_; asm volatile("v_mov_b32 %0, 0" : "=v"(z_)); _Pragma("unroll") for (int a = 0; a < 2; ++a) _Pragma("unroll") for (int b = 0; b < 2; ++b) _Pragma("unroll") for (int m = 0; m < 4; ++m) \
;         _Pragma("unroll") for (int n = 0; n < 2; ++n) acc[a][b][m][n] = (f32x4){z_, z_, z_, z_}; } while (0)
; template <class Epi, class Sched, bool ALIGN_EPI = false, bool SP2 = false, bool FP8 = false>
; __device__ __forceinline__ void gemm_phase(LAS unsigned char* lds, const Gemm g, const Sched& S, const Epi& E, int wbase) {
;     ...
;         }
;         if constexpr (ALIGN_EPI) { if (wr == 0) PG8_BAR; }
;         { int fr_ = fr, fq_ = fq; asm volatile("" : "+v"(fr_), "+v"(fq_));
;           if constexpr (Epi::HAS_PRE) E(acc, cur, wr, wc, fr_, fq_, pre_); else E(acc, cur, wr, wc, fr_, fq_); } S.done(cur);
;         if (!has_next) break;
;         if (E.reset(cur)) PG8_ZERO_ACC();
.Lpeel_after_1701:
	s_mov_b32 s100, 1
	v_readlane_b32 s68, v255, 22
	v_readlane_b32 s69, v255, 23
	s_and_b64 vcc, exec, s[16:17]
	s_cbranch_vccnz .LBB0_1704
	s_branch .LBB0_1705

;     __device__ __forceinline__ unsigned a_off(const Unit& u, const Gemm& g) const { return (unsigned)u.pm * (unsigned)(BM * 2) * (unsigned)g.K; }
;     __device__ __forceinline__ unsigned b_off(const Unit& u, const Gemm& g) const { return (unsigned)u.pn * (unsigned)(BM * 2) * (unsigned)g.K; }
;     __device__ __forceinline__ bool next(int i, Unit& u) const { return so.next(i, u); }
; template <class Epi, class Sched, bool ALIGN_EPI = false, bool SP2 = false, bool FP8 = false>
; __device__ __forceinline__ void gemm_phase(LAS unsigned char* lds, const Gemm g, const Sched& S, const Epi& E, int wbase) {
;     ...
;     for (int i = 0; i < 2; ++i) { int R, C; stage_rc(tid * 16 + i * 8192, R, C); const int Rb = Epi::PERM ? ((R & ~31) + perm32(R & 31)) : R;
;         voffA[i] = (unsigned)(R * K + C) * 2u; voffB[i] = (unsigned)(Rb * K + C) * 2u; }
;     const unsigned kstep = (unsigned)(BK * 2);
;     const unsigned hstep = (unsigned)HALF * (unsigned)K * 2u;
;     typedef __amdgpu_buffer_rsrc_t rsrc_t;
;     const rsrc_t rA0 = __builtin_amdgcn_make_buffer_rsrc((void*)g.A, 0, 0xffffffff, 0x00020000), rB0 = __builtin_amdgcn_make_buffer_rsrc((void*)g.Bt, 0, 0xffffffff, 0x00020000);
;     rsrc_t rA1 = rA0, rB1 = rB0;
;     if constexpr (Sched::TWO) { rA1 = __builtin_amdgcn_make_buffer_rsrc((void*)S.A1, 0, 0xffffffff, 0x00020000); rB1 = __builtin_amdgcn_make_buffer_rsrc((void*)S.Bt1, 0, 0xffffffff, 0x00020000); }
;     const unsigned ldsw = (unsigned)wid * 1024u;
;     const int aoff = lds_byte(wr * 64 + fr, fq * 8), boff = lds_byte(wc * 32 + fr, fq * 8);
;     ...
;     Unit cur, nxt; int ui = 0;
;     if (!S.next(0, cur)) return;
;     f32x4 acc[2][2][4][2];
;     ...
;     PG8_ZERO_ACC();
;     v8i_t At[4], B0[2], B1[2];
;     unsigned cA = S.a_off(cur, g), cB = S.b_off(cur, g); rsrc_t rAc = (Sched::TWO && cur.part) ? rA1 : rA0, rBc = (Sched::TWO && cur.part) ? rB1 : rB0;
;     S.a_ready(cur);
;     if constexpr (SP2) {
;         PG8_STAGE(PG8_SB(0, 0), rBc, cB, voffB); PG8_STAGE(PG8_SB(0, 1), rBc, cB + hstep, voffB); PG8_STAGE(PG8_SA(0, 0), rAc, cA, voffA); PG8_STAGE(PG8_SA(0, 1), rAc, cA + hstep, voffA);
;         if (wr == 1) PG8_BAR;
;         PG8_WAIT_V(2); PG8_BAR;
;         PG8_STAGE(PG8_SB(1, 0), rBc, cB + kstep, voffB); PG8_STAGE(PG8_SA(1, 0), rAc, cA + kstep, voffA); PG8_STAGE(PG8_SB(1, 1), rBc, cB + hstep + kstep, voffB);
;         PG8_WAIT_V(6); PG8_BAR;
.LBB0_1774:
	v_readlane_b32 s6, v255, 11
	s_cmp_eq_u32 s6, 1
	s_cselect_b32 s6, 0, 0x200000
	s_add_u32 s8, s10, 0x1f800000
	s_addc_u32 s9, s11, 0
	s_add_u32 s6, s10, s6
	s_addc_u32 s7, s11, 0
	s_add_u32 s10, s6, 0x17200000
	s_addc_u32 s11, s7, 0
	s_add_i32 s30, s22, 0x18000
	s_or_b32 s17, s54, 0x80
	s_mov_b32 s6, s38
	s_mov_b32 s7, s39
	s_mov_b32 m0, s30
	s_add_i32 s31, s22, 0x1a000
	s_waitcnt vmcnt(2)
	s_barrier
	buffer_load_dwordx4 v149, s[4:7], s17 offen lds
	s_mov_b32 m0, s31
	s_add_i32 s33, s22, 0x8000
	buffer_load_dwordx4 v151, s[4:7], s17 offen lds
	s_or_b32 s17, s55, 0x80
	s_mov_b32 m0, s33
	s_add_i32 s34, s22, 0xa000
	buffer_load_dwordx4 v148, s[36:39], s17 offen lds
	s_mov_b32 m0, s34
	s_add_i32 s35, s22, 0x1c000
	buffer_load_dwordx4 v150, s[36:39], s17 offen lds
	s_bitset1_b32 s16, 7
	s_mov_b32 m0, s35
	s_add_i32 s41, s22, 0x1e000
	buffer_load_dwordx4 v149, s[4:7], s16 offen lds
	s_mov_b32 m0, s41
	v_bfe_u32 v153, v4, 4, 2
	buffer_load_dwordx4 v151, s[4:7], s16 offen lds
	s_ashr_i32 s6, s14, 31
	s_lshr_b32 s6, s6, 26
	v_and_b32_e32 v152, 15, v4
	s_add_i32 s6, s14, s6
	v_lshlrev_b32_e32 v5, 4, v153
	v_lshlrev_b32_e32 v4, 2, v4
	s_ashr_i32 s43, s6, 6
	v_lshl_or_b32 v5, v152, 6, v5
	s_lshl_b32 s6, s12, 13
	v_and_b32_e32 v4, 32, v4
	v_bitop3_b32 v6, v5, s6, v4 bitop3:0xde
	s_lshl_b32 s6, s15, 5
	s_lshl_b32 s44, s12, 6
	s_and_b32 s12, s6, 0x60
	s_lshl_b32 s6, s12, 7
	s_cmp_gt_i32 s14, 63
	s_waitcnt vmcnt(6)
	s_cselect_b64 s[14:15], -1, 0
	s_add_i32 s45, s43, -2
	s_add_i32 s46, s22, 0xc000
	v_bitop3_b32 v4, v5, s6, v4 bitop3:0xde
	s_cmpk_lt_u32 s13, 0x100
	v_mov_b32_e32 v1, v0
	v_mov_b32_e32 v2, v0
	v_mov_b32_e32 v3, v0
	s_mov_b32 s42, 0
	s_cselect_b64 s[16:17], -1, 0
	s_mov_b32 s13, s40
	s_add_i32 s47, s22, 0xe000
	v_add_u32_e32 v154, 0, v4
	v_add_u32_e32 v155, 0, v6
	s_barrier
	s_mov_b32 s100, 0
	s_branch .LBB0_1777

;     __device__ __forceinline__ unsigned a_off(const Unit& u, const Gemm& g) const { return (unsigned)u.pm * (unsigned)(BM * 2) * (unsigned)g.K; }
;     __device__ __forceinline__ unsigned b_off(const Unit& u, const Gemm& g) const { return (unsigned)u.pn * (unsigned)(BM * 2) * (unsigned)g.K; }
;     __device__ __forceinline__ bool next(int i, Unit& u) const { return so.next(i, u); }
;     __device__ __forceinline__ unsigned a_off(const Unit& u, const Gemm& g) const { return (unsigned)u.pm * (unsigned)(BM * 2) * (unsigned)g.K; }
;     __device__ __forceinline__ bool next(int i, Unit& u) const { const bool ok = so.next(i >> 1, u); u.part = i & 1; return ok; }
;     __device__ __forceinline__ unsigned a_off(const Unit& u, const Gemm& g) const { return (unsigned)u.pm * (unsigned)(BM * 2) * (unsigned)g.K; }
;     __device__ __forceinline__ unsigned b_off(const Unit& u, const Gemm& g) const { return (unsigned)u.pn * (unsigned)(BM * 2) * (unsigned)g.K; }
; template <class Epi, class Sched, bool ALIGN_EPI = false, bool SP2 = false, bool FP8 = false>
; __device__ __forceinline__ void gemm_phase(LAS unsigned char* lds, const Gemm g, const Sched& S, const Epi& E, int wbase) {
;     ...
;         const bool has_next = S.next(ui + 1, nxt);
;         const unsigned nA = has_next ? S.a_off(nxt, g) : cA, nB = has_next ? S.b_off(nxt, g) : cB;
;         const rsrc_t rAn = (Sched::TWO && has_next) ? (nxt.part ? rA1 : rA0) : rAc, rBn = (Sched::TWO && has_next) ? (nxt.part ? rB1 : rB0) : rBc;
;         float pre_[8] = {0.f, 0.f, 0.f, 0.f, 0.f, 0.f, 0.f, 0.f};
;         if constexpr (Epi::HAS_PRE) E.pre_load(pre_, cur, wr);
;         for (int t = 0; t < nt; t += 2) {
;             const bool last = (t == nt - 2);
;             const unsigned a1 = cA + (unsigned)(t + 1) * kstep;
;             const unsigned a2 = last ? nA : cA + (unsigned)(t + 2) * kstep, b2 = last ? nB : cB + (unsigned)(t + 2) * kstep; const rsrc_t rA2 = (Sched::TWO && last) ? rAn : rAc, rB2 = (Sched::TWO && last) ? rBn : rBc;
;             const unsigned a3 = a2 + kstep, b3 = b2 + kstep;
;             if (last && has_next) S.a_ready(nxt);
;             if constexpr (SP2) {
;             PG8_LDB(B0, 0, 0); PG8_LDB(B1, 0, 1); PG8_SCHED; PG8_LDA(At, 0, 0); PG8_STAGE(PG8_SA(1, 1), rAc, a1 + hstep, voffA);
;             PG8_WAIT_V(8); PG8_WAIT_L(0); PG8_BAR; PG8_MMA(0, 0, At, B0); PG8_MMA(0, 1, At, B1); PG8_BAR; PG8_SCHED;
.LBB0_1779:
	s_lshl_b32 s53, s52, 18
	s_andn2_b64 vcc, exec, s[14:15]
	s_lshl_b32 s56, s48, 18
	s_cbranch_vccnz .LBB0_1783
	s_and_b64 s[6:7], s[18:19], exec
	v_mov_b64_e32 v[6:7], v[2:3]
	v_mov_b64_e32 v[22:23], v[2:3]
	v_mov_b64_e32 v[18:19], v[2:3]
	v_mov_b64_e32 v[38:39], v[2:3]
	v_mov_b64_e32 v[34:35], v[2:3]
	v_mov_b64_e32 v[54:55], v[2:3]
	v_mov_b64_e32 v[50:51], v[2:3]
	v_mov_b64_e32 v[14:15], v[2:3]
	v_mov_b64_e32 v[10:11], v[2:3]
	v_mov_b64_e32 v[30:31], v[2:3]
	v_mov_b64_e32 v[26:27], v[2:3]
	v_mov_b64_e32 v[46:47], v[2:3]
	v_mov_b64_e32 v[42:43], v[2:3]
	s_waitcnt vmcnt(37)
	v_mov_b64_e32 v[62:63], v[2:3]
	v_mov_b64_e32 v[58:59], v[2:3]
	s_waitcnt vmcnt(35)
	v_mov_b64_e32 v[70:71], v[2:3]
	v_mov_b64_e32 v[66:67], v[2:3]
	s_waitcnt vmcnt(31)
	v_mov_b64_e32 v[86:87], v[2:3]
	v_mov_b64_e32 v[82:83], v[2:3]
	s_waitcnt vmcnt(27)
	v_mov_b64_e32 v[102:103], v[2:3]
	v_mov_b64_e32 v[98:99], v[2:3]
	s_waitcnt vmcnt(23)
	v_mov_b64_e32 v[118:119], v[2:3]
	v_mov_b64_e32 v[114:115], v[2:3]
	v_mov_b64_e32 v[78:79], v[2:3]
	v_mov_b64_e32 v[74:75], v[2:3]
	v_mov_b64_e32 v[94:95], v[2:3]
	v_mov_b64_e32 v[90:91], v[2:3]
	v_mov_b64_e32 v[110:111], v[2:3]
	v_mov_b64_e32 v[106:107], v[2:3]
	v_mov_b64_e32 v[126:127], v[2:3]
	s_waitcnt vmcnt(22)
	v_mov_b64_e32 v[122:123], v[2:3]
	v_mov_b32_e32 v225, 1
	v_mov_b32_e32 v223, v233
	v_mov_b32_e32 v222, 0x358637bd
	s_cselect_b32 s59, s53, s55
	s_cselect_b32 s60, s56, s54
	s_add_i32 s61, s55, 0x80
	s_add_i32 s62, s54, 0x100
	s_mov_b32 s63, 0
	v_mov_b64_e32 v[4:5], v[0:1]
	v_mov_b64_e32 v[20:21], v[0:1]
	v_mov_b64_e32 v[16:17], v[0:1]
	v_mov_b64_e32 v[36:37], v[0:1]
	v_mov_b64_e32 v[32:33], v[0:1]
	v_mov_b64_e32 v[52:53], v[0:1]
	v_mov_b64_e32 v[48:49], v[0:1]
	v_mov_b64_e32 v[12:13], v[0:1]
	v_mov_b64_e32 v[8:9], v[0:1]
	v_mov_b64_e32 v[28:29], v[0:1]
	v_mov_b64_e32 v[24:25], v[0:1]
	v_mov_b64_e32 v[44:45], v[0:1]
	v_mov_b64_e32 v[40:41], v[0:1]
	v_mov_b64_e32 v[60:61], v[0:1]
	v_mov_b64_e32 v[56:57], v[0:1]
	v_mov_b64_e32 v[68:69], v[0:1]
	v_mov_b64_e32 v[64:65], v[0:1]
	v_mov_b64_e32 v[84:85], v[0:1]
	v_mov_b64_e32 v[80:81], v[0:1]
	v_mov_b64_e32 v[100:101], v[0:1]
	v_mov_b64_e32 v[96:97], v[0:1]
	v_mov_b64_e32 v[116:117], v[0:1]
	v_mov_b64_e32 v[112:113], v[0:1]
	v_mov_b64_e32 v[76:77], v[0:1]
	v_mov_b64_e32 v[72:73], v[0:1]
	v_mov_b64_e32 v[92:93], v[0:1]
	v_mov_b64_e32 v[88:89], v[0:1]
	v_mov_b64_e32 v[108:109], v[0:1]
	v_mov_b64_e32 v[104:105], v[0:1]
	v_mov_b64_e32 v[124:125], v[0:1]
	v_mov_b64_e32 v[120:121], v[0:1]
	s_cmp_eq_u32 s100, 1
	s_cbranch_scc0 .LBB0_1781
	v_add_u32_e32 v140, 0x10000, v154
	v_add_u32_e32 v144, 0x14000, v154
	ds_read_b128 v[128:131], v140
	ds_read_b128 v[132:135], v140 offset:1024
	ds_read_b128 v[136:139], v140 offset:2048
	ds_read_b128 v[140:143], v140 offset:3072
	ds_read_b128 v[156:159], v144
	ds_read_b128 v[160:163], v144 offset:1024
	ds_read_b128 v[164:167], v144 offset:2048
	ds_read_b128 v[168:171], v144 offset:3072
	s_add_i32 s6, s61, 0x80
	s_cmp_eq_u32 s45, s63
	s_cselect_b32 s65, s59, s6
	s_cselect_b32 s55, s60, s62
	s_or_b32 s54, s65, 0x80
	s_add_i32 s6, s21, s61
	s_mov_b32 m0, s46
	ds_read_b128 v[172:175], v155
	ds_read_b128 v[176:179], v155 offset:1024
	ds_read_b128 v[180:183], v155 offset:2048
	ds_read_b128 v[184:187], v155 offset:3072
	ds_read_b128 v[194:197], v155 offset:4096
	ds_read_b128 v[198:201], v155 offset:5120
	ds_read_b128 v[202:205], v155 offset:6144
	ds_read_b128 v[206:209], v155 offset:7168
	buffer_load_dwordx4 v148, s[36:39], s6 offen lds
	s_mov_b32 m0, s47
	s_nop 0
	buffer_load_dwordx4 v150, s[36:39], s6 offen lds
	s_waitcnt vmcnt(24)
	s_waitcnt lgkmcnt(0)
	s_barrier
	s_setprio 1
	s_waitcnt lgkmcnt(6)
	v_mfma_scale_f32_16x16x128_f8f6f4 v[120:123], v[128:135], v[172:179], v[120:123], v224, v224 op_sel_hi:[0,0,0]
	v_mfma_scale_f32_16x16x128_f8f6f4 v[124:127], v[136:143], v[172:179], v[124:127], v224, v224 op_sel_hi:[0,0,0]
	s_waitcnt lgkmcnt(4)
	v_mfma_scale_f32_16x16x128_f8f6f4 v[104:107], v[128:135], v[180:187], v[104:107], v224, v224 op_sel_hi:[0,0,0]
	v_mfma_scale_f32_16x16x128_f8f6f4 v[108:111], v[136:143], v[180:187], v[108:111], v224, v224 op_sel_hi:[0,0,0]
	s_waitcnt lgkmcnt(2)
	v_mfma_scale_f32_16x16x128_f8f6f4 v[144:147], v[128:135], v[194:201], v[88:91], v224, v224 op_sel_hi:[0,0,0]
	v_mfma_scale_f32_16x16x128_f8f6f4 v[188:191], v[136:143], v[194:201], v[92:95], v224, v224 op_sel_hi:[0,0,0]
	s_waitcnt lgkmcnt(0)
	v_mfma_scale_f32_16x16x128_f8f6f4 v[210:213], v[128:135], v[202:209], v[72:75], v224, v224 op_sel_hi:[0,0,0]
	v_mfma_scale_f32_16x16x128_f8f6f4 v[214:217], v[136:143], v[202:209], v[76:79], v224, v224 op_sel_hi:[0,0,0]
	s_setprio 0
	s_setprio 1
	v_mfma_scale_f32_16x16x128_f8f6f4 v[112:115], v[156:163], v[172:179], v[112:115], v224, v224 op_sel_hi:[0,0,0]
	v_mfma_scale_f32_16x16x128_f8f6f4 v[116:119], v[164:171], v[172:179], v[116:119], v224, v224 op_sel_hi:[0,0,0]
	v_mfma_scale_f32_16x16x128_f8f6f4 v[96:99], v[156:163], v[180:187], v[96:99], v224, v224 op_sel_hi:[0,0,0]
	v_mfma_scale_f32_16x16x128_f8f6f4 v[100:103], v[164:171], v[180:187], v[100:103], v224, v224 op_sel_hi:[0,0,0]
	v_mfma_scale_f32_16x16x128_f8f6f4 v[172:175], v[156:163], v[194:201], v[80:83], v224, v224 op_sel_hi:[0,0,0]
	v_mfma_scale_f32_16x16x128_f8f6f4 v[176:179], v[164:171], v[194:201], v[84:87], v224, v224 op_sel_hi:[0,0,0]
	v_mfma_scale_f32_16x16x128_f8f6f4 v[180:183], v[156:163], v[202:209], v[64:67], v224, v224 op_sel_hi:[0,0,0]
	v_mfma_scale_f32_16x16x128_f8f6f4 v[184:187], v[164:171], v[202:209], v[68:71], v224, v224 op_sel_hi:[0,0,0]
	s_setprio 0
	s_barrier
; #define PG8_STAGE(bufoff, rs_, soff_, voff) do { _Pragma("unroll") for (int _i = 0; _i < 2; ++_i) \
;         __builtin_amdgcn_raw_ptr_buffer_load_lds(rs_, (LAS void*)(lds + (bufoff) + ldsw + _i * 8192), 16, (int)(voff)[_i], (int)(soff_), 0, 0); } while (0)
; #define PG8_LDA(dst, b, h) do { _Pragma("unroll") for (int m = 0; m < 4; ++m) dst[m] = PG8_LD2(lds + PG8_SA(b, h) + aoff + m * 2048); } while (0)
; #define PG8_LDB(dst, b, h) do { _Pragma("unroll") for (int n = 0; n < 2; ++n) dst[n] = PG8_LD2(lds + PG8_SB(b, h) + boff + n * 2048); } while (0)
; #define PG8_WAIT_V(n) asm volatile("s_waitcnt vmcnt(" #n ")" ::: "memory")
; #define PG8_WAIT_L(n) asm volatile("s_waitcnt lgkmcnt(" #n ")" ::: "memory")
; #define PG8_BAR __builtin_amdgcn_s_barrier()
; #define PG8_SCHED __builtin_amdgcn_sched_barrier(0)
; template <class Epi, class Sched, bool ALIGN_EPI = false, bool SP2 = false, bool FP8 = false>
; __device__ __forceinline__ void gemm_phase(LAS unsigned char* lds, const Gemm g, const Sched& S, const Epi& E, int wbase) {
;     ...
;             PG8_LDA(At, 0, 1); PG8_STAGE(PG8_SB(0, 0), rB2, b2, voffB); PG8_STAGE(PG8_SB(0, 1), rB2, b2 + hstep, voffB); PG8_STAGE(PG8_SA(0, 0), rA2, a2, voffA);
;             PG8_WAIT_V(8); PG8_WAIT_L(0); PG8_BAR; PG8_MMA(1, 0, At, B0); PG8_MMA(1, 1, At, B1); PG8_BAR; PG8_SCHED;
;             PG8_LDB(B0, 1, 0); PG8_LDB(B1, 1, 1); PG8_SCHED; PG8_LDA(At, 1, 0); PG8_STAGE(PG8_SA(0, 1), rA2, a2 + hstep, voffA);
;             PG8_WAIT_V(8); PG8_WAIT_L(0); PG8_BAR; PG8_MMA(0, 0, At, B0); PG8_MMA(0, 1, At, B1); PG8_BAR; PG8_SCHED;
	s_mov_b32 m0, s23
	s_mov_b32 s6, s38
	s_mov_b32 s7, s39
	s_nop 0
	ds_read_b128 v[64:67], v155 offset:16384
	ds_read_b128 v[68:71], v155 offset:17408
	ds_read_b128 v[72:75], v155 offset:18432
	ds_read_b128 v[76:79], v155 offset:19456
	ds_read_b128 v[80:83], v155 offset:20480
	ds_read_b128 v[84:87], v155 offset:21504
	ds_read_b128 v[88:91], v155 offset:22528
	ds_read_b128 v[92:95], v155 offset:23552
	buffer_load_dwordx4 v149, s[4:7], s55 offen lds
	s_mov_b32 m0, s24
	s_add_i32 s66, s55, s21
	buffer_load_dwordx4 v151, s[4:7], s55 offen lds
	s_mov_b32 m0, s25
	s_nop 0
	buffer_load_dwordx4 v149, s[4:7], s66 offen lds
	s_mov_b32 m0, s26
	s_nop 0
	buffer_load_dwordx4 v151, s[4:7], s66 offen lds
	s_mov_b32 m0, s22
	s_nop 0
	buffer_load_dwordx4 v148, s[36:39], s65 offen lds
	s_mov_b32 m0, s27
	s_nop 0
	buffer_load_dwordx4 v150, s[36:39], s65 offen lds
	s_waitcnt vmcnt(24)
	s_waitcnt lgkmcnt(0)
	s_barrier
	s_setprio 1
	s_waitcnt lgkmcnt(6)
	v_mfma_scale_f32_16x16x128_f8f6f4 v[56:59], v[128:135], v[64:71], v[56:59], v224, v224 op_sel_hi:[0,0,0]
	v_mfma_scale_f32_16x16x128_f8f6f4 v[60:63], v[136:143], v[64:71], v[60:63], v224, v224 op_sel_hi:[0,0,0]
	s_waitcnt lgkmcnt(0)
	v_mfma_scale_f32_16x16x128_f8f6f4 v[8:11], v[128:135], v[88:95], v[8:11], v224, v224 op_sel_hi:[0,0,0]
	v_mfma_scale_f32_16x16x128_f8f6f4 v[192:195], v[128:135], v[72:79], v[40:43], v224, v224 op_sel_hi:[0,0,0]
	v_mfma_scale_f32_16x16x128_f8f6f4 v[196:199], v[136:143], v[72:79], v[44:47], v224, v224 op_sel_hi:[0,0,0]
	v_mfma_scale_f32_16x16x128_f8f6f4 v[200:203], v[128:135], v[80:87], v[24:27], v224, v224 op_sel_hi:[0,0,0]
	v_mfma_scale_f32_16x16x128_f8f6f4 v[204:207], v[136:143], v[80:87], v[28:31], v224, v224 op_sel_hi:[0,0,0]
	v_mfma_scale_f32_16x16x128_f8f6f4 v[218:221], v[136:143], v[88:95], v[12:15], v224, v224 op_sel_hi:[0,0,0]
	s_setprio 0
	s_setprio 1
	v_mfma_scale_f32_16x16x128_f8f6f4 v[52:55], v[164:171], v[64:71], v[52:55], v224, v224 op_sel_hi:[0,0,0]
	v_mfma_scale_f32_16x16x128_f8f6f4 v[226:229], v[156:163], v[64:71], v[48:51], v224, v224 op_sel_hi:[0,0,0]
	v_mfma_scale_f32_16x16x128_f8f6f4 v[230:233], v[156:163], v[72:79], v[32:35], v224, v224 op_sel_hi:[0,0,0]
	v_mfma_scale_f32_16x16x128_f8f6f4 v[234:237], v[164:171], v[72:79], v[36:39], v224, v224 op_sel_hi:[0,0,0]
	v_mfma_scale_f32_16x16x128_f8f6f4 v[238:241], v[156:163], v[80:87], v[16:19], v224, v224 op_sel_hi:[0,0,0]
	v_mfma_scale_f32_16x16x128_f8f6f4 v[242:245], v[164:171], v[80:87], v[20:23], v224, v224 op_sel_hi:[0,0,0]
	v_mfma_scale_f32_16x16x128_f8f6f4 v[246:249], v[156:163], v[88:95], v[4:7], v224, v224 op_sel_hi:[0,0,0]
	v_mfma_scale_f32_16x16x128_f8f6f4 v[250:253], v[164:171], v[88:95], v[0:3], v224, v224 op_sel_hi:[0,0,0]
	s_setprio 0
	s_barrier
	s_nop 1
	v_add_u32_e32 v16, 0x18000, v154
	v_add_u32_e32 v20, 0x1c000, v154
	s_nop 0
	ds_read_b128 v[0:3], v16
	ds_read_b128 v[4:7], v16 offset:1024
	ds_read_b128 v[12:15], v16 offset:2048
	ds_read_b128 v[16:19], v16 offset:3072
	ds_read_b128 v[128:131], v20
	ds_read_b128 v[132:135], v20 offset:1024
	ds_read_b128 v[136:139], v20 offset:2048
	ds_read_b128 v[140:143], v20 offset:3072
	s_add_i32 s65, s65, s21
	s_mov_b32 m0, s28
	ds_read_b128 v[20:23], v155 offset:32768
	ds_read_b128 v[24:27], v155 offset:33792
	ds_read_b128 v[28:31], v155 offset:34816
	ds_read_b128 v[32:35], v155 offset:35840
	ds_read_b128 v[36:39], v155 offset:36864
	ds_read_b128 v[40:43], v155 offset:37888
	ds_read_b128 v[44:47], v155 offset:38912
	ds_read_b128 v[48:51], v155 offset:39936
	buffer_load_dwordx4 v148, s[36:39], s65 offen lds
	s_mov_b32 m0, s29
	s_nop 0
	buffer_load_dwordx4 v150, s[36:39], s65 offen lds
	s_waitcnt vmcnt(8)
	s_waitcnt lgkmcnt(0)
	s_barrier
; #define PG8_STAGE(bufoff, rs_, soff_, voff) do { _Pragma("unroll") for (int _i = 0; _i < 2; ++_i) \
;         __builtin_amdgcn_raw_ptr_buffer_load_lds(rs_, (LAS void*)(lds + (bufoff) + ldsw + _i * 8192), 16, (int)(voff)[_i], (int)(soff_), 0, 0); } while (0)
; #define PG8_LDA(dst, b, h) do { _Pragma("unroll") for (int m = 0; m < 4; ++m) dst[m] = PG8_LD2(lds + PG8_SA(b, h) + aoff + m * 2048); } while (0)
; #define PG8_WAIT_V(n) asm volatile("s_waitcnt vmcnt(" #n ")" ::: "memory")
; #define PG8_WAIT_L(n) asm volatile("s_waitcnt lgkmcnt(" #n ")" ::: "memory")
; #define PG8_BAR __builtin_amdgcn_s_barrier()
; #define PG8_SCHED __builtin_amdgcn_sched_barrier(0)
; template <class Epi, class Sched, bool ALIGN_EPI = false, bool SP2 = false, bool FP8 = false>
; __device__ __forceinline__ void gemm_phase(LAS unsigned char* lds, const Gemm g, const Sched& S, const Epi& E, int wbase) {
;     ...
;             PG8_WAIT_V(8); PG8_WAIT_L(0); PG8_BAR; PG8_MMA(0, 0, At, B0); PG8_MMA(0, 1, At, B1); PG8_BAR; PG8_SCHED;
;             PG8_LDA(At, 1, 1); PG8_STAGE(PG8_SB(1, 0), rB2, b3, voffB); PG8_STAGE(PG8_SB(1, 1), rB2, b3 + hstep, voffB); PG8_STAGE(PG8_SA(1, 0), rA2, a3, voffA);
;             PG8_WAIT_V(8); PG8_WAIT_L(0); PG8_BAR; PG8_MMA(1, 0, At, B0); PG8_MMA(1, 1, At, B1); PG8_BAR; PG8_SCHED;
	s_setprio 1
	s_waitcnt lgkmcnt(6)
	v_mfma_scale_f32_16x16x128_f8f6f4 v[120:123], v[0:7], v[20:27], v[120:123], v224, v224 op_sel_hi:[0,0,0]
	v_mfma_scale_f32_16x16x128_f8f6f4 v[124:127], v[12:19], v[20:27], v[124:127], v224, v224 op_sel_hi:[0,0,0]
	s_waitcnt lgkmcnt(4)
	v_mfma_scale_f32_16x16x128_f8f6f4 v[104:107], v[0:7], v[28:35], v[104:107], v224, v224 op_sel_hi:[0,0,0]
	v_mfma_scale_f32_16x16x128_f8f6f4 v[108:111], v[12:19], v[28:35], v[108:111], v224, v224 op_sel_hi:[0,0,0]
	s_waitcnt lgkmcnt(2)
	v_mfma_scale_f32_16x16x128_f8f6f4 v[88:91], v[0:7], v[36:43], v[144:147], v224, v224 op_sel_hi:[0,0,0]
	v_mfma_scale_f32_16x16x128_f8f6f4 v[92:95], v[12:19], v[36:43], v[188:191], v224, v224 op_sel_hi:[0,0,0]
	s_waitcnt lgkmcnt(0)
	v_mfma_scale_f32_16x16x128_f8f6f4 v[72:75], v[0:7], v[44:51], v[210:213], v224, v224 op_sel_hi:[0,0,0]
	v_mfma_scale_f32_16x16x128_f8f6f4 v[76:79], v[12:19], v[44:51], v[214:217], v224, v224 op_sel_hi:[0,0,0]
	s_setprio 0
	s_setprio 1
	v_mfma_scale_f32_16x16x128_f8f6f4 v[112:115], v[128:135], v[20:27], v[112:115], v224, v224 op_sel_hi:[0,0,0]
	v_mfma_scale_f32_16x16x128_f8f6f4 v[116:119], v[136:143], v[20:27], v[116:119], v224, v224 op_sel_hi:[0,0,0]
	v_mfma_scale_f32_16x16x128_f8f6f4 v[96:99], v[128:135], v[28:35], v[96:99], v224, v224 op_sel_hi:[0,0,0]
	v_mfma_scale_f32_16x16x128_f8f6f4 v[100:103], v[136:143], v[28:35], v[100:103], v224, v224 op_sel_hi:[0,0,0]
	v_mfma_scale_f32_16x16x128_f8f6f4 v[80:83], v[128:135], v[36:43], v[172:175], v224, v224 op_sel_hi:[0,0,0]
	v_mfma_scale_f32_16x16x128_f8f6f4 v[84:87], v[136:143], v[36:43], v[176:179], v224, v224 op_sel_hi:[0,0,0]
	v_mfma_scale_f32_16x16x128_f8f6f4 v[64:67], v[128:135], v[44:51], v[180:183], v224, v224 op_sel_hi:[0,0,0]
	v_mfma_scale_f32_16x16x128_f8f6f4 v[68:71], v[136:143], v[44:51], v[184:187], v224, v224 op_sel_hi:[0,0,0]
	s_setprio 0
	s_barrier
	s_mov_b32 m0, s30
	s_bitset1_b32 s55, 7
	ds_read_b128 v[32:35], v155 offset:49152
	ds_read_b128 v[36:39], v155 offset:50176
	ds_read_b128 v[156:159], v155 offset:51200
	ds_read_b128 v[160:163], v155 offset:52224
	ds_read_b128 v[164:167], v155 offset:53248
	ds_read_b128 v[168:171], v155 offset:54272
	ds_read_b128 v[172:175], v155 offset:55296
	ds_read_b128 v[176:179], v155 offset:56320
	buffer_load_dwordx4 v149, s[4:7], s55 offen lds
	s_mov_b32 m0, s31
	s_nop 0
	buffer_load_dwordx4 v151, s[4:7], s55 offen lds
	s_add_i32 s55, s55, s21
	s_mov_b32 m0, s35
	s_nop 0
	buffer_load_dwordx4 v149, s[4:7], s55 offen lds
	s_mov_b32 m0, s41
	s_nop 0
	buffer_load_dwordx4 v151, s[4:7], s55 offen lds
	s_mov_b32 m0, s33
	s_nop 0
	buffer_load_dwordx4 v148, s[36:39], s54 offen lds
	s_mov_b32 m0, s34
	s_nop 0
	buffer_load_dwordx4 v150, s[36:39], s54 offen lds
	s_waitcnt vmcnt(8)
	s_waitcnt lgkmcnt(0)
	s_barrier
	s_setprio 1
	s_waitcnt lgkmcnt(6)
	v_mfma_scale_f32_16x16x128_f8f6f4 v[56:59], v[0:7], v[32:39], v[56:59], v224, v224 op_sel_hi:[0,0,0]
	v_mfma_scale_f32_16x16x128_f8f6f4 v[60:63], v[12:19], v[32:39], v[60:63], v224, v224 op_sel_hi:[0,0,0]
	s_waitcnt lgkmcnt(4)
	v_mfma_scale_f32_16x16x128_f8f6f4 v[40:43], v[0:7], v[156:163], v[192:195], v224, v224 op_sel_hi:[0,0,0]
	v_mfma_scale_f32_16x16x128_f8f6f4 v[44:47], v[12:19], v[156:163], v[196:199], v224, v224 op_sel_hi:[0,0,0]
	s_waitcnt lgkmcnt(2)
	v_mfma_scale_f32_16x16x128_f8f6f4 v[24:27], v[0:7], v[164:171], v[200:203], v224, v224 op_sel_hi:[0,0,0]
	v_mfma_scale_f32_16x16x128_f8f6f4 v[28:31], v[12:19], v[164:171], v[204:207], v224, v224 op_sel_hi:[0,0,0]
	s_waitcnt lgkmcnt(0)
	v_mfma_scale_f32_16x16x128_f8f6f4 v[8:11], v[0:7], v[172:179], v[8:11], v224, v224 op_sel_hi:[0,0,0]
	v_mfma_scale_f32_16x16x128_f8f6f4 v[12:15], v[12:19], v[172:179], v[218:221], v224, v224 op_sel_hi:[0,0,0]
	s_setprio 0
	s_setprio 1
	v_mfma_scale_f32_16x16x128_f8f6f4 v[48:51], v[128:135], v[32:39], v[226:229], v224, v224 op_sel_hi:[0,0,0]
	v_mfma_scale_f32_16x16x128_f8f6f4 v[52:55], v[136:143], v[32:39], v[52:55], v224, v224 op_sel_hi:[0,0,0]
	v_mfma_scale_f32_16x16x128_f8f6f4 v[32:35], v[128:135], v[156:163], v[230:233], v224, v224 op_sel_hi:[0,0,0]
	v_mfma_scale_f32_16x16x128_f8f6f4 v[36:39], v[136:143], v[156:163], v[234:237], v224, v224 op_sel_hi:[0,0,0]
	v_mfma_scale_f32_16x16x128_f8f6f4 v[16:19], v[128:135], v[164:171], v[238:241], v224, v224 op_sel_hi:[0,0,0]
	v_mfma_scale_f32_16x16x128_f8f6f4 v[20:23], v[136:143], v[164:171], v[242:245], v224, v224 op_sel_hi:[0,0,0]
	v_mfma_scale_f32_16x16x128_f8f6f4 v[4:7], v[128:135], v[172:179], v[246:249], v224, v224 op_sel_hi:[0,0,0]
	v_mfma_scale_f32_16x16x128_f8f6f4 v[0:3], v[136:143], v[172:179], v[250:253], v224, v224 op_sel_hi:[0,0,0]
	s_setprio 0
	s_barrier
	s_add_i32 s63, s63, 2
	s_addk_i32 s61, 0x100
	s_addk_i32 s62, 0x100
	s_cmp_ge_i32 s63, s43
	s_cbranch_scc0 .LBB0_1781
	s_branch .Lpeel_after_1781

; #define PG8_BAR __builtin_amdgcn_s_barrier()
; #define PG8_ZERO_ACC() do { float z_; asm volatile("v_mov_b32 %0, 0" : "=v"(z_)); _Pragma("unroll") for (int a = 0; a < 2; ++a) _Pragma("unroll") for (int b = 0; b < 2; ++b) _Pragma("unroll") for (int m = 0; m < 4; ++m) \
;         _Pragma("unroll") for (int n = 0; n < 2; ++n) acc[a][b][m][n] = (f32x4){z_, z_, z_, z_}; } while (0)
; template <class Epi, class Sched, bool ALIGN_EPI = false, bool SP2 = false, bool FP8 = false>
; __device__ __forceinline__ void gemm_phase(LAS unsigned char* lds, const Gemm g, const Sched& S, const Epi& E, int wbase) {
;     ...
;         }
;         if constexpr (ALIGN_EPI) { if (wr == 0) PG8_BAR; }
;         { int fr_ = fr, fq_ = fq; asm volatile("" : "+v"(fr_), "+v"(fq_));
;           if constexpr (Epi::HAS_PRE) E(acc, cur, wr, wc, fr_, fq_, pre_); else E(acc, cur, wr, wc, fr_, fq_); } S.done(cur);
;         if (!has_next) break;
;         if (E.reset(cur)) PG8_ZERO_ACC();
.Lpeel_after_1781:
	s_mov_b32 s100, 1
	v_mov_b32_e32 v230, v222
	v_mov_b32_e32 v233, v223
	v_mov_b32_e32 v231, v225
	v_mov_b32_e32 v234, 0xff61b1e6
	s_and_b64 vcc, exec, s[16:17]
	s_cbranch_vccnz .LBB0_1784
	s_branch .LBB0_1785

;     __device__ __forceinline__ unsigned a_off(const Unit& u, const Gemm& g) const { return (unsigned)u.pm * (unsigned)(BM * 2) * (unsigned)g.K; }
;     __device__ __forceinline__ unsigned b_off(const Unit& u, const Gemm& g) const { return (unsigned)u.pn * (unsigned)(BM * 2) * (unsigned)g.K; }
;     __device__ __forceinline__ bool next(int i, Unit& u) const { return so.next(i, u); }
; template <class Epi, class Sched, bool ALIGN_EPI = false, bool SP2 = false, bool FP8 = false>
; __device__ __forceinline__ void gemm_phase(LAS unsigned char* lds, const Gemm g, const Sched& S, const Epi& E, int wbase) {
;     ...
;     for (int i = 0; i < 2; ++i) { int R, C; stage_rc(tid * 16 + i * 8192, R, C); const int Rb = Epi::PERM ? ((R & ~31) + perm32(R & 31)) : R;
;         voffA[i] = (unsigned)(R * K + C) * 2u; voffB[i] = (unsigned)(Rb * K + C) * 2u; }
;     const unsigned kstep = (unsigned)(BK * 2);
;     const unsigned hstep = (unsigned)HALF * (unsigned)K * 2u;
;     typedef __amdgpu_buffer_rsrc_t rsrc_t;
;     const rsrc_t rA0 = __builtin_amdgcn_make_buffer_rsrc((void*)g.A, 0, 0xffffffff, 0x00020000), rB0 = __builtin_amdgcn_make_buffer_rsrc((void*)g.Bt, 0, 0xffffffff, 0x00020000);
;     rsrc_t rA1 = rA0, rB1 = rB0;
;     if constexpr (Sched::TWO) { rA1 = __builtin_amdgcn_make_buffer_rsrc((void*)S.A1, 0, 0xffffffff, 0x00020000); rB1 = __builtin_amdgcn_make_buffer_rsrc((void*)S.Bt1, 0, 0xffffffff, 0x00020000); }
;     const unsigned ldsw = (unsigned)wid * 1024u;
;     const int aoff = lds_byte(wr * 64 + fr, fq * 8), boff = lds_byte(wc * 32 + fr, fq * 8);
;     ...
;     Unit cur, nxt; int ui = 0;
;     if (!S.next(0, cur)) return;
;     f32x4 acc[2][2][4][2];
;     ...
;     PG8_ZERO_ACC();
;     v8i_t At[4], B0[2], B1[2];
;     unsigned cA = S.a_off(cur, g), cB = S.b_off(cur, g); rsrc_t rAc = (Sched::TWO && cur.part) ? rA1 : rA0, rBc = (Sched::TWO && cur.part) ? rB1 : rB0;
;     S.a_ready(cur);
;     if constexpr (SP2) {
;         PG8_STAGE(PG8_SB(0, 0), rBc, cB, voffB); PG8_STAGE(PG8_SB(0, 1), rBc, cB + hstep, voffB); PG8_STAGE(PG8_SA(0, 0), rAc, cA, voffA); PG8_STAGE(PG8_SA(0, 1), rAc, cA + hstep, voffA);
;         if (wr == 1) PG8_BAR;
;         PG8_WAIT_V(2); PG8_BAR;
;         PG8_STAGE(PG8_SB(1, 0), rBc, cB + kstep, voffB); PG8_STAGE(PG8_SA(1, 0), rAc, cA + kstep, voffA); PG8_STAGE(PG8_SB(1, 1), rBc, cB + hstep + kstep, voffB);
;         PG8_WAIT_V(6); PG8_BAR;
.LBB0_1843:
	v_readlane_b32 s6, v255, 10
	s_cmp_eq_u32 s6, 0
	s_mov_b32 s6, 0x13200000
	s_cselect_b32 s6, s6, 0x1b800000
	s_add_u32 s8, s10, s6
	s_addc_u32 s9, s11, 0
	v_readlane_b32 s6, v255, 11
	s_cmp_eq_u32 s6, 0
	s_cselect_b32 s6, 0, 0x200000
	s_add_u32 s6, s10, s6
	s_addc_u32 s7, s11, 0
	s_add_u32 s10, s6, 0x17200000
	s_addc_u32 s11, s7, 0
	s_add_i32 s34, s25, 0x18000
	s_or_b32 s17, s54, 0x80
	s_mov_b32 s6, s38
	s_mov_b32 s7, s39
	s_mov_b32 m0, s34
	s_add_i32 s35, s25, 0x1a000
	s_waitcnt vmcnt(2)
	s_barrier
	buffer_load_dwordx4 v171, s[4:7], s17 offen lds
	s_mov_b32 m0, s35
	s_add_i32 s41, s25, 0x8000
	buffer_load_dwordx4 v173, s[4:7], s17 offen lds
	s_or_b32 s17, s55, 0x80
	s_mov_b32 m0, s41
	s_add_i32 s42, s25, 0xa000
	buffer_load_dwordx4 v170, s[36:39], s17 offen lds
	s_mov_b32 m0, s42
	s_add_i32 s43, s25, 0x1c000
	buffer_load_dwordx4 v172, s[36:39], s17 offen lds
	s_bitset1_b32 s16, 7
	s_mov_b32 m0, s43
	s_add_i32 s44, s25, 0x1e000
	buffer_load_dwordx4 v171, s[4:7], s16 offen lds
	s_mov_b32 m0, s44
	v_bfe_u32 v175, v4, 4, 2
	buffer_load_dwordx4 v173, s[4:7], s16 offen lds
	s_ashr_i32 s6, s14, 31
	s_lshr_b32 s6, s6, 26
	v_and_b32_e32 v174, 15, v4
	s_add_i32 s6, s14, s6
	v_lshlrev_b32_e32 v5, 4, v175
	v_lshlrev_b32_e32 v4, 2, v4
	s_and_b32 s46, s12, 3
	s_ashr_i32 s47, s6, 6
	v_lshl_or_b32 v5, v174, 6, v5
	s_lshl_b32 s6, s15, 13
	v_and_b32_e32 v4, 32, v4
	s_lshl_b32 s48, s15, 6
	v_bitop3_b32 v6, v5, s6, v4 bitop3:0xde
	s_lshl_b32 s12, s46, 5
	s_lshl_b32 s6, s46, 12
	s_cmp_gt_i32 s14, 63
	s_cselect_b64 s[14:15], -1, 0
	s_add_i32 s52, s47, -2
	s_add_i32 s53, s25, 0xc000
	s_cmpk_lt_u32 s13, 0x100
	v_bitop3_b32 v4, v5, s6, v4 bitop3:0xde
	s_waitcnt vmcnt(6)
	s_cselect_b64 s[16:17], -1, 0
	s_add_i32 s56, s25, 0xe000
	s_lshl_b32 s6, s46, 6
	s_add_u32 s57, s8, s6
	v_mov_b32_e32 v1, v0
	v_mov_b32_e32 v2, v0
	v_mov_b32_e32 v3, v0
	s_mov_b32 s45, 0
	s_mov_b32 s13, s40
	s_addc_u32 s58, s9, 0
	v_add_u32_e32 v176, 0, v4
	v_add_u32_e32 v177, 0, v6
	s_barrier
	s_mov_b32 s100, 0
	s_branch .LBB0_1846

;     __device__ __forceinline__ unsigned a_off(const Unit& u, const Gemm& g) const { return (unsigned)u.pm * (unsigned)(BM * 2) * (unsigned)g.K; }
;     __device__ __forceinline__ unsigned b_off(const Unit& u, const Gemm& g) const { return (unsigned)u.pn * (unsigned)(BM * 2) * (unsigned)g.K; }
;     __device__ __forceinline__ bool next(int i, Unit& u) const { return so.next(i, u); }
;     __device__ __forceinline__ unsigned a_off(const Unit& u, const Gemm& g) const { return (unsigned)u.pm * (unsigned)(BM * 2) * (unsigned)g.K; }
;     __device__ __forceinline__ bool next(int i, Unit& u) const { const bool ok = so.next(i >> 1, u); u.part = i & 1; return ok; }
;     __device__ __forceinline__ unsigned a_off(const Unit& u, const Gemm& g) const { return (unsigned)u.pm * (unsigned)(BM * 2) * (unsigned)g.K; }
;     __device__ __forceinline__ unsigned b_off(const Unit& u, const Gemm& g) const { return (unsigned)u.pn * (unsigned)(BM * 2) * (unsigned)g.K; }
; template <class Epi, class Sched, bool ALIGN_EPI = false, bool SP2 = false, bool FP8 = false>
; __device__ __forceinline__ void gemm_phase(LAS unsigned char* lds, const Gemm g, const Sched& S, const Epi& E, int wbase) {
;     ...
;         const bool has_next = S.next(ui + 1, nxt);
;         const unsigned nA = has_next ? S.a_off(nxt, g) : cA, nB = has_next ? S.b_off(nxt, g) : cB;
;         const rsrc_t rAn = (Sched::TWO && has_next) ? (nxt.part ? rA1 : rA0) : rAc, rBn = (Sched::TWO && has_next) ? (nxt.part ? rB1 : rB0) : rBc;
;         float pre_[8] = {0.f, 0.f, 0.f, 0.f, 0.f, 0.f, 0.f, 0.f};
;         if constexpr (Epi::HAS_PRE) E.pre_load(pre_, cur, wr);
;         for (int t = 0; t < nt; t += 2) {
;             const bool last = (t == nt - 2);
;             const unsigned a1 = cA + (unsigned)(t + 1) * kstep;
;             const unsigned a2 = last ? nA : cA + (unsigned)(t + 2) * kstep, b2 = last ? nB : cB + (unsigned)(t + 2) * kstep; const rsrc_t rA2 = (Sched::TWO && last) ? rAn : rAc, rB2 = (Sched::TWO && last) ? rBn : rBc;
;             const unsigned a3 = a2 + kstep, b3 = b2 + kstep;
;             if (last && has_next) S.a_ready(nxt);
;             if constexpr (SP2) {
;             PG8_LDB(B0, 0, 0); PG8_LDB(B1, 0, 1); PG8_SCHED; PG8_LDA(At, 0, 0); PG8_STAGE(PG8_SA(1, 1), rAc, a1 + hstep, voffA);
;             PG8_WAIT_V(8); PG8_WAIT_L(0); PG8_BAR; PG8_MMA(0, 0, At, B0); PG8_MMA(0, 1, At, B1); PG8_BAR; PG8_SCHED;
.LBB0_1852:
	s_mul_i32 s61, s60, 0xe0000
	s_andn2_b64 vcc, exec, s[14:15]
	s_mul_i32 s62, s59, 0xe0000
	s_cbranch_vccnz .LBB0_1856
	s_and_b64 s[6:7], s[18:19], exec
	v_mov_b64_e32 v[6:7], v[2:3]
	v_mov_b64_e32 v[18:19], v[2:3]
	v_mov_b64_e32 v[22:23], v[2:3]
	v_mov_b64_e32 v[34:35], v[2:3]
	v_mov_b64_e32 v[38:39], v[2:3]
	v_mov_b64_e32 v[50:51], v[2:3]
	v_mov_b64_e32 v[54:55], v[2:3]
	v_mov_b64_e32 v[10:11], v[2:3]
	v_mov_b64_e32 v[14:15], v[2:3]
	v_mov_b64_e32 v[26:27], v[2:3]
	v_mov_b64_e32 v[30:31], v[2:3]
	v_mov_b64_e32 v[42:43], v[2:3]
	v_mov_b64_e32 v[46:47], v[2:3]
	v_mov_b64_e32 v[58:59], v[2:3]
	s_waitcnt vmcnt(37)
	v_mov_b64_e32 v[62:63], v[2:3]
	s_waitcnt vmcnt(36)
	v_mov_b64_e32 v[66:67], v[2:3]
	s_waitcnt vmcnt(35)
	v_mov_b64_e32 v[70:71], v[2:3]
	s_waitcnt vmcnt(32)
	v_mov_b64_e32 v[82:83], v[2:3]
	s_waitcnt vmcnt(31)
	v_mov_b64_e32 v[86:87], v[2:3]
	s_waitcnt vmcnt(28)
	v_mov_b64_e32 v[98:99], v[2:3]
	s_waitcnt vmcnt(27)
	v_mov_b64_e32 v[102:103], v[2:3]
	s_waitcnt vmcnt(24)
	v_mov_b64_e32 v[114:115], v[2:3]
	s_waitcnt vmcnt(23)
	v_mov_b64_e32 v[118:119], v[2:3]
	v_mov_b64_e32 v[74:75], v[2:3]
	v_mov_b64_e32 v[78:79], v[2:3]
	v_mov_b64_e32 v[90:91], v[2:3]
	v_mov_b64_e32 v[94:95], v[2:3]
	v_mov_b64_e32 v[106:107], v[2:3]
	v_mov_b64_e32 v[110:111], v[2:3]
	s_waitcnt vmcnt(22)
	v_mov_b64_e32 v[122:123], v[2:3]
	v_mov_b64_e32 v[126:127], v[2:3]
	v_mov_b32_e32 v223, 0xff61b1e6
	v_mov_b32_e32 v222, 1
	v_mov_b32_e32 v169, v233
	v_mov_b32_e32 v168, 0x358637bd
	s_cselect_b32 s21, s61, s55
	s_cselect_b32 s63, s62, s54
	s_add_i32 s65, s55, 0x80
	s_add_i32 s66, s54, 0x100
	s_mov_b32 s67, 0
	v_mov_b64_e32 v[4:5], v[0:1]
	v_mov_b64_e32 v[16:17], v[0:1]
	v_mov_b64_e32 v[20:21], v[0:1]
	v_mov_b64_e32 v[32:33], v[0:1]
	v_mov_b64_e32 v[36:37], v[0:1]
	v_mov_b64_e32 v[48:49], v[0:1]
	v_mov_b64_e32 v[52:53], v[0:1]
	v_mov_b64_e32 v[8:9], v[0:1]
	v_mov_b64_e32 v[12:13], v[0:1]
	v_mov_b64_e32 v[24:25], v[0:1]
	v_mov_b64_e32 v[28:29], v[0:1]
	v_mov_b64_e32 v[40:41], v[0:1]
	v_mov_b64_e32 v[44:45], v[0:1]
	v_mov_b64_e32 v[56:57], v[0:1]
	v_mov_b64_e32 v[60:61], v[0:1]
	v_mov_b64_e32 v[64:65], v[0:1]
	v_mov_b64_e32 v[68:69], v[0:1]
	v_mov_b64_e32 v[80:81], v[0:1]
	v_mov_b64_e32 v[84:85], v[0:1]
	v_mov_b64_e32 v[96:97], v[0:1]
	v_mov_b64_e32 v[100:101], v[0:1]
	v_mov_b64_e32 v[112:113], v[0:1]
	v_mov_b64_e32 v[116:117], v[0:1]
	v_mov_b64_e32 v[72:73], v[0:1]
	v_mov_b64_e32 v[76:77], v[0:1]
	v_mov_b64_e32 v[88:89], v[0:1]
	v_mov_b64_e32 v[92:93], v[0:1]
	v_mov_b64_e32 v[104:105], v[0:1]
	v_mov_b64_e32 v[108:109], v[0:1]
	v_mov_b64_e32 v[120:121], v[0:1]
	v_mov_b64_e32 v[124:125], v[0:1]
	s_cmp_eq_u32 s100, 1
	s_cbranch_scc0 .LBB0_1854
	v_add_u32_e32 v140, 0x10000, v176
	v_add_u32_e32 v156, 0x14000, v176
	ds_read_b128 v[128:131], v140
	ds_read_b128 v[132:135], v140 offset:1024
	ds_read_b128 v[136:139], v140 offset:2048
	ds_read_b128 v[140:143], v140 offset:3072
	ds_read_b128 v[144:147], v156
	ds_read_b128 v[148:151], v156 offset:1024
	ds_read_b128 v[152:155], v156 offset:2048
	ds_read_b128 v[156:159], v156 offset:3072
	s_add_i32 s6, s65, 0x80
	s_cmp_eq_u32 s52, s67
	s_cselect_b32 s68, s21, s6
	s_cselect_b32 s55, s63, s66
	s_or_b32 s54, s68, 0x80
	s_add_i32 s6, s24, s65
	s_mov_b32 m0, s53
	ds_read_b128 v[160:163], v177
	ds_read_b128 v[164:167], v177 offset:1024
	ds_read_b128 v[178:181], v177 offset:2048
	ds_read_b128 v[182:185], v177 offset:3072
	ds_read_b128 v[194:197], v177 offset:4096
	ds_read_b128 v[198:201], v177 offset:5120
	ds_read_b128 v[202:205], v177 offset:6144
	ds_read_b128 v[206:209], v177 offset:7168
	buffer_load_dwordx4 v170, s[36:39], s6 offen lds
	s_mov_b32 m0, s56
	s_nop 0
	buffer_load_dwordx4 v172, s[36:39], s6 offen lds
	s_waitcnt vmcnt(32)
	s_waitcnt lgkmcnt(0)
	s_barrier
	s_setprio 1
	s_waitcnt lgkmcnt(6)
	v_mfma_scale_f32_16x16x128_f8f6f4 v[124:127], v[128:135], v[160:167], v[124:127], v224, v224 op_sel_hi:[0,0,0]
	v_mfma_scale_f32_16x16x128_f8f6f4 v[120:123], v[136:143], v[160:167], v[120:123], v224, v224 op_sel_hi:[0,0,0]
	s_waitcnt lgkmcnt(4)
	v_mfma_scale_f32_16x16x128_f8f6f4 v[108:111], v[128:135], v[178:185], v[108:111], v224, v224 op_sel_hi:[0,0,0]
	v_mfma_scale_f32_16x16x128_f8f6f4 v[104:107], v[136:143], v[178:185], v[104:107], v224, v224 op_sel_hi:[0,0,0]
	s_waitcnt lgkmcnt(2)
	v_mfma_scale_f32_16x16x128_f8f6f4 v[186:189], v[128:135], v[194:201], v[92:95], v224, v224 op_sel_hi:[0,0,0]
	v_mfma_scale_f32_16x16x128_f8f6f4 v[190:193], v[136:143], v[194:201], v[88:91], v224, v224 op_sel_hi:[0,0,0]
	s_waitcnt lgkmcnt(0)
	v_mfma_scale_f32_16x16x128_f8f6f4 v[210:213], v[128:135], v[202:209], v[76:79], v224, v224 op_sel_hi:[0,0,0]
	v_mfma_scale_f32_16x16x128_f8f6f4 v[214:217], v[136:143], v[202:209], v[72:75], v224, v224 op_sel_hi:[0,0,0]
	s_setprio 0
	s_setprio 1
	v_mfma_scale_f32_16x16x128_f8f6f4 v[116:119], v[144:151], v[160:167], v[116:119], v224, v224 op_sel_hi:[0,0,0]
	v_mfma_scale_f32_16x16x128_f8f6f4 v[112:115], v[152:159], v[160:167], v[112:115], v224, v224 op_sel_hi:[0,0,0]
	v_mfma_scale_f32_16x16x128_f8f6f4 v[100:103], v[144:151], v[178:185], v[100:103], v224, v224 op_sel_hi:[0,0,0]
	v_mfma_scale_f32_16x16x128_f8f6f4 v[96:99], v[152:159], v[178:185], v[96:99], v224, v224 op_sel_hi:[0,0,0]
	v_mfma_scale_f32_16x16x128_f8f6f4 v[160:163], v[144:151], v[194:201], v[84:87], v224, v224 op_sel_hi:[0,0,0]
	v_mfma_scale_f32_16x16x128_f8f6f4 v[164:167], v[152:159], v[194:201], v[80:83], v224, v224 op_sel_hi:[0,0,0]
	v_mfma_scale_f32_16x16x128_f8f6f4 v[178:181], v[144:151], v[202:209], v[68:71], v224, v224 op_sel_hi:[0,0,0]
	v_mfma_scale_f32_16x16x128_f8f6f4 v[182:185], v[152:159], v[202:209], v[64:67], v224, v224 op_sel_hi:[0,0,0]
	s_setprio 0
	s_barrier
; #define PG8_STAGE(bufoff, rs_, soff_, voff) do { _Pragma("unroll") for (int _i = 0; _i < 2; ++_i) \
;         __builtin_amdgcn_raw_ptr_buffer_load_lds(rs_, (LAS void*)(lds + (bufoff) + ldsw + _i * 8192), 16, (int)(voff)[_i], (int)(soff_), 0, 0); } while (0)
; #define PG8_LDA(dst, b, h) do { _Pragma("unroll") for (int m = 0; m < 4; ++m) dst[m] = PG8_LD2(lds + PG8_SA(b, h) + aoff + m * 2048); } while (0)
; #define PG8_LDB(dst, b, h) do { _Pragma("unroll") for (int n = 0; n < 2; ++n) dst[n] = PG8_LD2(lds + PG8_SB(b, h) + boff + n * 2048); } while (0)
; #define PG8_WAIT_V(n) asm volatile("s_waitcnt vmcnt(" #n ")" ::: "memory")
; #define PG8_WAIT_L(n) asm volatile("s_waitcnt lgkmcnt(" #n ")" ::: "memory")
; #define PG8_BAR __builtin_amdgcn_s_barrier()
; #define PG8_SCHED __builtin_amdgcn_sched_barrier(0)
; template <class Epi, class Sched, bool ALIGN_EPI = false, bool SP2 = false, bool FP8 = false>
; __device__ __forceinline__ void gemm_phase(LAS unsigned char* lds, const Gemm g, const Sched& S, const Epi& E, int wbase) {
;     ...
;             PG8_LDA(At, 0, 1); PG8_STAGE(PG8_SB(0, 0), rB2, b2, voffB); PG8_STAGE(PG8_SB(0, 1), rB2, b2 + hstep, voffB); PG8_STAGE(PG8_SA(0, 0), rA2, a2, voffA);
;             PG8_WAIT_V(8); PG8_WAIT_L(0); PG8_BAR; PG8_MMA(1, 0, At, B0); PG8_MMA(1, 1, At, B1); PG8_BAR; PG8_SCHED;
;             PG8_LDB(B0, 1, 0); PG8_LDB(B1, 1, 1); PG8_SCHED; PG8_LDA(At, 1, 0); PG8_STAGE(PG8_SA(0, 1), rA2, a2 + hstep, voffA);
;             PG8_WAIT_V(8); PG8_WAIT_L(0); PG8_BAR; PG8_MMA(0, 0, At, B0); PG8_MMA(0, 1, At, B1); PG8_BAR; PG8_SCHED;
	s_mov_b32 m0, s26
	s_mov_b32 s6, s38
	s_mov_b32 s7, s39
	s_nop 1
	ds_read_b128 v[64:67], v177 offset:16384
	ds_read_b128 v[68:71], v177 offset:17408
	ds_read_b128 v[72:75], v177 offset:18432
	ds_read_b128 v[76:79], v177 offset:19456
	ds_read_b128 v[80:83], v177 offset:20480
	ds_read_b128 v[84:87], v177 offset:21504
	ds_read_b128 v[88:91], v177 offset:22528
	ds_read_b128 v[92:95], v177 offset:23552
	buffer_load_dwordx4 v171, s[4:7], s55 offen lds
	s_mov_b32 m0, s27
	s_add_i32 s69, s55, s24
	buffer_load_dwordx4 v173, s[4:7], s55 offen lds
	s_mov_b32 m0, s28
	s_nop 0
	buffer_load_dwordx4 v171, s[4:7], s69 offen lds
	s_mov_b32 m0, s29
	s_nop 0
	buffer_load_dwordx4 v173, s[4:7], s69 offen lds
	s_mov_b32 m0, s25
	s_nop 0
	buffer_load_dwordx4 v170, s[36:39], s68 offen lds
	s_mov_b32 m0, s30
	s_nop 0
	buffer_load_dwordx4 v172, s[36:39], s68 offen lds
	s_waitcnt vmcnt(32)
	s_waitcnt lgkmcnt(0)
	s_barrier
	s_setprio 1
	s_waitcnt lgkmcnt(6)
	v_mfma_scale_f32_16x16x128_f8f6f4 v[60:63], v[128:135], v[64:71], v[60:63], v224, v224 op_sel_hi:[0,0,0]
	v_mfma_scale_f32_16x16x128_f8f6f4 v[56:59], v[136:143], v[64:71], v[56:59], v224, v224 op_sel_hi:[0,0,0]
	s_waitcnt lgkmcnt(4)
	v_mfma_scale_f32_16x16x128_f8f6f4 v[194:197], v[128:135], v[72:79], v[44:47], v224, v224 op_sel_hi:[0,0,0]
	v_mfma_scale_f32_16x16x128_f8f6f4 v[198:201], v[136:143], v[72:79], v[40:43], v224, v224 op_sel_hi:[0,0,0]
	s_waitcnt lgkmcnt(2)
	v_mfma_scale_f32_16x16x128_f8f6f4 v[202:205], v[128:135], v[80:87], v[28:31], v224, v224 op_sel_hi:[0,0,0]
	v_mfma_scale_f32_16x16x128_f8f6f4 v[206:209], v[136:143], v[80:87], v[24:27], v224, v224 op_sel_hi:[0,0,0]
	s_waitcnt lgkmcnt(0)
	v_mfma_scale_f32_16x16x128_f8f6f4 v[218:221], v[128:135], v[88:95], v[12:15], v224, v224 op_sel_hi:[0,0,0]
	v_mfma_scale_f32_16x16x128_f8f6f4 v[226:229], v[136:143], v[88:95], v[8:11], v224, v224 op_sel_hi:[0,0,0]
	s_setprio 0
	s_setprio 1
	v_mfma_scale_f32_16x16x128_f8f6f4 v[52:55], v[144:151], v[64:71], v[52:55], v224, v224 op_sel_hi:[0,0,0]
	v_mfma_scale_f32_16x16x128_f8f6f4 v[48:51], v[152:159], v[64:71], v[48:51], v224, v224 op_sel_hi:[0,0,0]
	v_mfma_scale_f32_16x16x128_f8f6f4 v[230:233], v[144:151], v[72:79], v[36:39], v224, v224 op_sel_hi:[0,0,0]
	v_mfma_scale_f32_16x16x128_f8f6f4 v[234:237], v[152:159], v[72:79], v[32:35], v224, v224 op_sel_hi:[0,0,0]
	v_mfma_scale_f32_16x16x128_f8f6f4 v[238:241], v[144:151], v[80:87], v[20:23], v224, v224 op_sel_hi:[0,0,0]
	v_mfma_scale_f32_16x16x128_f8f6f4 v[242:245], v[152:159], v[80:87], v[16:19], v224, v224 op_sel_hi:[0,0,0]
	v_mfma_scale_f32_16x16x128_f8f6f4 v[246:249], v[144:151], v[88:95], v[4:7], v224, v224 op_sel_hi:[0,0,0]
	v_mfma_scale_f32_16x16x128_f8f6f4 v[250:253], v[152:159], v[88:95], v[0:3], v224, v224 op_sel_hi:[0,0,0]
	s_setprio 0
	s_barrier
	v_add_u32_e32 v8, 0x18000, v176
	s_nop 3
	ds_read_b128 v[0:3], v8
	ds_read_b128 v[4:7], v8 offset:1024
	ds_read_b128 v[16:19], v8 offset:2048
	ds_read_b128 v[20:23], v8 offset:3072
	v_add_u32_e32 v8, 0x1c000, v176
	ds_read_b128 v[128:131], v8
	ds_read_b128 v[132:135], v8 offset:1024
	ds_read_b128 v[136:139], v8 offset:2048
	ds_read_b128 v[140:143], v8 offset:3072
	s_add_i32 s68, s68, s24
	s_mov_b32 m0, s31
	ds_read_b128 v[8:11], v177 offset:32768
	ds_read_b128 v[12:15], v177 offset:33792
	ds_read_b128 v[24:27], v177 offset:34816
	ds_read_b128 v[28:31], v177 offset:35840
	ds_read_b128 v[32:35], v177 offset:36864
	ds_read_b128 v[36:39], v177 offset:37888
	ds_read_b128 v[40:43], v177 offset:38912
	ds_read_b128 v[44:47], v177 offset:39936
	buffer_load_dwordx4 v170, s[36:39], s68 offen lds
	s_mov_b32 m0, s33
	s_nop 0
	buffer_load_dwordx4 v172, s[36:39], s68 offen lds
	s_waitcnt vmcnt(8)
	s_waitcnt lgkmcnt(0)
	s_barrier
; #define PG8_STAGE(bufoff, rs_, soff_, voff) do { _Pragma("unroll") for (int _i = 0; _i < 2; ++_i) \
;         __builtin_amdgcn_raw_ptr_buffer_load_lds(rs_, (LAS void*)(lds + (bufoff) + ldsw + _i * 8192), 16, (int)(voff)[_i], (int)(soff_), 0, 0); } while (0)
; #define PG8_LDA(dst, b, h) do { _Pragma("unroll") for (int m = 0; m < 4; ++m) dst[m] = PG8_LD2(lds + PG8_SA(b, h) + aoff + m * 2048); } while (0)
; #define PG8_WAIT_V(n) asm volatile("s_waitcnt vmcnt(" #n ")" ::: "memory")
; #define PG8_WAIT_L(n) asm volatile("s_waitcnt lgkmcnt(" #n ")" ::: "memory")
; #define PG8_BAR __builtin_amdgcn_s_barrier()
; #define PG8_SCHED __builtin_amdgcn_sched_barrier(0)
; template <class Epi, class Sched, bool ALIGN_EPI = false, bool SP2 = false, bool FP8 = false>
; __device__ __forceinline__ void gemm_phase(LAS unsigned char* lds, const Gemm g, const Sched& S, const Epi& E, int wbase) {
;     ...
;             PG8_WAIT_V(8); PG8_WAIT_L(0); PG8_BAR; PG8_MMA(0, 0, At, B0); PG8_MMA(0, 1, At, B1); PG8_BAR; PG8_SCHED;
;             PG8_LDA(At, 1, 1); PG8_STAGE(PG8_SB(1, 0), rB2, b3, voffB); PG8_STAGE(PG8_SB(1, 1), rB2, b3 + hstep, voffB); PG8_STAGE(PG8_SA(1, 0), rA2, a3, voffA);
;             PG8_WAIT_V(8); PG8_WAIT_L(0); PG8_BAR; PG8_MMA(1, 0, At, B0); PG8_MMA(1, 1, At, B1); PG8_BAR; PG8_SCHED;
	s_setprio 1
	s_waitcnt lgkmcnt(6)
	v_mfma_scale_f32_16x16x128_f8f6f4 v[124:127], v[0:7], v[8:15], v[124:127], v224, v224 op_sel_hi:[0,0,0]
	v_mfma_scale_f32_16x16x128_f8f6f4 v[120:123], v[16:23], v[8:15], v[120:123], v224, v224 op_sel_hi:[0,0,0]
	s_waitcnt lgkmcnt(4)
	v_mfma_scale_f32_16x16x128_f8f6f4 v[108:111], v[0:7], v[24:31], v[108:111], v224, v224 op_sel_hi:[0,0,0]
	v_mfma_scale_f32_16x16x128_f8f6f4 v[104:107], v[16:23], v[24:31], v[104:107], v224, v224 op_sel_hi:[0,0,0]
	s_waitcnt lgkmcnt(2)
	v_mfma_scale_f32_16x16x128_f8f6f4 v[92:95], v[0:7], v[32:39], v[186:189], v224, v224 op_sel_hi:[0,0,0]
	v_mfma_scale_f32_16x16x128_f8f6f4 v[88:91], v[16:23], v[32:39], v[190:193], v224, v224 op_sel_hi:[0,0,0]
	s_waitcnt lgkmcnt(0)
	v_mfma_scale_f32_16x16x128_f8f6f4 v[76:79], v[0:7], v[40:47], v[210:213], v224, v224 op_sel_hi:[0,0,0]
	v_mfma_scale_f32_16x16x128_f8f6f4 v[72:75], v[16:23], v[40:47], v[214:217], v224, v224 op_sel_hi:[0,0,0]
	s_setprio 0
	s_setprio 1
	v_mfma_scale_f32_16x16x128_f8f6f4 v[116:119], v[128:135], v[8:15], v[116:119], v224, v224 op_sel_hi:[0,0,0]
	v_mfma_scale_f32_16x16x128_f8f6f4 v[112:115], v[136:143], v[8:15], v[112:115], v224, v224 op_sel_hi:[0,0,0]
	v_mfma_scale_f32_16x16x128_f8f6f4 v[100:103], v[128:135], v[24:31], v[100:103], v224, v224 op_sel_hi:[0,0,0]
	v_mfma_scale_f32_16x16x128_f8f6f4 v[96:99], v[136:143], v[24:31], v[96:99], v224, v224 op_sel_hi:[0,0,0]
	v_mfma_scale_f32_16x16x128_f8f6f4 v[84:87], v[128:135], v[32:39], v[160:163], v224, v224 op_sel_hi:[0,0,0]
	v_mfma_scale_f32_16x16x128_f8f6f4 v[80:83], v[136:143], v[32:39], v[164:167], v224, v224 op_sel_hi:[0,0,0]
	v_mfma_scale_f32_16x16x128_f8f6f4 v[68:71], v[128:135], v[40:47], v[178:181], v224, v224 op_sel_hi:[0,0,0]
	v_mfma_scale_f32_16x16x128_f8f6f4 v[64:67], v[136:143], v[40:47], v[182:185], v224, v224 op_sel_hi:[0,0,0]
	s_setprio 0
	s_barrier
	s_mov_b32 m0, s34
	s_bitset1_b32 s55, 7
	ds_read_b128 v[32:35], v177 offset:49152
	ds_read_b128 v[36:39], v177 offset:50176
	ds_read_b128 v[144:147], v177 offset:51200
	ds_read_b128 v[148:151], v177 offset:52224
	ds_read_b128 v[152:155], v177 offset:53248
	ds_read_b128 v[156:159], v177 offset:54272
	ds_read_b128 v[160:163], v177 offset:55296
	ds_read_b128 v[164:167], v177 offset:56320
	buffer_load_dwordx4 v171, s[4:7], s55 offen lds
	s_mov_b32 m0, s35
	s_nop 0
	buffer_load_dwordx4 v173, s[4:7], s55 offen lds
	s_add_i32 s55, s55, s24
	s_mov_b32 m0, s43
	s_nop 0
	buffer_load_dwordx4 v171, s[4:7], s55 offen lds
	s_mov_b32 m0, s44
	s_nop 0
	buffer_load_dwordx4 v173, s[4:7], s55 offen lds
	s_mov_b32 m0, s41
	s_nop 0
	buffer_load_dwordx4 v170, s[36:39], s54 offen lds
	s_mov_b32 m0, s42
	s_nop 0
	buffer_load_dwordx4 v172, s[36:39], s54 offen lds
	s_waitcnt vmcnt(8)
	s_waitcnt lgkmcnt(0)
	s_barrier
	s_setprio 1
	s_waitcnt lgkmcnt(6)
	v_mfma_scale_f32_16x16x128_f8f6f4 v[60:63], v[0:7], v[32:39], v[60:63], v224, v224 op_sel_hi:[0,0,0]
	v_mfma_scale_f32_16x16x128_f8f6f4 v[56:59], v[16:23], v[32:39], v[56:59], v224, v224 op_sel_hi:[0,0,0]
	s_waitcnt lgkmcnt(4)
	v_mfma_scale_f32_16x16x128_f8f6f4 v[44:47], v[0:7], v[144:151], v[194:197], v224, v224 op_sel_hi:[0,0,0]
	v_mfma_scale_f32_16x16x128_f8f6f4 v[40:43], v[16:23], v[144:151], v[198:201], v224, v224 op_sel_hi:[0,0,0]
	s_waitcnt lgkmcnt(2)
	v_mfma_scale_f32_16x16x128_f8f6f4 v[28:31], v[0:7], v[152:159], v[202:205], v224, v224 op_sel_hi:[0,0,0]
	v_mfma_scale_f32_16x16x128_f8f6f4 v[24:27], v[16:23], v[152:159], v[206:209], v224, v224 op_sel_hi:[0,0,0]
	s_waitcnt lgkmcnt(0)
	v_mfma_scale_f32_16x16x128_f8f6f4 v[12:15], v[0:7], v[160:167], v[218:221], v224, v224 op_sel_hi:[0,0,0]
	v_mfma_scale_f32_16x16x128_f8f6f4 v[8:11], v[16:23], v[160:167], v[226:229], v224, v224 op_sel_hi:[0,0,0]
	s_setprio 0
	s_setprio 1
	v_mfma_scale_f32_16x16x128_f8f6f4 v[52:55], v[128:135], v[32:39], v[52:55], v224, v224 op_sel_hi:[0,0,0]
	v_mfma_scale_f32_16x16x128_f8f6f4 v[48:51], v[136:143], v[32:39], v[48:51], v224, v224 op_sel_hi:[0,0,0]
	v_mfma_scale_f32_16x16x128_f8f6f4 v[36:39], v[128:135], v[144:151], v[230:233], v224, v224 op_sel_hi:[0,0,0]
	v_mfma_scale_f32_16x16x128_f8f6f4 v[32:35], v[136:143], v[144:151], v[234:237], v224, v224 op_sel_hi:[0,0,0]
	v_mfma_scale_f32_16x16x128_f8f6f4 v[20:23], v[128:135], v[152:159], v[238:241], v224, v224 op_sel_hi:[0,0,0]
	v_mfma_scale_f32_16x16x128_f8f6f4 v[16:19], v[136:143], v[152:159], v[242:245], v224, v224 op_sel_hi:[0,0,0]
	v_mfma_scale_f32_16x16x128_f8f6f4 v[4:7], v[128:135], v[160:167], v[246:249], v224, v224 op_sel_hi:[0,0,0]
	v_mfma_scale_f32_16x16x128_f8f6f4 v[0:3], v[136:143], v[160:167], v[250:253], v224, v224 op_sel_hi:[0,0,0]
	s_setprio 0
	s_barrier
	s_add_i32 s67, s67, 2
	s_addk_i32 s65, 0x100
	s_addk_i32 s66, 0x100
	s_cmp_ge_i32 s67, s47
	s_cbranch_scc0 .LBB0_1854
	s_branch .Lpeel_after_1854

; #define PG8_BAR __builtin_amdgcn_s_barrier()
; #define PG8_ZERO_ACC() do { float z_; asm volatile("v_mov_b32 %0, 0" : "=v"(z_)); _Pragma("unroll") for (int a = 0; a < 2; ++a) _Pragma("unroll") for (int b = 0; b < 2; ++b) _Pragma("unroll") for (int m = 0; m < 4; ++m) \
;         _Pragma("unroll") for (int n = 0; n < 2; ++n) acc[a][b][m][n] = (f32x4){z_, z_, z_, z_}; } while (0)
; template <class Epi, class Sched, bool ALIGN_EPI = false, bool SP2 = false, bool FP8 = false>
; __device__ __forceinline__ void gemm_phase(LAS unsigned char* lds, const Gemm g, const Sched& S, const Epi& E, int wbase) {
;     ...
;         }
;         if constexpr (ALIGN_EPI) { if (wr == 0) PG8_BAR; }
;         { int fr_ = fr, fq_ = fq; asm volatile("" : "+v"(fr_), "+v"(fq_));
;           if constexpr (Epi::HAS_PRE) E(acc, cur, wr, wc, fr_, fq_, pre_); else E(acc, cur, wr, wc, fr_, fq_); } S.done(cur);
;         if (!has_next) break;
;         if (E.reset(cur)) PG8_ZERO_ACC();
.Lpeel_after_1854:
	s_mov_b32 s100, 1
	v_readlane_b32 s68, v255, 22
	v_readlane_b32 s69, v255, 23
	v_mov_b32_e32 v230, v168
	v_mov_b32_e32 v233, v169
	v_mov_b32_e32 v231, v222
	v_mov_b32_e32 v234, v223
	s_and_b64 vcc, exec, s[16:17]
	s_cbranch_vccnz .LBB0_1857
	s_branch .LBB0_1858

; __device__ __forceinline__ int opaque_s(int x) { asm volatile("" : "+s"(x)); return x; }
; #define PG8_STAGE(bufoff, rs_, soff_, voff) do { _Pragma("unroll") for (int _i = 0; _i < 2; ++_i) \
;         __builtin_amdgcn_raw_ptr_buffer_load_lds(rs_, (LAS void*)(lds + (bufoff) + ldsw + _i * 8192), 16, (int)(voff)[_i], (int)(soff_), 0, 0); } while (0)
; #define PG8_WAIT_V(n) asm volatile("s_waitcnt vmcnt(" #n ")" ::: "memory")
; #define PG8_BAR __builtin_amdgcn_s_barrier()
; #define KWS (kargs()->ws)
; #define KOUT (kargs()->out)
; template <class Epi, class Sched, bool ALIGN_EPI = false, bool SP2 = false, bool FP8 = false>
; __device__ __forceinline__ void gemm_phase(LAS unsigned char* lds, const Gemm g, const Sched& S, const Epi& E, int wbase) {
;     ...
;     if constexpr (SP2) {
;         PG8_STAGE(PG8_SB(0, 0), rBc, cB, voffB); PG8_STAGE(PG8_SB(0, 1), rBc, cB + hstep, voffB); PG8_STAGE(PG8_SA(0, 0), rAc, cA, voffA); PG8_STAGE(PG8_SA(0, 1), rAc, cA + hstep, voffA);
;         if (wr == 1) PG8_BAR;
;         PG8_WAIT_V(2); PG8_BAR;
;         PG8_STAGE(PG8_SB(1, 0), rBc, cB + kstep, voffB); PG8_STAGE(PG8_SA(1, 0), rAc, cA + kstep, voffA); PG8_STAGE(PG8_SB(1, 1), rBc, cB + hstep + kstep, voffB);
;         PG8_WAIT_V(6); PG8_BAR;
; __global__ void __launch_bounds__(512, 2) mega(Ptrs Pdummy) {
;     ...
;         { unsigned char* ws = KWS; pg8::Gemm g{HBUF(hc), (const bf16*)(ws + WS_WPG) + (size_t)l * DM * DM, DM, 0}; pg8::StaticOrder S; S.init(M, DM, opaque_s(G), opaque_s(c));
;           pg8::EpiResid<1> E{HBUF(hc), HBUF(hc ^ 1), l + 1 < DEPTH ? nullptr : KOUT, SBUF(sc ^ 1), (const bf16*)(ws + WS_PP), SBUF(sc), ((INPROJ_FP8 || INPROJ_GATES_FP8 || ((INPROJ_FP8_MASK >> (l + 1)) & 1)) && l + 1 < DEPTH) ? ws + WS_HB8 : nullptr, 1.f, 0}; pg8::gemm_phase<pg8::EpiResid<1>, pg8::StaticOrder, true, true>(lds, g, S, E, wbase); sc ^= 1; hc ^= 1; }
.LBB0_1933:
	v_readlane_b32 s6, v255, 10
	s_cmp_eq_u32 s6, 1
	s_mov_b32 s6, 0x13200000
	s_cselect_b32 s6, s6, 0x1b800000
	s_add_u32 s10, s18, s6
	s_addc_u32 s11, s19, 0
	s_add_u32 s6, s18, 0x17200000
	s_addc_u32 s7, s19, 0
	v_readlane_b32 s16, v255, 11
	s_cmp_eq_u32 s16, 1
	s_cselect_b32 s12, 0, 0x200000
	s_add_u32 s12, s6, s12
	s_addc_u32 s13, s7, 0
	s_add_u32 s14, s18, 0x17800000
	s_addc_u32 s15, s19, 0
	s_cmp_eq_u32 s16, 0
	s_cselect_b32 s16, 0, 0x200000
	s_add_u32 s16, s6, s16
	s_addc_u32 s17, s7, 0
	s_add_u32 s18, s18, 0xb200000
	s_addc_u32 s19, s19, 0
	s_add_i32 s47, s34, 0x18000
	s_or_b32 s25, s54, 0x80
	s_mov_b32 s6, s38
	s_mov_b32 s7, s39
	s_mov_b32 m0, s47
	s_add_i32 s48, s34, 0x1a000
	s_waitcnt vmcnt(2)
	s_barrier
	buffer_load_dwordx4 v169, s[4:7], s25 offen lds
	s_mov_b32 m0, s48
	s_add_i32 s52, s34, 0x8000
	buffer_load_dwordx4 v171, s[4:7], s25 offen lds
	s_or_b32 s25, s55, 0x80
	s_mov_b32 m0, s52
	s_add_i32 s53, s34, 0xa000
	buffer_load_dwordx4 v168, s[36:39], s25 offen lds
	s_mov_b32 m0, s53
	s_add_i32 s56, s34, 0x1c000
	buffer_load_dwordx4 v170, s[36:39], s25 offen lds
	s_bitset1_b32 s24, 7
	s_mov_b32 m0, s56
	s_add_i32 s57, s34, 0x1e000
	buffer_load_dwordx4 v169, s[4:7], s24 offen lds
	s_mov_b32 m0, s57
	v_bfe_u32 v173, v4, 4, 2
	buffer_load_dwordx4 v171, s[4:7], s24 offen lds
	s_ashr_i32 s6, s22, 31
	s_lshr_b32 s6, s6, 26
	v_and_b32_e32 v172, 15, v4
	s_add_i32 s6, s22, s6
	v_lshlrev_b32_e32 v5, 4, v173
	v_lshlrev_b32_e32 v4, 2, v4
	s_and_b32 s59, s20, 3
	s_ashr_i32 s65, s6, 6
	v_lshl_or_b32 v5, v172, 6, v5
	s_lshl_b32 s6, s23, 13
	v_and_b32_e32 v4, 32, v4
	s_lshl_b32 s76, s23, 6
	v_bitop3_b32 v6, v5, s6, v4 bitop3:0xde
	s_lshl_b32 s20, s59, 5
	s_lshl_b32 s6, s59, 12
	s_cmp_gt_i32 s22, 63
	s_waitcnt vmcnt(6)
	s_cselect_b64 s[22:23], -1, 0
	s_add_i32 s77, s65, -2
	s_add_i32 s79, s34, 0xc000
	v_bitop3_b32 v4, v5, s6, v4 bitop3:0xde
	s_cmpk_lt_u32 s21, 0x100
	v_mov_b32_e32 v1, v0
	v_mov_b32_e32 v2, v0
	v_mov_b32_e32 v3, v0
	s_mov_b32 s58, 0
	s_cselect_b64 s[24:25], -1, 0
	s_mov_b32 s21, s40
	s_add_i32 s82, s34, 0xe000
	v_add_u32_e32 v174, 0, v4
	v_add_u32_e32 v175, 0, v6
	s_barrier
	s_mov_b32 s100, 0
	s_branch .LBB0_1936

; #define PG8_STAGE(bufoff, rs_, soff_, voff) do { _Pragma("unroll") for (int _i = 0; _i < 2; ++_i) \
;         __builtin_amdgcn_raw_ptr_buffer_load_lds(rs_, (LAS void*)(lds + (bufoff) + ldsw + _i * 8192), 16, (int)(voff)[_i], (int)(soff_), 0, 0); } while (0)
; #define PG8_LDA(dst, b, h) do { _Pragma("unroll") for (int m = 0; m < 4; ++m) dst[m] = PG8_LD2(lds + PG8_SA(b, h) + aoff + m * 2048); } while (0)
; #define PG8_LDB(dst, b, h) do { _Pragma("unroll") for (int n = 0; n < 2; ++n) dst[n] = PG8_LD2(lds + PG8_SB(b, h) + boff + n * 2048); } while (0)
; #define PG8_WAIT_V(n) asm volatile("s_waitcnt vmcnt(" #n ")" ::: "memory")
; #define PG8_WAIT_L(n) asm volatile("s_waitcnt lgkmcnt(" #n ")" ::: "memory")
; #define PG8_BAR __builtin_amdgcn_s_barrier()
; #define PG8_SCHED __builtin_amdgcn_sched_barrier(0)
; #define PG8_ZERO_ACC() do { float z_; asm volatile("v_mov_b32 %0, 0" : "=v"(z_)); _Pragma("unroll") for (int a = 0; a < 2; ++a) _Pragma("unroll") for (int b = 0; b < 2; ++b) _Pragma("unroll") for (int m = 0; m < 4; ++m) \
;         _Pragma("unroll") for (int n = 0; n < 2; ++n) acc[a][b][m][n] = (f32x4){z_, z_, z_, z_}; } while (0)
; template <class Epi, class Sched, bool ALIGN_EPI = false, bool SP2 = false, bool FP8 = false>
; __device__ __forceinline__ void gemm_phase(LAS unsigned char* lds, const Gemm g, const Sched& S, const Epi& E, int wbase) {
;     ...
;             if constexpr (SP2) {
;             PG8_LDB(B0, 0, 0); PG8_LDB(B1, 0, 1); PG8_SCHED; PG8_LDA(At, 0, 0); PG8_STAGE(PG8_SA(1, 1), rAc, a1 + hstep, voffA);
;             PG8_WAIT_V(8); PG8_WAIT_L(0); PG8_BAR; PG8_MMA(0, 0, At, B0); PG8_MMA(0, 1, At, B1); PG8_BAR; PG8_SCHED;
;             PG8_LDA(At, 0, 1); PG8_STAGE(PG8_SB(0, 0), rB2, b2, voffB); PG8_STAGE(PG8_SB(0, 1), rB2, b2 + hstep, voffB); PG8_STAGE(PG8_SA(0, 0), rA2, a2, voffA);
;             PG8_WAIT_V(8); PG8_WAIT_L(0); PG8_BAR; PG8_MMA(1, 0, At, B0); PG8_MMA(1, 1, At, B1); PG8_BAR; PG8_SCHED;
;     ...
;         if (E.reset(cur)) PG8_ZERO_ACC();
.LBB0_1942:
	s_mov_b32 s68, s94
	s_lshl_b32 s85, s84, 19
	s_andn2_b64 vcc, exec, s[22:23]
	s_lshl_b32 s94, s83, 19
	s_cbranch_vccnz .LBB0_1966
	s_and_b64 s[6:7], s[26:27], exec
	v_mov_b64_e32 v[6:7], v[2:3]
	v_mov_b64_e32 v[18:19], v[2:3]
	v_mov_b64_e32 v[22:23], v[2:3]
	v_mov_b64_e32 v[34:35], v[2:3]
	v_mov_b64_e32 v[38:39], v[2:3]
	v_mov_b64_e32 v[50:51], v[2:3]
	v_mov_b64_e32 v[54:55], v[2:3]
	v_mov_b64_e32 v[10:11], v[2:3]
	v_mov_b64_e32 v[14:15], v[2:3]
	v_mov_b64_e32 v[26:27], v[2:3]
	v_mov_b64_e32 v[30:31], v[2:3]
	v_mov_b64_e32 v[42:43], v[2:3]
	v_mov_b64_e32 v[46:47], v[2:3]
	v_mov_b64_e32 v[58:59], v[2:3]
	s_waitcnt vmcnt(37)
	v_mov_b64_e32 v[62:63], v[2:3]
	s_waitcnt vmcnt(36)
	v_mov_b64_e32 v[66:67], v[2:3]
	s_waitcnt vmcnt(35)
	v_mov_b64_e32 v[70:71], v[2:3]
	s_waitcnt vmcnt(32)
	v_mov_b64_e32 v[82:83], v[2:3]
	s_waitcnt vmcnt(31)
	v_mov_b64_e32 v[86:87], v[2:3]
	s_waitcnt vmcnt(28)
	v_mov_b64_e32 v[98:99], v[2:3]
	s_waitcnt vmcnt(27)
	v_mov_b64_e32 v[102:103], v[2:3]
	s_waitcnt vmcnt(24)
	v_mov_b64_e32 v[114:115], v[2:3]
	s_waitcnt vmcnt(23)
	v_mov_b64_e32 v[118:119], v[2:3]
	v_mov_b64_e32 v[74:75], v[2:3]
	v_mov_b64_e32 v[78:79], v[2:3]
	v_mov_b64_e32 v[90:91], v[2:3]
	v_mov_b64_e32 v[94:95], v[2:3]
	v_mov_b64_e32 v[106:107], v[2:3]
	v_mov_b64_e32 v[110:111], v[2:3]
	v_mov_b64_e32 v[130:131], v[2:3]
	v_mov_b64_e32 v[142:143], v[2:3]
	s_cselect_b32 s29, s85, s55
	s_cselect_b32 s60, s94, s54
	s_add_i32 s61, s55, 0x80
	s_add_i32 s62, s54, 0x100
	s_mov_b32 s63, 0
	v_mov_b64_e32 v[4:5], v[0:1]
	v_mov_b64_e32 v[16:17], v[0:1]
	v_mov_b64_e32 v[20:21], v[0:1]
	v_mov_b64_e32 v[32:33], v[0:1]
	v_mov_b64_e32 v[36:37], v[0:1]
	v_mov_b64_e32 v[48:49], v[0:1]
	v_mov_b64_e32 v[52:53], v[0:1]
	v_mov_b64_e32 v[8:9], v[0:1]
	v_mov_b64_e32 v[12:13], v[0:1]
	v_mov_b64_e32 v[24:25], v[0:1]
	v_mov_b64_e32 v[28:29], v[0:1]
	v_mov_b64_e32 v[40:41], v[0:1]
	v_mov_b64_e32 v[44:45], v[0:1]
	v_mov_b64_e32 v[56:57], v[0:1]
	v_mov_b64_e32 v[60:61], v[0:1]
	v_mov_b64_e32 v[64:65], v[0:1]
	v_mov_b64_e32 v[68:69], v[0:1]
	v_mov_b64_e32 v[80:81], v[0:1]
	v_mov_b64_e32 v[84:85], v[0:1]
	v_mov_b64_e32 v[96:97], v[0:1]
	v_mov_b64_e32 v[100:101], v[0:1]
	v_mov_b64_e32 v[112:113], v[0:1]
	v_mov_b64_e32 v[116:117], v[0:1]
	v_mov_b64_e32 v[72:73], v[0:1]
	v_mov_b64_e32 v[76:77], v[0:1]
	v_mov_b64_e32 v[88:89], v[0:1]
	v_mov_b64_e32 v[92:93], v[0:1]
	v_mov_b64_e32 v[104:105], v[0:1]
	v_mov_b64_e32 v[108:109], v[0:1]
	v_mov_b64_e32 v[128:129], v[0:1]
	v_mov_b64_e32 v[140:141], v[0:1]
	s_nop 0
	s_cmp_eq_u32 s100, 1
	s_cbranch_scc0 .LBB0_1944
	v_add_u32_e32 v136, 0x10000, v174
	v_add_u32_e32 v156, 0x14000, v174
	ds_read_b128 v[120:123], v136
	ds_read_b128 v[124:127], v136 offset:1024
	ds_read_b128 v[132:135], v136 offset:2048
	ds_read_b128 v[136:139], v136 offset:3072
	ds_read_b128 v[144:147], v156
	ds_read_b128 v[148:151], v156 offset:1024
	ds_read_b128 v[152:155], v156 offset:2048
	ds_read_b128 v[156:159], v156 offset:3072
	s_add_i32 s6, s61, 0x80
	s_cmp_eq_u32 s77, s63
	s_cselect_b32 s66, s29, s6
	s_cselect_b32 s55, s60, s62
	s_or_b32 s54, s66, 0x80
	s_add_i32 s6, s33, s61
	s_mov_b32 m0, s79
	ds_read_b128 v[160:163], v175
	ds_read_b128 v[164:167], v175 offset:1024
	ds_read_b128 v[176:179], v175 offset:2048
	ds_read_b128 v[180:183], v175 offset:3072
	ds_read_b128 v[184:187], v175 offset:4096
	ds_read_b128 v[188:191], v175 offset:5120
	ds_read_b128 v[192:195], v175 offset:6144
	ds_read_b128 v[196:199], v175 offset:7168
	buffer_load_dwordx4 v168, s[36:39], s6 offen lds
	s_mov_b32 m0, s82
	s_nop 0
	buffer_load_dwordx4 v170, s[36:39], s6 offen lds
	s_waitcnt vmcnt(48)
	s_waitcnt lgkmcnt(0)
	s_barrier
	s_setprio 1
	s_waitcnt lgkmcnt(7)
	v_mfma_f32_16x16x32_bf16 v[140:143], v[120:123], v[160:163], v[140:143]
	v_mfma_f32_16x16x32_bf16 v[128:131], v[132:135], v[160:163], v[128:131]
	s_waitcnt lgkmcnt(5)
	v_mfma_f32_16x16x32_bf16 v[108:111], v[120:123], v[176:179], v[108:111]
	v_mfma_f32_16x16x32_bf16 v[104:107], v[132:135], v[176:179], v[104:107]
	s_waitcnt lgkmcnt(3)
	v_mfma_f32_16x16x32_bf16 v[92:95], v[120:123], v[184:187], v[92:95]
	v_mfma_f32_16x16x32_bf16 v[88:91], v[132:135], v[184:187], v[88:91]
	s_waitcnt lgkmcnt(1)
	v_mfma_f32_16x16x32_bf16 v[76:79], v[120:123], v[192:195], v[76:79]
	v_mfma_f32_16x16x32_bf16 v[72:75], v[132:135], v[192:195], v[72:75]
	v_mfma_f32_16x16x32_bf16 v[140:143], v[124:127], v[164:167], v[140:143]
	v_mfma_f32_16x16x32_bf16 v[128:131], v[136:139], v[164:167], v[128:131]
	v_mfma_f32_16x16x32_bf16 v[108:111], v[124:127], v[180:183], v[108:111]
	v_mfma_f32_16x16x32_bf16 v[104:107], v[136:139], v[180:183], v[104:107]
	v_mfma_f32_16x16x32_bf16 v[92:95], v[124:127], v[188:191], v[92:95]
	v_mfma_f32_16x16x32_bf16 v[88:91], v[136:139], v[188:191], v[88:91]
	s_waitcnt lgkmcnt(0)
	v_mfma_f32_16x16x32_bf16 v[76:79], v[124:127], v[196:199], v[76:79]
	v_mfma_f32_16x16x32_bf16 v[72:75], v[136:139], v[196:199], v[72:75]
	s_setprio 0
	s_setprio 1
	v_mfma_f32_16x16x32_bf16 v[116:119], v[144:147], v[160:163], v[116:119]
	v_mfma_f32_16x16x32_bf16 v[112:115], v[152:155], v[160:163], v[112:115]
	v_mfma_f32_16x16x32_bf16 v[100:103], v[144:147], v[176:179], v[100:103]
	v_mfma_f32_16x16x32_bf16 v[96:99], v[152:155], v[176:179], v[96:99]
	v_mfma_f32_16x16x32_bf16 v[84:87], v[144:147], v[184:187], v[84:87]
	v_mfma_f32_16x16x32_bf16 v[80:83], v[152:155], v[184:187], v[80:83]
	v_mfma_f32_16x16x32_bf16 v[68:71], v[144:147], v[192:195], v[68:71]
	v_mfma_f32_16x16x32_bf16 v[64:67], v[152:155], v[192:195], v[64:67]
	v_mfma_f32_16x16x32_bf16 v[116:119], v[148:151], v[164:167], v[116:119]
	v_mfma_f32_16x16x32_bf16 v[112:115], v[156:159], v[164:167], v[112:115]
	v_mfma_f32_16x16x32_bf16 v[100:103], v[148:151], v[180:183], v[100:103]
	v_mfma_f32_16x16x32_bf16 v[96:99], v[156:159], v[180:183], v[96:99]
	v_mfma_f32_16x16x32_bf16 v[84:87], v[148:151], v[188:191], v[84:87]
	v_mfma_f32_16x16x32_bf16 v[80:83], v[156:159], v[188:191], v[80:83]
	v_mfma_f32_16x16x32_bf16 v[68:71], v[148:151], v[196:199], v[68:71]
	v_mfma_f32_16x16x32_bf16 v[64:67], v[156:159], v[196:199], v[64:67]
	s_setprio 0
	s_barrier
; #define PG8_STAGE(bufoff, rs_, soff_, voff) do { _Pragma("unroll") for (int _i = 0; _i < 2; ++_i) \
;         __builtin_amdgcn_raw_ptr_buffer_load_lds(rs_, (LAS void*)(lds + (bufoff) + ldsw + _i * 8192), 16, (int)(voff)[_i], (int)(soff_), 0, 0); } while (0)
; #define PG8_LDA(dst, b, h) do { _Pragma("unroll") for (int m = 0; m < 4; ++m) dst[m] = PG8_LD2(lds + PG8_SA(b, h) + aoff + m * 2048); } while (0)
; #define PG8_LDB(dst, b, h) do { _Pragma("unroll") for (int n = 0; n < 2; ++n) dst[n] = PG8_LD2(lds + PG8_SB(b, h) + boff + n * 2048); } while (0)
; #define PG8_WAIT_V(n) asm volatile("s_waitcnt vmcnt(" #n ")" ::: "memory")
; #define PG8_WAIT_L(n) asm volatile("s_waitcnt lgkmcnt(" #n ")" ::: "memory")
; #define PG8_BAR __builtin_amdgcn_s_barrier()
; #define PG8_SCHED __builtin_amdgcn_sched_barrier(0)
; template <class Epi, class Sched, bool ALIGN_EPI = false, bool SP2 = false, bool FP8 = false>
; __device__ __forceinline__ void gemm_phase(LAS unsigned char* lds, const Gemm g, const Sched& S, const Epi& E, int wbase) {
;     ...
;             PG8_LDA(At, 0, 1); PG8_STAGE(PG8_SB(0, 0), rB2, b2, voffB); PG8_STAGE(PG8_SB(0, 1), rB2, b2 + hstep, voffB); PG8_STAGE(PG8_SA(0, 0), rA2, a2, voffA);
;             PG8_WAIT_V(8); PG8_WAIT_L(0); PG8_BAR; PG8_MMA(1, 0, At, B0); PG8_MMA(1, 1, At, B1); PG8_BAR; PG8_SCHED;
;             PG8_LDB(B0, 1, 0); PG8_LDB(B1, 1, 1); PG8_SCHED; PG8_LDA(At, 1, 0); PG8_STAGE(PG8_SA(0, 1), rA2, a2 + hstep, voffA);
;             PG8_WAIT_V(8); PG8_WAIT_L(0); PG8_BAR; PG8_MMA(0, 0, At, B0); PG8_MMA(0, 1, At, B1); PG8_BAR; PG8_SCHED;
	s_mov_b32 m0, s35
	s_mov_b32 s6, s38
	s_mov_b32 s7, s39
	ds_read_b128 v[160:163], v175 offset:16384
	ds_read_b128 v[164:167], v175 offset:17408
	ds_read_b128 v[176:179], v175 offset:18432
	ds_read_b128 v[180:183], v175 offset:19456
	ds_read_b128 v[184:187], v175 offset:20480
	ds_read_b128 v[188:191], v175 offset:21504
	ds_read_b128 v[192:195], v175 offset:22528
	ds_read_b128 v[196:199], v175 offset:23552
	buffer_load_dwordx4 v169, s[4:7], s55 offen lds
	s_mov_b32 m0, s41
	s_add_i32 s67, s55, s33
	buffer_load_dwordx4 v171, s[4:7], s55 offen lds
	s_mov_b32 m0, s42
	s_nop 0
	buffer_load_dwordx4 v169, s[4:7], s67 offen lds
	s_mov_b32 m0, s43
	s_nop 0
	buffer_load_dwordx4 v171, s[4:7], s67 offen lds
	s_mov_b32 m0, s34
	s_nop 0
	buffer_load_dwordx4 v168, s[36:39], s66 offen lds
	s_mov_b32 m0, s44
	s_nop 0
	buffer_load_dwordx4 v170, s[36:39], s66 offen lds
	s_waitcnt vmcnt(48)
	s_waitcnt lgkmcnt(0)
	s_barrier
	s_setprio 1
	s_waitcnt lgkmcnt(7)
	v_mfma_f32_16x16x32_bf16 v[60:63], v[120:123], v[160:163], v[60:63]
	v_mfma_f32_16x16x32_bf16 v[56:59], v[132:135], v[160:163], v[56:59]
	s_waitcnt lgkmcnt(5)
	v_mfma_f32_16x16x32_bf16 v[44:47], v[120:123], v[176:179], v[44:47]
	v_mfma_f32_16x16x32_bf16 v[40:43], v[132:135], v[176:179], v[40:43]
	s_waitcnt lgkmcnt(3)
	v_mfma_f32_16x16x32_bf16 v[28:31], v[120:123], v[184:187], v[28:31]
	v_mfma_f32_16x16x32_bf16 v[24:27], v[132:135], v[184:187], v[24:27]
	s_waitcnt lgkmcnt(1)
	v_mfma_f32_16x16x32_bf16 v[12:15], v[120:123], v[192:195], v[12:15]
	v_mfma_f32_16x16x32_bf16 v[8:11], v[132:135], v[192:195], v[8:11]
	v_mfma_f32_16x16x32_bf16 v[60:63], v[124:127], v[164:167], v[60:63]
	v_mfma_f32_16x16x32_bf16 v[56:59], v[136:139], v[164:167], v[56:59]
	v_mfma_f32_16x16x32_bf16 v[44:47], v[124:127], v[180:183], v[44:47]
	v_mfma_f32_16x16x32_bf16 v[40:43], v[136:139], v[180:183], v[40:43]
	v_mfma_f32_16x16x32_bf16 v[28:31], v[124:127], v[188:191], v[28:31]
	v_mfma_f32_16x16x32_bf16 v[24:27], v[136:139], v[188:191], v[24:27]
	s_waitcnt lgkmcnt(0)
	v_mfma_f32_16x16x32_bf16 v[12:15], v[124:127], v[196:199], v[12:15]
	v_mfma_f32_16x16x32_bf16 v[8:11], v[136:139], v[196:199], v[8:11]
	s_setprio 0
	s_setprio 1
	v_mfma_f32_16x16x32_bf16 v[52:55], v[144:147], v[160:163], v[52:55]
	v_mfma_f32_16x16x32_bf16 v[48:51], v[152:155], v[160:163], v[48:51]
	v_mfma_f32_16x16x32_bf16 v[36:39], v[144:147], v[176:179], v[36:39]
	v_mfma_f32_16x16x32_bf16 v[32:35], v[152:155], v[176:179], v[32:35]
	v_mfma_f32_16x16x32_bf16 v[20:23], v[144:147], v[184:187], v[20:23]
	v_mfma_f32_16x16x32_bf16 v[16:19], v[152:155], v[184:187], v[16:19]
	v_mfma_f32_16x16x32_bf16 v[4:7], v[144:147], v[192:195], v[4:7]
	v_mfma_f32_16x16x32_bf16 v[0:3], v[152:155], v[192:195], v[0:3]
	v_mfma_f32_16x16x32_bf16 v[52:55], v[148:151], v[164:167], v[52:55]
	v_mfma_f32_16x16x32_bf16 v[48:51], v[156:159], v[164:167], v[48:51]
	v_mfma_f32_16x16x32_bf16 v[36:39], v[148:151], v[180:183], v[36:39]
	v_mfma_f32_16x16x32_bf16 v[32:35], v[156:159], v[180:183], v[32:35]
	v_mfma_f32_16x16x32_bf16 v[20:23], v[148:151], v[188:191], v[20:23]
	v_mfma_f32_16x16x32_bf16 v[16:19], v[156:159], v[188:191], v[16:19]
	v_mfma_f32_16x16x32_bf16 v[4:7], v[148:151], v[196:199], v[4:7]
	v_mfma_f32_16x16x32_bf16 v[0:3], v[156:159], v[196:199], v[0:3]
	s_setprio 0
	s_barrier
	v_add_u32_e32 v136, 0x18000, v174
	v_add_u32_e32 v156, 0x1c000, v174
	ds_read_b128 v[120:123], v136
	ds_read_b128 v[124:127], v136 offset:1024
	ds_read_b128 v[132:135], v136 offset:2048
	ds_read_b128 v[136:139], v136 offset:3072
	ds_read_b128 v[144:147], v156
	ds_read_b128 v[148:151], v156 offset:1024
	ds_read_b128 v[152:155], v156 offset:2048
	ds_read_b128 v[156:159], v156 offset:3072
	s_add_i32 s66, s66, s33
	s_mov_b32 m0, s45
	ds_read_b128 v[160:163], v175 offset:32768
	ds_read_b128 v[164:167], v175 offset:33792
	ds_read_b128 v[176:179], v175 offset:34816
	ds_read_b128 v[180:183], v175 offset:35840
	ds_read_b128 v[184:187], v175 offset:36864
	ds_read_b128 v[188:191], v175 offset:37888
	ds_read_b128 v[192:195], v175 offset:38912
	ds_read_b128 v[196:199], v175 offset:39936
	buffer_load_dwordx4 v168, s[36:39], s66 offen lds
	s_mov_b32 m0, s46
	s_nop 0
	buffer_load_dwordx4 v170, s[36:39], s66 offen lds
	s_waitcnt vmcnt(8)
	s_waitcnt lgkmcnt(0)
	s_barrier
; #define PG8_STAGE(bufoff, rs_, soff_, voff) do { _Pragma("unroll") for (int _i = 0; _i < 2; ++_i) \
;         __builtin_amdgcn_raw_ptr_buffer_load_lds(rs_, (LAS void*)(lds + (bufoff) + ldsw + _i * 8192), 16, (int)(voff)[_i], (int)(soff_), 0, 0); } while (0)
; #define PG8_LDA(dst, b, h) do { _Pragma("unroll") for (int m = 0; m < 4; ++m) dst[m] = PG8_LD2(lds + PG8_SA(b, h) + aoff + m * 2048); } while (0)
; #define PG8_LDB(dst, b, h) do { _Pragma("unroll") for (int n = 0; n < 2; ++n) dst[n] = PG8_LD2(lds + PG8_SB(b, h) + boff + n * 2048); } while (0)
; #define PG8_WAIT_V(n) asm volatile("s_waitcnt vmcnt(" #n ")" ::: "memory")
; #define PG8_WAIT_L(n) asm volatile("s_waitcnt lgkmcnt(" #n ")" ::: "memory")
; #define PG8_BAR __builtin_amdgcn_s_barrier()
; #define PG8_SCHED __builtin_amdgcn_sched_barrier(0)
; template <class Epi, class Sched, bool ALIGN_EPI = false, bool SP2 = false, bool FP8 = false>
; __device__ __forceinline__ void gemm_phase(LAS unsigned char* lds, const Gemm g, const Sched& S, const Epi& E, int wbase) {
;     ...
;         for (int t = 0; t < nt; t += 2) {
;             const bool last = (t == nt - 2);
;             const unsigned a1 = cA + (unsigned)(t + 1) * kstep;
;             const unsigned a2 = last ? nA : cA + (unsigned)(t + 2) * kstep, b2 = last ? nB : cB + (unsigned)(t + 2) * kstep; const rsrc_t rA2 = (Sched::TWO && last) ? rAn : rAc, rB2 = (Sched::TWO && last) ? rBn : rBc;
;     ...
;             PG8_LDB(B0, 1, 0); PG8_LDB(B1, 1, 1); PG8_SCHED; PG8_LDA(At, 1, 0); PG8_STAGE(PG8_SA(0, 1), rA2, a2 + hstep, voffA);
;             PG8_WAIT_V(8); PG8_WAIT_L(0); PG8_BAR; PG8_MMA(0, 0, At, B0); PG8_MMA(0, 1, At, B1); PG8_BAR; PG8_SCHED;
;             PG8_LDA(At, 1, 1); PG8_STAGE(PG8_SB(1, 0), rB2, b3, voffB); PG8_STAGE(PG8_SB(1, 1), rB2, b3 + hstep, voffB); PG8_STAGE(PG8_SA(1, 0), rA2, a3, voffA);
;             PG8_WAIT_V(8); PG8_WAIT_L(0); PG8_BAR; PG8_MMA(1, 0, At, B0); PG8_MMA(1, 1, At, B1); PG8_BAR; PG8_SCHED;
	s_setprio 1
	s_waitcnt lgkmcnt(7)
	v_mfma_f32_16x16x32_bf16 v[140:143], v[120:123], v[160:163], v[140:143]
	v_mfma_f32_16x16x32_bf16 v[128:131], v[132:135], v[160:163], v[128:131]
	s_waitcnt lgkmcnt(5)
	v_mfma_f32_16x16x32_bf16 v[108:111], v[120:123], v[176:179], v[108:111]
	v_mfma_f32_16x16x32_bf16 v[104:107], v[132:135], v[176:179], v[104:107]
	s_waitcnt lgkmcnt(3)
	v_mfma_f32_16x16x32_bf16 v[92:95], v[120:123], v[184:187], v[92:95]
	v_mfma_f32_16x16x32_bf16 v[88:91], v[132:135], v[184:187], v[88:91]
	s_waitcnt lgkmcnt(1)
	v_mfma_f32_16x16x32_bf16 v[76:79], v[120:123], v[192:195], v[76:79]
	v_mfma_f32_16x16x32_bf16 v[72:75], v[132:135], v[192:195], v[72:75]
	v_mfma_f32_16x16x32_bf16 v[140:143], v[124:127], v[164:167], v[140:143]
	v_mfma_f32_16x16x32_bf16 v[128:131], v[136:139], v[164:167], v[128:131]
	v_mfma_f32_16x16x32_bf16 v[108:111], v[124:127], v[180:183], v[108:111]
	v_mfma_f32_16x16x32_bf16 v[104:107], v[136:139], v[180:183], v[104:107]
	v_mfma_f32_16x16x32_bf16 v[92:95], v[124:127], v[188:191], v[92:95]
	v_mfma_f32_16x16x32_bf16 v[88:91], v[136:139], v[188:191], v[88:91]
	s_waitcnt lgkmcnt(0)
	v_mfma_f32_16x16x32_bf16 v[76:79], v[124:127], v[196:199], v[76:79]
	v_mfma_f32_16x16x32_bf16 v[72:75], v[136:139], v[196:199], v[72:75]
	s_setprio 0
	s_setprio 1
	v_mfma_f32_16x16x32_bf16 v[116:119], v[144:147], v[160:163], v[116:119]
	v_mfma_f32_16x16x32_bf16 v[112:115], v[152:155], v[160:163], v[112:115]
	v_mfma_f32_16x16x32_bf16 v[100:103], v[144:147], v[176:179], v[100:103]
	v_mfma_f32_16x16x32_bf16 v[96:99], v[152:155], v[176:179], v[96:99]
	v_mfma_f32_16x16x32_bf16 v[84:87], v[144:147], v[184:187], v[84:87]
	v_mfma_f32_16x16x32_bf16 v[80:83], v[152:155], v[184:187], v[80:83]
	v_mfma_f32_16x16x32_bf16 v[68:71], v[144:147], v[192:195], v[68:71]
	v_mfma_f32_16x16x32_bf16 v[64:67], v[152:155], v[192:195], v[64:67]
	v_mfma_f32_16x16x32_bf16 v[116:119], v[148:151], v[164:167], v[116:119]
	v_mfma_f32_16x16x32_bf16 v[112:115], v[156:159], v[164:167], v[112:115]
	v_mfma_f32_16x16x32_bf16 v[100:103], v[148:151], v[180:183], v[100:103]
	v_mfma_f32_16x16x32_bf16 v[96:99], v[156:159], v[180:183], v[96:99]
	v_mfma_f32_16x16x32_bf16 v[84:87], v[148:151], v[188:191], v[84:87]
	v_mfma_f32_16x16x32_bf16 v[80:83], v[156:159], v[188:191], v[80:83]
	v_mfma_f32_16x16x32_bf16 v[68:71], v[148:151], v[196:199], v[68:71]
	v_mfma_f32_16x16x32_bf16 v[64:67], v[156:159], v[196:199], v[64:67]
	s_setprio 0
	s_barrier
	s_mov_b32 m0, s47
	s_bitset1_b32 s55, 7
	ds_read_b128 v[160:163], v175 offset:49152
	ds_read_b128 v[164:167], v175 offset:50176
	ds_read_b128 v[176:179], v175 offset:51200
	ds_read_b128 v[180:183], v175 offset:52224
	ds_read_b128 v[184:187], v175 offset:53248
	ds_read_b128 v[188:191], v175 offset:54272
	ds_read_b128 v[192:195], v175 offset:55296
	ds_read_b128 v[196:199], v175 offset:56320
	buffer_load_dwordx4 v169, s[4:7], s55 offen lds
	s_mov_b32 m0, s48
	s_nop 0
	buffer_load_dwordx4 v171, s[4:7], s55 offen lds
	s_add_i32 s55, s55, s33
	s_mov_b32 m0, s56
	s_nop 0
	buffer_load_dwordx4 v169, s[4:7], s55 offen lds
	s_mov_b32 m0, s57
	s_nop 0
	buffer_load_dwordx4 v171, s[4:7], s55 offen lds
	s_mov_b32 m0, s52
	s_nop 0
	buffer_load_dwordx4 v168, s[36:39], s54 offen lds
	s_mov_b32 m0, s53
	s_nop 0
	buffer_load_dwordx4 v170, s[36:39], s54 offen lds
	s_waitcnt vmcnt(8)
	s_waitcnt lgkmcnt(0)
	s_barrier
	s_setprio 1
	s_waitcnt lgkmcnt(7)
	v_mfma_f32_16x16x32_bf16 v[60:63], v[120:123], v[160:163], v[60:63]
	v_mfma_f32_16x16x32_bf16 v[56:59], v[132:135], v[160:163], v[56:59]
	s_waitcnt lgkmcnt(5)
	v_mfma_f32_16x16x32_bf16 v[44:47], v[120:123], v[176:179], v[44:47]
	v_mfma_f32_16x16x32_bf16 v[40:43], v[132:135], v[176:179], v[40:43]
	s_waitcnt lgkmcnt(3)
	v_mfma_f32_16x16x32_bf16 v[28:31], v[120:123], v[184:187], v[28:31]
	v_mfma_f32_16x16x32_bf16 v[24:27], v[132:135], v[184:187], v[24:27]
	s_waitcnt lgkmcnt(1)
	v_mfma_f32_16x16x32_bf16 v[12:15], v[120:123], v[192:195], v[12:15]
	v_mfma_f32_16x16x32_bf16 v[8:11], v[132:135], v[192:195], v[8:11]
	v_mfma_f32_16x16x32_bf16 v[60:63], v[124:127], v[164:167], v[60:63]
	v_mfma_f32_16x16x32_bf16 v[56:59], v[136:139], v[164:167], v[56:59]
	v_mfma_f32_16x16x32_bf16 v[44:47], v[124:127], v[180:183], v[44:47]
	v_mfma_f32_16x16x32_bf16 v[40:43], v[136:139], v[180:183], v[40:43]
	v_mfma_f32_16x16x32_bf16 v[28:31], v[124:127], v[188:191], v[28:31]
	v_mfma_f32_16x16x32_bf16 v[24:27], v[136:139], v[188:191], v[24:27]
	s_waitcnt lgkmcnt(0)
	v_mfma_f32_16x16x32_bf16 v[12:15], v[124:127], v[196:199], v[12:15]
	v_mfma_f32_16x16x32_bf16 v[8:11], v[136:139], v[196:199], v[8:11]
	s_setprio 0
	s_setprio 1
	v_mfma_f32_16x16x32_bf16 v[52:55], v[144:147], v[160:163], v[52:55]
	v_mfma_f32_16x16x32_bf16 v[48:51], v[152:155], v[160:163], v[48:51]
	v_mfma_f32_16x16x32_bf16 v[36:39], v[144:147], v[176:179], v[36:39]
	v_mfma_f32_16x16x32_bf16 v[32:35], v[152:155], v[176:179], v[32:35]
	v_mfma_f32_16x16x32_bf16 v[20:23], v[144:147], v[184:187], v[20:23]
	v_mfma_f32_16x16x32_bf16 v[16:19], v[152:155], v[184:187], v[16:19]
	v_mfma_f32_16x16x32_bf16 v[4:7], v[144:147], v[192:195], v[4:7]
	v_mfma_f32_16x16x32_bf16 v[0:3], v[152:155], v[192:195], v[0:3]
	v_mfma_f32_16x16x32_bf16 v[52:55], v[148:151], v[164:167], v[52:55]
	v_mfma_f32_16x16x32_bf16 v[48:51], v[156:159], v[164:167], v[48:51]
	v_mfma_f32_16x16x32_bf16 v[36:39], v[148:151], v[180:183], v[36:39]
	v_mfma_f32_16x16x32_bf16 v[32:35], v[156:159], v[180:183], v[32:35]
	v_mfma_f32_16x16x32_bf16 v[20:23], v[148:151], v[188:191], v[20:23]
	v_mfma_f32_16x16x32_bf16 v[16:19], v[156:159], v[188:191], v[16:19]
	v_mfma_f32_16x16x32_bf16 v[4:7], v[148:151], v[196:199], v[4:7]
	v_mfma_f32_16x16x32_bf16 v[0:3], v[156:159], v[196:199], v[0:3]
	s_setprio 0
	s_barrier
	s_add_i32 s63, s63, 2
	s_addk_i32 s61, 0x100
	s_addk_i32 s62, 0x100
	s_cmp_ge_i32 s63, s65
	s_cbranch_scc0 .LBB0_1944
	s_branch .Lpeel_after_1944

; #define PG8_BAR __builtin_amdgcn_s_barrier()
; template <class Epi, class Sched, bool ALIGN_EPI = false, bool SP2 = false, bool FP8 = false>
; __device__ __forceinline__ void gemm_phase(LAS unsigned char* lds, const Gemm g, const Sched& S, const Epi& E, int wbase) {
;     ...
;         if constexpr (ALIGN_EPI) { if (wr == 0) PG8_BAR; }
.Lpeel_after_1944:
	s_mov_b32 s100, 1
	s_and_b64 vcc, exec, s[24:25]
	s_cbranch_vccz .LBB0_1947

; __device__ __forceinline__ int opaque_s(int x) { asm volatile("" : "+s"(x)); return x; }
; #define PG8_STAGE(bufoff, rs_, soff_, voff) do { _Pragma("unroll") for (int _i = 0; _i < 2; ++_i) \
;         __builtin_amdgcn_raw_ptr_buffer_load_lds(rs_, (LAS void*)(lds + (bufoff) + ldsw + _i * 8192), 16, (int)(voff)[_i], (int)(soff_), 0, 0); } while (0)
; #define PG8_WAIT_V(n) asm volatile("s_waitcnt vmcnt(" #n ")" ::: "memory")
; #define PG8_BAR __builtin_amdgcn_s_barrier()
; #define KWS (kargs()->ws)
; #define KOUT (kargs()->out)
; template <class Epi, class Sched, bool ALIGN_EPI = false, bool SP2 = false, bool FP8 = false>
; __device__ __forceinline__ void gemm_phase(LAS unsigned char* lds, const Gemm g, const Sched& S, const Epi& E, int wbase) {
;     ...
;     if constexpr (SP2) {
;         PG8_STAGE(PG8_SB(0, 0), rBc, cB, voffB); PG8_STAGE(PG8_SB(0, 1), rBc, cB + hstep, voffB); PG8_STAGE(PG8_SA(0, 0), rAc, cA, voffA); PG8_STAGE(PG8_SA(0, 1), rAc, cA + hstep, voffA);
;         if (wr == 1) PG8_BAR;
;         PG8_WAIT_V(2); PG8_BAR;
;         PG8_STAGE(PG8_SB(1, 0), rBc, cB + kstep, voffB); PG8_STAGE(PG8_SA(1, 0), rAc, cA + kstep, voffA); PG8_STAGE(PG8_SB(1, 1), rBc, cB + hstep + kstep, voffB);
;         PG8_WAIT_V(6); PG8_BAR;
; __global__ void __launch_bounds__(512, 2) mega(Ptrs Pdummy) {
;     ...
;           unsigned char* ws = KWS; pg8::Gemm g{(const bf16*)(ws + WS_HB8), (const bf16*)(ws + WS_WPG) + (size_t)l * DM * DM, DM / 2, 0}; pg8::StaticOrder S; S.init(M, DM, opaque_s(G), opaque_s(c));
;           pg8::EpiResid<1> E{HBUF(hc), HBUF(hc ^ 1), l + 1 < DEPTH ? nullptr : KOUT, SBUF(sc ^ 1), (const bf16*)(ws + WS_PP), SBUF(sc), nullptr, 1.f / WIN_SCALE, 0}; pg8::gemm_phase<pg8::EpiResid<1>, pg8::StaticOrder, true, true, true>(lds, g, S, E, wbase); sc ^= 1; hc ^= 1; }
.LBB0_1979:
	v_readlane_b32 s15, v255, 10
	s_cmp_eq_u32 s15, 0
	s_mov_b32 s14, 0x13200000
	s_cselect_b32 s10, s14, 0x1b800000
	s_add_u32 s10, s2, s10
	s_addc_u32 s11, s3, 0
	s_cmp_eq_u32 s15, 1
	s_cselect_b32 s14, s14, 0x1b800000
	s_add_u32 s16, s2, s14
	s_addc_u32 s17, s3, 0
	s_add_u32 s14, s2, 0x17200000
	s_addc_u32 s15, s3, 0
	v_readlane_b32 s22, v255, 11
	s_cmp_eq_u32 s22, 1
	s_cselect_b32 s18, 0, 0x200000
	s_add_u32 s18, s14, s18
	s_addc_u32 s19, s15, 0
	s_add_u32 s20, s2, 0x17800000
	s_addc_u32 s21, s3, 0
	s_cmp_eq_u32 s22, 0
	s_cselect_b32 s2, 0, 0x200000
	s_add_u32 s22, s14, s2
	s_addc_u32 s23, s15, 0
	s_add_i32 s56, s43, 0x18000
	s_or_b32 s2, s5, 0x80
	s_mov_b32 s14, s38
	s_mov_b32 s15, s39
	s_mov_b32 m0, s56
	s_add_i32 s57, s43, 0x1a000
	s_waitcnt vmcnt(2)
	s_barrier
	buffer_load_dwordx4 v175, s[12:15], s2 offen lds
	s_mov_b32 m0, s57
	s_add_i32 s58, s43, 0x8000
	buffer_load_dwordx4 v177, s[12:15], s2 offen lds
	s_or_b32 s2, s4, 0x80
	s_mov_b32 m0, s58
	s_add_i32 s59, s43, 0xa000
	buffer_load_dwordx4 v174, s[36:39], s2 offen lds
	s_mov_b32 m0, s59
	s_add_i32 s65, s43, 0x1c000
	buffer_load_dwordx4 v176, s[36:39], s2 offen lds
	s_bitset1_b32 s24, 7
	s_mov_b32 m0, s65
	s_add_i32 s76, s43, 0x1e000
	buffer_load_dwordx4 v175, s[12:15], s24 offen lds
	s_mov_b32 m0, s76
	s_ashr_i32 s2, s26, 31
	buffer_load_dwordx4 v177, s[12:15], s24 offen lds
	v_bfe_u32 v179, v4, 4, 2
	s_lshr_b32 s2, s2, 26
	v_and_b32_e32 v178, 15, v4
	s_add_i32 s2, s26, s2
	v_lshlrev_b32_e32 v5, 4, v179
	v_lshlrev_b32_e32 v4, 2, v4
	s_and_b32 s79, s8, 3
	s_ashr_i32 s82, s2, 6
	v_lshl_or_b32 v5, v178, 6, v5
	s_lshl_b32 s2, s9, 13
	v_and_b32_e32 v4, 32, v4
	s_lshl_b32 s83, s9, 6
	v_bitop3_b32 v6, v5, s2, v4 bitop3:0xde
	s_lshl_b32 s24, s79, 5
	s_lshl_b32 s2, s79, 12
	s_cmp_gt_i32 s26, 63
	s_cselect_b64 s[26:27], -1, 0
	s_add_i32 s84, s82, -2
	s_add_i32 s85, s43, 0xc000
	s_cmpk_lt_u32 s25, 0x100
	s_waitcnt vmcnt(6)
	s_cselect_b64 s[28:29], -1, 0
	s_add_i32 s8, s43, 0xe000
	v_bitop3_b32 v4, v5, s2, v4 bitop3:0xde
	s_cmp_lg_u64 s[6:7], 0
	v_mov_b32_e32 v1, v0
	v_mov_b32_e32 v2, v0
	v_mov_b32_e32 v3, v0
	s_mov_b32 s77, 0
	s_mov_b32 s25, s40
	s_cselect_b64 s[30:31], -1, 0
	v_add_u32_e32 v180, 0, v4
	v_add_u32_e32 v181, 0, v6
	s_barrier
	s_mov_b32 s100, 0
	s_branch .LBB0_1982

; #define PG8_STAGE(bufoff, rs_, soff_, voff) do { _Pragma("unroll") for (int _i = 0; _i < 2; ++_i) \
;         __builtin_amdgcn_raw_ptr_buffer_load_lds(rs_, (LAS void*)(lds + (bufoff) + ldsw + _i * 8192), 16, (int)(voff)[_i], (int)(soff_), 0, 0); } while (0)
; #define PG8_LDA(dst, b, h) do { _Pragma("unroll") for (int m = 0; m < 4; ++m) dst[m] = PG8_LD2(lds + PG8_SA(b, h) + aoff + m * 2048); } while (0)
; #define PG8_LDB(dst, b, h) do { _Pragma("unroll") for (int n = 0; n < 2; ++n) dst[n] = PG8_LD2(lds + PG8_SB(b, h) + boff + n * 2048); } while (0)
; #define PG8_WAIT_V(n) asm volatile("s_waitcnt vmcnt(" #n ")" ::: "memory")
; #define PG8_WAIT_L(n) asm volatile("s_waitcnt lgkmcnt(" #n ")" ::: "memory")
; #define PG8_BAR __builtin_amdgcn_s_barrier()
; #define PG8_SCHED __builtin_amdgcn_sched_barrier(0)
; #define PG8_ZERO_ACC() do { float z_; asm volatile("v_mov_b32 %0, 0" : "=v"(z_)); _Pragma("unroll") for (int a = 0; a < 2; ++a) _Pragma("unroll") for (int b = 0; b < 2; ++b) _Pragma("unroll") for (int m = 0; m < 4; ++m) \
;         _Pragma("unroll") for (int n = 0; n < 2; ++n) acc[a][b][m][n] = (f32x4){z_, z_, z_, z_}; } while (0)
; template <class Epi, class Sched, bool ALIGN_EPI = false, bool SP2 = false, bool FP8 = false>
; __device__ __forceinline__ void gemm_phase(LAS unsigned char* lds, const Gemm g, const Sched& S, const Epi& E, int wbase) {
;     ...
;             if constexpr (SP2) {
;             PG8_LDB(B0, 0, 0); PG8_LDB(B1, 0, 1); PG8_SCHED; PG8_LDA(At, 0, 0); PG8_STAGE(PG8_SA(1, 1), rAc, a1 + hstep, voffA);
;             PG8_WAIT_V(8); PG8_WAIT_L(0); PG8_BAR; PG8_MMA(0, 0, At, B0); PG8_MMA(0, 1, At, B1); PG8_BAR; PG8_SCHED;
;             PG8_LDA(At, 0, 1); PG8_STAGE(PG8_SB(0, 0), rB2, b2, voffB); PG8_STAGE(PG8_SB(0, 1), rB2, b2 + hstep, voffB); PG8_STAGE(PG8_SA(0, 0), rA2, a2, voffA);
;             PG8_WAIT_V(8); PG8_WAIT_L(0); PG8_BAR; PG8_MMA(1, 0, At, B0); PG8_MMA(1, 1, At, B1); PG8_BAR; PG8_SCHED;
;     ...
;         if (E.reset(cur)) PG8_ZERO_ACC();
.LBB0_1988:
	s_lshl_b32 s95, s94, 18
	s_andn2_b64 vcc, exec, s[26:27]
	s_lshl_b32 s96, s9, 18
	s_cbranch_vccnz .LBB0_1992
	s_and_b64 s[2:3], s[34:35], exec
	v_mov_b64_e32 v[6:7], v[2:3]
	v_mov_b64_e32 v[18:19], v[2:3]
	v_mov_b64_e32 v[22:23], v[2:3]
	v_mov_b64_e32 v[34:35], v[2:3]
	v_mov_b64_e32 v[38:39], v[2:3]
	v_mov_b64_e32 v[50:51], v[2:3]
	v_mov_b64_e32 v[54:55], v[2:3]
	v_mov_b64_e32 v[10:11], v[2:3]
	v_mov_b64_e32 v[14:15], v[2:3]
	v_mov_b64_e32 v[26:27], v[2:3]
	v_mov_b64_e32 v[30:31], v[2:3]
	v_mov_b64_e32 v[42:43], v[2:3]
	v_mov_b64_e32 v[46:47], v[2:3]
	v_mov_b64_e32 v[58:59], v[2:3]
	s_waitcnt vmcnt(37)
	v_mov_b64_e32 v[62:63], v[2:3]
	s_waitcnt vmcnt(36)
	v_mov_b64_e32 v[66:67], v[2:3]
	s_waitcnt vmcnt(35)
	v_mov_b64_e32 v[70:71], v[2:3]
	s_waitcnt vmcnt(32)
	v_mov_b64_e32 v[82:83], v[2:3]
	s_waitcnt vmcnt(31)
	v_mov_b64_e32 v[86:87], v[2:3]
	s_waitcnt vmcnt(28)
	v_mov_b64_e32 v[98:99], v[2:3]
	s_waitcnt vmcnt(27)
	v_mov_b64_e32 v[102:103], v[2:3]
	s_waitcnt vmcnt(24)
	v_mov_b64_e32 v[114:115], v[2:3]
	s_waitcnt vmcnt(23)
	v_mov_b64_e32 v[118:119], v[2:3]
	v_mov_b64_e32 v[74:75], v[2:3]
	v_mov_b64_e32 v[78:79], v[2:3]
	v_mov_b64_e32 v[90:91], v[2:3]
	v_mov_b64_e32 v[94:95], v[2:3]
	v_mov_b64_e32 v[106:107], v[2:3]
	v_mov_b64_e32 v[110:111], v[2:3]
	v_mov_b64_e32 v[130:131], v[2:3]
	v_mov_b64_e32 v[142:143], v[2:3]
	v_mov_b32_e32 v223, 0xff61b1e6
	v_mov_b32_e32 v222, 1
	v_mov_b32_e32 v173, v233
	v_mov_b32_e32 v172, 0x358637bd
	s_cselect_b32 s2, s95, s4
	s_cselect_b32 s3, s96, s5
	s_addk_i32 s4, 0x80
	s_addk_i32 s5, 0x100
	s_mov_b32 s61, 0
	v_mov_b64_e32 v[4:5], v[0:1]
	v_mov_b64_e32 v[16:17], v[0:1]
	v_mov_b64_e32 v[20:21], v[0:1]
	v_mov_b64_e32 v[32:33], v[0:1]
	v_mov_b64_e32 v[36:37], v[0:1]
	v_mov_b64_e32 v[48:49], v[0:1]
	v_mov_b64_e32 v[52:53], v[0:1]
	v_mov_b64_e32 v[8:9], v[0:1]
	v_mov_b64_e32 v[12:13], v[0:1]
	v_mov_b64_e32 v[24:25], v[0:1]
	v_mov_b64_e32 v[28:29], v[0:1]
	v_mov_b64_e32 v[40:41], v[0:1]
	v_mov_b64_e32 v[44:45], v[0:1]
	v_mov_b64_e32 v[56:57], v[0:1]
	v_mov_b64_e32 v[60:61], v[0:1]
	v_mov_b64_e32 v[64:65], v[0:1]
	v_mov_b64_e32 v[68:69], v[0:1]
	v_mov_b64_e32 v[80:81], v[0:1]
	v_mov_b64_e32 v[84:85], v[0:1]
	v_mov_b64_e32 v[96:97], v[0:1]
	v_mov_b64_e32 v[100:101], v[0:1]
	v_mov_b64_e32 v[112:113], v[0:1]
	v_mov_b64_e32 v[116:117], v[0:1]
	v_mov_b64_e32 v[72:73], v[0:1]
	v_mov_b64_e32 v[76:77], v[0:1]
	v_mov_b64_e32 v[88:89], v[0:1]
	v_mov_b64_e32 v[92:93], v[0:1]
	v_mov_b64_e32 v[104:105], v[0:1]
	v_mov_b64_e32 v[108:109], v[0:1]
	v_mov_b64_e32 v[128:129], v[0:1]
	v_mov_b64_e32 v[140:141], v[0:1]
	s_nop 0
	s_cmp_eq_u32 s100, 1
	s_cbranch_scc0 .LBB0_1990
	v_add_u32_e32 v136, 0x10000, v180
	v_add_u32_e32 v156, 0x14000, v180
	ds_read_b128 v[120:123], v136
	ds_read_b128 v[124:127], v136 offset:1024
	ds_read_b128 v[132:135], v136 offset:2048
	ds_read_b128 v[136:139], v136 offset:3072
	ds_read_b128 v[144:147], v156
	ds_read_b128 v[148:151], v156 offset:1024
	ds_read_b128 v[152:155], v156 offset:2048
	ds_read_b128 v[156:159], v156 offset:3072
	s_add_i32 s14, s4, 0x80
	s_cmp_eq_u32 s84, s61
	s_cselect_b32 s62, s2, s14
	s_cselect_b32 s55, s3, s5
	s_or_b32 s54, s62, 0x80
	s_add_i32 s14, s42, s4
	s_mov_b32 m0, s85
	ds_read_b128 v[160:163], v181
	ds_read_b128 v[164:167], v181 offset:1024
	ds_read_b128 v[182:185], v181 offset:2048
	ds_read_b128 v[186:189], v181 offset:3072
	ds_read_b128 v[194:197], v181 offset:4096
	ds_read_b128 v[198:201], v181 offset:5120
	ds_read_b128 v[202:205], v181 offset:6144
	ds_read_b128 v[206:209], v181 offset:7168
	buffer_load_dwordx4 v174, s[36:39], s14 offen lds
	s_mov_b32 m0, s8
	s_nop 0
	buffer_load_dwordx4 v176, s[36:39], s14 offen lds
	s_waitcnt vmcnt(48)
	s_waitcnt lgkmcnt(0)
	s_barrier
	s_setprio 1
	s_waitcnt lgkmcnt(6)
	v_mfma_scale_f32_16x16x128_f8f6f4 v[140:143], v[120:127], v[160:167], v[140:143], v224, v224 op_sel_hi:[0,0,0]
	v_mfma_scale_f32_16x16x128_f8f6f4 v[128:131], v[132:139], v[160:167], v[128:131], v224, v224 op_sel_hi:[0,0,0]
	s_waitcnt lgkmcnt(4)
	v_mfma_scale_f32_16x16x128_f8f6f4 v[108:111], v[120:127], v[182:189], v[108:111], v224, v224 op_sel_hi:[0,0,0]
	v_mfma_scale_f32_16x16x128_f8f6f4 v[104:107], v[132:139], v[182:189], v[104:107], v224, v224 op_sel_hi:[0,0,0]
	s_waitcnt lgkmcnt(2)
	v_mfma_scale_f32_16x16x128_f8f6f4 v[168:171], v[120:127], v[194:201], v[92:95], v224, v224 op_sel_hi:[0,0,0]
	v_mfma_scale_f32_16x16x128_f8f6f4 v[190:193], v[132:139], v[194:201], v[88:91], v224, v224 op_sel_hi:[0,0,0]
	s_waitcnt lgkmcnt(0)
	v_mfma_scale_f32_16x16x128_f8f6f4 v[210:213], v[120:127], v[202:209], v[76:79], v224, v224 op_sel_hi:[0,0,0]
	v_mfma_scale_f32_16x16x128_f8f6f4 v[214:217], v[132:139], v[202:209], v[72:75], v224, v224 op_sel_hi:[0,0,0]
	s_setprio 0
	s_setprio 1
	v_mfma_scale_f32_16x16x128_f8f6f4 v[116:119], v[144:151], v[160:167], v[116:119], v224, v224 op_sel_hi:[0,0,0]
	v_mfma_scale_f32_16x16x128_f8f6f4 v[112:115], v[152:159], v[160:167], v[112:115], v224, v224 op_sel_hi:[0,0,0]
	v_mfma_scale_f32_16x16x128_f8f6f4 v[100:103], v[144:151], v[182:189], v[100:103], v224, v224 op_sel_hi:[0,0,0]
	v_mfma_scale_f32_16x16x128_f8f6f4 v[96:99], v[152:159], v[182:189], v[96:99], v224, v224 op_sel_hi:[0,0,0]
	v_mfma_scale_f32_16x16x128_f8f6f4 v[160:163], v[144:151], v[194:201], v[84:87], v224, v224 op_sel_hi:[0,0,0]
	v_mfma_scale_f32_16x16x128_f8f6f4 v[164:167], v[152:159], v[194:201], v[80:83], v224, v224 op_sel_hi:[0,0,0]
	v_mfma_scale_f32_16x16x128_f8f6f4 v[182:185], v[144:151], v[202:209], v[68:71], v224, v224 op_sel_hi:[0,0,0]
	v_mfma_scale_f32_16x16x128_f8f6f4 v[186:189], v[152:159], v[202:209], v[64:67], v224, v224 op_sel_hi:[0,0,0]
	s_setprio 0
	s_barrier
; #define PG8_STAGE(bufoff, rs_, soff_, voff) do { _Pragma("unroll") for (int _i = 0; _i < 2; ++_i) \
;         __builtin_amdgcn_raw_ptr_buffer_load_lds(rs_, (LAS void*)(lds + (bufoff) + ldsw + _i * 8192), 16, (int)(voff)[_i], (int)(soff_), 0, 0); } while (0)
; #define PG8_LDA(dst, b, h) do { _Pragma("unroll") for (int m = 0; m < 4; ++m) dst[m] = PG8_LD2(lds + PG8_SA(b, h) + aoff + m * 2048); } while (0)
; #define PG8_LDB(dst, b, h) do { _Pragma("unroll") for (int n = 0; n < 2; ++n) dst[n] = PG8_LD2(lds + PG8_SB(b, h) + boff + n * 2048); } while (0)
; #define PG8_WAIT_V(n) asm volatile("s_waitcnt vmcnt(" #n ")" ::: "memory")
; #define PG8_WAIT_L(n) asm volatile("s_waitcnt lgkmcnt(" #n ")" ::: "memory")
; #define PG8_BAR __builtin_amdgcn_s_barrier()
; #define PG8_SCHED __builtin_amdgcn_sched_barrier(0)
; template <class Epi, class Sched, bool ALIGN_EPI = false, bool SP2 = false, bool FP8 = false>
; __device__ __forceinline__ void gemm_phase(LAS unsigned char* lds, const Gemm g, const Sched& S, const Epi& E, int wbase) {
;     ...
;             PG8_LDA(At, 0, 1); PG8_STAGE(PG8_SB(0, 0), rB2, b2, voffB); PG8_STAGE(PG8_SB(0, 1), rB2, b2 + hstep, voffB); PG8_STAGE(PG8_SA(0, 0), rA2, a2, voffA);
;             PG8_WAIT_V(8); PG8_WAIT_L(0); PG8_BAR; PG8_MMA(1, 0, At, B0); PG8_MMA(1, 1, At, B1); PG8_BAR; PG8_SCHED;
;             PG8_LDB(B0, 1, 0); PG8_LDB(B1, 1, 1); PG8_SCHED; PG8_LDA(At, 1, 0); PG8_STAGE(PG8_SA(0, 1), rA2, a2 + hstep, voffA);
;             PG8_WAIT_V(8); PG8_WAIT_L(0); PG8_BAR; PG8_MMA(0, 0, At, B0); PG8_MMA(0, 1, At, B1); PG8_BAR; PG8_SCHED;
	s_mov_b32 m0, s44
	s_mov_b32 s14, s38
	s_mov_b32 s15, s39
	s_nop 1
	ds_read_b128 v[64:67], v181 offset:16384
	ds_read_b128 v[68:71], v181 offset:17408
	ds_read_b128 v[72:75], v181 offset:18432
	ds_read_b128 v[76:79], v181 offset:19456
	ds_read_b128 v[80:83], v181 offset:20480
	ds_read_b128 v[84:87], v181 offset:21504
	ds_read_b128 v[88:91], v181 offset:22528
	ds_read_b128 v[92:95], v181 offset:23552
	buffer_load_dwordx4 v175, s[12:15], s55 offen lds
	s_mov_b32 m0, s45
	s_add_i32 s63, s55, s42
	buffer_load_dwordx4 v177, s[12:15], s55 offen lds
	s_mov_b32 m0, s46
	s_nop 0
	buffer_load_dwordx4 v175, s[12:15], s63 offen lds
	s_mov_b32 m0, s47
	s_nop 0
	buffer_load_dwordx4 v177, s[12:15], s63 offen lds
	s_mov_b32 m0, s43
	s_nop 0
	buffer_load_dwordx4 v174, s[36:39], s62 offen lds
	s_mov_b32 m0, s48
	s_nop 0
	buffer_load_dwordx4 v176, s[36:39], s62 offen lds
	s_waitcnt vmcnt(48)
	s_waitcnt lgkmcnt(0)
	s_barrier
	s_setprio 1
	s_waitcnt lgkmcnt(6)
	v_mfma_scale_f32_16x16x128_f8f6f4 v[60:63], v[120:127], v[64:71], v[60:63], v224, v224 op_sel_hi:[0,0,0]
	v_mfma_scale_f32_16x16x128_f8f6f4 v[56:59], v[132:139], v[64:71], v[56:59], v224, v224 op_sel_hi:[0,0,0]
	s_waitcnt lgkmcnt(4)
	v_mfma_scale_f32_16x16x128_f8f6f4 v[194:197], v[120:127], v[72:79], v[44:47], v224, v224 op_sel_hi:[0,0,0]
	v_mfma_scale_f32_16x16x128_f8f6f4 v[198:201], v[132:139], v[72:79], v[40:43], v224, v224 op_sel_hi:[0,0,0]
	s_waitcnt lgkmcnt(2)
	v_mfma_scale_f32_16x16x128_f8f6f4 v[202:205], v[120:127], v[80:87], v[28:31], v224, v224 op_sel_hi:[0,0,0]
	v_mfma_scale_f32_16x16x128_f8f6f4 v[206:209], v[132:139], v[80:87], v[24:27], v224, v224 op_sel_hi:[0,0,0]
	s_waitcnt lgkmcnt(0)
	v_mfma_scale_f32_16x16x128_f8f6f4 v[218:221], v[120:127], v[88:95], v[12:15], v224, v224 op_sel_hi:[0,0,0]
	v_mfma_scale_f32_16x16x128_f8f6f4 v[226:229], v[132:139], v[88:95], v[8:11], v224, v224 op_sel_hi:[0,0,0]
	s_setprio 0
	s_setprio 1
	v_mfma_scale_f32_16x16x128_f8f6f4 v[52:55], v[144:151], v[64:71], v[52:55], v224, v224 op_sel_hi:[0,0,0]
	v_mfma_scale_f32_16x16x128_f8f6f4 v[48:51], v[152:159], v[64:71], v[48:51], v224, v224 op_sel_hi:[0,0,0]
	v_mfma_scale_f32_16x16x128_f8f6f4 v[230:233], v[144:151], v[72:79], v[36:39], v224, v224 op_sel_hi:[0,0,0]
	v_mfma_scale_f32_16x16x128_f8f6f4 v[234:237], v[152:159], v[72:79], v[32:35], v224, v224 op_sel_hi:[0,0,0]
	v_mfma_scale_f32_16x16x128_f8f6f4 v[238:241], v[144:151], v[80:87], v[20:23], v224, v224 op_sel_hi:[0,0,0]
	v_mfma_scale_f32_16x16x128_f8f6f4 v[242:245], v[152:159], v[80:87], v[16:19], v224, v224 op_sel_hi:[0,0,0]
	v_mfma_scale_f32_16x16x128_f8f6f4 v[246:249], v[144:151], v[88:95], v[4:7], v224, v224 op_sel_hi:[0,0,0]
	v_mfma_scale_f32_16x16x128_f8f6f4 v[250:253], v[152:159], v[88:95], v[0:3], v224, v224 op_sel_hi:[0,0,0]
	s_setprio 0
	s_barrier
	v_add_u32_e32 v8, 0x18000, v180
	s_nop 3
	ds_read_b128 v[0:3], v8
	ds_read_b128 v[4:7], v8 offset:1024
	ds_read_b128 v[16:19], v8 offset:2048
	ds_read_b128 v[20:23], v8 offset:3072
	v_add_u32_e32 v8, 0x1c000, v180
	ds_read_b128 v[120:123], v8
	ds_read_b128 v[124:127], v8 offset:1024
	ds_read_b128 v[132:135], v8 offset:2048
	ds_read_b128 v[136:139], v8 offset:3072
	s_add_i32 s62, s62, s42
	s_mov_b32 m0, s52
	ds_read_b128 v[8:11], v181 offset:32768
	ds_read_b128 v[12:15], v181 offset:33792
	ds_read_b128 v[24:27], v181 offset:34816
	ds_read_b128 v[28:31], v181 offset:35840
	ds_read_b128 v[32:35], v181 offset:36864
	ds_read_b128 v[36:39], v181 offset:37888
	ds_read_b128 v[40:43], v181 offset:38912
	ds_read_b128 v[44:47], v181 offset:39936
	buffer_load_dwordx4 v174, s[36:39], s62 offen lds
	s_mov_b32 m0, s53
	s_nop 0
	buffer_load_dwordx4 v176, s[36:39], s62 offen lds
	s_waitcnt vmcnt(8)
	s_waitcnt lgkmcnt(0)
	s_barrier
; #define PG8_STAGE(bufoff, rs_, soff_, voff) do { _Pragma("unroll") for (int _i = 0; _i < 2; ++_i) \
;         __builtin_amdgcn_raw_ptr_buffer_load_lds(rs_, (LAS void*)(lds + (bufoff) + ldsw + _i * 8192), 16, (int)(voff)[_i], (int)(soff_), 0, 0); } while (0)
; #define PG8_LDA(dst, b, h) do { _Pragma("unroll") for (int m = 0; m < 4; ++m) dst[m] = PG8_LD2(lds + PG8_SA(b, h) + aoff + m * 2048); } while (0)
; #define PG8_LDB(dst, b, h) do { _Pragma("unroll") for (int n = 0; n < 2; ++n) dst[n] = PG8_LD2(lds + PG8_SB(b, h) + boff + n * 2048); } while (0)
; #define PG8_WAIT_V(n) asm volatile("s_waitcnt vmcnt(" #n ")" ::: "memory")
; #define PG8_WAIT_L(n) asm volatile("s_waitcnt lgkmcnt(" #n ")" ::: "memory")
; #define PG8_BAR __builtin_amdgcn_s_barrier()
; #define PG8_SCHED __builtin_amdgcn_sched_barrier(0)
; template <class Epi, class Sched, bool ALIGN_EPI = false, bool SP2 = false, bool FP8 = false>
; __device__ __forceinline__ void gemm_phase(LAS unsigned char* lds, const Gemm g, const Sched& S, const Epi& E, int wbase) {
;     ...
;         for (int t = 0; t < nt; t += 2) {
;             const bool last = (t == nt - 2);
;             const unsigned a1 = cA + (unsigned)(t + 1) * kstep;
;             const unsigned a2 = last ? nA : cA + (unsigned)(t + 2) * kstep, b2 = last ? nB : cB + (unsigned)(t + 2) * kstep; const rsrc_t rA2 = (Sched::TWO && last) ? rAn : rAc, rB2 = (Sched::TWO && last) ? rBn : rBc;
;     ...
;             PG8_LDB(B0, 1, 0); PG8_LDB(B1, 1, 1); PG8_SCHED; PG8_LDA(At, 1, 0); PG8_STAGE(PG8_SA(0, 1), rA2, a2 + hstep, voffA);
;             PG8_WAIT_V(8); PG8_WAIT_L(0); PG8_BAR; PG8_MMA(0, 0, At, B0); PG8_MMA(0, 1, At, B1); PG8_BAR; PG8_SCHED;
;             PG8_LDA(At, 1, 1); PG8_STAGE(PG8_SB(1, 0), rB2, b3, voffB); PG8_STAGE(PG8_SB(1, 1), rB2, b3 + hstep, voffB); PG8_STAGE(PG8_SA(1, 0), rA2, a3, voffA);
;             PG8_WAIT_V(8); PG8_WAIT_L(0); PG8_BAR; PG8_MMA(1, 0, At, B0); PG8_MMA(1, 1, At, B1); PG8_BAR; PG8_SCHED;
	s_setprio 1
	s_waitcnt lgkmcnt(6)
	v_mfma_scale_f32_16x16x128_f8f6f4 v[140:143], v[0:7], v[8:15], v[140:143], v224, v224 op_sel_hi:[0,0,0]
	v_mfma_scale_f32_16x16x128_f8f6f4 v[128:131], v[16:23], v[8:15], v[128:131], v224, v224 op_sel_hi:[0,0,0]
	s_waitcnt lgkmcnt(4)
	v_mfma_scale_f32_16x16x128_f8f6f4 v[108:111], v[0:7], v[24:31], v[108:111], v224, v224 op_sel_hi:[0,0,0]
	v_mfma_scale_f32_16x16x128_f8f6f4 v[104:107], v[16:23], v[24:31], v[104:107], v224, v224 op_sel_hi:[0,0,0]
	s_waitcnt lgkmcnt(2)
	v_mfma_scale_f32_16x16x128_f8f6f4 v[92:95], v[0:7], v[32:39], v[168:171], v224, v224 op_sel_hi:[0,0,0]
	v_mfma_scale_f32_16x16x128_f8f6f4 v[88:91], v[16:23], v[32:39], v[190:193], v224, v224 op_sel_hi:[0,0,0]
	s_waitcnt lgkmcnt(0)
	v_mfma_scale_f32_16x16x128_f8f6f4 v[76:79], v[0:7], v[40:47], v[210:213], v224, v224 op_sel_hi:[0,0,0]
	v_mfma_scale_f32_16x16x128_f8f6f4 v[72:75], v[16:23], v[40:47], v[214:217], v224, v224 op_sel_hi:[0,0,0]
	s_setprio 0
	s_setprio 1
	v_mfma_scale_f32_16x16x128_f8f6f4 v[116:119], v[120:127], v[8:15], v[116:119], v224, v224 op_sel_hi:[0,0,0]
	v_mfma_scale_f32_16x16x128_f8f6f4 v[112:115], v[132:139], v[8:15], v[112:115], v224, v224 op_sel_hi:[0,0,0]
	v_mfma_scale_f32_16x16x128_f8f6f4 v[100:103], v[120:127], v[24:31], v[100:103], v224, v224 op_sel_hi:[0,0,0]
	v_mfma_scale_f32_16x16x128_f8f6f4 v[96:99], v[132:139], v[24:31], v[96:99], v224, v224 op_sel_hi:[0,0,0]
	v_mfma_scale_f32_16x16x128_f8f6f4 v[84:87], v[120:127], v[32:39], v[160:163], v224, v224 op_sel_hi:[0,0,0]
	v_mfma_scale_f32_16x16x128_f8f6f4 v[80:83], v[132:139], v[32:39], v[164:167], v224, v224 op_sel_hi:[0,0,0]
	v_mfma_scale_f32_16x16x128_f8f6f4 v[68:71], v[120:127], v[40:47], v[182:185], v224, v224 op_sel_hi:[0,0,0]
	v_mfma_scale_f32_16x16x128_f8f6f4 v[64:67], v[132:139], v[40:47], v[186:189], v224, v224 op_sel_hi:[0,0,0]
	s_setprio 0
	s_barrier
	s_mov_b32 m0, s56
	s_bitset1_b32 s55, 7
	ds_read_b128 v[32:35], v181 offset:49152
	ds_read_b128 v[36:39], v181 offset:50176
	ds_read_b128 v[144:147], v181 offset:51200
	ds_read_b128 v[148:151], v181 offset:52224
	ds_read_b128 v[152:155], v181 offset:53248
	ds_read_b128 v[156:159], v181 offset:54272
	ds_read_b128 v[160:163], v181 offset:55296
	ds_read_b128 v[164:167], v181 offset:56320
	buffer_load_dwordx4 v175, s[12:15], s55 offen lds
	s_mov_b32 m0, s57
	s_nop 0
	buffer_load_dwordx4 v177, s[12:15], s55 offen lds
	s_add_i32 s55, s55, s42
	s_mov_b32 m0, s65
	s_nop 0
	buffer_load_dwordx4 v175, s[12:15], s55 offen lds
	s_mov_b32 m0, s76
	s_nop 0
	buffer_load_dwordx4 v177, s[12:15], s55 offen lds
	s_mov_b32 m0, s58
	s_nop 0
	buffer_load_dwordx4 v174, s[36:39], s54 offen lds
	s_mov_b32 m0, s59
	s_nop 0
	buffer_load_dwordx4 v176, s[36:39], s54 offen lds
	s_waitcnt vmcnt(8)
	s_waitcnt lgkmcnt(0)
	s_barrier
	s_setprio 1
	s_waitcnt lgkmcnt(6)
	v_mfma_scale_f32_16x16x128_f8f6f4 v[60:63], v[0:7], v[32:39], v[60:63], v224, v224 op_sel_hi:[0,0,0]
	v_mfma_scale_f32_16x16x128_f8f6f4 v[56:59], v[16:23], v[32:39], v[56:59], v224, v224 op_sel_hi:[0,0,0]
	s_waitcnt lgkmcnt(4)
	v_mfma_scale_f32_16x16x128_f8f6f4 v[44:47], v[0:7], v[144:151], v[194:197], v224, v224 op_sel_hi:[0,0,0]
	v_mfma_scale_f32_16x16x128_f8f6f4 v[40:43], v[16:23], v[144:151], v[198:201], v224, v224 op_sel_hi:[0,0,0]
	s_waitcnt lgkmcnt(2)
	v_mfma_scale_f32_16x16x128_f8f6f4 v[28:31], v[0:7], v[152:159], v[202:205], v224, v224 op_sel_hi:[0,0,0]
	v_mfma_scale_f32_16x16x128_f8f6f4 v[24:27], v[16:23], v[152:159], v[206:209], v224, v224 op_sel_hi:[0,0,0]
	s_waitcnt lgkmcnt(0)
	v_mfma_scale_f32_16x16x128_f8f6f4 v[12:15], v[0:7], v[160:167], v[218:221], v224, v224 op_sel_hi:[0,0,0]
	v_mfma_scale_f32_16x16x128_f8f6f4 v[8:11], v[16:23], v[160:167], v[226:229], v224, v224 op_sel_hi:[0,0,0]
	s_setprio 0
	s_setprio 1
	v_mfma_scale_f32_16x16x128_f8f6f4 v[52:55], v[120:127], v[32:39], v[52:55], v224, v224 op_sel_hi:[0,0,0]
	v_mfma_scale_f32_16x16x128_f8f6f4 v[48:51], v[132:139], v[32:39], v[48:51], v224, v224 op_sel_hi:[0,0,0]
	v_mfma_scale_f32_16x16x128_f8f6f4 v[36:39], v[120:127], v[144:151], v[230:233], v224, v224 op_sel_hi:[0,0,0]
	v_mfma_scale_f32_16x16x128_f8f6f4 v[32:35], v[132:139], v[144:151], v[234:237], v224, v224 op_sel_hi:[0,0,0]
	v_mfma_scale_f32_16x16x128_f8f6f4 v[20:23], v[120:127], v[152:159], v[238:241], v224, v224 op_sel_hi:[0,0,0]
	v_mfma_scale_f32_16x16x128_f8f6f4 v[16:19], v[132:139], v[152:159], v[242:245], v224, v224 op_sel_hi:[0,0,0]
	v_mfma_scale_f32_16x16x128_f8f6f4 v[4:7], v[120:127], v[160:167], v[246:249], v224, v224 op_sel_hi:[0,0,0]
	v_mfma_scale_f32_16x16x128_f8f6f4 v[0:3], v[132:139], v[160:167], v[250:253], v224, v224 op_sel_hi:[0,0,0]
	s_setprio 0
	s_barrier
	s_add_i32 s61, s61, 2
	s_addk_i32 s4, 0x100
	s_addk_i32 s5, 0x100
	s_cmp_ge_i32 s61, s82
	s_cbranch_scc0 .LBB0_1990
	s_branch .Lpeel_after_1990

; #define PG8_BAR __builtin_amdgcn_s_barrier()
; template <class Epi, class Sched, bool ALIGN_EPI = false, bool SP2 = false, bool FP8 = false>
; __device__ __forceinline__ void gemm_phase(LAS unsigned char* lds, const Gemm g, const Sched& S, const Epi& E, int wbase) {
;     ...
;         if constexpr (ALIGN_EPI) { if (wr == 0) PG8_BAR; }
.Lpeel_after_1990:
	s_mov_b32 s100, 1
	v_mov_b32_e32 v230, v172
	v_mov_b32_e32 v233, v173
	v_mov_b32_e32 v231, v222
	v_mov_b32_e32 v234, v223
	s_and_b64 vcc, exec, s[28:29]
	s_cbranch_vccnz .LBB0_1993
	s_branch .LBB0_1994

; __global__ void __launch_bounds__(512, 2) mega(Ptrs Pdummy) {
	.amdhsa_kernel _Z4mega4Ptrs
		.amdhsa_group_segment_fixed_size 0
		.amdhsa_private_segment_fixed_size 0
		.amdhsa_kernarg_size 512
		.amdhsa_user_sgpr_count 2
		.amdhsa_user_sgpr_dispatch_ptr 0
		.amdhsa_user_sgpr_queue_ptr 0
		.amdhsa_user_sgpr_kernarg_segment_ptr 1
		.amdhsa_user_sgpr_dispatch_id 0
		.amdhsa_user_sgpr_kernarg_preload_length 0
		.amdhsa_user_sgpr_kernarg_preload_offset 0
		.amdhsa_user_sgpr_private_segment_size 0
		.amdhsa_uses_dynamic_stack 0
		.amdhsa_enable_private_segment 0
		.amdhsa_system_sgpr_workgroup_id_x 1
		.amdhsa_system_sgpr_workgroup_id_y 0
		.amdhsa_system_sgpr_workgroup_id_z 0
		.amdhsa_system_sgpr_workgroup_info 0
		.amdhsa_system_vgpr_workitem_id 0
		.amdhsa_next_free_vgpr 256
		.amdhsa_next_free_sgpr 102
		.amdhsa_accum_offset 256
		.amdhsa_reserve_vcc 1
		.amdhsa_float_round_mode_32 0
		.amdhsa_float_round_mode_16_64 0
		.amdhsa_float_denorm_mode_32 3
		.amdhsa_float_denorm_mode_16_64 3
		.amdhsa_dx10_clamp 1
		.amdhsa_ieee_mode 1
		.amdhsa_fp16_overflow 0
		.amdhsa_tg_split 0
		.amdhsa_exception_fp_ieee_invalid_op 0
		.amdhsa_exception_fp_denorm_src 0
		.amdhsa_exception_fp_ieee_div_zero 0
		.amdhsa_exception_fp_ieee_overflow 0
		.amdhsa_exception_fp_ieee_underflow 0
		.amdhsa_exception_fp_ieee_inexact 0
		.amdhsa_exception_int_div_zero 0
	.end_amdhsa_kernel

; __global__ void __launch_bounds__(512, 2) mega(Ptrs Pdummy) {
amdhsa.kernels:
  - .agpr_count:     0
    .args:
      - .offset:         0
        .size:           256
        .value_kind:     by_value
      - .offset:         256
        .size:           4
        .value_kind:     hidden_block_count_x
      - .offset:         260
        .size:           4
        .value_kind:     hidden_block_count_y
      - .offset:         264
        .size:           4
        .value_kind:     hidden_block_count_z
      - .offset:         268
        .size:           2
        .value_kind:     hidden_group_size_x
      - .offset:         270
        .size:           2
        .value_kind:     hidden_group_size_y
      - .offset:         272
        .size:           2
        .value_kind:     hidden_group_size_z
      - .offset:         274
        .size:           2
        .value_kind:     hidden_remainder_x
      - .offset:         276
        .size:           2
        .value_kind:     hidden_remainder_y
      - .offset:         278
        .size:           2
        .value_kind:     hidden_remainder_z
      - .offset:         296
        .size:           8
        .value_kind:     hidden_global_offset_x
      - .offset:         304
        .size:           8
        .value_kind:     hidden_global_offset_y
      - .offset:         312
        .size:           8
        .value_kind:     hidden_global_offset_z
      - .offset:         320
        .size:           2
        .value_kind:     hidden_grid_dims
      - .offset:         376
        .size:           4
        .value_kind:     hidden_dynamic_lds_size
    .group_segment_fixed_size: 0
    .kernarg_segment_align: 8
    .kernarg_segment_size: 512
    .language:       OpenCL C
    .language_version:
      - 2
      - 0
    .max_flat_workgroup_size: 512
    .name:           _Z4mega4Ptrs
    .private_segment_fixed_size: 0
    .sgpr_count:     108
    .sgpr_spill_count: 57
    .symbol:         _Z4mega4Ptrs.kd
    .uniform_work_group_size: 1
    .uses_dynamic_stack: false
    .vgpr_count:     256
    .vgpr_spill_count: 0
    .wavefront_size: 64
